# MoE-down units stream 8 column blocks (2 units per workgroup instead of 4); SWA V staging: 3 loads in flight, one wait
# speedup vs baseline: 1.0523x; 1.0113x over previous
; #define LAS __attribute__((address_space(3)))
; __device__ __forceinline__ void swa_unit(Frame& F, int b, int kvh, int qb) {
;     ...
;     for (int task = tid; task < 1536; task += NTHREADS) { const int key = task >> 3, c = task & 7, kg = K0 + key;
;         u32x4 v = (u32x4){0u, 0u, 0u, 0u};
;         if (kg >= 0) v = *(const u32x4*)(PROJ + (rowb + kg) * LDP + C_SV + kvh * 64 + 8 * c);
;         *(LAS u32x4*)(Vl + key * SWA_KROW + 16 * c) = v; }
;     __syncthreads();
;     const int qh = kvh * 8 + F.wave;
;     const float sink2 = F.sinks[qh] * 1.4426950408889634f;
.LBB0_278:
	s_or_b64 exec, exec, s[44:45]
	v_add_u32_e32 v6, s10, v114
	v_mov_b32_e32 v7, v83
	v_add_u32_e32 v172, 64, v6
	v_mov_b32_e32 v173, v83
	v_add_u32_e32 v174, 0x80, v6
	v_mov_b32_e32 v175, v83
	v_mov_b32_e32 v101, v83
	s_lshl_b32 s0, s5, 1
	v_cmp_lt_i32_e32 vcc, -1, v6
	v_mov_b32_e32 v176, 0
	v_mov_b32_e32 v177, 0
	v_mov_b32_e32 v178, 0
	v_mov_b32_e32 v179, 0
	s_and_saveexec_b64 s[46:47], vcc
	v_lshl_add_u64 v[188:189], s[90:91], 0, v[6:7]
	v_mov_b64_e32 v[190:191], s[96:97]
	v_mad_u64_u32 v[190:191], s[50:51], v188, s85, v[190:191]
	v_mad_i32_i24 v191, v189, s85, v191
	v_lshl_add_u64 v[188:189], v[190:191], 0, s[0:1]
	v_lshl_add_u64 v[188:189], v[188:189], 0, v[100:101]
	v_add_co_u32_e32 v188, vcc, 0x4000, v188
	s_nop 1
	v_addc_co_u32_e32 v189, vcc, 0, v189, vcc
	global_load_dwordx4 v[176:179], v[188:189], off offset:512
	s_or_b64 exec, exec, s[46:47]
	v_cmp_lt_i32_e32 vcc, -1, v172
	v_mov_b32_e32 v180, 0
	v_mov_b32_e32 v181, 0
	v_mov_b32_e32 v182, 0
	v_mov_b32_e32 v183, 0
	s_and_saveexec_b64 s[46:47], vcc
	v_lshl_add_u64 v[188:189], s[90:91], 0, v[172:173]
	v_mov_b64_e32 v[190:191], s[96:97]
	v_mad_u64_u32 v[190:191], s[50:51], v188, s85, v[190:191]
	v_mad_i32_i24 v191, v189, s85, v191
	v_lshl_add_u64 v[188:189], v[190:191], 0, s[0:1]
	v_lshl_add_u64 v[188:189], v[188:189], 0, v[100:101]
	v_add_co_u32_e32 v188, vcc, 0x4000, v188
	s_nop 1
	v_addc_co_u32_e32 v189, vcc, 0, v189, vcc
	global_load_dwordx4 v[180:183], v[188:189], off offset:512
	s_or_b64 exec, exec, s[46:47]
	v_cmp_lt_i32_e32 vcc, -1, v174
	v_mov_b32_e32 v184, 0
	v_mov_b32_e32 v185, 0
	v_mov_b32_e32 v186, 0
	v_mov_b32_e32 v187, 0
	s_and_saveexec_b64 s[46:47], vcc
	v_lshl_add_u64 v[188:189], s[90:91], 0, v[174:175]
	v_mov_b64_e32 v[190:191], s[96:97]
	v_mad_u64_u32 v[190:191], s[50:51], v188, s85, v[190:191]
	v_mad_i32_i24 v191, v189, s85, v191
	v_lshl_add_u64 v[188:189], v[190:191], 0, s[0:1]
	v_lshl_add_u64 v[188:189], v[188:189], 0, v[100:101]
	v_add_co_u32_e32 v188, vcc, 0x4000, v188
	s_nop 1
	v_addc_co_u32_e32 v189, vcc, 0, v189, vcc
	global_load_dwordx4 v[184:187], v[188:189], off offset:512
	s_or_b64 exec, exec, s[46:47]
	s_waitcnt vmcnt(0)
	ds_write_b128 v115, v[176:179]
	ds_write_b128 v115, v[180:183] offset:9216
	ds_write_b128 v115, v[184:187] offset:18432
.LBB0_282:
	s_lshl_b32 s0, s4, 3
	v_readlane_b32 s4, v254, 23
	s_add_i32 s0, s0, s4
	s_lshl_b32 s4, s0, 2
	v_mov_b32_e32 v2, s4
	s_waitcnt lgkmcnt(0)
	s_barrier
	global_load_dword v2, v2, s[78:79]
	s_and_b32 s10, s89, 0x7f
	v_readlane_b32 s5, v254, 24
	s_lshl_b32 s84, s10, 6
	s_add_i32 s4, s84, 0xffffff80
	s_lshl_b32 s5, s0, 6
	s_cmp_gt_u32 s10, 1
	v_readlane_b32 s46, v254, 58
	s_cselect_b64 s[74:75], -1, 0
	v_readlane_b32 s47, v254, 59
	s_mov_b32 s11, 0
	s_and_b64 s[44:45], s[74:75], s[8:9]
	s_and_b64 s[46:47], s[74:75], s[46:47]
	s_and_b64 s[48:49], s[74:75], s[12:13]
	s_and_b64 s[50:51], s[74:75], s[14:15]
	s_and_b64 s[52:53], s[74:75], s[16:17]
	s_and_b64 s[54:55], s[74:75], s[18:19]
	s_and_b64 s[56:57], s[74:75], s[20:21]
	s_and_b64 s[58:59], s[74:75], s[22:23]
	s_and_b64 s[60:61], s[74:75], s[24:25]
	s_and_b64 s[62:63], s[74:75], s[26:27]
	s_and_b64 s[64:65], s[74:75], s[28:29]
	s_and_b64 s[66:67], s[74:75], s[30:31]
	s_and_b64 s[68:69], s[74:75], s[34:35]
	s_and_b64 s[70:71], s[74:75], s[36:37]
	s_and_b64 s[72:73], s[74:75], s[38:39]
	s_and_b64 s[74:75], s[74:75], s[40:41]
	s_mov_b64 s[94:95], -1
	s_waitcnt vmcnt(0)
	v_mul_f32_e32 v99, 0x3fb8aa3b, v2
	s_branch .LBB0_284

; #define MOE_UNIT(idx_, x_, RMAX, CBN, e_, rb_, cb_, ok_) do { int b_ = 0; ok_ = false; for (int k_ = 0; k_ < 8; ++k_) { const int ee_ = (x_) + 8 * k_, n_ = ((ecnt[ee_] + (RMAX) - 1) / (RMAX)) * (CBN); \
;         if ((idx_) < b_ + n_) { e_ = ee_; rb_ = ((idx_) - b_) / (CBN); cb_ = ((idx_) - b_) % (CBN); ok_ = true; break; } b_ += n_; } } while (0)
; __global__ void __launch_bounds__(NTHREADS, 2) hymba_fwd(Args args) {
;     ...
;         const int x = F.bid & 7;
;         for (int j = F.bid >> 3; ; j += F.G >> 3) { int e = 0, rb = 0, cq = 0; bool ok; MOE_UNIT(j, x, mu::DR, (32 / mu::DCB), e, rb, cq, ok); if (!ok) break;
;             const int n = ecnt[e], nrb = (n + mu::DR - 1) / mu::DR, base = n / nrb, rem = n % nrb, r0 = rb * base + (rb < rem ? rb : rem), nv = base + (rb < rem ? 1 : 0);
.LBB0_792:
	v_mov_b32_e32 v2, s13
	ds_read_b32 v2, v2
	s_waitcnt lgkmcnt(0)
	v_readfirstlane_b32 s10, v2
	s_addk_i32 s10, 0x13f
	s_mul_hi_i32 s10, s10, 0x66666667
	s_lshr_b32 s11, s10, 31
	s_ashr_i32 s10, s10, 7
	s_add_i32 s10, s10, s11
	s_lshl_b32 s10, s10, 2
	s_add_i32 s54, s10, s22
	s_cmp_ge_i32 s33, s54
	s_cselect_b64 s[10:11], -1, 0
	s_and_b64 vcc, exec, s[10:11]
	s_cbranch_vccnz .LBB0_794
	s_sub_i32 s6, s33, s22
	s_ashr_i32 s7, s6, 31
	s_lshr_b32 s7, s7, 30
	s_add_i32 s8, s6, s7
	s_ashr_i32 s7, s8, 2
	s_and_b32 s8, s8, -4
	s_sub_i32 s14, s6, s8
	s_mov_b64 s[8:9], -1
	s_mov_b32 s6, s12
	s_mov_b32 s54, s22

; __device__ __forceinline__ void moe_down_stream(PG8_LAS unsigned char* lds, int e, int cb0, int slot0, int nv, const bf16_t* HIDp, const float* Wd, bf16_t* Y, const float* slot_w, const int* slot_dst) {
;     constexpr int K = 512, NT = 8 * DCB, RB = 4096 * 4;
;     const int tid = threadIdx.x, wid = __builtin_amdgcn_readfirstlane(tid >> 6), lane = tid & 63, wr = wid >> 1, wc = wid & 1, fr = lane & 15, fq = lane >> 4;
;     unsigned aoff[5];
; #pragma unroll
;     for (int i = 0; i < 5; ++i) { const int R = 8 * (wid + 8 * i) + (lane >> 3), C = 8 * ((lane & 7) ^ ((R >> 1) & 7)); const int w4 = R / DRW; int r = 4 * (R - DRW * w4) + w4; r = r < nv ? r : r % nv;
;         aoff[i] = ((unsigned)(slot0 + r) * (unsigned)K + (unsigned)C) * 2u; }
;     const int c0_ = 2 * lane, R0 = 64 * (c0_ >> 6) + 16 * (2 * ((c0_ >> 5) & 1) + ((c0_ >> 2) & 1)) + 4 * ((c0_ >> 3) & 3) + (c0_ & 3);
;     const char* Bb = (const char*)(Wd + (size_t)e * K * 4096 + 128 * cb0 + 2 * lane) + (size_t)(8 * wid) * RB;
;     const unsigned bw0 = (unsigned)(R0 * 128 + ((wid ^ ((R0 >> 1) & 7)) * 16)), bw1 = bw0 + 128u;
;     const int nvw = (nv - wr + 3) >> 2, mcnt = nvw <= 0 ? 0 : (((nvw + 15) >> 4) > DNM ? DNM : ((nvw + 15) >> 4));
;     unsigned amask = 0u;
; #pragma unroll
;     for (int i = 0; i < 5; ++i) { const int grp = 4 * i + (wid >> 1), w4 = grp / DNM, mf = grp % DNM, nv4 = (nv - w4 + 3) >> 2, mc4 = nv4 <= 0 ? 0 : ((nv4 + 15) >> 4); if (mf < mc4) amask |= 1u << i; }
;     LAS int* ldst = (LAS int*)(lds + MD_TAB_OFF); LAS float* lw = (LAS float*)(ldst + DR);
;     PG8_LAS unsigned char* stg = lds + MD_STG_OFF + wid * 2048;
;     __syncthreads();
;     for (int r = tid; r < DR; r += 512) { const bool ok = r < nv; ldst[r] = ok ? slot_dst[slot0 + r] : -1; lw[r] = ok ? slot_w[slot0 + r] : 0.f; }
;     asm volatile("s_waitcnt vmcnt(0)" ::: "memory");
;     ...
;     f32x4 acc[DNM][4];
; #pragma unroll
;     for (int m = 0; m < DNM; ++m)
; #pragma unroll
;         for (int n = 0; n < 4; ++n) acc[m][n] = (f32x4){0.f, 0.f, 0.f, 0.f};
;     f32x2 s0[8], s1[8];
;     MD_GLDS_A(0, 0); MD_B_ISSUE(s0, 0); MD_B_ISSUE(s1, 1);
;     MD_B_WAIT(s0, 8); MD_B_WRITE(s0, 0); __builtin_amdgcn_sched_barrier(0); MD_B_ISSUE(s0, 2);
;     asm volatile("s_waitcnt vmcnt(16)" ::: "memory");
;     asm volatile("s_waitcnt lgkmcnt(0)" ::: "memory"); __builtin_amdgcn_s_barrier(); asm volatile("" ::: "memory");
.Lmd_used_4:
	v_bfe_u32 v180, v131, 1, 3
	v_xor_b32_e32 v180, v171, v180
	v_lshlrev_b32_e32 v180, 4, v180
	v_lshl_add_u32 v180, v170, 7, v180
	s_mul_i32 s57, s67, 0x2800
	v_add_u32_e32 v135, s57, v180
	v_xor_b32_e32 v137, 64, v135
	s_lshl_b32 s57, s10, 13
	s_add_i32 s57, s57, 0x1e000
	v_add_u32_e32 v139, s57, v180
	v_xor_b32_e32 v141, 64, v139
	v_lshrrev_b32_e32 v164, 4, v131
	v_lshlrev_b32_e32 v95, 5, v164
	v_bfe_u32 v164, v131, 1, 1
	v_lshl_or_b32 v95, v164, 4, v95
	v_bfe_u32 v164, v131, 2, 2
	v_lshl_or_b32 v95, v164, 2, v95
	v_and_b32_e32 v165, 1, v131
	v_lshl_or_b32 v95, v165, 1, v95
	v_lshl_or_b32 v164, v164, 1, v165
	v_xor_b32_e32 v164, s66, v164
	v_lshlrev_b32_e32 v95, 7, v95
	v_lshl_or_b32 v95, v164, 4, v95
	v_add_u32_e32 v95, 0x1e000, v95
	s_lshl_b32 s57, s67, 2
	v_lshl_add_u32 v82, v170, 4, s57
	v_add_u32_e32 v82, 0x27340, v82
	v_lshl_add_u32 v83, v130, 4, s57
	v_add_u32_e32 v83, 0x26e40, v83
	v_and_b32_e32 v164, 7, v170
	v_xor_b32_e32 v165, v171, v164
	v_lshlrev_b32_e32 v165, 4, v165
	v_lshl_or_b32 v84, v164, 7, v165
	v_lshrrev_b32_e32 v164, 3, v170
	v_lshl_or_b32 v84, v164, 13, v84
	v_and_b32_e32 v164, 7, v131
	v_xor_b32_e32 v165, v130, v164
	v_and_b32_e32 v165, 7, v165
	v_lshlrev_b32_e32 v165, 4, v165
	v_lshl_or_b32 v85, v130, 7, v165
	s_lshl_b32 s57, s14, 8
	s_lshl_b32 s58, s10, 7
	s_add_i32 s57, s57, s58
	s_add_u32 s58, s96, s57
	s_addc_u32 s59, s97, 0
	v_lshlrev_b32_e32 v164, 4, v164
	v_mov_b32_e32 v165, 0
	v_lshl_add_u64 v[86:87], v[164:165], 0, s[58:59]
	v_readlane_b32 s58, v254, 25
	v_readlane_b32 s59, v254, 26
	s_lshl_b64 s[60:61], s[6:7], 23
	s_add_u32 s58, s58, s60
	s_addc_u32 s59, s59, s61
	s_lshl_b32 s60, s14, 9
	s_add_u32 s58, s58, s60
	s_addc_u32 s59, s59, 0
	s_lshl_b32 s60, s66, 17
	s_add_u32 s58, s58, s60
	s_addc_u32 s59, s59, 0
	v_lshlrev_b32_e32 v164, 3, v131
	v_mov_b32_e32 v165, 0
	v_lshl_add_u64 v[132:133], v[164:165], 0, s[58:59]
	s_mov_b64 s[24:25], 0x4000
	s_mov_b64 s[26:27], 0x8000
	s_mov_b64 s[28:29], 0xc000
	s_mov_b64 s[36:37], 0x10000
	s_mov_b64 s[38:39], 0x14000
	s_mov_b64 s[40:41], 0x18000
	s_mov_b64 s[42:43], 0x1c000
	s_mov_b32 s34, 0xff900800
	s_mov_b32 s35, 0x100000
	s_mov_b32 s53, 0xfffffc80
	s_mov_b32 s32, 0x80
	v_readlane_b32 s58, v254, 31
	v_readlane_b32 s59, v254, 32
	s_add_u32 s58, s58, 0x4b000000
	s_addc_u32 s59, s59, 0
	v_lshlrev_b32_e32 v164, 4, v131
	v_mov_b32_e32 v165, 0
	v_lshl_add_u64 v[168:169], v[164:165], 0, s[58:59]
	s_mov_b64 s[30:31], s[16:17]
	s_mov_b32 s46, 0
	s_mov_b32 s47, 0xa000
	s_mov_b32 s48, 0x14000
	s_mov_b32 s51, 4
	s_mov_b32 s50, 0
	s_mov_b32 s52, 1
	s_add_i32 m0, s74, 0x0
	s_nop 0
	global_load_lds_dwordx4 v88, s[30:31]
	s_add_i32 m0, s74, 0x2000
	s_nop 0
	global_load_lds_dwordx4 v90, s[30:31]
	s_add_i32 m0, s74, 0x4000
	s_nop 0
	global_load_lds_dwordx4 v92, s[30:31]
	s_add_i32 m0, s74, 0x6000
	s_nop 0
	global_load_lds_dwordx4 v94, s[30:31]
	s_add_i32 m0, s74, 0x8000
	s_nop 0
	global_load_lds_dwordx4 v96, s[30:31]
	s_add_u32 s30, s30, 0x80
	s_addc_u32 s31, s31, 0
	s_add_i32 m0, s74, 0xa000
	s_nop 0
	global_load_lds_dwordx4 v88, s[30:31]
	s_add_i32 m0, s74, 0xc000
	s_nop 0
	global_load_lds_dwordx4 v90, s[30:31]
	s_add_i32 m0, s74, 0xe000
	s_nop 0
	global_load_lds_dwordx4 v92, s[30:31]
	s_add_i32 m0, s74, 0x10000
	s_nop 0
	global_load_lds_dwordx4 v94, s[30:31]
	s_add_i32 m0, s74, 0x12000
	s_nop 0
	global_load_lds_dwordx4 v96, s[30:31]
	s_mov_b32 s44, 0x100000
	s_mov_b32 s45, 0
	global_load_dwordx2 v[98:99], v[132:133], off
	v_lshl_add_u64 v[180:181], v[132:133], 0, s[24:25]
	global_load_dwordx2 v[100:101], v[180:181], off
	v_lshl_add_u64 v[180:181], v[132:133], 0, s[26:27]
	global_load_dwordx2 v[102:103], v[180:181], off
	v_lshl_add_u64 v[180:181], v[132:133], 0, s[28:29]
	global_load_dwordx2 v[104:105], v[180:181], off
	v_lshl_add_u64 v[180:181], v[132:133], 0, s[36:37]
	global_load_dwordx2 v[106:107], v[180:181], off
	v_lshl_add_u64 v[180:181], v[132:133], 0, s[38:39]
	global_load_dwordx2 v[108:109], v[180:181], off
	v_lshl_add_u64 v[180:181], v[132:133], 0, s[40:41]
	global_load_dwordx2 v[110:111], v[180:181], off
	v_lshl_add_u64 v[180:181], v[132:133], 0, s[42:43]
	global_load_dwordx2 v[112:113], v[180:181], off
	v_lshl_add_u64 v[132:133], v[132:133], 0, s[44:45]
	global_load_dwordx2 v[114:115], v[132:133], off
	v_lshl_add_u64 v[180:181], v[132:133], 0, s[24:25]
	global_load_dwordx2 v[116:117], v[180:181], off
	v_lshl_add_u64 v[180:181], v[132:133], 0, s[26:27]
	global_load_dwordx2 v[118:119], v[180:181], off
	v_lshl_add_u64 v[180:181], v[132:133], 0, s[28:29]
	global_load_dwordx2 v[120:121], v[180:181], off
	v_lshl_add_u64 v[180:181], v[132:133], 0, s[36:37]
	global_load_dwordx2 v[122:123], v[180:181], off
	v_lshl_add_u64 v[180:181], v[132:133], 0, s[38:39]
	global_load_dwordx2 v[124:125], v[180:181], off
	v_lshl_add_u64 v[180:181], v[132:133], 0, s[40:41]
	global_load_dwordx2 v[126:127], v[180:181], off
	v_lshl_add_u64 v[180:181], v[132:133], 0, s[42:43]
	global_load_dwordx2 v[128:129], v[180:181], off
	v_lshl_add_u64 v[132:133], v[132:133], 0, s[44:45]
	global_load_dwordx2 v[186:187], v[132:133], off
	v_lshl_add_u64 v[180:181], v[132:133], 0, s[24:25]
	global_load_dwordx2 v[188:189], v[180:181], off
	v_lshl_add_u64 v[180:181], v[132:133], 0, s[26:27]
	global_load_dwordx2 v[190:191], v[180:181], off
	v_lshl_add_u64 v[180:181], v[132:133], 0, s[28:29]
	global_load_dwordx2 v[192:193], v[180:181], off
	v_lshl_add_u64 v[180:181], v[132:133], 0, s[36:37]
	global_load_dwordx2 v[194:195], v[180:181], off
	v_lshl_add_u64 v[180:181], v[132:133], 0, s[38:39]
	global_load_dwordx2 v[196:197], v[180:181], off
	v_lshl_add_u64 v[180:181], v[132:133], 0, s[40:41]
; #define MD_GLDS_A(buf, tau) do { _Pragma("unroll") for (int i = 0; i < 5; ++i) if (amask & (1u << i)) \
;         __builtin_amdgcn_global_load_lds((const unsigned*)((const char*)HIDp + aoff[i] + (size_t)((tau) & 7) * 128), (PG8_LAS unsigned*)(MD_SA(buf) + wid * 1024 + i * 8192), 16, 0, 0); } while (0)
; #define MD_B_ISSUE(sb, tau) do { const char* kb_ = Bb + (size_t)((tau) >> 3) * 512 + (size_t)((tau) & 7) * (64 * (size_t)RB); _Pragma("unroll") for (int j = 0; j < 8; ++j) { const char* p_ = kb_ + (size_t)j * RB; \
;         asm volatile("global_load_dwordx2 %0, %1, off" : "=&v"(sb[j]) : "v"(p_) : "memory"); } } while (0)
; #define MD_B_WAIT(sb, N) asm volatile("s_waitcnt vmcnt(%8)" : "+v"(sb[0]), "+v"(sb[1]), "+v"(sb[2]), "+v"(sb[3]), "+v"(sb[4]), "+v"(sb[5]), "+v"(sb[6]), "+v"(sb[7]) : "n"(N) : "memory")
; __device__ __forceinline__ void moe_down_stream(PG8_LAS unsigned char* lds, int e, int cb0, int slot0, int nv, const bf16_t* HIDp, const float* Wd, bf16_t* Y, const float* slot_w, const int* slot_dst) {
;     ...
;     f32x4 acc[DNM][4];
; #pragma unroll
;     for (int m = 0; m < DNM; ++m)
; #pragma unroll
;         for (int n = 0; n < 4; ++n) acc[m][n] = (f32x4){0.f, 0.f, 0.f, 0.f};
;     f32x2 s0[8], s1[8];
;     MD_GLDS_A(0, 0); MD_B_ISSUE(s0, 0); MD_B_ISSUE(s1, 1);
;     MD_B_WAIT(s0, 8); MD_B_WRITE(s0, 0); __builtin_amdgcn_sched_barrier(0); MD_B_ISSUE(s0, 2);
;     asm volatile("s_waitcnt vmcnt(16)" ::: "memory");
;     asm volatile("s_waitcnt lgkmcnt(0)" ::: "memory"); __builtin_amdgcn_s_barrier(); asm volatile("" ::: "memory");
; #pragma unroll 1
;     for (int t = 0; t < NT; t += 2) {
;         if (t + 2 < NT) MD_B_WAIT(s1, 8); else MD_B_WAIT(s1, 0);
;         MD_B_WRITE(s1, 1); __builtin_amdgcn_sched_barrier(0); MD_GLDS_A(1, t + 1); __builtin_amdgcn_sched_barrier(0);
;         if (t + 3 < NT) MD_B_ISSUE(s1, t + 3);
;         MD_COMPUTE(0);
	global_load_dwordx2 v[198:199], v[180:181], off
	v_lshl_add_u64 v[180:181], v[132:133], 0, s[42:43]
	global_load_dwordx2 v[200:201], v[180:181], off
	v_lshl_add_u64 v[132:133], v[132:133], 0, s[44:45]
	global_load_dwordx2 v[202:203], v[132:133], off
	v_lshl_add_u64 v[180:181], v[132:133], 0, s[24:25]
	global_load_dwordx2 v[204:205], v[180:181], off
	v_lshl_add_u64 v[180:181], v[132:133], 0, s[26:27]
	global_load_dwordx2 v[206:207], v[180:181], off
	v_lshl_add_u64 v[180:181], v[132:133], 0, s[28:29]
	global_load_dwordx2 v[208:209], v[180:181], off
	v_lshl_add_u64 v[180:181], v[132:133], 0, s[36:37]
	global_load_dwordx2 v[210:211], v[180:181], off
	v_lshl_add_u64 v[180:181], v[132:133], 0, s[38:39]
	global_load_dwordx2 v[212:213], v[180:181], off
	v_lshl_add_u64 v[180:181], v[132:133], 0, s[40:41]
	global_load_dwordx2 v[214:215], v[180:181], off
	v_lshl_add_u64 v[180:181], v[132:133], 0, s[42:43]
	global_load_dwordx2 v[216:217], v[180:181], off
	v_mov_b32_e32 v78, 0
	v_mov_b32_e32 v79, 0
	v_mov_b32_e32 v80, 0
	v_mov_b32_e32 v81, 0
	v_mov_b32_e32 v74, 0
	v_mov_b32_e32 v75, 0
	v_mov_b32_e32 v76, 0
	v_mov_b32_e32 v77, 0
	v_mov_b32_e32 v70, 0
	v_mov_b32_e32 v71, 0
	v_mov_b32_e32 v72, 0
	v_mov_b32_e32 v73, 0
	v_mov_b32_e32 v66, 0
	v_mov_b32_e32 v67, 0
	v_mov_b32_e32 v68, 0
	v_mov_b32_e32 v69, 0
	v_mov_b32_e32 v62, 0
	v_mov_b32_e32 v63, 0
	v_mov_b32_e32 v64, 0
	v_mov_b32_e32 v65, 0
	v_mov_b32_e32 v58, 0
	v_mov_b32_e32 v59, 0
	v_mov_b32_e32 v60, 0
	v_mov_b32_e32 v61, 0
	v_mov_b32_e32 v54, 0
	v_mov_b32_e32 v55, 0
	v_mov_b32_e32 v56, 0
	v_mov_b32_e32 v57, 0
	v_mov_b32_e32 v50, 0
	v_mov_b32_e32 v51, 0
	v_mov_b32_e32 v52, 0
	v_mov_b32_e32 v53, 0
	v_mov_b32_e32 v46, 0
	v_mov_b32_e32 v47, 0
	v_mov_b32_e32 v48, 0
	v_mov_b32_e32 v49, 0
	v_mov_b32_e32 v42, 0
	v_mov_b32_e32 v43, 0
	v_mov_b32_e32 v44, 0
	v_mov_b32_e32 v45, 0
	v_mov_b32_e32 v38, 0
	v_mov_b32_e32 v39, 0
	v_mov_b32_e32 v40, 0
	v_mov_b32_e32 v41, 0
	v_mov_b32_e32 v34, 0
	v_mov_b32_e32 v35, 0
	v_mov_b32_e32 v36, 0
	v_mov_b32_e32 v37, 0
	v_mov_b32_e32 v18, 0
	v_mov_b32_e32 v19, 0
	v_mov_b32_e32 v20, 0
	v_mov_b32_e32 v21, 0
	v_mov_b32_e32 v22, 0
	v_mov_b32_e32 v23, 0
	v_mov_b32_e32 v24, 0
	v_mov_b32_e32 v25, 0
	v_mov_b32_e32 v26, 0
	v_mov_b32_e32 v27, 0
	v_mov_b32_e32 v28, 0
	v_mov_b32_e32 v29, 0
	v_mov_b32_e32 v30, 0
	v_mov_b32_e32 v31, 0
	v_mov_b32_e32 v32, 0
	v_mov_b32_e32 v33, 0
	v_mov_b32_e32 v2, 0
	v_mov_b32_e32 v3, 0
	v_mov_b32_e32 v4, 0
	v_mov_b32_e32 v5, 0
	v_mov_b32_e32 v6, 0
	v_mov_b32_e32 v7, 0
	v_mov_b32_e32 v8, 0
	v_mov_b32_e32 v9, 0
	v_mov_b32_e32 v10, 0
	v_mov_b32_e32 v11, 0
	v_mov_b32_e32 v12, 0
	v_mov_b32_e32 v13, 0
	v_mov_b32_e32 v14, 0
	v_mov_b32_e32 v15, 0
	v_mov_b32_e32 v16, 0
	v_mov_b32_e32 v17, 0
	s_waitcnt vmcnt(24)
	v_cvt_pk_bf16_f32 v172, v98, v100
	v_cvt_pk_bf16_f32 v173, v102, v104
	v_cvt_pk_bf16_f32 v174, v106, v108
	v_cvt_pk_bf16_f32 v175, v110, v112
	v_cvt_pk_bf16_f32 v176, v99, v101
	v_cvt_pk_bf16_f32 v177, v103, v105
	v_cvt_pk_bf16_f32 v178, v107, v109
	v_cvt_pk_bf16_f32 v179, v111, v113
	ds_write_b128 v95, v[172:175] offset:0
	ds_write_b128 v95, v[176:179] offset:128
	v_lshl_add_u64 v[132:133], v[132:133], 0, s[44:45]
	global_load_dwordx2 v[98:99], v[132:133], off
	v_lshl_add_u64 v[180:181], v[132:133], 0, s[24:25]
	global_load_dwordx2 v[100:101], v[180:181], off
	v_lshl_add_u64 v[180:181], v[132:133], 0, s[26:27]
	global_load_dwordx2 v[102:103], v[180:181], off
	v_lshl_add_u64 v[180:181], v[132:133], 0, s[28:29]
	global_load_dwordx2 v[104:105], v[180:181], off
	v_lshl_add_u64 v[180:181], v[132:133], 0, s[36:37]
	global_load_dwordx2 v[106:107], v[180:181], off
	v_lshl_add_u64 v[180:181], v[132:133], 0, s[38:39]
	global_load_dwordx2 v[108:109], v[180:181], off
	v_lshl_add_u64 v[180:181], v[132:133], 0, s[40:41]
	global_load_dwordx2 v[110:111], v[180:181], off
	v_lshl_add_u64 v[180:181], v[132:133], 0, s[42:43]
	global_load_dwordx2 v[112:113], v[180:181], off
	s_waitcnt lgkmcnt(0)
	s_barrier
	s_cmp_gt_u32 s66, 3
	s_cbranch_scc1 .Lmd_grpY
	s_waitcnt vmcnt(24)
	v_cvt_pk_bf16_f32 v172, v114, v116
	v_cvt_pk_bf16_f32 v173, v118, v120
	v_cvt_pk_bf16_f32 v174, v122, v124
	v_cvt_pk_bf16_f32 v175, v126, v128
	v_cvt_pk_bf16_f32 v176, v115, v117
	v_cvt_pk_bf16_f32 v177, v119, v121
	v_cvt_pk_bf16_f32 v178, v123, v125
	v_cvt_pk_bf16_f32 v179, v127, v129
	ds_write_b128 v95, v[172:175] offset:19456
	ds_write_b128 v95, v[176:179] offset:19584
	v_add_u32_e32 v91, s46, v135
	v_add_u32_e32 v93, s46, v137
	ds_read_b128 v[238:241], v139 offset:0
	ds_read_b128 v[242:245], v139 offset:2048
	ds_read_b128 v[246:249], v139 offset:4096
	ds_read_b128 v[250:253], v139 offset:6144
	ds_read_b128 v[218:221], v91 offset:0
	ds_read_b128 v[222:225], v91 offset:2048
	ds_read_b128 v[226:229], v91 offset:4096
	ds_read_b128 v[230:233], v91 offset:6144
	ds_read_b128 v[234:237], v91 offset:8192
	s_add_i32 s49, s48, s74
	s_add_i32 s52, s52, 1
	s_and_b32 s54, s52, 7
	s_cmp_eq_u32 s54, 0
	s_cselect_b32 s54, s53, s32
	s_cselect_b32 s55, -1, 0
	s_add_u32 s30, s30, s54
	s_addc_u32 s31, s31, s55
	s_waitcnt lgkmcnt(0)
; #define MD_GLDS_A(buf, tau) do { _Pragma("unroll") for (int i = 0; i < 5; ++i) if (amask & (1u << i)) \
;         __builtin_amdgcn_global_load_lds((const unsigned*)((const char*)HIDp + aoff[i] + (size_t)((tau) & 7) * 128), (PG8_LAS unsigned*)(MD_SA(buf) + wid * 1024 + i * 8192), 16, 0, 0); } while (0)
; #define MD_B_ISSUE(sb, tau) do { const char* kb_ = Bb + (size_t)((tau) >> 3) * 512 + (size_t)((tau) & 7) * (64 * (size_t)RB); _Pragma("unroll") for (int j = 0; j < 8; ++j) { const char* p_ = kb_ + (size_t)j * RB; \
;         asm volatile("global_load_dwordx2 %0, %1, off" : "=&v"(sb[j]) : "v"(p_) : "memory"); } } while (0)
; #define MD_B_WAIT(sb, N) asm volatile("s_waitcnt vmcnt(%8)" : "+v"(sb[0]), "+v"(sb[1]), "+v"(sb[2]), "+v"(sb[3]), "+v"(sb[4]), "+v"(sb[5]), "+v"(sb[6]), "+v"(sb[7]) : "n"(N) : "memory")
; __device__ __forceinline__ void moe_down_stream(PG8_LAS unsigned char* lds, int e, int cb0, int slot0, int nv, const bf16_t* HIDp, const float* Wd, bf16_t* Y, const float* slot_w, const int* slot_dst) {
;     ...
;     f32x4 acc[DNM][4];
; #pragma unroll
;     for (int m = 0; m < DNM; ++m)
; #pragma unroll
;         for (int n = 0; n < 4; ++n) acc[m][n] = (f32x4){0.f, 0.f, 0.f, 0.f};
;     f32x2 s0[8], s1[8];
;     MD_GLDS_A(0, 0); MD_B_ISSUE(s0, 0); MD_B_ISSUE(s1, 1);
;     MD_B_WAIT(s0, 8); MD_B_WRITE(s0, 0); __builtin_amdgcn_sched_barrier(0); MD_B_ISSUE(s0, 2);
;     asm volatile("s_waitcnt vmcnt(16)" ::: "memory");
;     asm volatile("s_waitcnt lgkmcnt(0)" ::: "memory"); __builtin_amdgcn_s_barrier(); asm volatile("" ::: "memory");
; #pragma unroll 1
;     for (int t = 0; t < NT; t += 2) {
;         if (t + 2 < NT) MD_B_WAIT(s1, 8); else MD_B_WAIT(s1, 0);
;         MD_B_WRITE(s1, 1); __builtin_amdgcn_sched_barrier(0); MD_GLDS_A(1, t + 1); __builtin_amdgcn_sched_barrier(0);
;         if (t + 3 < NT) MD_B_ISSUE(s1, t + 3);
;         MD_COMPUTE(0);
;         MD_END(t + 3 >= NT);
;         if (t + 2 < NT) { MD_B_WAIT(s0, 8); MD_B_WRITE(s0, 0); __builtin_amdgcn_sched_barrier(0); MD_GLDS_A(0, t + 2); __builtin_amdgcn_sched_barrier(0); }
;         if (t + 4 < NT) MD_B_ISSUE(s0, t + 4);
;         MD_COMPUTE(1);
;         MD_END(t + 4 >= NT);
	v_mfma_f32_16x16x32_bf16 v[78:81], v[238:241], v[218:221], v[78:81]
	v_mfma_f32_16x16x32_bf16 v[74:77], v[242:245], v[218:221], v[74:77]
	v_mfma_f32_16x16x32_bf16 v[70:73], v[246:249], v[218:221], v[70:73]
	v_mfma_f32_16x16x32_bf16 v[66:69], v[250:253], v[218:221], v[66:69]
	ds_read_b128 v[218:221], v93 offset:0
	ds_read_b128 v[142:145], v141 offset:0
	s_mov_b32 m0, s49
	s_nop 0
	global_load_lds_dwordx4 v88, s[30:31]
	v_mfma_f32_16x16x32_bf16 v[62:65], v[238:241], v[222:225], v[62:65]
	v_mfma_f32_16x16x32_bf16 v[58:61], v[242:245], v[222:225], v[58:61]
	v_mfma_f32_16x16x32_bf16 v[54:57], v[246:249], v[222:225], v[54:57]
	v_mfma_f32_16x16x32_bf16 v[50:53], v[250:253], v[222:225], v[50:53]
	ds_read_b128 v[222:225], v93 offset:2048
	ds_read_b128 v[146:149], v141 offset:2048
	s_add_i32 m0, s49, 0x2000
	s_nop 0
	global_load_lds_dwordx4 v90, s[30:31]
	v_mfma_f32_16x16x32_bf16 v[46:49], v[238:241], v[226:229], v[46:49]
	v_mfma_f32_16x16x32_bf16 v[42:45], v[242:245], v[226:229], v[42:45]
	v_mfma_f32_16x16x32_bf16 v[38:41], v[246:249], v[226:229], v[38:41]
	v_mfma_f32_16x16x32_bf16 v[34:37], v[250:253], v[226:229], v[34:37]
	ds_read_b128 v[226:229], v93 offset:4096
	ds_read_b128 v[156:159], v141 offset:4096
	s_add_i32 m0, s49, 0x4000
	s_nop 0
	global_load_lds_dwordx4 v92, s[30:31]
	v_mfma_f32_16x16x32_bf16 v[18:21], v[238:241], v[230:233], v[18:21]
	v_mfma_f32_16x16x32_bf16 v[22:25], v[242:245], v[230:233], v[22:25]
	v_mfma_f32_16x16x32_bf16 v[26:29], v[246:249], v[230:233], v[26:29]
	v_mfma_f32_16x16x32_bf16 v[30:33], v[250:253], v[230:233], v[30:33]
	ds_read_b128 v[230:233], v93 offset:6144
	ds_read_b128 v[160:163], v141 offset:6144
	s_add_i32 m0, s49, 0x6000
	s_nop 0
	global_load_lds_dwordx4 v94, s[30:31]
	v_mfma_f32_16x16x32_bf16 v[2:5], v[238:241], v[234:237], v[2:5]
	v_mfma_f32_16x16x32_bf16 v[6:9], v[242:245], v[234:237], v[6:9]
	v_mfma_f32_16x16x32_bf16 v[10:13], v[246:249], v[234:237], v[10:13]
	v_mfma_f32_16x16x32_bf16 v[14:17], v[250:253], v[234:237], v[14:17]
	ds_read_b128 v[234:237], v93 offset:8192
	s_add_i32 m0, s49, 0x8000
	s_nop 0
	global_load_lds_dwordx4 v96, s[30:31]
	s_waitcnt lgkmcnt(0)
	v_mfma_f32_16x16x32_bf16 v[78:81], v[142:145], v[218:221], v[78:81]
	v_mfma_f32_16x16x32_bf16 v[74:77], v[146:149], v[218:221], v[74:77]
	v_mfma_f32_16x16x32_bf16 v[70:73], v[156:159], v[218:221], v[70:73]
	v_mfma_f32_16x16x32_bf16 v[66:69], v[160:163], v[218:221], v[66:69]
	s_add_i32 s51, s51, 1
	s_and_b32 s54, s51, 7
	s_cmp_eq_u32 s54, 0
	s_cselect_b32 s44, s34, s35
	s_cselect_b32 s45, -1, 0
	v_lshl_add_u64 v[132:133], v[132:133], 0, s[44:45]
	global_load_dwordx2 v[114:115], v[132:133], off
	v_lshl_add_u64 v[180:181], v[132:133], 0, s[24:25]
	global_load_dwordx2 v[116:117], v[180:181], off
	v_mfma_f32_16x16x32_bf16 v[62:65], v[142:145], v[222:225], v[62:65]
	v_mfma_f32_16x16x32_bf16 v[58:61], v[146:149], v[222:225], v[58:61]
	v_mfma_f32_16x16x32_bf16 v[54:57], v[156:159], v[222:225], v[54:57]
	v_mfma_f32_16x16x32_bf16 v[50:53], v[160:163], v[222:225], v[50:53]
	v_lshl_add_u64 v[180:181], v[132:133], 0, s[26:27]
	global_load_dwordx2 v[118:119], v[180:181], off
	v_lshl_add_u64 v[180:181], v[132:133], 0, s[28:29]
	global_load_dwordx2 v[120:121], v[180:181], off
	v_mfma_f32_16x16x32_bf16 v[46:49], v[142:145], v[226:229], v[46:49]
	v_mfma_f32_16x16x32_bf16 v[42:45], v[146:149], v[226:229], v[42:45]
	v_mfma_f32_16x16x32_bf16 v[38:41], v[156:159], v[226:229], v[38:41]
	v_mfma_f32_16x16x32_bf16 v[34:37], v[160:163], v[226:229], v[34:37]
	v_lshl_add_u64 v[180:181], v[132:133], 0, s[36:37]
	global_load_dwordx2 v[122:123], v[180:181], off
	v_lshl_add_u64 v[180:181], v[132:133], 0, s[38:39]
	global_load_dwordx2 v[124:125], v[180:181], off
	v_mfma_f32_16x16x32_bf16 v[18:21], v[142:145], v[230:233], v[18:21]
	v_mfma_f32_16x16x32_bf16 v[22:25], v[146:149], v[230:233], v[22:25]
	v_mfma_f32_16x16x32_bf16 v[26:29], v[156:159], v[230:233], v[26:29]
	v_mfma_f32_16x16x32_bf16 v[30:33], v[160:163], v[230:233], v[30:33]
	v_lshl_add_u64 v[180:181], v[132:133], 0, s[40:41]
	global_load_dwordx2 v[126:127], v[180:181], off
	v_lshl_add_u64 v[180:181], v[132:133], 0, s[42:43]
	global_load_dwordx2 v[128:129], v[180:181], off
	v_mfma_f32_16x16x32_bf16 v[2:5], v[142:145], v[234:237], v[2:5]
	v_mfma_f32_16x16x32_bf16 v[6:9], v[146:149], v[234:237], v[6:9]
	v_mfma_f32_16x16x32_bf16 v[10:13], v[156:159], v[234:237], v[10:13]
	v_mfma_f32_16x16x32_bf16 v[14:17], v[160:163], v[234:237], v[14:17]
	s_waitcnt lgkmcnt(0)
	s_barrier
; #define MD_GLDS_A(buf, tau) do { _Pragma("unroll") for (int i = 0; i < 5; ++i) if (amask & (1u << i)) \
;         __builtin_amdgcn_global_load_lds((const unsigned*)((const char*)HIDp + aoff[i] + (size_t)((tau) & 7) * 128), (PG8_LAS unsigned*)(MD_SA(buf) + wid * 1024 + i * 8192), 16, 0, 0); } while (0)
; #define MD_B_ISSUE(sb, tau) do { const char* kb_ = Bb + (size_t)((tau) >> 3) * 512 + (size_t)((tau) & 7) * (64 * (size_t)RB); _Pragma("unroll") for (int j = 0; j < 8; ++j) { const char* p_ = kb_ + (size_t)j * RB; \
;         asm volatile("global_load_dwordx2 %0, %1, off" : "=&v"(sb[j]) : "v"(p_) : "memory"); } } while (0)
; #define MD_B_WAIT(sb, N) asm volatile("s_waitcnt vmcnt(%8)" : "+v"(sb[0]), "+v"(sb[1]), "+v"(sb[2]), "+v"(sb[3]), "+v"(sb[4]), "+v"(sb[5]), "+v"(sb[6]), "+v"(sb[7]) : "n"(N) : "memory")
; __device__ __forceinline__ void moe_down_stream(PG8_LAS unsigned char* lds, int e, int cb0, int slot0, int nv, const bf16_t* HIDp, const float* Wd, bf16_t* Y, const float* slot_w, const int* slot_dst) {
;     ...
;     f32x4 acc[DNM][4];
; #pragma unroll
;     for (int m = 0; m < DNM; ++m)
; #pragma unroll
;         for (int n = 0; n < 4; ++n) acc[m][n] = (f32x4){0.f, 0.f, 0.f, 0.f};
;     f32x2 s0[8], s1[8];
;     MD_GLDS_A(0, 0); MD_B_ISSUE(s0, 0); MD_B_ISSUE(s1, 1);
;     MD_B_WAIT(s0, 8); MD_B_WRITE(s0, 0); __builtin_amdgcn_sched_barrier(0); MD_B_ISSUE(s0, 2);
;     asm volatile("s_waitcnt vmcnt(16)" ::: "memory");
;     asm volatile("s_waitcnt lgkmcnt(0)" ::: "memory"); __builtin_amdgcn_s_barrier(); asm volatile("" ::: "memory");
; #pragma unroll 1
;     for (int t = 0; t < NT; t += 2) {
;         if (t + 2 < NT) MD_B_WAIT(s1, 8); else MD_B_WAIT(s1, 0);
;         MD_B_WRITE(s1, 1); __builtin_amdgcn_sched_barrier(0); MD_GLDS_A(1, t + 1); __builtin_amdgcn_sched_barrier(0);
;         if (t + 3 < NT) MD_B_ISSUE(s1, t + 3);
;         MD_COMPUTE(0);
;         MD_END(t + 3 >= NT);
;         if (t + 2 < NT) { MD_B_WAIT(s0, 8); MD_B_WRITE(s0, 0); __builtin_amdgcn_sched_barrier(0); MD_GLDS_A(0, t + 2); __builtin_amdgcn_sched_barrier(0); }
;         if (t + 4 < NT) MD_B_ISSUE(s0, t + 4);
;         MD_COMPUTE(1);
;         MD_END(t + 4 >= NT);
	s_mov_b32 s49, s46
	s_mov_b32 s46, s47
	s_mov_b32 s47, s48
	s_mov_b32 s48, s49
	s_add_i32 s50, s50, 1
	s_waitcnt vmcnt(29)
	v_cvt_pk_bf16_f32 v172, v186, v188
	v_cvt_pk_bf16_f32 v173, v190, v192
	v_cvt_pk_bf16_f32 v174, v194, v196
	v_cvt_pk_bf16_f32 v175, v198, v200
	v_cvt_pk_bf16_f32 v176, v187, v189
	v_cvt_pk_bf16_f32 v177, v191, v193
	v_cvt_pk_bf16_f32 v178, v195, v197
	v_cvt_pk_bf16_f32 v179, v199, v201
	ds_write_b128 v95, v[172:175] offset:0
	ds_write_b128 v95, v[176:179] offset:128
	v_add_u32_e32 v91, s46, v135
	v_add_u32_e32 v93, s46, v137
	ds_read_b128 v[238:241], v139 offset:19456
	ds_read_b128 v[242:245], v139 offset:21504
	ds_read_b128 v[246:249], v139 offset:23552
	ds_read_b128 v[250:253], v139 offset:25600
	ds_read_b128 v[218:221], v91 offset:0
	ds_read_b128 v[222:225], v91 offset:2048
	ds_read_b128 v[226:229], v91 offset:4096
	ds_read_b128 v[230:233], v91 offset:6144
	ds_read_b128 v[234:237], v91 offset:8192
	s_add_i32 s49, s48, s74
	s_add_i32 s52, s52, 1
	s_and_b32 s54, s52, 7
	s_cmp_eq_u32 s54, 0
	s_cselect_b32 s54, s53, s32
	s_cselect_b32 s55, -1, 0
	s_add_u32 s30, s30, s54
	s_addc_u32 s31, s31, s55
	s_waitcnt lgkmcnt(0)
	v_mfma_f32_16x16x32_bf16 v[78:81], v[238:241], v[218:221], v[78:81]
	v_mfma_f32_16x16x32_bf16 v[74:77], v[242:245], v[218:221], v[74:77]
	v_mfma_f32_16x16x32_bf16 v[70:73], v[246:249], v[218:221], v[70:73]
	v_mfma_f32_16x16x32_bf16 v[66:69], v[250:253], v[218:221], v[66:69]
	ds_read_b128 v[218:221], v93 offset:0
	ds_read_b128 v[142:145], v141 offset:19456
	s_mov_b32 m0, s49
	s_nop 0
	global_load_lds_dwordx4 v88, s[30:31]
	v_mfma_f32_16x16x32_bf16 v[62:65], v[238:241], v[222:225], v[62:65]
	v_mfma_f32_16x16x32_bf16 v[58:61], v[242:245], v[222:225], v[58:61]
	v_mfma_f32_16x16x32_bf16 v[54:57], v[246:249], v[222:225], v[54:57]
	v_mfma_f32_16x16x32_bf16 v[50:53], v[250:253], v[222:225], v[50:53]
	ds_read_b128 v[222:225], v93 offset:2048
	ds_read_b128 v[146:149], v141 offset:21504
	s_add_i32 m0, s49, 0x2000
	s_nop 0
	global_load_lds_dwordx4 v90, s[30:31]
	v_mfma_f32_16x16x32_bf16 v[46:49], v[238:241], v[226:229], v[46:49]
	v_mfma_f32_16x16x32_bf16 v[42:45], v[242:245], v[226:229], v[42:45]
	v_mfma_f32_16x16x32_bf16 v[38:41], v[246:249], v[226:229], v[38:41]
	v_mfma_f32_16x16x32_bf16 v[34:37], v[250:253], v[226:229], v[34:37]
	ds_read_b128 v[226:229], v93 offset:4096
	ds_read_b128 v[156:159], v141 offset:23552
	s_add_i32 m0, s49, 0x4000
	s_nop 0
	global_load_lds_dwordx4 v92, s[30:31]
	v_mfma_f32_16x16x32_bf16 v[18:21], v[238:241], v[230:233], v[18:21]
	v_mfma_f32_16x16x32_bf16 v[22:25], v[242:245], v[230:233], v[22:25]
	v_mfma_f32_16x16x32_bf16 v[26:29], v[246:249], v[230:233], v[26:29]
	v_mfma_f32_16x16x32_bf16 v[30:33], v[250:253], v[230:233], v[30:33]
	ds_read_b128 v[230:233], v93 offset:6144
	ds_read_b128 v[160:163], v141 offset:25600
	s_add_i32 m0, s49, 0x6000
	s_nop 0
	global_load_lds_dwordx4 v94, s[30:31]
	v_mfma_f32_16x16x32_bf16 v[2:5], v[238:241], v[234:237], v[2:5]
	v_mfma_f32_16x16x32_bf16 v[6:9], v[242:245], v[234:237], v[6:9]
	v_mfma_f32_16x16x32_bf16 v[10:13], v[246:249], v[234:237], v[10:13]
	v_mfma_f32_16x16x32_bf16 v[14:17], v[250:253], v[234:237], v[14:17]
	ds_read_b128 v[234:237], v93 offset:8192
	s_add_i32 m0, s49, 0x8000
	s_nop 0
	global_load_lds_dwordx4 v96, s[30:31]
	s_waitcnt lgkmcnt(0)
	v_mfma_f32_16x16x32_bf16 v[78:81], v[142:145], v[218:221], v[78:81]
	v_mfma_f32_16x16x32_bf16 v[74:77], v[146:149], v[218:221], v[74:77]
	v_mfma_f32_16x16x32_bf16 v[70:73], v[156:159], v[218:221], v[70:73]
	v_mfma_f32_16x16x32_bf16 v[66:69], v[160:163], v[218:221], v[66:69]
	s_add_i32 s51, s51, 1
	s_and_b32 s54, s51, 7
	s_cmp_eq_u32 s54, 0
	s_cselect_b32 s44, s34, s35
	s_cselect_b32 s45, -1, 0
	v_lshl_add_u64 v[132:133], v[132:133], 0, s[44:45]
	global_load_dwordx2 v[186:187], v[132:133], off
	v_lshl_add_u64 v[180:181], v[132:133], 0, s[24:25]
	global_load_dwordx2 v[188:189], v[180:181], off
	v_mfma_f32_16x16x32_bf16 v[62:65], v[142:145], v[222:225], v[62:65]
	v_mfma_f32_16x16x32_bf16 v[58:61], v[146:149], v[222:225], v[58:61]
	v_mfma_f32_16x16x32_bf16 v[54:57], v[156:159], v[222:225], v[54:57]
	v_mfma_f32_16x16x32_bf16 v[50:53], v[160:163], v[222:225], v[50:53]
	v_lshl_add_u64 v[180:181], v[132:133], 0, s[26:27]
	global_load_dwordx2 v[190:191], v[180:181], off
	v_lshl_add_u64 v[180:181], v[132:133], 0, s[28:29]
	global_load_dwordx2 v[192:193], v[180:181], off
	v_mfma_f32_16x16x32_bf16 v[46:49], v[142:145], v[226:229], v[46:49]
	v_mfma_f32_16x16x32_bf16 v[42:45], v[146:149], v[226:229], v[42:45]
	v_mfma_f32_16x16x32_bf16 v[38:41], v[156:159], v[226:229], v[38:41]
	v_mfma_f32_16x16x32_bf16 v[34:37], v[160:163], v[226:229], v[34:37]
	v_lshl_add_u64 v[180:181], v[132:133], 0, s[36:37]
	global_load_dwordx2 v[194:195], v[180:181], off
	v_lshl_add_u64 v[180:181], v[132:133], 0, s[38:39]
	global_load_dwordx2 v[196:197], v[180:181], off
	v_mfma_f32_16x16x32_bf16 v[18:21], v[142:145], v[230:233], v[18:21]
	v_mfma_f32_16x16x32_bf16 v[22:25], v[146:149], v[230:233], v[22:25]
	v_mfma_f32_16x16x32_bf16 v[26:29], v[156:159], v[230:233], v[26:29]
	v_mfma_f32_16x16x32_bf16 v[30:33], v[160:163], v[230:233], v[30:33]
	v_lshl_add_u64 v[180:181], v[132:133], 0, s[40:41]
	global_load_dwordx2 v[198:199], v[180:181], off
	v_lshl_add_u64 v[180:181], v[132:133], 0, s[42:43]
	global_load_dwordx2 v[200:201], v[180:181], off
	v_mfma_f32_16x16x32_bf16 v[2:5], v[142:145], v[234:237], v[2:5]
	v_mfma_f32_16x16x32_bf16 v[6:9], v[146:149], v[234:237], v[6:9]
	v_mfma_f32_16x16x32_bf16 v[10:13], v[156:159], v[234:237], v[10:13]
	v_mfma_f32_16x16x32_bf16 v[14:17], v[160:163], v[234:237], v[14:17]
	s_waitcnt vmcnt(21)
	s_waitcnt lgkmcnt(0)
	s_barrier
; #define MD_GLDS_A(buf, tau) do { _Pragma("unroll") for (int i = 0; i < 5; ++i) if (amask & (1u << i)) \
;         __builtin_amdgcn_global_load_lds((const unsigned*)((const char*)HIDp + aoff[i] + (size_t)((tau) & 7) * 128), (PG8_LAS unsigned*)(MD_SA(buf) + wid * 1024 + i * 8192), 16, 0, 0); } while (0)
; #define MD_B_ISSUE(sb, tau) do { const char* kb_ = Bb + (size_t)((tau) >> 3) * 512 + (size_t)((tau) & 7) * (64 * (size_t)RB); _Pragma("unroll") for (int j = 0; j < 8; ++j) { const char* p_ = kb_ + (size_t)j * RB; \
;         asm volatile("global_load_dwordx2 %0, %1, off" : "=&v"(sb[j]) : "v"(p_) : "memory"); } } while (0)
; #define MD_B_WAIT(sb, N) asm volatile("s_waitcnt vmcnt(%8)" : "+v"(sb[0]), "+v"(sb[1]), "+v"(sb[2]), "+v"(sb[3]), "+v"(sb[4]), "+v"(sb[5]), "+v"(sb[6]), "+v"(sb[7]) : "n"(N) : "memory")
; __device__ __forceinline__ void moe_down_stream(PG8_LAS unsigned char* lds, int e, int cb0, int slot0, int nv, const bf16_t* HIDp, const float* Wd, bf16_t* Y, const float* slot_w, const int* slot_dst) {
;     ...
;     f32x4 acc[DNM][4];
; #pragma unroll
;     for (int m = 0; m < DNM; ++m)
; #pragma unroll
;         for (int n = 0; n < 4; ++n) acc[m][n] = (f32x4){0.f, 0.f, 0.f, 0.f};
;     f32x2 s0[8], s1[8];
;     MD_GLDS_A(0, 0); MD_B_ISSUE(s0, 0); MD_B_ISSUE(s1, 1);
;     MD_B_WAIT(s0, 8); MD_B_WRITE(s0, 0); __builtin_amdgcn_sched_barrier(0); MD_B_ISSUE(s0, 2);
;     asm volatile("s_waitcnt vmcnt(16)" ::: "memory");
;     asm volatile("s_waitcnt lgkmcnt(0)" ::: "memory"); __builtin_amdgcn_s_barrier(); asm volatile("" ::: "memory");
; #pragma unroll 1
;     for (int t = 0; t < NT; t += 2) {
;         if (t + 2 < NT) MD_B_WAIT(s1, 8); else MD_B_WAIT(s1, 0);
;         MD_B_WRITE(s1, 1); __builtin_amdgcn_sched_barrier(0); MD_GLDS_A(1, t + 1); __builtin_amdgcn_sched_barrier(0);
;         if (t + 3 < NT) MD_B_ISSUE(s1, t + 3);
;         MD_COMPUTE(0);
;         MD_END(t + 3 >= NT);
;         if (t + 2 < NT) { MD_B_WAIT(s0, 8); MD_B_WRITE(s0, 0); __builtin_amdgcn_sched_barrier(0); MD_GLDS_A(0, t + 2); __builtin_amdgcn_sched_barrier(0); }
;         if (t + 4 < NT) MD_B_ISSUE(s0, t + 4);
;         MD_COMPUTE(1);
;         MD_END(t + 4 >= NT);
	s_mov_b32 s49, s46
	s_mov_b32 s46, s47
	s_mov_b32 s47, s48
	s_mov_b32 s48, s49
	s_add_i32 s50, s50, 1
	v_cvt_pk_bf16_f32 v172, v202, v204
	v_cvt_pk_bf16_f32 v173, v206, v208
	v_cvt_pk_bf16_f32 v174, v210, v212
	v_cvt_pk_bf16_f32 v175, v214, v216
	v_cvt_pk_bf16_f32 v176, v203, v205
	v_cvt_pk_bf16_f32 v177, v207, v209
	v_cvt_pk_bf16_f32 v178, v211, v213
	v_cvt_pk_bf16_f32 v179, v215, v217
	ds_write_b128 v95, v[172:175] offset:19456
	ds_write_b128 v95, v[176:179] offset:19584
	v_add_u32_e32 v91, s46, v135
	v_add_u32_e32 v93, s46, v137
	ds_read_b128 v[238:241], v139 offset:0
	ds_read_b128 v[242:245], v139 offset:2048
	ds_read_b128 v[246:249], v139 offset:4096
	ds_read_b128 v[250:253], v139 offset:6144
	ds_read_b128 v[218:221], v91 offset:0
	ds_read_b128 v[222:225], v91 offset:2048
	ds_read_b128 v[226:229], v91 offset:4096
	ds_read_b128 v[230:233], v91 offset:6144
	ds_read_b128 v[234:237], v91 offset:8192
	s_add_i32 s49, s48, s74
	s_add_i32 s52, s52, 1
	s_and_b32 s54, s52, 7
	s_cmp_eq_u32 s54, 0
	s_cselect_b32 s54, s53, s32
	s_cselect_b32 s55, -1, 0
	s_add_u32 s30, s30, s54
	s_addc_u32 s31, s31, s55
	s_waitcnt lgkmcnt(0)
	v_mfma_f32_16x16x32_bf16 v[78:81], v[238:241], v[218:221], v[78:81]
	v_mfma_f32_16x16x32_bf16 v[74:77], v[242:245], v[218:221], v[74:77]
	v_mfma_f32_16x16x32_bf16 v[70:73], v[246:249], v[218:221], v[70:73]
	v_mfma_f32_16x16x32_bf16 v[66:69], v[250:253], v[218:221], v[66:69]
	ds_read_b128 v[218:221], v93 offset:0
	ds_read_b128 v[142:145], v141 offset:0
	s_mov_b32 m0, s49
	s_nop 0
	global_load_lds_dwordx4 v88, s[30:31]
	v_mfma_f32_16x16x32_bf16 v[62:65], v[238:241], v[222:225], v[62:65]
	v_mfma_f32_16x16x32_bf16 v[58:61], v[242:245], v[222:225], v[58:61]
	v_mfma_f32_16x16x32_bf16 v[54:57], v[246:249], v[222:225], v[54:57]
	v_mfma_f32_16x16x32_bf16 v[50:53], v[250:253], v[222:225], v[50:53]
	ds_read_b128 v[222:225], v93 offset:2048
	ds_read_b128 v[146:149], v141 offset:2048
	s_add_i32 m0, s49, 0x2000
	s_nop 0
	global_load_lds_dwordx4 v90, s[30:31]
	v_mfma_f32_16x16x32_bf16 v[46:49], v[238:241], v[226:229], v[46:49]
	v_mfma_f32_16x16x32_bf16 v[42:45], v[242:245], v[226:229], v[42:45]
	v_mfma_f32_16x16x32_bf16 v[38:41], v[246:249], v[226:229], v[38:41]
	v_mfma_f32_16x16x32_bf16 v[34:37], v[250:253], v[226:229], v[34:37]
	ds_read_b128 v[226:229], v93 offset:4096
	ds_read_b128 v[156:159], v141 offset:4096
	s_add_i32 m0, s49, 0x4000
	s_nop 0
	global_load_lds_dwordx4 v92, s[30:31]
	v_mfma_f32_16x16x32_bf16 v[18:21], v[238:241], v[230:233], v[18:21]
	v_mfma_f32_16x16x32_bf16 v[22:25], v[242:245], v[230:233], v[22:25]
	v_mfma_f32_16x16x32_bf16 v[26:29], v[246:249], v[230:233], v[26:29]
	v_mfma_f32_16x16x32_bf16 v[30:33], v[250:253], v[230:233], v[30:33]
	ds_read_b128 v[230:233], v93 offset:6144
	ds_read_b128 v[160:163], v141 offset:6144
	s_add_i32 m0, s49, 0x6000
	s_nop 0
	global_load_lds_dwordx4 v94, s[30:31]
	v_mfma_f32_16x16x32_bf16 v[2:5], v[238:241], v[234:237], v[2:5]
	v_mfma_f32_16x16x32_bf16 v[6:9], v[242:245], v[234:237], v[6:9]
	v_mfma_f32_16x16x32_bf16 v[10:13], v[246:249], v[234:237], v[10:13]
	v_mfma_f32_16x16x32_bf16 v[14:17], v[250:253], v[234:237], v[14:17]
	ds_read_b128 v[234:237], v93 offset:8192
	s_add_i32 m0, s49, 0x8000
	s_nop 0
	global_load_lds_dwordx4 v96, s[30:31]
	s_waitcnt lgkmcnt(0)
	v_mfma_f32_16x16x32_bf16 v[78:81], v[142:145], v[218:221], v[78:81]
	v_mfma_f32_16x16x32_bf16 v[74:77], v[146:149], v[218:221], v[74:77]
	v_mfma_f32_16x16x32_bf16 v[70:73], v[156:159], v[218:221], v[70:73]
	v_mfma_f32_16x16x32_bf16 v[66:69], v[160:163], v[218:221], v[66:69]
	s_add_i32 s51, s51, 1
	s_and_b32 s54, s51, 7
	s_cmp_eq_u32 s54, 0
	s_cselect_b32 s44, s34, s35
	s_cselect_b32 s45, -1, 0
	v_lshl_add_u64 v[132:133], v[132:133], 0, s[44:45]
	global_load_dwordx2 v[202:203], v[132:133], off
	v_lshl_add_u64 v[180:181], v[132:133], 0, s[24:25]
	global_load_dwordx2 v[204:205], v[180:181], off
	v_mfma_f32_16x16x32_bf16 v[62:65], v[142:145], v[222:225], v[62:65]
	v_mfma_f32_16x16x32_bf16 v[58:61], v[146:149], v[222:225], v[58:61]
	v_mfma_f32_16x16x32_bf16 v[54:57], v[156:159], v[222:225], v[54:57]
	v_mfma_f32_16x16x32_bf16 v[50:53], v[160:163], v[222:225], v[50:53]
	v_lshl_add_u64 v[180:181], v[132:133], 0, s[26:27]
	global_load_dwordx2 v[206:207], v[180:181], off
	v_lshl_add_u64 v[180:181], v[132:133], 0, s[28:29]
	global_load_dwordx2 v[208:209], v[180:181], off
	v_mfma_f32_16x16x32_bf16 v[46:49], v[142:145], v[226:229], v[46:49]
	v_mfma_f32_16x16x32_bf16 v[42:45], v[146:149], v[226:229], v[42:45]
	v_mfma_f32_16x16x32_bf16 v[38:41], v[156:159], v[226:229], v[38:41]
	v_mfma_f32_16x16x32_bf16 v[34:37], v[160:163], v[226:229], v[34:37]
	v_lshl_add_u64 v[180:181], v[132:133], 0, s[36:37]
	global_load_dwordx2 v[210:211], v[180:181], off
	v_lshl_add_u64 v[180:181], v[132:133], 0, s[38:39]
	global_load_dwordx2 v[212:213], v[180:181], off
	v_mfma_f32_16x16x32_bf16 v[18:21], v[142:145], v[230:233], v[18:21]
	v_mfma_f32_16x16x32_bf16 v[22:25], v[146:149], v[230:233], v[22:25]
	v_mfma_f32_16x16x32_bf16 v[26:29], v[156:159], v[230:233], v[26:29]
	v_mfma_f32_16x16x32_bf16 v[30:33], v[160:163], v[230:233], v[30:33]
	v_lshl_add_u64 v[180:181], v[132:133], 0, s[40:41]
	global_load_dwordx2 v[214:215], v[180:181], off
	v_lshl_add_u64 v[180:181], v[132:133], 0, s[42:43]
	global_load_dwordx2 v[216:217], v[180:181], off
	v_mfma_f32_16x16x32_bf16 v[2:5], v[142:145], v[234:237], v[2:5]
	v_mfma_f32_16x16x32_bf16 v[6:9], v[146:149], v[234:237], v[6:9]
	v_mfma_f32_16x16x32_bf16 v[10:13], v[156:159], v[234:237], v[10:13]
	v_mfma_f32_16x16x32_bf16 v[14:17], v[160:163], v[234:237], v[14:17]
	s_waitcnt vmcnt(21)
	s_waitcnt lgkmcnt(0)
	s_barrier
; #define MD_GLDS_A(buf, tau) do { _Pragma("unroll") for (int i = 0; i < 5; ++i) if (amask & (1u << i)) \
;         __builtin_amdgcn_global_load_lds((const unsigned*)((const char*)HIDp + aoff[i] + (size_t)((tau) & 7) * 128), (PG8_LAS unsigned*)(MD_SA(buf) + wid * 1024 + i * 8192), 16, 0, 0); } while (0)
; #define MD_B_ISSUE(sb, tau) do { const char* kb_ = Bb + (size_t)((tau) >> 3) * 512 + (size_t)((tau) & 7) * (64 * (size_t)RB); _Pragma("unroll") for (int j = 0; j < 8; ++j) { const char* p_ = kb_ + (size_t)j * RB; \
;         asm volatile("global_load_dwordx2 %0, %1, off" : "=&v"(sb[j]) : "v"(p_) : "memory"); } } while (0)
; #define MD_B_WAIT(sb, N) asm volatile("s_waitcnt vmcnt(%8)" : "+v"(sb[0]), "+v"(sb[1]), "+v"(sb[2]), "+v"(sb[3]), "+v"(sb[4]), "+v"(sb[5]), "+v"(sb[6]), "+v"(sb[7]) : "n"(N) : "memory")
; __device__ __forceinline__ void moe_down_stream(PG8_LAS unsigned char* lds, int e, int cb0, int slot0, int nv, const bf16_t* HIDp, const float* Wd, bf16_t* Y, const float* slot_w, const int* slot_dst) {
;     ...
;     f32x4 acc[DNM][4];
; #pragma unroll
;     for (int m = 0; m < DNM; ++m)
; #pragma unroll
;         for (int n = 0; n < 4; ++n) acc[m][n] = (f32x4){0.f, 0.f, 0.f, 0.f};
;     f32x2 s0[8], s1[8];
;     MD_GLDS_A(0, 0); MD_B_ISSUE(s0, 0); MD_B_ISSUE(s1, 1);
;     MD_B_WAIT(s0, 8); MD_B_WRITE(s0, 0); __builtin_amdgcn_sched_barrier(0); MD_B_ISSUE(s0, 2);
;     asm volatile("s_waitcnt vmcnt(16)" ::: "memory");
;     asm volatile("s_waitcnt lgkmcnt(0)" ::: "memory"); __builtin_amdgcn_s_barrier(); asm volatile("" ::: "memory");
; #pragma unroll 1
;     for (int t = 0; t < NT; t += 2) {
;         if (t + 2 < NT) MD_B_WAIT(s1, 8); else MD_B_WAIT(s1, 0);
;         MD_B_WRITE(s1, 1); __builtin_amdgcn_sched_barrier(0); MD_GLDS_A(1, t + 1); __builtin_amdgcn_sched_barrier(0);
;         if (t + 3 < NT) MD_B_ISSUE(s1, t + 3);
;         MD_COMPUTE(0);
;         MD_END(t + 3 >= NT);
;         if (t + 2 < NT) { MD_B_WAIT(s0, 8); MD_B_WRITE(s0, 0); __builtin_amdgcn_sched_barrier(0); MD_GLDS_A(0, t + 2); __builtin_amdgcn_sched_barrier(0); }
;         if (t + 4 < NT) MD_B_ISSUE(s0, t + 4);
;         MD_COMPUTE(1);
;         MD_END(t + 4 >= NT);
	s_mov_b32 s49, s46
	s_mov_b32 s46, s47
	s_mov_b32 s47, s48
	s_mov_b32 s48, s49
	s_add_i32 s50, s50, 1
	v_cvt_pk_bf16_f32 v172, v98, v100
	v_cvt_pk_bf16_f32 v173, v102, v104
	v_cvt_pk_bf16_f32 v174, v106, v108
	v_cvt_pk_bf16_f32 v175, v110, v112
	v_cvt_pk_bf16_f32 v176, v99, v101
	v_cvt_pk_bf16_f32 v177, v103, v105
	v_cvt_pk_bf16_f32 v178, v107, v109
	v_cvt_pk_bf16_f32 v179, v111, v113
	ds_write_b128 v95, v[172:175] offset:0
	ds_write_b128 v95, v[176:179] offset:128
	v_add_u32_e32 v91, s46, v135
	v_add_u32_e32 v93, s46, v137
	ds_read_b128 v[238:241], v139 offset:19456
	ds_read_b128 v[242:245], v139 offset:21504
	ds_read_b128 v[246:249], v139 offset:23552
	ds_read_b128 v[250:253], v139 offset:25600
	ds_read_b128 v[218:221], v91 offset:0
	ds_read_b128 v[222:225], v91 offset:2048
	ds_read_b128 v[226:229], v91 offset:4096
	ds_read_b128 v[230:233], v91 offset:6144
	ds_read_b128 v[234:237], v91 offset:8192
	s_add_i32 s49, s48, s74
	s_add_i32 s52, s52, 1
	s_and_b32 s54, s52, 7
	s_cmp_eq_u32 s54, 0
	s_cselect_b32 s54, s53, s32
	s_cselect_b32 s55, -1, 0
	s_add_u32 s30, s30, s54
	s_addc_u32 s31, s31, s55
	s_waitcnt lgkmcnt(0)
	v_mfma_f32_16x16x32_bf16 v[78:81], v[238:241], v[218:221], v[78:81]
	v_mfma_f32_16x16x32_bf16 v[74:77], v[242:245], v[218:221], v[74:77]
	v_mfma_f32_16x16x32_bf16 v[70:73], v[246:249], v[218:221], v[70:73]
	v_mfma_f32_16x16x32_bf16 v[66:69], v[250:253], v[218:221], v[66:69]
	ds_read_b128 v[218:221], v93 offset:0
	ds_read_b128 v[142:145], v141 offset:19456
	s_mov_b32 m0, s49
	s_nop 0
	global_load_lds_dwordx4 v88, s[30:31]
	v_mfma_f32_16x16x32_bf16 v[62:65], v[238:241], v[222:225], v[62:65]
	v_mfma_f32_16x16x32_bf16 v[58:61], v[242:245], v[222:225], v[58:61]
	v_mfma_f32_16x16x32_bf16 v[54:57], v[246:249], v[222:225], v[54:57]
	v_mfma_f32_16x16x32_bf16 v[50:53], v[250:253], v[222:225], v[50:53]
	ds_read_b128 v[222:225], v93 offset:2048
	ds_read_b128 v[146:149], v141 offset:21504
	s_add_i32 m0, s49, 0x2000
	s_nop 0
	global_load_lds_dwordx4 v90, s[30:31]
	v_mfma_f32_16x16x32_bf16 v[46:49], v[238:241], v[226:229], v[46:49]
	v_mfma_f32_16x16x32_bf16 v[42:45], v[242:245], v[226:229], v[42:45]
	v_mfma_f32_16x16x32_bf16 v[38:41], v[246:249], v[226:229], v[38:41]
	v_mfma_f32_16x16x32_bf16 v[34:37], v[250:253], v[226:229], v[34:37]
	ds_read_b128 v[226:229], v93 offset:4096
	ds_read_b128 v[156:159], v141 offset:23552
	s_add_i32 m0, s49, 0x4000
	s_nop 0
	global_load_lds_dwordx4 v92, s[30:31]
	v_mfma_f32_16x16x32_bf16 v[18:21], v[238:241], v[230:233], v[18:21]
	v_mfma_f32_16x16x32_bf16 v[22:25], v[242:245], v[230:233], v[22:25]
	v_mfma_f32_16x16x32_bf16 v[26:29], v[246:249], v[230:233], v[26:29]
	v_mfma_f32_16x16x32_bf16 v[30:33], v[250:253], v[230:233], v[30:33]
	ds_read_b128 v[230:233], v93 offset:6144
	ds_read_b128 v[160:163], v141 offset:25600
	s_add_i32 m0, s49, 0x6000
	s_nop 0
	global_load_lds_dwordx4 v94, s[30:31]
	v_mfma_f32_16x16x32_bf16 v[2:5], v[238:241], v[234:237], v[2:5]
	v_mfma_f32_16x16x32_bf16 v[6:9], v[242:245], v[234:237], v[6:9]
	v_mfma_f32_16x16x32_bf16 v[10:13], v[246:249], v[234:237], v[10:13]
	v_mfma_f32_16x16x32_bf16 v[14:17], v[250:253], v[234:237], v[14:17]
	ds_read_b128 v[234:237], v93 offset:8192
	s_add_i32 m0, s49, 0x8000
	s_nop 0
	global_load_lds_dwordx4 v96, s[30:31]
	s_waitcnt lgkmcnt(0)
	v_mfma_f32_16x16x32_bf16 v[78:81], v[142:145], v[218:221], v[78:81]
	v_mfma_f32_16x16x32_bf16 v[74:77], v[146:149], v[218:221], v[74:77]
	v_mfma_f32_16x16x32_bf16 v[70:73], v[156:159], v[218:221], v[70:73]
	v_mfma_f32_16x16x32_bf16 v[66:69], v[160:163], v[218:221], v[66:69]
	s_add_i32 s51, s51, 1
	s_and_b32 s54, s51, 7
	s_cmp_eq_u32 s54, 0
	s_cselect_b32 s44, s34, s35
	s_cselect_b32 s45, -1, 0
	v_lshl_add_u64 v[132:133], v[132:133], 0, s[44:45]
	global_load_dwordx2 v[98:99], v[132:133], off
	v_lshl_add_u64 v[180:181], v[132:133], 0, s[24:25]
	global_load_dwordx2 v[100:101], v[180:181], off
	v_mfma_f32_16x16x32_bf16 v[62:65], v[142:145], v[222:225], v[62:65]
	v_mfma_f32_16x16x32_bf16 v[58:61], v[146:149], v[222:225], v[58:61]
	v_mfma_f32_16x16x32_bf16 v[54:57], v[156:159], v[222:225], v[54:57]
	v_mfma_f32_16x16x32_bf16 v[50:53], v[160:163], v[222:225], v[50:53]
	v_lshl_add_u64 v[180:181], v[132:133], 0, s[26:27]
	global_load_dwordx2 v[102:103], v[180:181], off
	v_lshl_add_u64 v[180:181], v[132:133], 0, s[28:29]
	global_load_dwordx2 v[104:105], v[180:181], off
	v_mfma_f32_16x16x32_bf16 v[46:49], v[142:145], v[226:229], v[46:49]
	v_mfma_f32_16x16x32_bf16 v[42:45], v[146:149], v[226:229], v[42:45]
	v_mfma_f32_16x16x32_bf16 v[38:41], v[156:159], v[226:229], v[38:41]
	v_mfma_f32_16x16x32_bf16 v[34:37], v[160:163], v[226:229], v[34:37]
	v_lshl_add_u64 v[180:181], v[132:133], 0, s[36:37]
	global_load_dwordx2 v[106:107], v[180:181], off
	v_lshl_add_u64 v[180:181], v[132:133], 0, s[38:39]
	global_load_dwordx2 v[108:109], v[180:181], off
	v_mfma_f32_16x16x32_bf16 v[18:21], v[142:145], v[230:233], v[18:21]
	v_mfma_f32_16x16x32_bf16 v[22:25], v[146:149], v[230:233], v[22:25]
	v_mfma_f32_16x16x32_bf16 v[26:29], v[156:159], v[230:233], v[26:29]
	v_mfma_f32_16x16x32_bf16 v[30:33], v[160:163], v[230:233], v[30:33]
	v_lshl_add_u64 v[180:181], v[132:133], 0, s[40:41]
	global_load_dwordx2 v[110:111], v[180:181], off
	v_lshl_add_u64 v[180:181], v[132:133], 0, s[42:43]
	global_load_dwordx2 v[112:113], v[180:181], off
	v_mfma_f32_16x16x32_bf16 v[2:5], v[142:145], v[234:237], v[2:5]
	v_mfma_f32_16x16x32_bf16 v[6:9], v[146:149], v[234:237], v[6:9]
	v_mfma_f32_16x16x32_bf16 v[10:13], v[156:159], v[234:237], v[10:13]
	v_mfma_f32_16x16x32_bf16 v[14:17], v[160:163], v[234:237], v[14:17]
	s_waitcnt vmcnt(21)
	s_waitcnt lgkmcnt(0)
	s_barrier
	s_mov_b32 s49, s46
	s_mov_b32 s46, s47
	s_mov_b32 s47, s48
	s_mov_b32 s48, s49
	s_add_i32 s50, s50, 1
	s_mov_b32 s56, 13
; #define MD_GLDS_A(buf, tau) do { _Pragma("unroll") for (int i = 0; i < 5; ++i) if (amask & (1u << i)) \
;         __builtin_amdgcn_global_load_lds((const unsigned*)((const char*)HIDp + aoff[i] + (size_t)((tau) & 7) * 128), (PG8_LAS unsigned*)(MD_SA(buf) + wid * 1024 + i * 8192), 16, 0, 0); } while (0)
; #define MD_B_ISSUE(sb, tau) do { const char* kb_ = Bb + (size_t)((tau) >> 3) * 512 + (size_t)((tau) & 7) * (64 * (size_t)RB); _Pragma("unroll") for (int j = 0; j < 8; ++j) { const char* p_ = kb_ + (size_t)j * RB; \
;         asm volatile("global_load_dwordx2 %0, %1, off" : "=&v"(sb[j]) : "v"(p_) : "memory"); } } while (0)
; #define MD_B_WAIT(sb, N) asm volatile("s_waitcnt vmcnt(%8)" : "+v"(sb[0]), "+v"(sb[1]), "+v"(sb[2]), "+v"(sb[3]), "+v"(sb[4]), "+v"(sb[5]), "+v"(sb[6]), "+v"(sb[7]) : "n"(N) : "memory")
; __device__ __forceinline__ void moe_down_stream(PG8_LAS unsigned char* lds, int e, int cb0, int slot0, int nv, const bf16_t* HIDp, const float* Wd, bf16_t* Y, const float* slot_w, const int* slot_dst) {
;     ...
;     f32x4 acc[DNM][4];
; #pragma unroll
;     for (int m = 0; m < DNM; ++m)
; #pragma unroll
;         for (int n = 0; n < 4; ++n) acc[m][n] = (f32x4){0.f, 0.f, 0.f, 0.f};
;     f32x2 s0[8], s1[8];
;     MD_GLDS_A(0, 0); MD_B_ISSUE(s0, 0); MD_B_ISSUE(s1, 1);
;     MD_B_WAIT(s0, 8); MD_B_WRITE(s0, 0); __builtin_amdgcn_sched_barrier(0); MD_B_ISSUE(s0, 2);
;     asm volatile("s_waitcnt vmcnt(16)" ::: "memory");
;     asm volatile("s_waitcnt lgkmcnt(0)" ::: "memory"); __builtin_amdgcn_s_barrier(); asm volatile("" ::: "memory");
; #pragma unroll 1
;     for (int t = 0; t < NT; t += 2) {
;         if (t + 2 < NT) MD_B_WAIT(s1, 8); else MD_B_WAIT(s1, 0);
;         MD_B_WRITE(s1, 1); __builtin_amdgcn_sched_barrier(0); MD_GLDS_A(1, t + 1); __builtin_amdgcn_sched_barrier(0);
;         if (t + 3 < NT) MD_B_ISSUE(s1, t + 3);
;         MD_COMPUTE(0);
;         MD_END(t + 3 >= NT);
;         if (t + 2 < NT) { MD_B_WAIT(s0, 8); MD_B_WRITE(s0, 0); __builtin_amdgcn_sched_barrier(0); MD_GLDS_A(0, t + 2); __builtin_amdgcn_sched_barrier(0); }
;         if (t + 4 < NT) MD_B_ISSUE(s0, t + 4);
;         MD_COMPUTE(1);
;         MD_END(t + 4 >= NT);
.Lmd_loop_X:
	v_cvt_pk_bf16_f32 v172, v114, v116
	v_cvt_pk_bf16_f32 v173, v118, v120
	v_cvt_pk_bf16_f32 v174, v122, v124
	v_cvt_pk_bf16_f32 v175, v126, v128
	v_cvt_pk_bf16_f32 v176, v115, v117
	v_cvt_pk_bf16_f32 v177, v119, v121
	v_cvt_pk_bf16_f32 v178, v123, v125
	v_cvt_pk_bf16_f32 v179, v127, v129
	ds_write_b128 v95, v[172:175] offset:19456
	ds_write_b128 v95, v[176:179] offset:19584
	v_add_u32_e32 v91, s46, v135
	v_add_u32_e32 v93, s46, v137
	ds_read_b128 v[238:241], v139 offset:0
	ds_read_b128 v[242:245], v139 offset:2048
	ds_read_b128 v[246:249], v139 offset:4096
	ds_read_b128 v[250:253], v139 offset:6144
	ds_read_b128 v[218:221], v91 offset:0
	ds_read_b128 v[222:225], v91 offset:2048
	ds_read_b128 v[226:229], v91 offset:4096
	ds_read_b128 v[230:233], v91 offset:6144
	ds_read_b128 v[234:237], v91 offset:8192
	s_add_i32 s49, s48, s74
	s_add_i32 s52, s52, 1
	s_and_b32 s54, s52, 7
	s_cmp_eq_u32 s54, 0
	s_cselect_b32 s54, s53, s32
	s_cselect_b32 s55, -1, 0
	s_add_u32 s30, s30, s54
	s_addc_u32 s31, s31, s55
	s_waitcnt lgkmcnt(0)
	v_mfma_f32_16x16x32_bf16 v[78:81], v[238:241], v[218:221], v[78:81]
	v_mfma_f32_16x16x32_bf16 v[74:77], v[242:245], v[218:221], v[74:77]
	v_mfma_f32_16x16x32_bf16 v[70:73], v[246:249], v[218:221], v[70:73]
	v_mfma_f32_16x16x32_bf16 v[66:69], v[250:253], v[218:221], v[66:69]
	ds_read_b128 v[218:221], v93 offset:0
	ds_read_b128 v[142:145], v141 offset:0
	s_mov_b32 m0, s49
	s_nop 0
	global_load_lds_dwordx4 v88, s[30:31]
	v_mfma_f32_16x16x32_bf16 v[62:65], v[238:241], v[222:225], v[62:65]
	v_mfma_f32_16x16x32_bf16 v[58:61], v[242:245], v[222:225], v[58:61]
	v_mfma_f32_16x16x32_bf16 v[54:57], v[246:249], v[222:225], v[54:57]
	v_mfma_f32_16x16x32_bf16 v[50:53], v[250:253], v[222:225], v[50:53]
	ds_read_b128 v[222:225], v93 offset:2048
	ds_read_b128 v[146:149], v141 offset:2048
	s_add_i32 m0, s49, 0x2000
	s_nop 0
	global_load_lds_dwordx4 v90, s[30:31]
	v_mfma_f32_16x16x32_bf16 v[46:49], v[238:241], v[226:229], v[46:49]
	v_mfma_f32_16x16x32_bf16 v[42:45], v[242:245], v[226:229], v[42:45]
	v_mfma_f32_16x16x32_bf16 v[38:41], v[246:249], v[226:229], v[38:41]
	v_mfma_f32_16x16x32_bf16 v[34:37], v[250:253], v[226:229], v[34:37]
	ds_read_b128 v[226:229], v93 offset:4096
	ds_read_b128 v[156:159], v141 offset:4096
	s_add_i32 m0, s49, 0x4000
	s_nop 0
	global_load_lds_dwordx4 v92, s[30:31]
	v_mfma_f32_16x16x32_bf16 v[18:21], v[238:241], v[230:233], v[18:21]
	v_mfma_f32_16x16x32_bf16 v[22:25], v[242:245], v[230:233], v[22:25]
	v_mfma_f32_16x16x32_bf16 v[26:29], v[246:249], v[230:233], v[26:29]
	v_mfma_f32_16x16x32_bf16 v[30:33], v[250:253], v[230:233], v[30:33]
	ds_read_b128 v[230:233], v93 offset:6144
	ds_read_b128 v[160:163], v141 offset:6144
	s_add_i32 m0, s49, 0x6000
	s_nop 0
	global_load_lds_dwordx4 v94, s[30:31]
	v_mfma_f32_16x16x32_bf16 v[2:5], v[238:241], v[234:237], v[2:5]
	v_mfma_f32_16x16x32_bf16 v[6:9], v[242:245], v[234:237], v[6:9]
	v_mfma_f32_16x16x32_bf16 v[10:13], v[246:249], v[234:237], v[10:13]
	v_mfma_f32_16x16x32_bf16 v[14:17], v[250:253], v[234:237], v[14:17]
	ds_read_b128 v[234:237], v93 offset:8192
	s_add_i32 m0, s49, 0x8000
	s_nop 0
	global_load_lds_dwordx4 v96, s[30:31]
	s_waitcnt lgkmcnt(0)
	v_mfma_f32_16x16x32_bf16 v[78:81], v[142:145], v[218:221], v[78:81]
	v_mfma_f32_16x16x32_bf16 v[74:77], v[146:149], v[218:221], v[74:77]
	v_mfma_f32_16x16x32_bf16 v[70:73], v[156:159], v[218:221], v[70:73]
	v_mfma_f32_16x16x32_bf16 v[66:69], v[160:163], v[218:221], v[66:69]
	s_add_i32 s51, s51, 1
	s_and_b32 s54, s51, 7
	s_cmp_eq_u32 s54, 0
	s_cselect_b32 s44, s34, s35
	s_cselect_b32 s45, -1, 0
	v_lshl_add_u64 v[132:133], v[132:133], 0, s[44:45]
	global_load_dwordx2 v[114:115], v[132:133], off
	v_lshl_add_u64 v[180:181], v[132:133], 0, s[24:25]
	global_load_dwordx2 v[116:117], v[180:181], off
	v_mfma_f32_16x16x32_bf16 v[62:65], v[142:145], v[222:225], v[62:65]
	v_mfma_f32_16x16x32_bf16 v[58:61], v[146:149], v[222:225], v[58:61]
	v_mfma_f32_16x16x32_bf16 v[54:57], v[156:159], v[222:225], v[54:57]
	v_mfma_f32_16x16x32_bf16 v[50:53], v[160:163], v[222:225], v[50:53]
	v_lshl_add_u64 v[180:181], v[132:133], 0, s[26:27]
	global_load_dwordx2 v[118:119], v[180:181], off
	v_lshl_add_u64 v[180:181], v[132:133], 0, s[28:29]
	global_load_dwordx2 v[120:121], v[180:181], off
	v_mfma_f32_16x16x32_bf16 v[46:49], v[142:145], v[226:229], v[46:49]
	v_mfma_f32_16x16x32_bf16 v[42:45], v[146:149], v[226:229], v[42:45]
	v_mfma_f32_16x16x32_bf16 v[38:41], v[156:159], v[226:229], v[38:41]
	v_mfma_f32_16x16x32_bf16 v[34:37], v[160:163], v[226:229], v[34:37]
	v_lshl_add_u64 v[180:181], v[132:133], 0, s[36:37]
	global_load_dwordx2 v[122:123], v[180:181], off
	v_lshl_add_u64 v[180:181], v[132:133], 0, s[38:39]
	global_load_dwordx2 v[124:125], v[180:181], off
	v_mfma_f32_16x16x32_bf16 v[18:21], v[142:145], v[230:233], v[18:21]
	v_mfma_f32_16x16x32_bf16 v[22:25], v[146:149], v[230:233], v[22:25]
	v_mfma_f32_16x16x32_bf16 v[26:29], v[156:159], v[230:233], v[26:29]
	v_mfma_f32_16x16x32_bf16 v[30:33], v[160:163], v[230:233], v[30:33]
	v_lshl_add_u64 v[180:181], v[132:133], 0, s[40:41]
	global_load_dwordx2 v[126:127], v[180:181], off
	v_lshl_add_u64 v[180:181], v[132:133], 0, s[42:43]
	global_load_dwordx2 v[128:129], v[180:181], off
	v_mfma_f32_16x16x32_bf16 v[2:5], v[142:145], v[234:237], v[2:5]
	v_mfma_f32_16x16x32_bf16 v[6:9], v[146:149], v[234:237], v[6:9]
	v_mfma_f32_16x16x32_bf16 v[10:13], v[156:159], v[234:237], v[10:13]
	v_mfma_f32_16x16x32_bf16 v[14:17], v[160:163], v[234:237], v[14:17]
	s_waitcnt vmcnt(21)
	s_waitcnt lgkmcnt(0)
	s_barrier
; #define MD_GLDS_A(buf, tau) do { _Pragma("unroll") for (int i = 0; i < 5; ++i) if (amask & (1u << i)) \
;         __builtin_amdgcn_global_load_lds((const unsigned*)((const char*)HIDp + aoff[i] + (size_t)((tau) & 7) * 128), (PG8_LAS unsigned*)(MD_SA(buf) + wid * 1024 + i * 8192), 16, 0, 0); } while (0)
; #define MD_B_ISSUE(sb, tau) do { const char* kb_ = Bb + (size_t)((tau) >> 3) * 512 + (size_t)((tau) & 7) * (64 * (size_t)RB); _Pragma("unroll") for (int j = 0; j < 8; ++j) { const char* p_ = kb_ + (size_t)j * RB; \
;         asm volatile("global_load_dwordx2 %0, %1, off" : "=&v"(sb[j]) : "v"(p_) : "memory"); } } while (0)
; #define MD_B_WAIT(sb, N) asm volatile("s_waitcnt vmcnt(%8)" : "+v"(sb[0]), "+v"(sb[1]), "+v"(sb[2]), "+v"(sb[3]), "+v"(sb[4]), "+v"(sb[5]), "+v"(sb[6]), "+v"(sb[7]) : "n"(N) : "memory")
; __device__ __forceinline__ void moe_down_stream(PG8_LAS unsigned char* lds, int e, int cb0, int slot0, int nv, const bf16_t* HIDp, const float* Wd, bf16_t* Y, const float* slot_w, const int* slot_dst) {
;     ...
;     f32x4 acc[DNM][4];
; #pragma unroll
;     for (int m = 0; m < DNM; ++m)
; #pragma unroll
;         for (int n = 0; n < 4; ++n) acc[m][n] = (f32x4){0.f, 0.f, 0.f, 0.f};
;     f32x2 s0[8], s1[8];
;     MD_GLDS_A(0, 0); MD_B_ISSUE(s0, 0); MD_B_ISSUE(s1, 1);
;     MD_B_WAIT(s0, 8); MD_B_WRITE(s0, 0); __builtin_amdgcn_sched_barrier(0); MD_B_ISSUE(s0, 2);
;     asm volatile("s_waitcnt vmcnt(16)" ::: "memory");
;     asm volatile("s_waitcnt lgkmcnt(0)" ::: "memory"); __builtin_amdgcn_s_barrier(); asm volatile("" ::: "memory");
; #pragma unroll 1
;     for (int t = 0; t < NT; t += 2) {
;         if (t + 2 < NT) MD_B_WAIT(s1, 8); else MD_B_WAIT(s1, 0);
;         MD_B_WRITE(s1, 1); __builtin_amdgcn_sched_barrier(0); MD_GLDS_A(1, t + 1); __builtin_amdgcn_sched_barrier(0);
;         if (t + 3 < NT) MD_B_ISSUE(s1, t + 3);
;         MD_COMPUTE(0);
;         MD_END(t + 3 >= NT);
;         if (t + 2 < NT) { MD_B_WAIT(s0, 8); MD_B_WRITE(s0, 0); __builtin_amdgcn_sched_barrier(0); MD_GLDS_A(0, t + 2); __builtin_amdgcn_sched_barrier(0); }
;         if (t + 4 < NT) MD_B_ISSUE(s0, t + 4);
;         MD_COMPUTE(1);
;         MD_END(t + 4 >= NT);
	s_mov_b32 s49, s46
	s_mov_b32 s46, s47
	s_mov_b32 s47, s48
	s_mov_b32 s48, s49
	s_add_i32 s50, s50, 1
	v_cvt_pk_bf16_f32 v172, v186, v188
	v_cvt_pk_bf16_f32 v173, v190, v192
	v_cvt_pk_bf16_f32 v174, v194, v196
	v_cvt_pk_bf16_f32 v175, v198, v200
	v_cvt_pk_bf16_f32 v176, v187, v189
	v_cvt_pk_bf16_f32 v177, v191, v193
	v_cvt_pk_bf16_f32 v178, v195, v197
	v_cvt_pk_bf16_f32 v179, v199, v201
	ds_write_b128 v95, v[172:175] offset:0
	ds_write_b128 v95, v[176:179] offset:128
	v_add_u32_e32 v91, s46, v135
	v_add_u32_e32 v93, s46, v137
	ds_read_b128 v[238:241], v139 offset:19456
	ds_read_b128 v[242:245], v139 offset:21504
	ds_read_b128 v[246:249], v139 offset:23552
	ds_read_b128 v[250:253], v139 offset:25600
	ds_read_b128 v[218:221], v91 offset:0
	ds_read_b128 v[222:225], v91 offset:2048
	ds_read_b128 v[226:229], v91 offset:4096
	ds_read_b128 v[230:233], v91 offset:6144
	ds_read_b128 v[234:237], v91 offset:8192
	s_add_i32 s49, s48, s74
	s_add_i32 s52, s52, 1
	s_and_b32 s54, s52, 7
	s_cmp_eq_u32 s54, 0
	s_cselect_b32 s54, s53, s32
	s_cselect_b32 s55, -1, 0
	s_add_u32 s30, s30, s54
	s_addc_u32 s31, s31, s55
	s_waitcnt lgkmcnt(0)
	v_mfma_f32_16x16x32_bf16 v[78:81], v[238:241], v[218:221], v[78:81]
	v_mfma_f32_16x16x32_bf16 v[74:77], v[242:245], v[218:221], v[74:77]
	v_mfma_f32_16x16x32_bf16 v[70:73], v[246:249], v[218:221], v[70:73]
	v_mfma_f32_16x16x32_bf16 v[66:69], v[250:253], v[218:221], v[66:69]
	ds_read_b128 v[218:221], v93 offset:0
	ds_read_b128 v[142:145], v141 offset:19456
	s_mov_b32 m0, s49
	s_nop 0
	global_load_lds_dwordx4 v88, s[30:31]
	v_mfma_f32_16x16x32_bf16 v[62:65], v[238:241], v[222:225], v[62:65]
	v_mfma_f32_16x16x32_bf16 v[58:61], v[242:245], v[222:225], v[58:61]
	v_mfma_f32_16x16x32_bf16 v[54:57], v[246:249], v[222:225], v[54:57]
	v_mfma_f32_16x16x32_bf16 v[50:53], v[250:253], v[222:225], v[50:53]
	ds_read_b128 v[222:225], v93 offset:2048
	ds_read_b128 v[146:149], v141 offset:21504
	s_add_i32 m0, s49, 0x2000
	s_nop 0
	global_load_lds_dwordx4 v90, s[30:31]
	v_mfma_f32_16x16x32_bf16 v[46:49], v[238:241], v[226:229], v[46:49]
	v_mfma_f32_16x16x32_bf16 v[42:45], v[242:245], v[226:229], v[42:45]
	v_mfma_f32_16x16x32_bf16 v[38:41], v[246:249], v[226:229], v[38:41]
	v_mfma_f32_16x16x32_bf16 v[34:37], v[250:253], v[226:229], v[34:37]
	ds_read_b128 v[226:229], v93 offset:4096
	ds_read_b128 v[156:159], v141 offset:23552
	s_add_i32 m0, s49, 0x4000
	s_nop 0
	global_load_lds_dwordx4 v92, s[30:31]
	v_mfma_f32_16x16x32_bf16 v[18:21], v[238:241], v[230:233], v[18:21]
	v_mfma_f32_16x16x32_bf16 v[22:25], v[242:245], v[230:233], v[22:25]
	v_mfma_f32_16x16x32_bf16 v[26:29], v[246:249], v[230:233], v[26:29]
	v_mfma_f32_16x16x32_bf16 v[30:33], v[250:253], v[230:233], v[30:33]
	ds_read_b128 v[230:233], v93 offset:6144
	ds_read_b128 v[160:163], v141 offset:25600
	s_add_i32 m0, s49, 0x6000
	s_nop 0
	global_load_lds_dwordx4 v94, s[30:31]
	v_mfma_f32_16x16x32_bf16 v[2:5], v[238:241], v[234:237], v[2:5]
	v_mfma_f32_16x16x32_bf16 v[6:9], v[242:245], v[234:237], v[6:9]
	v_mfma_f32_16x16x32_bf16 v[10:13], v[246:249], v[234:237], v[10:13]
	v_mfma_f32_16x16x32_bf16 v[14:17], v[250:253], v[234:237], v[14:17]
	ds_read_b128 v[234:237], v93 offset:8192
	s_add_i32 m0, s49, 0x8000
	s_nop 0
	global_load_lds_dwordx4 v96, s[30:31]
	s_waitcnt lgkmcnt(0)
	v_mfma_f32_16x16x32_bf16 v[78:81], v[142:145], v[218:221], v[78:81]
	v_mfma_f32_16x16x32_bf16 v[74:77], v[146:149], v[218:221], v[74:77]
	v_mfma_f32_16x16x32_bf16 v[70:73], v[156:159], v[218:221], v[70:73]
	v_mfma_f32_16x16x32_bf16 v[66:69], v[160:163], v[218:221], v[66:69]
	s_add_i32 s51, s51, 1
	s_and_b32 s54, s51, 7
	s_cmp_eq_u32 s54, 0
	s_cselect_b32 s44, s34, s35
	s_cselect_b32 s45, -1, 0
	v_lshl_add_u64 v[132:133], v[132:133], 0, s[44:45]
	global_load_dwordx2 v[186:187], v[132:133], off
	v_lshl_add_u64 v[180:181], v[132:133], 0, s[24:25]
	global_load_dwordx2 v[188:189], v[180:181], off
	v_mfma_f32_16x16x32_bf16 v[62:65], v[142:145], v[222:225], v[62:65]
	v_mfma_f32_16x16x32_bf16 v[58:61], v[146:149], v[222:225], v[58:61]
	v_mfma_f32_16x16x32_bf16 v[54:57], v[156:159], v[222:225], v[54:57]
	v_mfma_f32_16x16x32_bf16 v[50:53], v[160:163], v[222:225], v[50:53]
	v_lshl_add_u64 v[180:181], v[132:133], 0, s[26:27]
	global_load_dwordx2 v[190:191], v[180:181], off
	v_lshl_add_u64 v[180:181], v[132:133], 0, s[28:29]
	global_load_dwordx2 v[192:193], v[180:181], off
	v_mfma_f32_16x16x32_bf16 v[46:49], v[142:145], v[226:229], v[46:49]
	v_mfma_f32_16x16x32_bf16 v[42:45], v[146:149], v[226:229], v[42:45]
	v_mfma_f32_16x16x32_bf16 v[38:41], v[156:159], v[226:229], v[38:41]
	v_mfma_f32_16x16x32_bf16 v[34:37], v[160:163], v[226:229], v[34:37]
	v_lshl_add_u64 v[180:181], v[132:133], 0, s[36:37]
	global_load_dwordx2 v[194:195], v[180:181], off
	v_lshl_add_u64 v[180:181], v[132:133], 0, s[38:39]
	global_load_dwordx2 v[196:197], v[180:181], off
	v_mfma_f32_16x16x32_bf16 v[18:21], v[142:145], v[230:233], v[18:21]
	v_mfma_f32_16x16x32_bf16 v[22:25], v[146:149], v[230:233], v[22:25]
	v_mfma_f32_16x16x32_bf16 v[26:29], v[156:159], v[230:233], v[26:29]
	v_mfma_f32_16x16x32_bf16 v[30:33], v[160:163], v[230:233], v[30:33]
	v_lshl_add_u64 v[180:181], v[132:133], 0, s[40:41]
	global_load_dwordx2 v[198:199], v[180:181], off
	v_lshl_add_u64 v[180:181], v[132:133], 0, s[42:43]
	global_load_dwordx2 v[200:201], v[180:181], off
	v_mfma_f32_16x16x32_bf16 v[2:5], v[142:145], v[234:237], v[2:5]
	v_mfma_f32_16x16x32_bf16 v[6:9], v[146:149], v[234:237], v[6:9]
	v_mfma_f32_16x16x32_bf16 v[10:13], v[156:159], v[234:237], v[10:13]
	v_mfma_f32_16x16x32_bf16 v[14:17], v[160:163], v[234:237], v[14:17]
	s_waitcnt vmcnt(21)
	s_waitcnt lgkmcnt(0)
	s_barrier
; #define MD_GLDS_A(buf, tau) do { _Pragma("unroll") for (int i = 0; i < 5; ++i) if (amask & (1u << i)) \
;         __builtin_amdgcn_global_load_lds((const unsigned*)((const char*)HIDp + aoff[i] + (size_t)((tau) & 7) * 128), (PG8_LAS unsigned*)(MD_SA(buf) + wid * 1024 + i * 8192), 16, 0, 0); } while (0)
; #define MD_B_ISSUE(sb, tau) do { const char* kb_ = Bb + (size_t)((tau) >> 3) * 512 + (size_t)((tau) & 7) * (64 * (size_t)RB); _Pragma("unroll") for (int j = 0; j < 8; ++j) { const char* p_ = kb_ + (size_t)j * RB; \
;         asm volatile("global_load_dwordx2 %0, %1, off" : "=&v"(sb[j]) : "v"(p_) : "memory"); } } while (0)
; #define MD_B_WAIT(sb, N) asm volatile("s_waitcnt vmcnt(%8)" : "+v"(sb[0]), "+v"(sb[1]), "+v"(sb[2]), "+v"(sb[3]), "+v"(sb[4]), "+v"(sb[5]), "+v"(sb[6]), "+v"(sb[7]) : "n"(N) : "memory")
; __device__ __forceinline__ void moe_down_stream(PG8_LAS unsigned char* lds, int e, int cb0, int slot0, int nv, const bf16_t* HIDp, const float* Wd, bf16_t* Y, const float* slot_w, const int* slot_dst) {
;     ...
;     f32x4 acc[DNM][4];
; #pragma unroll
;     for (int m = 0; m < DNM; ++m)
; #pragma unroll
;         for (int n = 0; n < 4; ++n) acc[m][n] = (f32x4){0.f, 0.f, 0.f, 0.f};
;     f32x2 s0[8], s1[8];
;     MD_GLDS_A(0, 0); MD_B_ISSUE(s0, 0); MD_B_ISSUE(s1, 1);
;     MD_B_WAIT(s0, 8); MD_B_WRITE(s0, 0); __builtin_amdgcn_sched_barrier(0); MD_B_ISSUE(s0, 2);
;     asm volatile("s_waitcnt vmcnt(16)" ::: "memory");
;     asm volatile("s_waitcnt lgkmcnt(0)" ::: "memory"); __builtin_amdgcn_s_barrier(); asm volatile("" ::: "memory");
; #pragma unroll 1
;     for (int t = 0; t < NT; t += 2) {
;         if (t + 2 < NT) MD_B_WAIT(s1, 8); else MD_B_WAIT(s1, 0);
;         MD_B_WRITE(s1, 1); __builtin_amdgcn_sched_barrier(0); MD_GLDS_A(1, t + 1); __builtin_amdgcn_sched_barrier(0);
;         if (t + 3 < NT) MD_B_ISSUE(s1, t + 3);
;         MD_COMPUTE(0);
;         MD_END(t + 3 >= NT);
;         if (t + 2 < NT) { MD_B_WAIT(s0, 8); MD_B_WRITE(s0, 0); __builtin_amdgcn_sched_barrier(0); MD_GLDS_A(0, t + 2); __builtin_amdgcn_sched_barrier(0); }
;         if (t + 4 < NT) MD_B_ISSUE(s0, t + 4);
;         MD_COMPUTE(1);
;         MD_END(t + 4 >= NT);
	s_mov_b32 s49, s46
	s_mov_b32 s46, s47
	s_mov_b32 s47, s48
	s_mov_b32 s48, s49
	s_add_i32 s50, s50, 1
	v_cvt_pk_bf16_f32 v172, v202, v204
	v_cvt_pk_bf16_f32 v173, v206, v208
	v_cvt_pk_bf16_f32 v174, v210, v212
	v_cvt_pk_bf16_f32 v175, v214, v216
	v_cvt_pk_bf16_f32 v176, v203, v205
	v_cvt_pk_bf16_f32 v177, v207, v209
	v_cvt_pk_bf16_f32 v178, v211, v213
	v_cvt_pk_bf16_f32 v179, v215, v217
	ds_write_b128 v95, v[172:175] offset:19456
	ds_write_b128 v95, v[176:179] offset:19584
	v_add_u32_e32 v91, s46, v135
	v_add_u32_e32 v93, s46, v137
	ds_read_b128 v[238:241], v139 offset:0
	ds_read_b128 v[242:245], v139 offset:2048
	ds_read_b128 v[246:249], v139 offset:4096
	ds_read_b128 v[250:253], v139 offset:6144
	ds_read_b128 v[218:221], v91 offset:0
	ds_read_b128 v[222:225], v91 offset:2048
	ds_read_b128 v[226:229], v91 offset:4096
	ds_read_b128 v[230:233], v91 offset:6144
	ds_read_b128 v[234:237], v91 offset:8192
	s_add_i32 s49, s48, s74
	s_add_i32 s52, s52, 1
	s_and_b32 s54, s52, 7
	s_cmp_eq_u32 s54, 0
	s_cselect_b32 s54, s53, s32
	s_cselect_b32 s55, -1, 0
	s_add_u32 s30, s30, s54
	s_addc_u32 s31, s31, s55
	s_waitcnt lgkmcnt(0)
	v_mfma_f32_16x16x32_bf16 v[78:81], v[238:241], v[218:221], v[78:81]
	v_mfma_f32_16x16x32_bf16 v[74:77], v[242:245], v[218:221], v[74:77]
	v_mfma_f32_16x16x32_bf16 v[70:73], v[246:249], v[218:221], v[70:73]
	v_mfma_f32_16x16x32_bf16 v[66:69], v[250:253], v[218:221], v[66:69]
	ds_read_b128 v[218:221], v93 offset:0
	ds_read_b128 v[142:145], v141 offset:0
	s_mov_b32 m0, s49
	s_nop 0
	global_load_lds_dwordx4 v88, s[30:31]
	v_mfma_f32_16x16x32_bf16 v[62:65], v[238:241], v[222:225], v[62:65]
	v_mfma_f32_16x16x32_bf16 v[58:61], v[242:245], v[222:225], v[58:61]
	v_mfma_f32_16x16x32_bf16 v[54:57], v[246:249], v[222:225], v[54:57]
	v_mfma_f32_16x16x32_bf16 v[50:53], v[250:253], v[222:225], v[50:53]
	ds_read_b128 v[222:225], v93 offset:2048
	ds_read_b128 v[146:149], v141 offset:2048
	s_add_i32 m0, s49, 0x2000
	s_nop 0
	global_load_lds_dwordx4 v90, s[30:31]
	v_mfma_f32_16x16x32_bf16 v[46:49], v[238:241], v[226:229], v[46:49]
	v_mfma_f32_16x16x32_bf16 v[42:45], v[242:245], v[226:229], v[42:45]
	v_mfma_f32_16x16x32_bf16 v[38:41], v[246:249], v[226:229], v[38:41]
	v_mfma_f32_16x16x32_bf16 v[34:37], v[250:253], v[226:229], v[34:37]
	ds_read_b128 v[226:229], v93 offset:4096
	ds_read_b128 v[156:159], v141 offset:4096
	s_add_i32 m0, s49, 0x4000
	s_nop 0
	global_load_lds_dwordx4 v92, s[30:31]
	v_mfma_f32_16x16x32_bf16 v[18:21], v[238:241], v[230:233], v[18:21]
	v_mfma_f32_16x16x32_bf16 v[22:25], v[242:245], v[230:233], v[22:25]
	v_mfma_f32_16x16x32_bf16 v[26:29], v[246:249], v[230:233], v[26:29]
	v_mfma_f32_16x16x32_bf16 v[30:33], v[250:253], v[230:233], v[30:33]
	ds_read_b128 v[230:233], v93 offset:6144
	ds_read_b128 v[160:163], v141 offset:6144
	s_add_i32 m0, s49, 0x6000
	s_nop 0
	global_load_lds_dwordx4 v94, s[30:31]
	v_mfma_f32_16x16x32_bf16 v[2:5], v[238:241], v[234:237], v[2:5]
	v_mfma_f32_16x16x32_bf16 v[6:9], v[242:245], v[234:237], v[6:9]
	v_mfma_f32_16x16x32_bf16 v[10:13], v[246:249], v[234:237], v[10:13]
	v_mfma_f32_16x16x32_bf16 v[14:17], v[250:253], v[234:237], v[14:17]
	ds_read_b128 v[234:237], v93 offset:8192
	s_add_i32 m0, s49, 0x8000
	s_nop 0
	global_load_lds_dwordx4 v96, s[30:31]
	s_waitcnt lgkmcnt(0)
	v_mfma_f32_16x16x32_bf16 v[78:81], v[142:145], v[218:221], v[78:81]
	v_mfma_f32_16x16x32_bf16 v[74:77], v[146:149], v[218:221], v[74:77]
	v_mfma_f32_16x16x32_bf16 v[70:73], v[156:159], v[218:221], v[70:73]
	v_mfma_f32_16x16x32_bf16 v[66:69], v[160:163], v[218:221], v[66:69]
	s_add_i32 s51, s51, 1
	s_and_b32 s54, s51, 7
	s_cmp_eq_u32 s54, 0
	s_cselect_b32 s44, s34, s35
	s_cselect_b32 s45, -1, 0
	v_lshl_add_u64 v[132:133], v[132:133], 0, s[44:45]
	global_load_dwordx2 v[202:203], v[132:133], off
	v_lshl_add_u64 v[180:181], v[132:133], 0, s[24:25]
	global_load_dwordx2 v[204:205], v[180:181], off
	v_mfma_f32_16x16x32_bf16 v[62:65], v[142:145], v[222:225], v[62:65]
	v_mfma_f32_16x16x32_bf16 v[58:61], v[146:149], v[222:225], v[58:61]
	v_mfma_f32_16x16x32_bf16 v[54:57], v[156:159], v[222:225], v[54:57]
	v_mfma_f32_16x16x32_bf16 v[50:53], v[160:163], v[222:225], v[50:53]
	v_lshl_add_u64 v[180:181], v[132:133], 0, s[26:27]
	global_load_dwordx2 v[206:207], v[180:181], off
	v_lshl_add_u64 v[180:181], v[132:133], 0, s[28:29]
	global_load_dwordx2 v[208:209], v[180:181], off
	v_mfma_f32_16x16x32_bf16 v[46:49], v[142:145], v[226:229], v[46:49]
	v_mfma_f32_16x16x32_bf16 v[42:45], v[146:149], v[226:229], v[42:45]
	v_mfma_f32_16x16x32_bf16 v[38:41], v[156:159], v[226:229], v[38:41]
	v_mfma_f32_16x16x32_bf16 v[34:37], v[160:163], v[226:229], v[34:37]
	v_lshl_add_u64 v[180:181], v[132:133], 0, s[36:37]
	global_load_dwordx2 v[210:211], v[180:181], off
	v_lshl_add_u64 v[180:181], v[132:133], 0, s[38:39]
	global_load_dwordx2 v[212:213], v[180:181], off
	v_mfma_f32_16x16x32_bf16 v[18:21], v[142:145], v[230:233], v[18:21]
	v_mfma_f32_16x16x32_bf16 v[22:25], v[146:149], v[230:233], v[22:25]
	v_mfma_f32_16x16x32_bf16 v[26:29], v[156:159], v[230:233], v[26:29]
	v_mfma_f32_16x16x32_bf16 v[30:33], v[160:163], v[230:233], v[30:33]
	v_lshl_add_u64 v[180:181], v[132:133], 0, s[40:41]
	global_load_dwordx2 v[214:215], v[180:181], off
	v_lshl_add_u64 v[180:181], v[132:133], 0, s[42:43]
	global_load_dwordx2 v[216:217], v[180:181], off
	v_mfma_f32_16x16x32_bf16 v[2:5], v[142:145], v[234:237], v[2:5]
	v_mfma_f32_16x16x32_bf16 v[6:9], v[146:149], v[234:237], v[6:9]
	v_mfma_f32_16x16x32_bf16 v[10:13], v[156:159], v[234:237], v[10:13]
	v_mfma_f32_16x16x32_bf16 v[14:17], v[160:163], v[234:237], v[14:17]
	s_waitcnt vmcnt(21)
	s_waitcnt lgkmcnt(0)
	s_barrier
; #define MD_GLDS_A(buf, tau) do { _Pragma("unroll") for (int i = 0; i < 5; ++i) if (amask & (1u << i)) \
;         __builtin_amdgcn_global_load_lds((const unsigned*)((const char*)HIDp + aoff[i] + (size_t)((tau) & 7) * 128), (PG8_LAS unsigned*)(MD_SA(buf) + wid * 1024 + i * 8192), 16, 0, 0); } while (0)
; #define MD_B_ISSUE(sb, tau) do { const char* kb_ = Bb + (size_t)((tau) >> 3) * 512 + (size_t)((tau) & 7) * (64 * (size_t)RB); _Pragma("unroll") for (int j = 0; j < 8; ++j) { const char* p_ = kb_ + (size_t)j * RB; \
;         asm volatile("global_load_dwordx2 %0, %1, off" : "=&v"(sb[j]) : "v"(p_) : "memory"); } } while (0)
; #define MD_B_WAIT(sb, N) asm volatile("s_waitcnt vmcnt(%8)" : "+v"(sb[0]), "+v"(sb[1]), "+v"(sb[2]), "+v"(sb[3]), "+v"(sb[4]), "+v"(sb[5]), "+v"(sb[6]), "+v"(sb[7]) : "n"(N) : "memory")
; __device__ __forceinline__ void moe_down_stream(PG8_LAS unsigned char* lds, int e, int cb0, int slot0, int nv, const bf16_t* HIDp, const float* Wd, bf16_t* Y, const float* slot_w, const int* slot_dst) {
;     ...
;     f32x4 acc[DNM][4];
; #pragma unroll
;     for (int m = 0; m < DNM; ++m)
; #pragma unroll
;         for (int n = 0; n < 4; ++n) acc[m][n] = (f32x4){0.f, 0.f, 0.f, 0.f};
;     f32x2 s0[8], s1[8];
;     MD_GLDS_A(0, 0); MD_B_ISSUE(s0, 0); MD_B_ISSUE(s1, 1);
;     MD_B_WAIT(s0, 8); MD_B_WRITE(s0, 0); __builtin_amdgcn_sched_barrier(0); MD_B_ISSUE(s0, 2);
;     asm volatile("s_waitcnt vmcnt(16)" ::: "memory");
;     asm volatile("s_waitcnt lgkmcnt(0)" ::: "memory"); __builtin_amdgcn_s_barrier(); asm volatile("" ::: "memory");
; #pragma unroll 1
;     for (int t = 0; t < NT; t += 2) {
;         if (t + 2 < NT) MD_B_WAIT(s1, 8); else MD_B_WAIT(s1, 0);
;         MD_B_WRITE(s1, 1); __builtin_amdgcn_sched_barrier(0); MD_GLDS_A(1, t + 1); __builtin_amdgcn_sched_barrier(0);
;         if (t + 3 < NT) MD_B_ISSUE(s1, t + 3);
;         MD_COMPUTE(0);
;         MD_END(t + 3 >= NT);
;         if (t + 2 < NT) { MD_B_WAIT(s0, 8); MD_B_WRITE(s0, 0); __builtin_amdgcn_sched_barrier(0); MD_GLDS_A(0, t + 2); __builtin_amdgcn_sched_barrier(0); }
;         if (t + 4 < NT) MD_B_ISSUE(s0, t + 4);
;         MD_COMPUTE(1);
;         MD_END(t + 4 >= NT);
	s_mov_b32 s49, s46
	s_mov_b32 s46, s47
	s_mov_b32 s47, s48
	s_mov_b32 s48, s49
	s_add_i32 s50, s50, 1
	v_cvt_pk_bf16_f32 v172, v98, v100
	v_cvt_pk_bf16_f32 v173, v102, v104
	v_cvt_pk_bf16_f32 v174, v106, v108
	v_cvt_pk_bf16_f32 v175, v110, v112
	v_cvt_pk_bf16_f32 v176, v99, v101
	v_cvt_pk_bf16_f32 v177, v103, v105
	v_cvt_pk_bf16_f32 v178, v107, v109
	v_cvt_pk_bf16_f32 v179, v111, v113
	ds_write_b128 v95, v[172:175] offset:0
	ds_write_b128 v95, v[176:179] offset:128
	v_add_u32_e32 v91, s46, v135
	v_add_u32_e32 v93, s46, v137
	ds_read_b128 v[238:241], v139 offset:19456
	ds_read_b128 v[242:245], v139 offset:21504
	ds_read_b128 v[246:249], v139 offset:23552
	ds_read_b128 v[250:253], v139 offset:25600
	ds_read_b128 v[218:221], v91 offset:0
	ds_read_b128 v[222:225], v91 offset:2048
	ds_read_b128 v[226:229], v91 offset:4096
	ds_read_b128 v[230:233], v91 offset:6144
	ds_read_b128 v[234:237], v91 offset:8192
	s_add_i32 s49, s48, s74
	s_add_i32 s52, s52, 1
	s_and_b32 s54, s52, 7
	s_cmp_eq_u32 s54, 0
	s_cselect_b32 s54, s53, s32
	s_cselect_b32 s55, -1, 0
	s_add_u32 s30, s30, s54
	s_addc_u32 s31, s31, s55
	s_waitcnt lgkmcnt(0)
	v_mfma_f32_16x16x32_bf16 v[78:81], v[238:241], v[218:221], v[78:81]
	v_mfma_f32_16x16x32_bf16 v[74:77], v[242:245], v[218:221], v[74:77]
	v_mfma_f32_16x16x32_bf16 v[70:73], v[246:249], v[218:221], v[70:73]
	v_mfma_f32_16x16x32_bf16 v[66:69], v[250:253], v[218:221], v[66:69]
	ds_read_b128 v[218:221], v93 offset:0
	ds_read_b128 v[142:145], v141 offset:19456
	s_mov_b32 m0, s49
	s_nop 0
	global_load_lds_dwordx4 v88, s[30:31]
	v_mfma_f32_16x16x32_bf16 v[62:65], v[238:241], v[222:225], v[62:65]
	v_mfma_f32_16x16x32_bf16 v[58:61], v[242:245], v[222:225], v[58:61]
	v_mfma_f32_16x16x32_bf16 v[54:57], v[246:249], v[222:225], v[54:57]
	v_mfma_f32_16x16x32_bf16 v[50:53], v[250:253], v[222:225], v[50:53]
	ds_read_b128 v[222:225], v93 offset:2048
	ds_read_b128 v[146:149], v141 offset:21504
	s_add_i32 m0, s49, 0x2000
	s_nop 0
	global_load_lds_dwordx4 v90, s[30:31]
	v_mfma_f32_16x16x32_bf16 v[46:49], v[238:241], v[226:229], v[46:49]
	v_mfma_f32_16x16x32_bf16 v[42:45], v[242:245], v[226:229], v[42:45]
	v_mfma_f32_16x16x32_bf16 v[38:41], v[246:249], v[226:229], v[38:41]
	v_mfma_f32_16x16x32_bf16 v[34:37], v[250:253], v[226:229], v[34:37]
	ds_read_b128 v[226:229], v93 offset:4096
	ds_read_b128 v[156:159], v141 offset:23552
	s_add_i32 m0, s49, 0x4000
	s_nop 0
	global_load_lds_dwordx4 v92, s[30:31]
	v_mfma_f32_16x16x32_bf16 v[18:21], v[238:241], v[230:233], v[18:21]
	v_mfma_f32_16x16x32_bf16 v[22:25], v[242:245], v[230:233], v[22:25]
	v_mfma_f32_16x16x32_bf16 v[26:29], v[246:249], v[230:233], v[26:29]
	v_mfma_f32_16x16x32_bf16 v[30:33], v[250:253], v[230:233], v[30:33]
	ds_read_b128 v[230:233], v93 offset:6144
	ds_read_b128 v[160:163], v141 offset:25600
	s_add_i32 m0, s49, 0x6000
	s_nop 0
	global_load_lds_dwordx4 v94, s[30:31]
	v_mfma_f32_16x16x32_bf16 v[2:5], v[238:241], v[234:237], v[2:5]
	v_mfma_f32_16x16x32_bf16 v[6:9], v[242:245], v[234:237], v[6:9]
	v_mfma_f32_16x16x32_bf16 v[10:13], v[246:249], v[234:237], v[10:13]
	v_mfma_f32_16x16x32_bf16 v[14:17], v[250:253], v[234:237], v[14:17]
	ds_read_b128 v[234:237], v93 offset:8192
	s_add_i32 m0, s49, 0x8000
	s_nop 0
	global_load_lds_dwordx4 v96, s[30:31]
	s_waitcnt lgkmcnt(0)
	v_mfma_f32_16x16x32_bf16 v[78:81], v[142:145], v[218:221], v[78:81]
	v_mfma_f32_16x16x32_bf16 v[74:77], v[146:149], v[218:221], v[74:77]
	v_mfma_f32_16x16x32_bf16 v[70:73], v[156:159], v[218:221], v[70:73]
	v_mfma_f32_16x16x32_bf16 v[66:69], v[160:163], v[218:221], v[66:69]
	s_add_i32 s51, s51, 1
	s_and_b32 s54, s51, 7
	s_cmp_eq_u32 s54, 0
	s_cselect_b32 s44, s34, s35
	s_cselect_b32 s45, -1, 0
	v_lshl_add_u64 v[132:133], v[132:133], 0, s[44:45]
	global_load_dwordx2 v[98:99], v[132:133], off
	v_lshl_add_u64 v[180:181], v[132:133], 0, s[24:25]
	global_load_dwordx2 v[100:101], v[180:181], off
	v_mfma_f32_16x16x32_bf16 v[62:65], v[142:145], v[222:225], v[62:65]
	v_mfma_f32_16x16x32_bf16 v[58:61], v[146:149], v[222:225], v[58:61]
	v_mfma_f32_16x16x32_bf16 v[54:57], v[156:159], v[222:225], v[54:57]
	v_mfma_f32_16x16x32_bf16 v[50:53], v[160:163], v[222:225], v[50:53]
	v_lshl_add_u64 v[180:181], v[132:133], 0, s[26:27]
	global_load_dwordx2 v[102:103], v[180:181], off
	v_lshl_add_u64 v[180:181], v[132:133], 0, s[28:29]
	global_load_dwordx2 v[104:105], v[180:181], off
	v_mfma_f32_16x16x32_bf16 v[46:49], v[142:145], v[226:229], v[46:49]
	v_mfma_f32_16x16x32_bf16 v[42:45], v[146:149], v[226:229], v[42:45]
	v_mfma_f32_16x16x32_bf16 v[38:41], v[156:159], v[226:229], v[38:41]
	v_mfma_f32_16x16x32_bf16 v[34:37], v[160:163], v[226:229], v[34:37]
	v_lshl_add_u64 v[180:181], v[132:133], 0, s[36:37]
	global_load_dwordx2 v[106:107], v[180:181], off
	v_lshl_add_u64 v[180:181], v[132:133], 0, s[38:39]
	global_load_dwordx2 v[108:109], v[180:181], off
	v_mfma_f32_16x16x32_bf16 v[18:21], v[142:145], v[230:233], v[18:21]
	v_mfma_f32_16x16x32_bf16 v[22:25], v[146:149], v[230:233], v[22:25]
	v_mfma_f32_16x16x32_bf16 v[26:29], v[156:159], v[230:233], v[26:29]
	v_mfma_f32_16x16x32_bf16 v[30:33], v[160:163], v[230:233], v[30:33]
	v_lshl_add_u64 v[180:181], v[132:133], 0, s[40:41]
	global_load_dwordx2 v[110:111], v[180:181], off
	v_lshl_add_u64 v[180:181], v[132:133], 0, s[42:43]
	global_load_dwordx2 v[112:113], v[180:181], off
	v_mfma_f32_16x16x32_bf16 v[2:5], v[142:145], v[234:237], v[2:5]
	v_mfma_f32_16x16x32_bf16 v[6:9], v[146:149], v[234:237], v[6:9]
	v_mfma_f32_16x16x32_bf16 v[10:13], v[156:159], v[234:237], v[10:13]
	v_mfma_f32_16x16x32_bf16 v[14:17], v[160:163], v[234:237], v[14:17]
	s_waitcnt vmcnt(21)
	s_waitcnt lgkmcnt(0)
	s_barrier
; #define PG8_LAS __attribute__((address_space(3)))
; __device__ __forceinline__ unsigned cvtpk(float lo, float hi) { f32x2 v = {lo, hi}; bf16x2_t b = __builtin_convertvector(v, bf16x2_t); return __builtin_bit_cast(unsigned, b); }
; __device__ __forceinline__ void moe_down_stream(PG8_LAS unsigned char* lds, int e, int cb0, int slot0, int nv, const bf16_t* HIDp, const float* Wd, bf16_t* Y, const float* slot_w, const int* slot_dst) {
;     ...
;         if (((t + 1) & 7) == 7) {
;             const int cb = cb0 + ((t + 1) >> 3);
; #pragma unroll
;             for (int m = 0; m < DNM; ++m) {
;                 const float w_ = lw[4 * (16 * m + fr) + wr];
; #pragma unroll
;                 for (int p = 0; p < 2; ++p) { const f32x4 v0 = acc[m][2 * p] * w_, v1 = acc[m][2 * p + 1] * w_; u32x4 w; w.x = cvtpk(v0[0], v0[1]); w.y = cvtpk(v0[2], v0[3]); w.z = cvtpk(v1[0], v1[1]); w.w = cvtpk(v1[2], v1[3]);
;                     *(PG8_LAS u32x4*)(stg + fr * 128 + (((4 * p + fq) ^ (fr & 7)) * 16)) = w; }
; #pragma unroll
;                 for (int hh = 0; hh < 2; ++hh) { const int r = (lane >> 3) + 8 * hh, cc = lane & 7; const u32x4 d = *(const PG8_LAS u32x4*)(stg + r * 128 + ((cc ^ (r & 7)) * 16)); const int dst_ = ldst[4 * (16 * m + r) + wr];
;                     if (dst_ >= 0) *(u32x4*)(Y + (size_t)dst_ * D + 128 * cb + 64 * wc + 8 * cc) = d; }
; #pragma unroll
;                 for (int n = 0; n < 4; ++n) acc[m][n] = (f32x4){0.f, 0.f, 0.f, 0.f}; } }
	s_mov_b32 s49, s46
	s_mov_b32 s46, s47
	s_mov_b32 s47, s48
	s_mov_b32 s48, s49
	s_add_i32 s50, s50, 1
	s_and_b32 s54, s50, 7
	s_cmp_lg_u32 s54, 0
	s_cbranch_scc1 .Lmd_noepi_X
	s_add_i32 s54, s48, s74
	v_add_u32_e32 v164, s54, v84
	v_add_u32_e32 v165, s54, v85
	ds_read_b32 v150, v82 offset:0
	ds_read_b32 v151, v83 offset:0
	ds_read_b32 v166, v83 offset:128
	s_waitcnt lgkmcnt(2)
	v_mul_f32_e32 v78, v150, v78
	v_mul_f32_e32 v79, v150, v79
	v_mul_f32_e32 v80, v150, v80
	v_mul_f32_e32 v81, v150, v81
	v_mul_f32_e32 v74, v150, v74
	v_mul_f32_e32 v75, v150, v75
	v_mul_f32_e32 v76, v150, v76
	v_mul_f32_e32 v77, v150, v77
	v_cvt_pk_bf16_f32 v182, v78, v79
	v_cvt_pk_bf16_f32 v183, v80, v81
	v_cvt_pk_bf16_f32 v184, v74, v75
	v_cvt_pk_bf16_f32 v185, v76, v77
	ds_write_b128 v164, v[182:185]
	v_mul_f32_e32 v70, v150, v70
	v_mul_f32_e32 v71, v150, v71
	v_mul_f32_e32 v72, v150, v72
	v_mul_f32_e32 v73, v150, v73
	v_mul_f32_e32 v66, v150, v66
	v_mul_f32_e32 v67, v150, v67
	v_mul_f32_e32 v68, v150, v68
	v_mul_f32_e32 v69, v150, v69
	v_cvt_pk_bf16_f32 v182, v70, v71
	v_cvt_pk_bf16_f32 v183, v72, v73
	v_cvt_pk_bf16_f32 v184, v66, v67
	v_cvt_pk_bf16_f32 v185, v68, v69
	v_xor_b32_e32 v167, 64, v164
	ds_write_b128 v167, v[182:185]
	v_mov_b32_e32 v78, 0
	v_mov_b32_e32 v74, 0
	v_mov_b32_e32 v70, 0
	v_mov_b32_e32 v66, 0
	v_mov_b32_e32 v79, 0
	v_mov_b32_e32 v75, 0
	v_mov_b32_e32 v71, 0
	v_mov_b32_e32 v67, 0
	v_mov_b32_e32 v80, 0
	v_mov_b32_e32 v76, 0
	v_mov_b32_e32 v72, 0
	v_mov_b32_e32 v68, 0
	v_mov_b32_e32 v81, 0
	v_mov_b32_e32 v77, 0
	v_mov_b32_e32 v73, 0
	v_mov_b32_e32 v69, 0
	ds_read_b128 v[182:185], v165 offset:0
	v_cmp_lt_i32_e32 vcc, -1, v151
	v_lshlrev_b32_e32 v148, 13, v151
	v_mov_b32_e32 v149, 0
	v_lshl_add_u64 v[148:149], v[148:149], 0, v[86:87]
	v_cndmask_b32_e32 v148, v168, v148, vcc
	v_cndmask_b32_e32 v149, v169, v149, vcc
	s_waitcnt lgkmcnt(0)
	global_store_dwordx4 v[148:149], v[182:185], off
	ds_read_b128 v[182:185], v165 offset:8192
	v_cmp_lt_i32_e32 vcc, -1, v166
	v_lshlrev_b32_e32 v148, 13, v166
	v_mov_b32_e32 v149, 0
	v_lshl_add_u64 v[148:149], v[148:149], 0, v[86:87]
	v_cndmask_b32_e32 v148, v168, v148, vcc
	v_cndmask_b32_e32 v149, v169, v149, vcc
	s_waitcnt lgkmcnt(0)
	global_store_dwordx4 v[148:149], v[182:185], off
	ds_read_b32 v150, v82 offset:256
	ds_read_b32 v151, v83 offset:256
	ds_read_b32 v166, v83 offset:384
	s_waitcnt lgkmcnt(2)
	v_mul_f32_e32 v62, v150, v62
	v_mul_f32_e32 v63, v150, v63
	v_mul_f32_e32 v64, v150, v64
	v_mul_f32_e32 v65, v150, v65
	v_mul_f32_e32 v58, v150, v58
	v_mul_f32_e32 v59, v150, v59
	v_mul_f32_e32 v60, v150, v60
	v_mul_f32_e32 v61, v150, v61
	v_cvt_pk_bf16_f32 v182, v62, v63
	v_cvt_pk_bf16_f32 v183, v64, v65
	v_cvt_pk_bf16_f32 v184, v58, v59
	v_cvt_pk_bf16_f32 v185, v60, v61
	ds_write_b128 v164, v[182:185]
	v_mul_f32_e32 v54, v150, v54
	v_mul_f32_e32 v55, v150, v55
	v_mul_f32_e32 v56, v150, v56
	v_mul_f32_e32 v57, v150, v57
	v_mul_f32_e32 v50, v150, v50
	v_mul_f32_e32 v51, v150, v51
	v_mul_f32_e32 v52, v150, v52
	v_mul_f32_e32 v53, v150, v53
	v_cvt_pk_bf16_f32 v182, v54, v55
	v_cvt_pk_bf16_f32 v183, v56, v57
	v_cvt_pk_bf16_f32 v184, v50, v51
	v_cvt_pk_bf16_f32 v185, v52, v53
	v_xor_b32_e32 v167, 64, v164
	ds_write_b128 v167, v[182:185]
	v_mov_b32_e32 v62, 0
	v_mov_b32_e32 v58, 0
	v_mov_b32_e32 v54, 0
	v_mov_b32_e32 v50, 0
	v_mov_b32_e32 v63, 0
	v_mov_b32_e32 v59, 0
	v_mov_b32_e32 v55, 0
	v_mov_b32_e32 v51, 0
	v_mov_b32_e32 v64, 0
	v_mov_b32_e32 v60, 0
	v_mov_b32_e32 v56, 0
	v_mov_b32_e32 v52, 0
	v_mov_b32_e32 v65, 0
	v_mov_b32_e32 v61, 0
	v_mov_b32_e32 v57, 0
	v_mov_b32_e32 v53, 0
	ds_read_b128 v[182:185], v165 offset:0
	v_cmp_lt_i32_e32 vcc, -1, v151
	v_lshlrev_b32_e32 v148, 13, v151
	v_mov_b32_e32 v149, 0
	v_lshl_add_u64 v[148:149], v[148:149], 0, v[86:87]
	v_cndmask_b32_e32 v148, v168, v148, vcc
	v_cndmask_b32_e32 v149, v169, v149, vcc
	s_waitcnt lgkmcnt(0)
	global_store_dwordx4 v[148:149], v[182:185], off
	ds_read_b128 v[182:185], v165 offset:8192
	v_cmp_lt_i32_e32 vcc, -1, v166
	v_lshlrev_b32_e32 v148, 13, v166
	v_mov_b32_e32 v149, 0
	v_lshl_add_u64 v[148:149], v[148:149], 0, v[86:87]
	v_cndmask_b32_e32 v148, v168, v148, vcc
	v_cndmask_b32_e32 v149, v169, v149, vcc
	s_waitcnt lgkmcnt(0)
	global_store_dwordx4 v[148:149], v[182:185], off
	ds_read_b32 v150, v82 offset:512
	ds_read_b32 v151, v83 offset:512
	ds_read_b32 v166, v83 offset:640
	s_waitcnt lgkmcnt(2)
	v_mul_f32_e32 v46, v150, v46
	v_mul_f32_e32 v47, v150, v47
	v_mul_f32_e32 v48, v150, v48
	v_mul_f32_e32 v49, v150, v49
	v_mul_f32_e32 v42, v150, v42
	v_mul_f32_e32 v43, v150, v43
	v_mul_f32_e32 v44, v150, v44
	v_mul_f32_e32 v45, v150, v45
	v_cvt_pk_bf16_f32 v182, v46, v47
	v_cvt_pk_bf16_f32 v183, v48, v49
	v_cvt_pk_bf16_f32 v184, v42, v43
	v_cvt_pk_bf16_f32 v185, v44, v45
	ds_write_b128 v164, v[182:185]
	v_mul_f32_e32 v38, v150, v38
	v_mul_f32_e32 v39, v150, v39
	v_mul_f32_e32 v40, v150, v40
	v_mul_f32_e32 v41, v150, v41
	v_mul_f32_e32 v34, v150, v34
	v_mul_f32_e32 v35, v150, v35
	v_mul_f32_e32 v36, v150, v36
	v_mul_f32_e32 v37, v150, v37
	v_cvt_pk_bf16_f32 v182, v38, v39
	v_cvt_pk_bf16_f32 v183, v40, v41
	v_cvt_pk_bf16_f32 v184, v34, v35
	v_cvt_pk_bf16_f32 v185, v36, v37
	v_xor_b32_e32 v167, 64, v164
	ds_write_b128 v167, v[182:185]
	v_mov_b32_e32 v46, 0
	v_mov_b32_e32 v42, 0
	v_mov_b32_e32 v38, 0
	v_mov_b32_e32 v34, 0
	v_mov_b32_e32 v47, 0
	v_mov_b32_e32 v43, 0
	v_mov_b32_e32 v39, 0
	v_mov_b32_e32 v35, 0
	v_mov_b32_e32 v48, 0
	v_mov_b32_e32 v44, 0
	v_mov_b32_e32 v40, 0
	v_mov_b32_e32 v36, 0
	v_mov_b32_e32 v49, 0
	v_mov_b32_e32 v45, 0
	v_mov_b32_e32 v41, 0
	v_mov_b32_e32 v37, 0
	ds_read_b128 v[182:185], v165 offset:0
	v_cmp_lt_i32_e32 vcc, -1, v151
	v_lshlrev_b32_e32 v148, 13, v151
	v_mov_b32_e32 v149, 0
	v_lshl_add_u64 v[148:149], v[148:149], 0, v[86:87]
	v_cndmask_b32_e32 v148, v168, v148, vcc
	v_cndmask_b32_e32 v149, v169, v149, vcc
	s_waitcnt lgkmcnt(0)
; #define PG8_LAS __attribute__((address_space(3)))
; __device__ __forceinline__ unsigned cvtpk(float lo, float hi) { f32x2 v = {lo, hi}; bf16x2_t b = __builtin_convertvector(v, bf16x2_t); return __builtin_bit_cast(unsigned, b); }
; __device__ __forceinline__ void moe_down_stream(PG8_LAS unsigned char* lds, int e, int cb0, int slot0, int nv, const bf16_t* HIDp, const float* Wd, bf16_t* Y, const float* slot_w, const int* slot_dst) {
;     ...
;         if (((t + 1) & 7) == 7) {
;             const int cb = cb0 + ((t + 1) >> 3);
; #pragma unroll
;             for (int m = 0; m < DNM; ++m) {
;                 const float w_ = lw[4 * (16 * m + fr) + wr];
; #pragma unroll
;                 for (int p = 0; p < 2; ++p) { const f32x4 v0 = acc[m][2 * p] * w_, v1 = acc[m][2 * p + 1] * w_; u32x4 w; w.x = cvtpk(v0[0], v0[1]); w.y = cvtpk(v0[2], v0[3]); w.z = cvtpk(v1[0], v1[1]); w.w = cvtpk(v1[2], v1[3]);
;                     *(PG8_LAS u32x4*)(stg + fr * 128 + (((4 * p + fq) ^ (fr & 7)) * 16)) = w; }
; #pragma unroll
;                 for (int hh = 0; hh < 2; ++hh) { const int r = (lane >> 3) + 8 * hh, cc = lane & 7; const u32x4 d = *(const PG8_LAS u32x4*)(stg + r * 128 + ((cc ^ (r & 7)) * 16)); const int dst_ = ldst[4 * (16 * m + r) + wr];
;                     if (dst_ >= 0) *(u32x4*)(Y + (size_t)dst_ * D + 128 * cb + 64 * wc + 8 * cc) = d; }
; #pragma unroll
;                 for (int n = 0; n < 4; ++n) acc[m][n] = (f32x4){0.f, 0.f, 0.f, 0.f}; } }
	global_store_dwordx4 v[148:149], v[182:185], off
	ds_read_b128 v[182:185], v165 offset:8192
	v_cmp_lt_i32_e32 vcc, -1, v166
	v_lshlrev_b32_e32 v148, 13, v166
	v_mov_b32_e32 v149, 0
	v_lshl_add_u64 v[148:149], v[148:149], 0, v[86:87]
	v_cndmask_b32_e32 v148, v168, v148, vcc
	v_cndmask_b32_e32 v149, v169, v149, vcc
	s_waitcnt lgkmcnt(0)
	global_store_dwordx4 v[148:149], v[182:185], off
	ds_read_b32 v150, v82 offset:768
	ds_read_b32 v151, v83 offset:768
	ds_read_b32 v166, v83 offset:896
	s_waitcnt lgkmcnt(2)
	v_mul_f32_e32 v18, v150, v18
	v_mul_f32_e32 v19, v150, v19
	v_mul_f32_e32 v20, v150, v20
	v_mul_f32_e32 v21, v150, v21
	v_mul_f32_e32 v22, v150, v22
	v_mul_f32_e32 v23, v150, v23
	v_mul_f32_e32 v24, v150, v24
	v_mul_f32_e32 v25, v150, v25
	v_cvt_pk_bf16_f32 v182, v18, v19
	v_cvt_pk_bf16_f32 v183, v20, v21
	v_cvt_pk_bf16_f32 v184, v22, v23
	v_cvt_pk_bf16_f32 v185, v24, v25
	ds_write_b128 v164, v[182:185]
	v_mul_f32_e32 v26, v150, v26
	v_mul_f32_e32 v27, v150, v27
	v_mul_f32_e32 v28, v150, v28
	v_mul_f32_e32 v29, v150, v29
	v_mul_f32_e32 v30, v150, v30
	v_mul_f32_e32 v31, v150, v31
	v_mul_f32_e32 v32, v150, v32
	v_mul_f32_e32 v33, v150, v33
	v_cvt_pk_bf16_f32 v182, v26, v27
	v_cvt_pk_bf16_f32 v183, v28, v29
	v_cvt_pk_bf16_f32 v184, v30, v31
	v_cvt_pk_bf16_f32 v185, v32, v33
	v_xor_b32_e32 v167, 64, v164
	ds_write_b128 v167, v[182:185]
	v_mov_b32_e32 v18, 0
	v_mov_b32_e32 v22, 0
	v_mov_b32_e32 v26, 0
	v_mov_b32_e32 v30, 0
	v_mov_b32_e32 v19, 0
	v_mov_b32_e32 v23, 0
	v_mov_b32_e32 v27, 0
	v_mov_b32_e32 v31, 0
	v_mov_b32_e32 v20, 0
	v_mov_b32_e32 v24, 0
	v_mov_b32_e32 v28, 0
	v_mov_b32_e32 v32, 0
	v_mov_b32_e32 v21, 0
	v_mov_b32_e32 v25, 0
	v_mov_b32_e32 v29, 0
	v_mov_b32_e32 v33, 0
	ds_read_b128 v[182:185], v165 offset:0
	v_cmp_lt_i32_e32 vcc, -1, v151
	v_lshlrev_b32_e32 v148, 13, v151
	v_mov_b32_e32 v149, 0
	v_lshl_add_u64 v[148:149], v[148:149], 0, v[86:87]
	v_cndmask_b32_e32 v148, v168, v148, vcc
	v_cndmask_b32_e32 v149, v169, v149, vcc
	s_waitcnt lgkmcnt(0)
	global_store_dwordx4 v[148:149], v[182:185], off
	ds_read_b128 v[182:185], v165 offset:8192
	v_cmp_lt_i32_e32 vcc, -1, v166
	v_lshlrev_b32_e32 v148, 13, v166
	v_mov_b32_e32 v149, 0
	v_lshl_add_u64 v[148:149], v[148:149], 0, v[86:87]
	v_cndmask_b32_e32 v148, v168, v148, vcc
	v_cndmask_b32_e32 v149, v169, v149, vcc
	s_waitcnt lgkmcnt(0)
	global_store_dwordx4 v[148:149], v[182:185], off
	ds_read_b32 v150, v82 offset:1024
	ds_read_b32 v151, v83 offset:1024
	ds_read_b32 v166, v83 offset:1152
	s_waitcnt lgkmcnt(2)
	v_mul_f32_e32 v2, v150, v2
	v_mul_f32_e32 v3, v150, v3
	v_mul_f32_e32 v4, v150, v4
	v_mul_f32_e32 v5, v150, v5
	v_mul_f32_e32 v6, v150, v6
	v_mul_f32_e32 v7, v150, v7
	v_mul_f32_e32 v8, v150, v8
	v_mul_f32_e32 v9, v150, v9
	v_cvt_pk_bf16_f32 v182, v2, v3
	v_cvt_pk_bf16_f32 v183, v4, v5
	v_cvt_pk_bf16_f32 v184, v6, v7
	v_cvt_pk_bf16_f32 v185, v8, v9
	ds_write_b128 v164, v[182:185]
	v_mul_f32_e32 v10, v150, v10
	v_mul_f32_e32 v11, v150, v11
	v_mul_f32_e32 v12, v150, v12
	v_mul_f32_e32 v13, v150, v13
	v_mul_f32_e32 v14, v150, v14
	v_mul_f32_e32 v15, v150, v15
	v_mul_f32_e32 v16, v150, v16
	v_mul_f32_e32 v17, v150, v17
	v_cvt_pk_bf16_f32 v182, v10, v11
	v_cvt_pk_bf16_f32 v183, v12, v13
	v_cvt_pk_bf16_f32 v184, v14, v15
	v_cvt_pk_bf16_f32 v185, v16, v17
	v_xor_b32_e32 v167, 64, v164
	ds_write_b128 v167, v[182:185]
	v_mov_b32_e32 v2, 0
	v_mov_b32_e32 v6, 0
	v_mov_b32_e32 v10, 0
	v_mov_b32_e32 v14, 0
	v_mov_b32_e32 v3, 0
	v_mov_b32_e32 v7, 0
	v_mov_b32_e32 v11, 0
	v_mov_b32_e32 v15, 0
	v_mov_b32_e32 v4, 0
	v_mov_b32_e32 v8, 0
	v_mov_b32_e32 v12, 0
	v_mov_b32_e32 v16, 0
	v_mov_b32_e32 v5, 0
	v_mov_b32_e32 v9, 0
	v_mov_b32_e32 v13, 0
	v_mov_b32_e32 v17, 0
	ds_read_b128 v[182:185], v165 offset:0
	v_cmp_lt_i32_e32 vcc, -1, v151
	v_lshlrev_b32_e32 v148, 13, v151
	v_mov_b32_e32 v149, 0
	v_lshl_add_u64 v[148:149], v[148:149], 0, v[86:87]
	v_cndmask_b32_e32 v148, v168, v148, vcc
	v_cndmask_b32_e32 v149, v169, v149, vcc
	s_waitcnt lgkmcnt(0)
	global_store_dwordx4 v[148:149], v[182:185], off
	ds_read_b128 v[182:185], v165 offset:8192
	v_cmp_lt_i32_e32 vcc, -1, v166
	v_lshlrev_b32_e32 v148, 13, v166
	v_mov_b32_e32 v149, 0
	v_lshl_add_u64 v[148:149], v[148:149], 0, v[86:87]
	v_cndmask_b32_e32 v148, v168, v148, vcc
	v_cndmask_b32_e32 v149, v169, v149, vcc
	s_waitcnt lgkmcnt(0)
	global_store_dwordx4 v[148:149], v[182:185], off
	v_add_co_u32_e32 v86, vcc, 0x400, v86
	s_nop 1
	v_addc_co_u32_e32 v87, vcc, 0, v87, vcc
	s_waitcnt lgkmcnt(0)
; #define MD_GLDS_A(buf, tau) do { _Pragma("unroll") for (int i = 0; i < 5; ++i) if (amask & (1u << i)) \
;         __builtin_amdgcn_global_load_lds((const unsigned*)((const char*)HIDp + aoff[i] + (size_t)((tau) & 7) * 128), (PG8_LAS unsigned*)(MD_SA(buf) + wid * 1024 + i * 8192), 16, 0, 0); } while (0)
; #define MD_B_ISSUE(sb, tau) do { const char* kb_ = Bb + (size_t)((tau) >> 3) * 512 + (size_t)((tau) & 7) * (64 * (size_t)RB); _Pragma("unroll") for (int j = 0; j < 8; ++j) { const char* p_ = kb_ + (size_t)j * RB; \
;         asm volatile("global_load_dwordx2 %0, %1, off" : "=&v"(sb[j]) : "v"(p_) : "memory"); } } while (0)
; #define MD_B_WAIT(sb, N) asm volatile("s_waitcnt vmcnt(%8)" : "+v"(sb[0]), "+v"(sb[1]), "+v"(sb[2]), "+v"(sb[3]), "+v"(sb[4]), "+v"(sb[5]), "+v"(sb[6]), "+v"(sb[7]) : "n"(N) : "memory")
; #define MD_END(last) do { if (last) asm volatile("s_waitcnt vmcnt(0)" ::: "memory"); else asm volatile("s_waitcnt vmcnt(8)" ::: "memory"); \
;         asm volatile("s_waitcnt lgkmcnt(0)" ::: "memory"); __builtin_amdgcn_s_barrier(); asm volatile("" ::: "memory"); } while (0)
; __device__ __forceinline__ void moe_down_stream(PG8_LAS unsigned char* lds, int e, int cb0, int slot0, int nv, const bf16_t* HIDp, const float* Wd, bf16_t* Y, const float* slot_w, const int* slot_dst) {
;     ...
;     for (int t = 0; t < NT; t += 2) {
;         if (t + 2 < NT) MD_B_WAIT(s1, 8); else MD_B_WAIT(s1, 0);
;         MD_B_WRITE(s1, 1); __builtin_amdgcn_sched_barrier(0); MD_GLDS_A(1, t + 1); __builtin_amdgcn_sched_barrier(0);
;         if (t + 3 < NT) MD_B_ISSUE(s1, t + 3);
;         MD_COMPUTE(0);
;         MD_END(t + 3 >= NT);
;         if (t + 2 < NT) { MD_B_WAIT(s0, 8); MD_B_WRITE(s0, 0); __builtin_amdgcn_sched_barrier(0); MD_GLDS_A(0, t + 2); __builtin_amdgcn_sched_barrier(0); }
;         if (t + 4 < NT) MD_B_ISSUE(s0, t + 4);
;         MD_COMPUTE(1);
;         MD_END(t + 4 >= NT);
.Lmd_noepi_X:
	s_sub_u32 s56, s56, 1
	s_cmp_lg_u32 s56, 0
	s_cbranch_scc1 .Lmd_loop_X
	v_cvt_pk_bf16_f32 v172, v114, v116
	v_cvt_pk_bf16_f32 v173, v118, v120
	v_cvt_pk_bf16_f32 v174, v122, v124
	v_cvt_pk_bf16_f32 v175, v126, v128
	v_cvt_pk_bf16_f32 v176, v115, v117
	v_cvt_pk_bf16_f32 v177, v119, v121
	v_cvt_pk_bf16_f32 v178, v123, v125
	v_cvt_pk_bf16_f32 v179, v127, v129
	ds_write_b128 v95, v[172:175] offset:19456
	ds_write_b128 v95, v[176:179] offset:19584
	v_add_u32_e32 v91, s46, v135
	v_add_u32_e32 v93, s46, v137
	ds_read_b128 v[238:241], v139 offset:0
	ds_read_b128 v[242:245], v139 offset:2048
	ds_read_b128 v[246:249], v139 offset:4096
	ds_read_b128 v[250:253], v139 offset:6144
	ds_read_b128 v[218:221], v91 offset:0
	ds_read_b128 v[222:225], v91 offset:2048
	ds_read_b128 v[226:229], v91 offset:4096
	ds_read_b128 v[230:233], v91 offset:6144
	ds_read_b128 v[234:237], v91 offset:8192
	s_add_i32 s49, s48, s74
	s_add_i32 s52, s52, 1
	s_and_b32 s54, s52, 7
	s_cmp_eq_u32 s54, 0
	s_cselect_b32 s54, s53, s32
	s_cselect_b32 s55, -1, 0
	s_add_u32 s30, s30, s54
	s_addc_u32 s31, s31, s55
	s_waitcnt lgkmcnt(0)
	v_mfma_f32_16x16x32_bf16 v[78:81], v[238:241], v[218:221], v[78:81]
	v_mfma_f32_16x16x32_bf16 v[74:77], v[242:245], v[218:221], v[74:77]
	v_mfma_f32_16x16x32_bf16 v[70:73], v[246:249], v[218:221], v[70:73]
	v_mfma_f32_16x16x32_bf16 v[66:69], v[250:253], v[218:221], v[66:69]
	ds_read_b128 v[218:221], v93 offset:0
	ds_read_b128 v[142:145], v141 offset:0
	s_mov_b32 m0, s49
	s_nop 0
	global_load_lds_dwordx4 v88, s[30:31]
	v_mfma_f32_16x16x32_bf16 v[62:65], v[238:241], v[222:225], v[62:65]
	v_mfma_f32_16x16x32_bf16 v[58:61], v[242:245], v[222:225], v[58:61]
	v_mfma_f32_16x16x32_bf16 v[54:57], v[246:249], v[222:225], v[54:57]
	v_mfma_f32_16x16x32_bf16 v[50:53], v[250:253], v[222:225], v[50:53]
	ds_read_b128 v[222:225], v93 offset:2048
	ds_read_b128 v[146:149], v141 offset:2048
	s_add_i32 m0, s49, 0x2000
	s_nop 0
	global_load_lds_dwordx4 v90, s[30:31]
	v_mfma_f32_16x16x32_bf16 v[46:49], v[238:241], v[226:229], v[46:49]
	v_mfma_f32_16x16x32_bf16 v[42:45], v[242:245], v[226:229], v[42:45]
	v_mfma_f32_16x16x32_bf16 v[38:41], v[246:249], v[226:229], v[38:41]
	v_mfma_f32_16x16x32_bf16 v[34:37], v[250:253], v[226:229], v[34:37]
	ds_read_b128 v[226:229], v93 offset:4096
	ds_read_b128 v[156:159], v141 offset:4096
	s_add_i32 m0, s49, 0x4000
	s_nop 0
	global_load_lds_dwordx4 v92, s[30:31]
	v_mfma_f32_16x16x32_bf16 v[18:21], v[238:241], v[230:233], v[18:21]
	v_mfma_f32_16x16x32_bf16 v[22:25], v[242:245], v[230:233], v[22:25]
	v_mfma_f32_16x16x32_bf16 v[26:29], v[246:249], v[230:233], v[26:29]
	v_mfma_f32_16x16x32_bf16 v[30:33], v[250:253], v[230:233], v[30:33]
	ds_read_b128 v[230:233], v93 offset:6144
	ds_read_b128 v[160:163], v141 offset:6144
	s_add_i32 m0, s49, 0x6000
	s_nop 0
	global_load_lds_dwordx4 v94, s[30:31]
	v_mfma_f32_16x16x32_bf16 v[2:5], v[238:241], v[234:237], v[2:5]
	v_mfma_f32_16x16x32_bf16 v[6:9], v[242:245], v[234:237], v[6:9]
	v_mfma_f32_16x16x32_bf16 v[10:13], v[246:249], v[234:237], v[10:13]
	v_mfma_f32_16x16x32_bf16 v[14:17], v[250:253], v[234:237], v[14:17]
	ds_read_b128 v[234:237], v93 offset:8192
	s_add_i32 m0, s49, 0x8000
	s_nop 0
	global_load_lds_dwordx4 v96, s[30:31]
	s_waitcnt lgkmcnt(0)
	v_mfma_f32_16x16x32_bf16 v[78:81], v[142:145], v[218:221], v[78:81]
	v_mfma_f32_16x16x32_bf16 v[74:77], v[146:149], v[218:221], v[74:77]
	v_mfma_f32_16x16x32_bf16 v[70:73], v[156:159], v[218:221], v[70:73]
	v_mfma_f32_16x16x32_bf16 v[66:69], v[160:163], v[218:221], v[66:69]
	s_add_i32 s51, s51, 1
	s_and_b32 s54, s51, 7
	s_cmp_eq_u32 s54, 0
	s_cselect_b32 s44, s34, s35
	s_cselect_b32 s45, -1, 0
	v_lshl_add_u64 v[132:133], v[132:133], 0, s[44:45]
	global_load_dwordx2 v[114:115], v[132:133], off
	v_lshl_add_u64 v[180:181], v[132:133], 0, s[24:25]
	global_load_dwordx2 v[116:117], v[180:181], off
	v_mfma_f32_16x16x32_bf16 v[62:65], v[142:145], v[222:225], v[62:65]
	v_mfma_f32_16x16x32_bf16 v[58:61], v[146:149], v[222:225], v[58:61]
	v_mfma_f32_16x16x32_bf16 v[54:57], v[156:159], v[222:225], v[54:57]
	v_mfma_f32_16x16x32_bf16 v[50:53], v[160:163], v[222:225], v[50:53]
	v_lshl_add_u64 v[180:181], v[132:133], 0, s[26:27]
	global_load_dwordx2 v[118:119], v[180:181], off
	v_lshl_add_u64 v[180:181], v[132:133], 0, s[28:29]
	global_load_dwordx2 v[120:121], v[180:181], off
	v_mfma_f32_16x16x32_bf16 v[46:49], v[142:145], v[226:229], v[46:49]
	v_mfma_f32_16x16x32_bf16 v[42:45], v[146:149], v[226:229], v[42:45]
	v_mfma_f32_16x16x32_bf16 v[38:41], v[156:159], v[226:229], v[38:41]
	v_mfma_f32_16x16x32_bf16 v[34:37], v[160:163], v[226:229], v[34:37]
	v_lshl_add_u64 v[180:181], v[132:133], 0, s[36:37]
	global_load_dwordx2 v[122:123], v[180:181], off
	v_lshl_add_u64 v[180:181], v[132:133], 0, s[38:39]
	global_load_dwordx2 v[124:125], v[180:181], off
	v_mfma_f32_16x16x32_bf16 v[18:21], v[142:145], v[230:233], v[18:21]
	v_mfma_f32_16x16x32_bf16 v[22:25], v[146:149], v[230:233], v[22:25]
	v_mfma_f32_16x16x32_bf16 v[26:29], v[156:159], v[230:233], v[26:29]
	v_mfma_f32_16x16x32_bf16 v[30:33], v[160:163], v[230:233], v[30:33]
	v_lshl_add_u64 v[180:181], v[132:133], 0, s[40:41]
	global_load_dwordx2 v[126:127], v[180:181], off
	v_lshl_add_u64 v[180:181], v[132:133], 0, s[42:43]
	global_load_dwordx2 v[128:129], v[180:181], off
	v_mfma_f32_16x16x32_bf16 v[2:5], v[142:145], v[234:237], v[2:5]
	v_mfma_f32_16x16x32_bf16 v[6:9], v[146:149], v[234:237], v[6:9]
	v_mfma_f32_16x16x32_bf16 v[10:13], v[156:159], v[234:237], v[10:13]
	v_mfma_f32_16x16x32_bf16 v[14:17], v[160:163], v[234:237], v[14:17]
	s_waitcnt vmcnt(21)
	s_waitcnt lgkmcnt(0)
	s_barrier
; #define MD_GLDS_A(buf, tau) do { _Pragma("unroll") for (int i = 0; i < 5; ++i) if (amask & (1u << i)) \
;         __builtin_amdgcn_global_load_lds((const unsigned*)((const char*)HIDp + aoff[i] + (size_t)((tau) & 7) * 128), (PG8_LAS unsigned*)(MD_SA(buf) + wid * 1024 + i * 8192), 16, 0, 0); } while (0)
; #define MD_B_ISSUE(sb, tau) do { const char* kb_ = Bb + (size_t)((tau) >> 3) * 512 + (size_t)((tau) & 7) * (64 * (size_t)RB); _Pragma("unroll") for (int j = 0; j < 8; ++j) { const char* p_ = kb_ + (size_t)j * RB; \
;         asm volatile("global_load_dwordx2 %0, %1, off" : "=&v"(sb[j]) : "v"(p_) : "memory"); } } while (0)
; #define MD_B_WAIT(sb, N) asm volatile("s_waitcnt vmcnt(%8)" : "+v"(sb[0]), "+v"(sb[1]), "+v"(sb[2]), "+v"(sb[3]), "+v"(sb[4]), "+v"(sb[5]), "+v"(sb[6]), "+v"(sb[7]) : "n"(N) : "memory")
; __device__ __forceinline__ void moe_down_stream(PG8_LAS unsigned char* lds, int e, int cb0, int slot0, int nv, const bf16_t* HIDp, const float* Wd, bf16_t* Y, const float* slot_w, const int* slot_dst) {
;     ...
;     f32x4 acc[DNM][4];
; #pragma unroll
;     for (int m = 0; m < DNM; ++m)
; #pragma unroll
;         for (int n = 0; n < 4; ++n) acc[m][n] = (f32x4){0.f, 0.f, 0.f, 0.f};
;     f32x2 s0[8], s1[8];
;     MD_GLDS_A(0, 0); MD_B_ISSUE(s0, 0); MD_B_ISSUE(s1, 1);
;     MD_B_WAIT(s0, 8); MD_B_WRITE(s0, 0); __builtin_amdgcn_sched_barrier(0); MD_B_ISSUE(s0, 2);
;     asm volatile("s_waitcnt vmcnt(16)" ::: "memory");
;     asm volatile("s_waitcnt lgkmcnt(0)" ::: "memory"); __builtin_amdgcn_s_barrier(); asm volatile("" ::: "memory");
; #pragma unroll 1
;     for (int t = 0; t < NT; t += 2) {
;         if (t + 2 < NT) MD_B_WAIT(s1, 8); else MD_B_WAIT(s1, 0);
;         MD_B_WRITE(s1, 1); __builtin_amdgcn_sched_barrier(0); MD_GLDS_A(1, t + 1); __builtin_amdgcn_sched_barrier(0);
;         if (t + 3 < NT) MD_B_ISSUE(s1, t + 3);
;         MD_COMPUTE(0);
;         MD_END(t + 3 >= NT);
;         if (t + 2 < NT) { MD_B_WAIT(s0, 8); MD_B_WRITE(s0, 0); __builtin_amdgcn_sched_barrier(0); MD_GLDS_A(0, t + 2); __builtin_amdgcn_sched_barrier(0); }
;         if (t + 4 < NT) MD_B_ISSUE(s0, t + 4);
;         MD_COMPUTE(1);
;         MD_END(t + 4 >= NT);
	s_mov_b32 s49, s46
	s_mov_b32 s46, s47
	s_mov_b32 s47, s48
	s_mov_b32 s48, s49
	s_add_i32 s50, s50, 1
	v_cvt_pk_bf16_f32 v172, v186, v188
	v_cvt_pk_bf16_f32 v173, v190, v192
	v_cvt_pk_bf16_f32 v174, v194, v196
	v_cvt_pk_bf16_f32 v175, v198, v200
	v_cvt_pk_bf16_f32 v176, v187, v189
	v_cvt_pk_bf16_f32 v177, v191, v193
	v_cvt_pk_bf16_f32 v178, v195, v197
	v_cvt_pk_bf16_f32 v179, v199, v201
	ds_write_b128 v95, v[172:175] offset:0
	ds_write_b128 v95, v[176:179] offset:128
	v_add_u32_e32 v91, s46, v135
	v_add_u32_e32 v93, s46, v137
	ds_read_b128 v[238:241], v139 offset:19456
	ds_read_b128 v[242:245], v139 offset:21504
	ds_read_b128 v[246:249], v139 offset:23552
	ds_read_b128 v[250:253], v139 offset:25600
	ds_read_b128 v[218:221], v91 offset:0
	ds_read_b128 v[222:225], v91 offset:2048
	ds_read_b128 v[226:229], v91 offset:4096
	ds_read_b128 v[230:233], v91 offset:6144
	ds_read_b128 v[234:237], v91 offset:8192
	s_add_i32 s49, s48, s74
	s_add_i32 s52, s52, 1
	s_and_b32 s54, s52, 7
	s_cmp_eq_u32 s54, 0
	s_cselect_b32 s54, s53, s32
	s_cselect_b32 s55, -1, 0
	s_add_u32 s30, s30, s54
	s_addc_u32 s31, s31, s55
	s_waitcnt lgkmcnt(0)
	v_mfma_f32_16x16x32_bf16 v[78:81], v[238:241], v[218:221], v[78:81]
	v_mfma_f32_16x16x32_bf16 v[74:77], v[242:245], v[218:221], v[74:77]
	v_mfma_f32_16x16x32_bf16 v[70:73], v[246:249], v[218:221], v[70:73]
	v_mfma_f32_16x16x32_bf16 v[66:69], v[250:253], v[218:221], v[66:69]
	ds_read_b128 v[218:221], v93 offset:0
	ds_read_b128 v[142:145], v141 offset:19456
	s_mov_b32 m0, s49
	s_nop 0
	global_load_lds_dwordx4 v88, s[30:31]
	v_mfma_f32_16x16x32_bf16 v[62:65], v[238:241], v[222:225], v[62:65]
	v_mfma_f32_16x16x32_bf16 v[58:61], v[242:245], v[222:225], v[58:61]
	v_mfma_f32_16x16x32_bf16 v[54:57], v[246:249], v[222:225], v[54:57]
	v_mfma_f32_16x16x32_bf16 v[50:53], v[250:253], v[222:225], v[50:53]
	ds_read_b128 v[222:225], v93 offset:2048
	ds_read_b128 v[146:149], v141 offset:21504
	s_add_i32 m0, s49, 0x2000
	s_nop 0
	global_load_lds_dwordx4 v90, s[30:31]
	v_mfma_f32_16x16x32_bf16 v[46:49], v[238:241], v[226:229], v[46:49]
	v_mfma_f32_16x16x32_bf16 v[42:45], v[242:245], v[226:229], v[42:45]
	v_mfma_f32_16x16x32_bf16 v[38:41], v[246:249], v[226:229], v[38:41]
	v_mfma_f32_16x16x32_bf16 v[34:37], v[250:253], v[226:229], v[34:37]
	ds_read_b128 v[226:229], v93 offset:4096
	ds_read_b128 v[156:159], v141 offset:23552
	s_add_i32 m0, s49, 0x4000
	s_nop 0
	global_load_lds_dwordx4 v92, s[30:31]
	v_mfma_f32_16x16x32_bf16 v[18:21], v[238:241], v[230:233], v[18:21]
	v_mfma_f32_16x16x32_bf16 v[22:25], v[242:245], v[230:233], v[22:25]
	v_mfma_f32_16x16x32_bf16 v[26:29], v[246:249], v[230:233], v[26:29]
	v_mfma_f32_16x16x32_bf16 v[30:33], v[250:253], v[230:233], v[30:33]
	ds_read_b128 v[230:233], v93 offset:6144
	ds_read_b128 v[160:163], v141 offset:25600
	s_add_i32 m0, s49, 0x6000
	s_nop 0
	global_load_lds_dwordx4 v94, s[30:31]
	v_mfma_f32_16x16x32_bf16 v[2:5], v[238:241], v[234:237], v[2:5]
	v_mfma_f32_16x16x32_bf16 v[6:9], v[242:245], v[234:237], v[6:9]
	v_mfma_f32_16x16x32_bf16 v[10:13], v[246:249], v[234:237], v[10:13]
	v_mfma_f32_16x16x32_bf16 v[14:17], v[250:253], v[234:237], v[14:17]
	ds_read_b128 v[234:237], v93 offset:8192
	s_add_i32 m0, s49, 0x8000
	s_nop 0
	global_load_lds_dwordx4 v96, s[30:31]
	s_waitcnt lgkmcnt(0)
	v_mfma_f32_16x16x32_bf16 v[78:81], v[142:145], v[218:221], v[78:81]
	v_mfma_f32_16x16x32_bf16 v[74:77], v[146:149], v[218:221], v[74:77]
	v_mfma_f32_16x16x32_bf16 v[70:73], v[156:159], v[218:221], v[70:73]
	v_mfma_f32_16x16x32_bf16 v[66:69], v[160:163], v[218:221], v[66:69]
	s_add_i32 s51, s51, 1
	s_and_b32 s54, s51, 7
	s_cmp_eq_u32 s54, 0
	s_cselect_b32 s44, s34, s35
	s_cselect_b32 s45, -1, 0
	v_lshl_add_u64 v[132:133], v[132:133], 0, s[44:45]
	global_load_dwordx2 v[186:187], v[132:133], off
	v_lshl_add_u64 v[180:181], v[132:133], 0, s[24:25]
	global_load_dwordx2 v[188:189], v[180:181], off
	v_mfma_f32_16x16x32_bf16 v[62:65], v[142:145], v[222:225], v[62:65]
	v_mfma_f32_16x16x32_bf16 v[58:61], v[146:149], v[222:225], v[58:61]
	v_mfma_f32_16x16x32_bf16 v[54:57], v[156:159], v[222:225], v[54:57]
	v_mfma_f32_16x16x32_bf16 v[50:53], v[160:163], v[222:225], v[50:53]
	v_lshl_add_u64 v[180:181], v[132:133], 0, s[26:27]
	global_load_dwordx2 v[190:191], v[180:181], off
	v_lshl_add_u64 v[180:181], v[132:133], 0, s[28:29]
	global_load_dwordx2 v[192:193], v[180:181], off
	v_mfma_f32_16x16x32_bf16 v[46:49], v[142:145], v[226:229], v[46:49]
	v_mfma_f32_16x16x32_bf16 v[42:45], v[146:149], v[226:229], v[42:45]
	v_mfma_f32_16x16x32_bf16 v[38:41], v[156:159], v[226:229], v[38:41]
	v_mfma_f32_16x16x32_bf16 v[34:37], v[160:163], v[226:229], v[34:37]
	v_lshl_add_u64 v[180:181], v[132:133], 0, s[36:37]
	global_load_dwordx2 v[194:195], v[180:181], off
	v_lshl_add_u64 v[180:181], v[132:133], 0, s[38:39]
	global_load_dwordx2 v[196:197], v[180:181], off
	v_mfma_f32_16x16x32_bf16 v[18:21], v[142:145], v[230:233], v[18:21]
	v_mfma_f32_16x16x32_bf16 v[22:25], v[146:149], v[230:233], v[22:25]
	v_mfma_f32_16x16x32_bf16 v[26:29], v[156:159], v[230:233], v[26:29]
	v_mfma_f32_16x16x32_bf16 v[30:33], v[160:163], v[230:233], v[30:33]
	v_lshl_add_u64 v[180:181], v[132:133], 0, s[40:41]
	global_load_dwordx2 v[198:199], v[180:181], off
	v_lshl_add_u64 v[180:181], v[132:133], 0, s[42:43]
	global_load_dwordx2 v[200:201], v[180:181], off
	v_mfma_f32_16x16x32_bf16 v[2:5], v[142:145], v[234:237], v[2:5]
	v_mfma_f32_16x16x32_bf16 v[6:9], v[146:149], v[234:237], v[6:9]
	v_mfma_f32_16x16x32_bf16 v[10:13], v[156:159], v[234:237], v[10:13]
	v_mfma_f32_16x16x32_bf16 v[14:17], v[160:163], v[234:237], v[14:17]
	s_waitcnt vmcnt(21)
	s_waitcnt lgkmcnt(0)
	s_barrier
; #define MD_GLDS_A(buf, tau) do { _Pragma("unroll") for (int i = 0; i < 5; ++i) if (amask & (1u << i)) \
;         __builtin_amdgcn_global_load_lds((const unsigned*)((const char*)HIDp + aoff[i] + (size_t)((tau) & 7) * 128), (PG8_LAS unsigned*)(MD_SA(buf) + wid * 1024 + i * 8192), 16, 0, 0); } while (0)
; #define MD_B_ISSUE(sb, tau) do { const char* kb_ = Bb + (size_t)((tau) >> 3) * 512 + (size_t)((tau) & 7) * (64 * (size_t)RB); _Pragma("unroll") for (int j = 0; j < 8; ++j) { const char* p_ = kb_ + (size_t)j * RB; \
;         asm volatile("global_load_dwordx2 %0, %1, off" : "=&v"(sb[j]) : "v"(p_) : "memory"); } } while (0)
; #define MD_B_WAIT(sb, N) asm volatile("s_waitcnt vmcnt(%8)" : "+v"(sb[0]), "+v"(sb[1]), "+v"(sb[2]), "+v"(sb[3]), "+v"(sb[4]), "+v"(sb[5]), "+v"(sb[6]), "+v"(sb[7]) : "n"(N) : "memory")
; __device__ __forceinline__ void moe_down_stream(PG8_LAS unsigned char* lds, int e, int cb0, int slot0, int nv, const bf16_t* HIDp, const float* Wd, bf16_t* Y, const float* slot_w, const int* slot_dst) {
;     ...
;     f32x4 acc[DNM][4];
; #pragma unroll
;     for (int m = 0; m < DNM; ++m)
; #pragma unroll
;         for (int n = 0; n < 4; ++n) acc[m][n] = (f32x4){0.f, 0.f, 0.f, 0.f};
;     f32x2 s0[8], s1[8];
;     MD_GLDS_A(0, 0); MD_B_ISSUE(s0, 0); MD_B_ISSUE(s1, 1);
;     MD_B_WAIT(s0, 8); MD_B_WRITE(s0, 0); __builtin_amdgcn_sched_barrier(0); MD_B_ISSUE(s0, 2);
;     asm volatile("s_waitcnt vmcnt(16)" ::: "memory");
;     asm volatile("s_waitcnt lgkmcnt(0)" ::: "memory"); __builtin_amdgcn_s_barrier(); asm volatile("" ::: "memory");
; #pragma unroll 1
;     for (int t = 0; t < NT; t += 2) {
;         if (t + 2 < NT) MD_B_WAIT(s1, 8); else MD_B_WAIT(s1, 0);
;         MD_B_WRITE(s1, 1); __builtin_amdgcn_sched_barrier(0); MD_GLDS_A(1, t + 1); __builtin_amdgcn_sched_barrier(0);
;         if (t + 3 < NT) MD_B_ISSUE(s1, t + 3);
;         MD_COMPUTE(0);
;         MD_END(t + 3 >= NT);
;         if (t + 2 < NT) { MD_B_WAIT(s0, 8); MD_B_WRITE(s0, 0); __builtin_amdgcn_sched_barrier(0); MD_GLDS_A(0, t + 2); __builtin_amdgcn_sched_barrier(0); }
;         if (t + 4 < NT) MD_B_ISSUE(s0, t + 4);
;         MD_COMPUTE(1);
;         MD_END(t + 4 >= NT);
	s_mov_b32 s49, s46
	s_mov_b32 s46, s47
	s_mov_b32 s47, s48
	s_mov_b32 s48, s49
	s_add_i32 s50, s50, 1
	v_cvt_pk_bf16_f32 v172, v202, v204
	v_cvt_pk_bf16_f32 v173, v206, v208
	v_cvt_pk_bf16_f32 v174, v210, v212
	v_cvt_pk_bf16_f32 v175, v214, v216
	v_cvt_pk_bf16_f32 v176, v203, v205
	v_cvt_pk_bf16_f32 v177, v207, v209
	v_cvt_pk_bf16_f32 v178, v211, v213
	v_cvt_pk_bf16_f32 v179, v215, v217
	ds_write_b128 v95, v[172:175] offset:19456
	ds_write_b128 v95, v[176:179] offset:19584
	v_add_u32_e32 v91, s46, v135
	v_add_u32_e32 v93, s46, v137
	ds_read_b128 v[238:241], v139 offset:0
	ds_read_b128 v[242:245], v139 offset:2048
	ds_read_b128 v[246:249], v139 offset:4096
	ds_read_b128 v[250:253], v139 offset:6144
	ds_read_b128 v[218:221], v91 offset:0
	ds_read_b128 v[222:225], v91 offset:2048
	ds_read_b128 v[226:229], v91 offset:4096
	ds_read_b128 v[230:233], v91 offset:6144
	ds_read_b128 v[234:237], v91 offset:8192
	s_add_i32 s49, s48, s74
	s_add_i32 s52, s52, 1
	s_and_b32 s54, s52, 7
	s_cmp_eq_u32 s54, 0
	s_cselect_b32 s54, s53, s32
	s_cselect_b32 s55, -1, 0
	s_add_u32 s30, s30, s54
	s_addc_u32 s31, s31, s55
	s_waitcnt lgkmcnt(0)
	v_mfma_f32_16x16x32_bf16 v[78:81], v[238:241], v[218:221], v[78:81]
	v_mfma_f32_16x16x32_bf16 v[74:77], v[242:245], v[218:221], v[74:77]
	v_mfma_f32_16x16x32_bf16 v[70:73], v[246:249], v[218:221], v[70:73]
	v_mfma_f32_16x16x32_bf16 v[66:69], v[250:253], v[218:221], v[66:69]
	ds_read_b128 v[218:221], v93 offset:0
	ds_read_b128 v[142:145], v141 offset:0
	s_mov_b32 m0, s49
	s_nop 0
	global_load_lds_dwordx4 v88, s[30:31]
	v_mfma_f32_16x16x32_bf16 v[62:65], v[238:241], v[222:225], v[62:65]
	v_mfma_f32_16x16x32_bf16 v[58:61], v[242:245], v[222:225], v[58:61]
	v_mfma_f32_16x16x32_bf16 v[54:57], v[246:249], v[222:225], v[54:57]
	v_mfma_f32_16x16x32_bf16 v[50:53], v[250:253], v[222:225], v[50:53]
	ds_read_b128 v[222:225], v93 offset:2048
	ds_read_b128 v[146:149], v141 offset:2048
	s_add_i32 m0, s49, 0x2000
	s_nop 0
	global_load_lds_dwordx4 v90, s[30:31]
	v_mfma_f32_16x16x32_bf16 v[46:49], v[238:241], v[226:229], v[46:49]
	v_mfma_f32_16x16x32_bf16 v[42:45], v[242:245], v[226:229], v[42:45]
	v_mfma_f32_16x16x32_bf16 v[38:41], v[246:249], v[226:229], v[38:41]
	v_mfma_f32_16x16x32_bf16 v[34:37], v[250:253], v[226:229], v[34:37]
	ds_read_b128 v[226:229], v93 offset:4096
	ds_read_b128 v[156:159], v141 offset:4096
	s_add_i32 m0, s49, 0x4000
	s_nop 0
	global_load_lds_dwordx4 v92, s[30:31]
	v_mfma_f32_16x16x32_bf16 v[18:21], v[238:241], v[230:233], v[18:21]
	v_mfma_f32_16x16x32_bf16 v[22:25], v[242:245], v[230:233], v[22:25]
	v_mfma_f32_16x16x32_bf16 v[26:29], v[246:249], v[230:233], v[26:29]
	v_mfma_f32_16x16x32_bf16 v[30:33], v[250:253], v[230:233], v[30:33]
	ds_read_b128 v[230:233], v93 offset:6144
	ds_read_b128 v[160:163], v141 offset:6144
	s_add_i32 m0, s49, 0x6000
	s_nop 0
	global_load_lds_dwordx4 v94, s[30:31]
	v_mfma_f32_16x16x32_bf16 v[2:5], v[238:241], v[234:237], v[2:5]
	v_mfma_f32_16x16x32_bf16 v[6:9], v[242:245], v[234:237], v[6:9]
	v_mfma_f32_16x16x32_bf16 v[10:13], v[246:249], v[234:237], v[10:13]
	v_mfma_f32_16x16x32_bf16 v[14:17], v[250:253], v[234:237], v[14:17]
	ds_read_b128 v[234:237], v93 offset:8192
	s_add_i32 m0, s49, 0x8000
	s_nop 0
	global_load_lds_dwordx4 v96, s[30:31]
	s_waitcnt lgkmcnt(0)
	v_mfma_f32_16x16x32_bf16 v[78:81], v[142:145], v[218:221], v[78:81]
	v_mfma_f32_16x16x32_bf16 v[74:77], v[146:149], v[218:221], v[74:77]
	v_mfma_f32_16x16x32_bf16 v[70:73], v[156:159], v[218:221], v[70:73]
	v_mfma_f32_16x16x32_bf16 v[66:69], v[160:163], v[218:221], v[66:69]
	s_add_i32 s51, s51, 1
	s_and_b32 s54, s51, 7
	s_cmp_eq_u32 s54, 0
	s_cselect_b32 s44, s34, s35
	s_cselect_b32 s45, -1, 0
	v_lshl_add_u64 v[132:133], v[132:133], 0, s[44:45]
	global_load_dwordx2 v[202:203], v[132:133], off
	v_lshl_add_u64 v[180:181], v[132:133], 0, s[24:25]
	global_load_dwordx2 v[204:205], v[180:181], off
	v_mfma_f32_16x16x32_bf16 v[62:65], v[142:145], v[222:225], v[62:65]
	v_mfma_f32_16x16x32_bf16 v[58:61], v[146:149], v[222:225], v[58:61]
	v_mfma_f32_16x16x32_bf16 v[54:57], v[156:159], v[222:225], v[54:57]
	v_mfma_f32_16x16x32_bf16 v[50:53], v[160:163], v[222:225], v[50:53]
	v_lshl_add_u64 v[180:181], v[132:133], 0, s[26:27]
	global_load_dwordx2 v[206:207], v[180:181], off
	v_lshl_add_u64 v[180:181], v[132:133], 0, s[28:29]
	global_load_dwordx2 v[208:209], v[180:181], off
	v_mfma_f32_16x16x32_bf16 v[46:49], v[142:145], v[226:229], v[46:49]
	v_mfma_f32_16x16x32_bf16 v[42:45], v[146:149], v[226:229], v[42:45]
	v_mfma_f32_16x16x32_bf16 v[38:41], v[156:159], v[226:229], v[38:41]
	v_mfma_f32_16x16x32_bf16 v[34:37], v[160:163], v[226:229], v[34:37]
	v_lshl_add_u64 v[180:181], v[132:133], 0, s[36:37]
	global_load_dwordx2 v[210:211], v[180:181], off
	v_lshl_add_u64 v[180:181], v[132:133], 0, s[38:39]
	global_load_dwordx2 v[212:213], v[180:181], off
	v_mfma_f32_16x16x32_bf16 v[18:21], v[142:145], v[230:233], v[18:21]
	v_mfma_f32_16x16x32_bf16 v[22:25], v[146:149], v[230:233], v[22:25]
	v_mfma_f32_16x16x32_bf16 v[26:29], v[156:159], v[230:233], v[26:29]
	v_mfma_f32_16x16x32_bf16 v[30:33], v[160:163], v[230:233], v[30:33]
	v_lshl_add_u64 v[180:181], v[132:133], 0, s[40:41]
	global_load_dwordx2 v[214:215], v[180:181], off
	v_lshl_add_u64 v[180:181], v[132:133], 0, s[42:43]
	global_load_dwordx2 v[216:217], v[180:181], off
	v_mfma_f32_16x16x32_bf16 v[2:5], v[142:145], v[234:237], v[2:5]
	v_mfma_f32_16x16x32_bf16 v[6:9], v[146:149], v[234:237], v[6:9]
	v_mfma_f32_16x16x32_bf16 v[10:13], v[156:159], v[234:237], v[10:13]
	v_mfma_f32_16x16x32_bf16 v[14:17], v[160:163], v[234:237], v[14:17]
	s_waitcnt vmcnt(21)
	s_waitcnt lgkmcnt(0)
	s_barrier
; #define MD_GLDS_A(buf, tau) do { _Pragma("unroll") for (int i = 0; i < 5; ++i) if (amask & (1u << i)) \
;         __builtin_amdgcn_global_load_lds((const unsigned*)((const char*)HIDp + aoff[i] + (size_t)((tau) & 7) * 128), (PG8_LAS unsigned*)(MD_SA(buf) + wid * 1024 + i * 8192), 16, 0, 0); } while (0)
; #define MD_B_ISSUE(sb, tau) do { const char* kb_ = Bb + (size_t)((tau) >> 3) * 512 + (size_t)((tau) & 7) * (64 * (size_t)RB); _Pragma("unroll") for (int j = 0; j < 8; ++j) { const char* p_ = kb_ + (size_t)j * RB; \
;         asm volatile("global_load_dwordx2 %0, %1, off" : "=&v"(sb[j]) : "v"(p_) : "memory"); } } while (0)
; #define MD_B_WAIT(sb, N) asm volatile("s_waitcnt vmcnt(%8)" : "+v"(sb[0]), "+v"(sb[1]), "+v"(sb[2]), "+v"(sb[3]), "+v"(sb[4]), "+v"(sb[5]), "+v"(sb[6]), "+v"(sb[7]) : "n"(N) : "memory")
; __device__ __forceinline__ void moe_down_stream(PG8_LAS unsigned char* lds, int e, int cb0, int slot0, int nv, const bf16_t* HIDp, const float* Wd, bf16_t* Y, const float* slot_w, const int* slot_dst) {
;     ...
;     f32x4 acc[DNM][4];
; #pragma unroll
;     for (int m = 0; m < DNM; ++m)
; #pragma unroll
;         for (int n = 0; n < 4; ++n) acc[m][n] = (f32x4){0.f, 0.f, 0.f, 0.f};
;     f32x2 s0[8], s1[8];
;     MD_GLDS_A(0, 0); MD_B_ISSUE(s0, 0); MD_B_ISSUE(s1, 1);
;     MD_B_WAIT(s0, 8); MD_B_WRITE(s0, 0); __builtin_amdgcn_sched_barrier(0); MD_B_ISSUE(s0, 2);
;     asm volatile("s_waitcnt vmcnt(16)" ::: "memory");
;     asm volatile("s_waitcnt lgkmcnt(0)" ::: "memory"); __builtin_amdgcn_s_barrier(); asm volatile("" ::: "memory");
; #pragma unroll 1
;     for (int t = 0; t < NT; t += 2) {
;         if (t + 2 < NT) MD_B_WAIT(s1, 8); else MD_B_WAIT(s1, 0);
;         MD_B_WRITE(s1, 1); __builtin_amdgcn_sched_barrier(0); MD_GLDS_A(1, t + 1); __builtin_amdgcn_sched_barrier(0);
;         if (t + 3 < NT) MD_B_ISSUE(s1, t + 3);
;         MD_COMPUTE(0);
;         MD_END(t + 3 >= NT);
;         if (t + 2 < NT) { MD_B_WAIT(s0, 8); MD_B_WRITE(s0, 0); __builtin_amdgcn_sched_barrier(0); MD_GLDS_A(0, t + 2); __builtin_amdgcn_sched_barrier(0); }
;         if (t + 4 < NT) MD_B_ISSUE(s0, t + 4);
;         MD_COMPUTE(1);
;         MD_END(t + 4 >= NT);
	s_mov_b32 s49, s46
	s_mov_b32 s46, s47
	s_mov_b32 s47, s48
	s_mov_b32 s48, s49
	s_add_i32 s50, s50, 1
	v_cvt_pk_bf16_f32 v172, v98, v100
	v_cvt_pk_bf16_f32 v173, v102, v104
	v_cvt_pk_bf16_f32 v174, v106, v108
	v_cvt_pk_bf16_f32 v175, v110, v112
	v_cvt_pk_bf16_f32 v176, v99, v101
	v_cvt_pk_bf16_f32 v177, v103, v105
	v_cvt_pk_bf16_f32 v178, v107, v109
	v_cvt_pk_bf16_f32 v179, v111, v113
	ds_write_b128 v95, v[172:175] offset:0
	ds_write_b128 v95, v[176:179] offset:128
	v_add_u32_e32 v91, s46, v135
	v_add_u32_e32 v93, s46, v137
	ds_read_b128 v[238:241], v139 offset:19456
	ds_read_b128 v[242:245], v139 offset:21504
	ds_read_b128 v[246:249], v139 offset:23552
	ds_read_b128 v[250:253], v139 offset:25600
	ds_read_b128 v[218:221], v91 offset:0
	ds_read_b128 v[222:225], v91 offset:2048
	ds_read_b128 v[226:229], v91 offset:4096
	ds_read_b128 v[230:233], v91 offset:6144
	ds_read_b128 v[234:237], v91 offset:8192
	s_add_i32 s49, s48, s74
	s_add_i32 s52, s52, 1
	s_and_b32 s54, s52, 7
	s_cmp_eq_u32 s54, 0
	s_cselect_b32 s54, s53, s32
	s_cselect_b32 s55, -1, 0
	s_add_u32 s30, s30, s54
	s_addc_u32 s31, s31, s55
	s_waitcnt lgkmcnt(0)
	v_mfma_f32_16x16x32_bf16 v[78:81], v[238:241], v[218:221], v[78:81]
	v_mfma_f32_16x16x32_bf16 v[74:77], v[242:245], v[218:221], v[74:77]
	v_mfma_f32_16x16x32_bf16 v[70:73], v[246:249], v[218:221], v[70:73]
	v_mfma_f32_16x16x32_bf16 v[66:69], v[250:253], v[218:221], v[66:69]
	ds_read_b128 v[218:221], v93 offset:0
	ds_read_b128 v[142:145], v141 offset:19456
	s_mov_b32 m0, s49
	s_nop 0
	global_load_lds_dwordx4 v88, s[30:31]
	v_mfma_f32_16x16x32_bf16 v[62:65], v[238:241], v[222:225], v[62:65]
	v_mfma_f32_16x16x32_bf16 v[58:61], v[242:245], v[222:225], v[58:61]
	v_mfma_f32_16x16x32_bf16 v[54:57], v[246:249], v[222:225], v[54:57]
	v_mfma_f32_16x16x32_bf16 v[50:53], v[250:253], v[222:225], v[50:53]
	ds_read_b128 v[222:225], v93 offset:2048
	ds_read_b128 v[146:149], v141 offset:21504
	s_add_i32 m0, s49, 0x2000
	s_nop 0
	global_load_lds_dwordx4 v90, s[30:31]
	v_mfma_f32_16x16x32_bf16 v[46:49], v[238:241], v[226:229], v[46:49]
	v_mfma_f32_16x16x32_bf16 v[42:45], v[242:245], v[226:229], v[42:45]
	v_mfma_f32_16x16x32_bf16 v[38:41], v[246:249], v[226:229], v[38:41]
	v_mfma_f32_16x16x32_bf16 v[34:37], v[250:253], v[226:229], v[34:37]
	ds_read_b128 v[226:229], v93 offset:4096
	ds_read_b128 v[156:159], v141 offset:23552
	s_add_i32 m0, s49, 0x4000
	s_nop 0
	global_load_lds_dwordx4 v92, s[30:31]
	v_mfma_f32_16x16x32_bf16 v[18:21], v[238:241], v[230:233], v[18:21]
	v_mfma_f32_16x16x32_bf16 v[22:25], v[242:245], v[230:233], v[22:25]
	v_mfma_f32_16x16x32_bf16 v[26:29], v[246:249], v[230:233], v[26:29]
	v_mfma_f32_16x16x32_bf16 v[30:33], v[250:253], v[230:233], v[30:33]
	ds_read_b128 v[230:233], v93 offset:6144
	ds_read_b128 v[160:163], v141 offset:25600
	s_add_i32 m0, s49, 0x6000
	s_nop 0
	global_load_lds_dwordx4 v94, s[30:31]
	v_mfma_f32_16x16x32_bf16 v[2:5], v[238:241], v[234:237], v[2:5]
	v_mfma_f32_16x16x32_bf16 v[6:9], v[242:245], v[234:237], v[6:9]
	v_mfma_f32_16x16x32_bf16 v[10:13], v[246:249], v[234:237], v[10:13]
	v_mfma_f32_16x16x32_bf16 v[14:17], v[250:253], v[234:237], v[14:17]
	ds_read_b128 v[234:237], v93 offset:8192
	s_add_i32 m0, s49, 0x8000
	s_nop 0
	global_load_lds_dwordx4 v96, s[30:31]
	s_waitcnt lgkmcnt(0)
	v_mfma_f32_16x16x32_bf16 v[78:81], v[142:145], v[218:221], v[78:81]
	v_mfma_f32_16x16x32_bf16 v[74:77], v[146:149], v[218:221], v[74:77]
	v_mfma_f32_16x16x32_bf16 v[70:73], v[156:159], v[218:221], v[70:73]
	v_mfma_f32_16x16x32_bf16 v[66:69], v[160:163], v[218:221], v[66:69]
	v_mfma_f32_16x16x32_bf16 v[62:65], v[142:145], v[222:225], v[62:65]
	v_mfma_f32_16x16x32_bf16 v[58:61], v[146:149], v[222:225], v[58:61]
	v_mfma_f32_16x16x32_bf16 v[54:57], v[156:159], v[222:225], v[54:57]
	v_mfma_f32_16x16x32_bf16 v[50:53], v[160:163], v[222:225], v[50:53]
	v_mfma_f32_16x16x32_bf16 v[46:49], v[142:145], v[226:229], v[46:49]
	v_mfma_f32_16x16x32_bf16 v[42:45], v[146:149], v[226:229], v[42:45]
	v_mfma_f32_16x16x32_bf16 v[38:41], v[156:159], v[226:229], v[38:41]
	v_mfma_f32_16x16x32_bf16 v[34:37], v[160:163], v[226:229], v[34:37]
	v_mfma_f32_16x16x32_bf16 v[18:21], v[142:145], v[230:233], v[18:21]
	v_mfma_f32_16x16x32_bf16 v[22:25], v[146:149], v[230:233], v[22:25]
	v_mfma_f32_16x16x32_bf16 v[26:29], v[156:159], v[230:233], v[26:29]
	v_mfma_f32_16x16x32_bf16 v[30:33], v[160:163], v[230:233], v[30:33]
	v_mfma_f32_16x16x32_bf16 v[2:5], v[142:145], v[234:237], v[2:5]
	v_mfma_f32_16x16x32_bf16 v[6:9], v[146:149], v[234:237], v[6:9]
	v_mfma_f32_16x16x32_bf16 v[10:13], v[156:159], v[234:237], v[10:13]
	v_mfma_f32_16x16x32_bf16 v[14:17], v[160:163], v[234:237], v[14:17]
	s_waitcnt vmcnt(13)
	s_waitcnt lgkmcnt(0)
	s_barrier
; #define MD_GLDS_A(buf, tau) do { _Pragma("unroll") for (int i = 0; i < 5; ++i) if (amask & (1u << i)) \
;         __builtin_amdgcn_global_load_lds((const unsigned*)((const char*)HIDp + aoff[i] + (size_t)((tau) & 7) * 128), (PG8_LAS unsigned*)(MD_SA(buf) + wid * 1024 + i * 8192), 16, 0, 0); } while (0)
; #define MD_B_ISSUE(sb, tau) do { const char* kb_ = Bb + (size_t)((tau) >> 3) * 512 + (size_t)((tau) & 7) * (64 * (size_t)RB); _Pragma("unroll") for (int j = 0; j < 8; ++j) { const char* p_ = kb_ + (size_t)j * RB; \
;         asm volatile("global_load_dwordx2 %0, %1, off" : "=&v"(sb[j]) : "v"(p_) : "memory"); } } while (0)
; #define MD_B_WAIT(sb, N) asm volatile("s_waitcnt vmcnt(%8)" : "+v"(sb[0]), "+v"(sb[1]), "+v"(sb[2]), "+v"(sb[3]), "+v"(sb[4]), "+v"(sb[5]), "+v"(sb[6]), "+v"(sb[7]) : "n"(N) : "memory")
; __device__ __forceinline__ void moe_down_stream(PG8_LAS unsigned char* lds, int e, int cb0, int slot0, int nv, const bf16_t* HIDp, const float* Wd, bf16_t* Y, const float* slot_w, const int* slot_dst) {
;     ...
;     f32x4 acc[DNM][4];
; #pragma unroll
;     for (int m = 0; m < DNM; ++m)
; #pragma unroll
;         for (int n = 0; n < 4; ++n) acc[m][n] = (f32x4){0.f, 0.f, 0.f, 0.f};
;     f32x2 s0[8], s1[8];
;     MD_GLDS_A(0, 0); MD_B_ISSUE(s0, 0); MD_B_ISSUE(s1, 1);
;     MD_B_WAIT(s0, 8); MD_B_WRITE(s0, 0); __builtin_amdgcn_sched_barrier(0); MD_B_ISSUE(s0, 2);
;     asm volatile("s_waitcnt vmcnt(16)" ::: "memory");
;     asm volatile("s_waitcnt lgkmcnt(0)" ::: "memory"); __builtin_amdgcn_s_barrier(); asm volatile("" ::: "memory");
; #pragma unroll 1
;     for (int t = 0; t < NT; t += 2) {
;         if (t + 2 < NT) MD_B_WAIT(s1, 8); else MD_B_WAIT(s1, 0);
;         MD_B_WRITE(s1, 1); __builtin_amdgcn_sched_barrier(0); MD_GLDS_A(1, t + 1); __builtin_amdgcn_sched_barrier(0);
;         if (t + 3 < NT) MD_B_ISSUE(s1, t + 3);
;         MD_COMPUTE(0);
;         MD_END(t + 3 >= NT);
;         if (t + 2 < NT) { MD_B_WAIT(s0, 8); MD_B_WRITE(s0, 0); __builtin_amdgcn_sched_barrier(0); MD_GLDS_A(0, t + 2); __builtin_amdgcn_sched_barrier(0); }
;         if (t + 4 < NT) MD_B_ISSUE(s0, t + 4);
;         MD_COMPUTE(1);
;         MD_END(t + 4 >= NT);
	s_mov_b32 s49, s46
	s_mov_b32 s46, s47
	s_mov_b32 s47, s48
	s_mov_b32 s48, s49
	s_add_i32 s50, s50, 1
	v_cvt_pk_bf16_f32 v172, v114, v116
	v_cvt_pk_bf16_f32 v173, v118, v120
	v_cvt_pk_bf16_f32 v174, v122, v124
	v_cvt_pk_bf16_f32 v175, v126, v128
	v_cvt_pk_bf16_f32 v176, v115, v117
	v_cvt_pk_bf16_f32 v177, v119, v121
	v_cvt_pk_bf16_f32 v178, v123, v125
	v_cvt_pk_bf16_f32 v179, v127, v129
	ds_write_b128 v95, v[172:175] offset:19456
	ds_write_b128 v95, v[176:179] offset:19584
	v_add_u32_e32 v91, s46, v135
	v_add_u32_e32 v93, s46, v137
	ds_read_b128 v[238:241], v139 offset:0
	ds_read_b128 v[242:245], v139 offset:2048
	ds_read_b128 v[246:249], v139 offset:4096
	ds_read_b128 v[250:253], v139 offset:6144
	ds_read_b128 v[218:221], v91 offset:0
	ds_read_b128 v[222:225], v91 offset:2048
	ds_read_b128 v[226:229], v91 offset:4096
	ds_read_b128 v[230:233], v91 offset:6144
	ds_read_b128 v[234:237], v91 offset:8192
	s_add_i32 s49, s48, s74
	s_add_i32 s52, s52, 1
	s_and_b32 s54, s52, 7
	s_cmp_eq_u32 s54, 0
	s_cselect_b32 s54, s53, s32
	s_cselect_b32 s55, -1, 0
	s_add_u32 s30, s30, s54
	s_addc_u32 s31, s31, s55
	s_waitcnt lgkmcnt(0)
	v_mfma_f32_16x16x32_bf16 v[78:81], v[238:241], v[218:221], v[78:81]
	v_mfma_f32_16x16x32_bf16 v[74:77], v[242:245], v[218:221], v[74:77]
	v_mfma_f32_16x16x32_bf16 v[70:73], v[246:249], v[218:221], v[70:73]
	v_mfma_f32_16x16x32_bf16 v[66:69], v[250:253], v[218:221], v[66:69]
	ds_read_b128 v[218:221], v93 offset:0
	ds_read_b128 v[142:145], v141 offset:0
	s_mov_b32 m0, s49
	s_nop 0
	global_load_lds_dwordx4 v88, s[30:31]
	v_mfma_f32_16x16x32_bf16 v[62:65], v[238:241], v[222:225], v[62:65]
	v_mfma_f32_16x16x32_bf16 v[58:61], v[242:245], v[222:225], v[58:61]
	v_mfma_f32_16x16x32_bf16 v[54:57], v[246:249], v[222:225], v[54:57]
	v_mfma_f32_16x16x32_bf16 v[50:53], v[250:253], v[222:225], v[50:53]
	ds_read_b128 v[222:225], v93 offset:2048
	ds_read_b128 v[146:149], v141 offset:2048
	s_add_i32 m0, s49, 0x2000
	s_nop 0
	global_load_lds_dwordx4 v90, s[30:31]
	v_mfma_f32_16x16x32_bf16 v[46:49], v[238:241], v[226:229], v[46:49]
	v_mfma_f32_16x16x32_bf16 v[42:45], v[242:245], v[226:229], v[42:45]
	v_mfma_f32_16x16x32_bf16 v[38:41], v[246:249], v[226:229], v[38:41]
	v_mfma_f32_16x16x32_bf16 v[34:37], v[250:253], v[226:229], v[34:37]
	ds_read_b128 v[226:229], v93 offset:4096
	ds_read_b128 v[156:159], v141 offset:4096
	s_add_i32 m0, s49, 0x4000
	s_nop 0
	global_load_lds_dwordx4 v92, s[30:31]
	v_mfma_f32_16x16x32_bf16 v[18:21], v[238:241], v[230:233], v[18:21]
	v_mfma_f32_16x16x32_bf16 v[22:25], v[242:245], v[230:233], v[22:25]
	v_mfma_f32_16x16x32_bf16 v[26:29], v[246:249], v[230:233], v[26:29]
	v_mfma_f32_16x16x32_bf16 v[30:33], v[250:253], v[230:233], v[30:33]
	ds_read_b128 v[230:233], v93 offset:6144
	ds_read_b128 v[160:163], v141 offset:6144
	s_add_i32 m0, s49, 0x6000
	s_nop 0
	global_load_lds_dwordx4 v94, s[30:31]
	v_mfma_f32_16x16x32_bf16 v[2:5], v[238:241], v[234:237], v[2:5]
	v_mfma_f32_16x16x32_bf16 v[6:9], v[242:245], v[234:237], v[6:9]
	v_mfma_f32_16x16x32_bf16 v[10:13], v[246:249], v[234:237], v[10:13]
	v_mfma_f32_16x16x32_bf16 v[14:17], v[250:253], v[234:237], v[14:17]
	ds_read_b128 v[234:237], v93 offset:8192
	s_add_i32 m0, s49, 0x8000
	s_nop 0
	global_load_lds_dwordx4 v96, s[30:31]
	s_waitcnt lgkmcnt(0)
	v_mfma_f32_16x16x32_bf16 v[78:81], v[142:145], v[218:221], v[78:81]
	v_mfma_f32_16x16x32_bf16 v[74:77], v[146:149], v[218:221], v[74:77]
	v_mfma_f32_16x16x32_bf16 v[70:73], v[156:159], v[218:221], v[70:73]
	v_mfma_f32_16x16x32_bf16 v[66:69], v[160:163], v[218:221], v[66:69]
	v_mfma_f32_16x16x32_bf16 v[62:65], v[142:145], v[222:225], v[62:65]
	v_mfma_f32_16x16x32_bf16 v[58:61], v[146:149], v[222:225], v[58:61]
	v_mfma_f32_16x16x32_bf16 v[54:57], v[156:159], v[222:225], v[54:57]
	v_mfma_f32_16x16x32_bf16 v[50:53], v[160:163], v[222:225], v[50:53]
	v_mfma_f32_16x16x32_bf16 v[46:49], v[142:145], v[226:229], v[46:49]
	v_mfma_f32_16x16x32_bf16 v[42:45], v[146:149], v[226:229], v[42:45]
	v_mfma_f32_16x16x32_bf16 v[38:41], v[156:159], v[226:229], v[38:41]
	v_mfma_f32_16x16x32_bf16 v[34:37], v[160:163], v[226:229], v[34:37]
	v_mfma_f32_16x16x32_bf16 v[18:21], v[142:145], v[230:233], v[18:21]
	v_mfma_f32_16x16x32_bf16 v[22:25], v[146:149], v[230:233], v[22:25]
	v_mfma_f32_16x16x32_bf16 v[26:29], v[156:159], v[230:233], v[26:29]
	v_mfma_f32_16x16x32_bf16 v[30:33], v[160:163], v[230:233], v[30:33]
	v_mfma_f32_16x16x32_bf16 v[2:5], v[142:145], v[234:237], v[2:5]
	v_mfma_f32_16x16x32_bf16 v[6:9], v[146:149], v[234:237], v[6:9]
	v_mfma_f32_16x16x32_bf16 v[10:13], v[156:159], v[234:237], v[10:13]
	v_mfma_f32_16x16x32_bf16 v[14:17], v[160:163], v[234:237], v[14:17]
	s_waitcnt vmcnt(5)
	s_waitcnt lgkmcnt(0)
	s_barrier
; #define MD_GLDS_A(buf, tau) do { _Pragma("unroll") for (int i = 0; i < 5; ++i) if (amask & (1u << i)) \
;         __builtin_amdgcn_global_load_lds((const unsigned*)((const char*)HIDp + aoff[i] + (size_t)((tau) & 7) * 128), (PG8_LAS unsigned*)(MD_SA(buf) + wid * 1024 + i * 8192), 16, 0, 0); } while (0)
; #define MD_B_ISSUE(sb, tau) do { const char* kb_ = Bb + (size_t)((tau) >> 3) * 512 + (size_t)((tau) & 7) * (64 * (size_t)RB); _Pragma("unroll") for (int j = 0; j < 8; ++j) { const char* p_ = kb_ + (size_t)j * RB; \
;         asm volatile("global_load_dwordx2 %0, %1, off" : "=&v"(sb[j]) : "v"(p_) : "memory"); } } while (0)
; #define MD_B_WAIT(sb, N) asm volatile("s_waitcnt vmcnt(%8)" : "+v"(sb[0]), "+v"(sb[1]), "+v"(sb[2]), "+v"(sb[3]), "+v"(sb[4]), "+v"(sb[5]), "+v"(sb[6]), "+v"(sb[7]) : "n"(N) : "memory")
; #define MD_END(last) do { if (last) asm volatile("s_waitcnt vmcnt(0)" ::: "memory"); else asm volatile("s_waitcnt vmcnt(8)" ::: "memory"); \
;         asm volatile("s_waitcnt lgkmcnt(0)" ::: "memory"); __builtin_amdgcn_s_barrier(); asm volatile("" ::: "memory"); } while (0)
; __device__ __forceinline__ void moe_down_stream(PG8_LAS unsigned char* lds, int e, int cb0, int slot0, int nv, const bf16_t* HIDp, const float* Wd, bf16_t* Y, const float* slot_w, const int* slot_dst) {
;     ...
;     for (int t = 0; t < NT; t += 2) {
;         if (t + 2 < NT) MD_B_WAIT(s1, 8); else MD_B_WAIT(s1, 0);
;         MD_B_WRITE(s1, 1); __builtin_amdgcn_sched_barrier(0); MD_GLDS_A(1, t + 1); __builtin_amdgcn_sched_barrier(0);
;         if (t + 3 < NT) MD_B_ISSUE(s1, t + 3);
;         MD_COMPUTE(0);
;         MD_END(t + 3 >= NT);
;         if (t + 2 < NT) { MD_B_WAIT(s0, 8); MD_B_WRITE(s0, 0); __builtin_amdgcn_sched_barrier(0); MD_GLDS_A(0, t + 2); __builtin_amdgcn_sched_barrier(0); }
;         if (t + 4 < NT) MD_B_ISSUE(s0, t + 4);
;         MD_COMPUTE(1);
;         MD_END(t + 4 >= NT);
	s_mov_b32 s49, s46
	s_mov_b32 s46, s47
	s_mov_b32 s47, s48
	s_mov_b32 s48, s49
	s_add_i32 s50, s50, 1
	v_cvt_pk_bf16_f32 v172, v186, v188
	v_cvt_pk_bf16_f32 v173, v190, v192
	v_cvt_pk_bf16_f32 v174, v194, v196
	v_cvt_pk_bf16_f32 v175, v198, v200
	v_cvt_pk_bf16_f32 v176, v187, v189
	v_cvt_pk_bf16_f32 v177, v191, v193
	v_cvt_pk_bf16_f32 v178, v195, v197
	v_cvt_pk_bf16_f32 v179, v199, v201
	ds_write_b128 v95, v[172:175] offset:0
	ds_write_b128 v95, v[176:179] offset:128
	v_add_u32_e32 v91, s46, v135
	v_add_u32_e32 v93, s46, v137
	ds_read_b128 v[238:241], v139 offset:19456
	ds_read_b128 v[242:245], v139 offset:21504
	ds_read_b128 v[246:249], v139 offset:23552
	ds_read_b128 v[250:253], v139 offset:25600
	ds_read_b128 v[218:221], v91 offset:0
	ds_read_b128 v[222:225], v91 offset:2048
	ds_read_b128 v[226:229], v91 offset:4096
	ds_read_b128 v[230:233], v91 offset:6144
	ds_read_b128 v[234:237], v91 offset:8192
	s_add_i32 s49, s48, s74
	s_add_i32 s52, s52, 1
	s_and_b32 s54, s52, 7
	s_cmp_eq_u32 s54, 0
	s_cselect_b32 s54, s53, s32
	s_cselect_b32 s55, -1, 0
	s_add_u32 s30, s30, s54
	s_addc_u32 s31, s31, s55
	s_waitcnt lgkmcnt(0)
	v_mfma_f32_16x16x32_bf16 v[78:81], v[238:241], v[218:221], v[78:81]
	v_mfma_f32_16x16x32_bf16 v[74:77], v[242:245], v[218:221], v[74:77]
	v_mfma_f32_16x16x32_bf16 v[70:73], v[246:249], v[218:221], v[70:73]
	v_mfma_f32_16x16x32_bf16 v[66:69], v[250:253], v[218:221], v[66:69]
	ds_read_b128 v[218:221], v93 offset:0
	ds_read_b128 v[142:145], v141 offset:19456
	s_mov_b32 m0, s49
	s_nop 0
	global_load_lds_dwordx4 v88, s[30:31]
	v_mfma_f32_16x16x32_bf16 v[62:65], v[238:241], v[222:225], v[62:65]
	v_mfma_f32_16x16x32_bf16 v[58:61], v[242:245], v[222:225], v[58:61]
	v_mfma_f32_16x16x32_bf16 v[54:57], v[246:249], v[222:225], v[54:57]
	v_mfma_f32_16x16x32_bf16 v[50:53], v[250:253], v[222:225], v[50:53]
	ds_read_b128 v[222:225], v93 offset:2048
	ds_read_b128 v[146:149], v141 offset:21504
	s_add_i32 m0, s49, 0x2000
	s_nop 0
	global_load_lds_dwordx4 v90, s[30:31]
	v_mfma_f32_16x16x32_bf16 v[46:49], v[238:241], v[226:229], v[46:49]
	v_mfma_f32_16x16x32_bf16 v[42:45], v[242:245], v[226:229], v[42:45]
	v_mfma_f32_16x16x32_bf16 v[38:41], v[246:249], v[226:229], v[38:41]
	v_mfma_f32_16x16x32_bf16 v[34:37], v[250:253], v[226:229], v[34:37]
	ds_read_b128 v[226:229], v93 offset:4096
	ds_read_b128 v[156:159], v141 offset:23552
	s_add_i32 m0, s49, 0x4000
	s_nop 0
	global_load_lds_dwordx4 v92, s[30:31]
	v_mfma_f32_16x16x32_bf16 v[18:21], v[238:241], v[230:233], v[18:21]
	v_mfma_f32_16x16x32_bf16 v[22:25], v[242:245], v[230:233], v[22:25]
	v_mfma_f32_16x16x32_bf16 v[26:29], v[246:249], v[230:233], v[26:29]
	v_mfma_f32_16x16x32_bf16 v[30:33], v[250:253], v[230:233], v[30:33]
	ds_read_b128 v[230:233], v93 offset:6144
	ds_read_b128 v[160:163], v141 offset:25600
	s_add_i32 m0, s49, 0x6000
	s_nop 0
	global_load_lds_dwordx4 v94, s[30:31]
	v_mfma_f32_16x16x32_bf16 v[2:5], v[238:241], v[234:237], v[2:5]
	v_mfma_f32_16x16x32_bf16 v[6:9], v[242:245], v[234:237], v[6:9]
	v_mfma_f32_16x16x32_bf16 v[10:13], v[246:249], v[234:237], v[10:13]
	v_mfma_f32_16x16x32_bf16 v[14:17], v[250:253], v[234:237], v[14:17]
	ds_read_b128 v[234:237], v93 offset:8192
	s_add_i32 m0, s49, 0x8000
	s_nop 0
	global_load_lds_dwordx4 v96, s[30:31]
	s_waitcnt lgkmcnt(0)
	v_mfma_f32_16x16x32_bf16 v[78:81], v[142:145], v[218:221], v[78:81]
	v_mfma_f32_16x16x32_bf16 v[74:77], v[146:149], v[218:221], v[74:77]
	v_mfma_f32_16x16x32_bf16 v[70:73], v[156:159], v[218:221], v[70:73]
	v_mfma_f32_16x16x32_bf16 v[66:69], v[160:163], v[218:221], v[66:69]
	v_mfma_f32_16x16x32_bf16 v[62:65], v[142:145], v[222:225], v[62:65]
	v_mfma_f32_16x16x32_bf16 v[58:61], v[146:149], v[222:225], v[58:61]
	v_mfma_f32_16x16x32_bf16 v[54:57], v[156:159], v[222:225], v[54:57]
	v_mfma_f32_16x16x32_bf16 v[50:53], v[160:163], v[222:225], v[50:53]
	v_mfma_f32_16x16x32_bf16 v[46:49], v[142:145], v[226:229], v[46:49]
	v_mfma_f32_16x16x32_bf16 v[42:45], v[146:149], v[226:229], v[42:45]
	v_mfma_f32_16x16x32_bf16 v[38:41], v[156:159], v[226:229], v[38:41]
	v_mfma_f32_16x16x32_bf16 v[34:37], v[160:163], v[226:229], v[34:37]
	v_mfma_f32_16x16x32_bf16 v[18:21], v[142:145], v[230:233], v[18:21]
	v_mfma_f32_16x16x32_bf16 v[22:25], v[146:149], v[230:233], v[22:25]
	v_mfma_f32_16x16x32_bf16 v[26:29], v[156:159], v[230:233], v[26:29]
	v_mfma_f32_16x16x32_bf16 v[30:33], v[160:163], v[230:233], v[30:33]
	v_mfma_f32_16x16x32_bf16 v[2:5], v[142:145], v[234:237], v[2:5]
	v_mfma_f32_16x16x32_bf16 v[6:9], v[146:149], v[234:237], v[6:9]
	v_mfma_f32_16x16x32_bf16 v[10:13], v[156:159], v[234:237], v[10:13]
	v_mfma_f32_16x16x32_bf16 v[14:17], v[160:163], v[234:237], v[14:17]
	s_waitcnt vmcnt(5)
	s_waitcnt lgkmcnt(0)
	s_barrier
; #define MD_GLDS_A(buf, tau) do { _Pragma("unroll") for (int i = 0; i < 5; ++i) if (amask & (1u << i)) \
;         __builtin_amdgcn_global_load_lds((const unsigned*)((const char*)HIDp + aoff[i] + (size_t)((tau) & 7) * 128), (PG8_LAS unsigned*)(MD_SA(buf) + wid * 1024 + i * 8192), 16, 0, 0); } while (0)
; #define MD_B_ISSUE(sb, tau) do { const char* kb_ = Bb + (size_t)((tau) >> 3) * 512 + (size_t)((tau) & 7) * (64 * (size_t)RB); _Pragma("unroll") for (int j = 0; j < 8; ++j) { const char* p_ = kb_ + (size_t)j * RB; \
;         asm volatile("global_load_dwordx2 %0, %1, off" : "=&v"(sb[j]) : "v"(p_) : "memory"); } } while (0)
; #define MD_B_WAIT(sb, N) asm volatile("s_waitcnt vmcnt(%8)" : "+v"(sb[0]), "+v"(sb[1]), "+v"(sb[2]), "+v"(sb[3]), "+v"(sb[4]), "+v"(sb[5]), "+v"(sb[6]), "+v"(sb[7]) : "n"(N) : "memory")
; #define MD_END(last) do { if (last) asm volatile("s_waitcnt vmcnt(0)" ::: "memory"); else asm volatile("s_waitcnt vmcnt(8)" ::: "memory"); \
;         asm volatile("s_waitcnt lgkmcnt(0)" ::: "memory"); __builtin_amdgcn_s_barrier(); asm volatile("" ::: "memory"); } while (0)
; __device__ __forceinline__ void moe_down_stream(PG8_LAS unsigned char* lds, int e, int cb0, int slot0, int nv, const bf16_t* HIDp, const float* Wd, bf16_t* Y, const float* slot_w, const int* slot_dst) {
;     ...
;     for (int t = 0; t < NT; t += 2) {
;         if (t + 2 < NT) MD_B_WAIT(s1, 8); else MD_B_WAIT(s1, 0);
;         MD_B_WRITE(s1, 1); __builtin_amdgcn_sched_barrier(0); MD_GLDS_A(1, t + 1); __builtin_amdgcn_sched_barrier(0);
;         if (t + 3 < NT) MD_B_ISSUE(s1, t + 3);
;         MD_COMPUTE(0);
;         MD_END(t + 3 >= NT);
;         if (t + 2 < NT) { MD_B_WAIT(s0, 8); MD_B_WRITE(s0, 0); __builtin_amdgcn_sched_barrier(0); MD_GLDS_A(0, t + 2); __builtin_amdgcn_sched_barrier(0); }
;         if (t + 4 < NT) MD_B_ISSUE(s0, t + 4);
;         MD_COMPUTE(1);
;         MD_END(t + 4 >= NT);
	s_mov_b32 s49, s46
	s_mov_b32 s46, s47
	s_mov_b32 s47, s48
	s_mov_b32 s48, s49
	s_add_i32 s50, s50, 1
	v_cvt_pk_bf16_f32 v172, v202, v204
	v_cvt_pk_bf16_f32 v173, v206, v208
	v_cvt_pk_bf16_f32 v174, v210, v212
	v_cvt_pk_bf16_f32 v175, v214, v216
	v_cvt_pk_bf16_f32 v176, v203, v205
	v_cvt_pk_bf16_f32 v177, v207, v209
	v_cvt_pk_bf16_f32 v178, v211, v213
	v_cvt_pk_bf16_f32 v179, v215, v217
	ds_write_b128 v95, v[172:175] offset:19456
	ds_write_b128 v95, v[176:179] offset:19584
	v_add_u32_e32 v91, s46, v135
	v_add_u32_e32 v93, s46, v137
	ds_read_b128 v[238:241], v139 offset:0
	ds_read_b128 v[242:245], v139 offset:2048
	ds_read_b128 v[246:249], v139 offset:4096
	ds_read_b128 v[250:253], v139 offset:6144
	ds_read_b128 v[218:221], v91 offset:0
	ds_read_b128 v[222:225], v91 offset:2048
	ds_read_b128 v[226:229], v91 offset:4096
	ds_read_b128 v[230:233], v91 offset:6144
	ds_read_b128 v[234:237], v91 offset:8192
	s_waitcnt lgkmcnt(0)
	v_mfma_f32_16x16x32_bf16 v[78:81], v[238:241], v[218:221], v[78:81]
	v_mfma_f32_16x16x32_bf16 v[74:77], v[242:245], v[218:221], v[74:77]
	v_mfma_f32_16x16x32_bf16 v[70:73], v[246:249], v[218:221], v[70:73]
	v_mfma_f32_16x16x32_bf16 v[66:69], v[250:253], v[218:221], v[66:69]
	ds_read_b128 v[218:221], v93 offset:0
	ds_read_b128 v[142:145], v141 offset:0
	v_mfma_f32_16x16x32_bf16 v[62:65], v[238:241], v[222:225], v[62:65]
	v_mfma_f32_16x16x32_bf16 v[58:61], v[242:245], v[222:225], v[58:61]
	v_mfma_f32_16x16x32_bf16 v[54:57], v[246:249], v[222:225], v[54:57]
	v_mfma_f32_16x16x32_bf16 v[50:53], v[250:253], v[222:225], v[50:53]
	ds_read_b128 v[222:225], v93 offset:2048
	ds_read_b128 v[146:149], v141 offset:2048
	v_mfma_f32_16x16x32_bf16 v[46:49], v[238:241], v[226:229], v[46:49]
	v_mfma_f32_16x16x32_bf16 v[42:45], v[242:245], v[226:229], v[42:45]
	v_mfma_f32_16x16x32_bf16 v[38:41], v[246:249], v[226:229], v[38:41]
	v_mfma_f32_16x16x32_bf16 v[34:37], v[250:253], v[226:229], v[34:37]
	ds_read_b128 v[226:229], v93 offset:4096
	ds_read_b128 v[156:159], v141 offset:4096
	v_mfma_f32_16x16x32_bf16 v[18:21], v[238:241], v[230:233], v[18:21]
	v_mfma_f32_16x16x32_bf16 v[22:25], v[242:245], v[230:233], v[22:25]
	v_mfma_f32_16x16x32_bf16 v[26:29], v[246:249], v[230:233], v[26:29]
	v_mfma_f32_16x16x32_bf16 v[30:33], v[250:253], v[230:233], v[30:33]
	ds_read_b128 v[230:233], v93 offset:6144
	ds_read_b128 v[160:163], v141 offset:6144
	v_mfma_f32_16x16x32_bf16 v[2:5], v[238:241], v[234:237], v[2:5]
	v_mfma_f32_16x16x32_bf16 v[6:9], v[242:245], v[234:237], v[6:9]
	v_mfma_f32_16x16x32_bf16 v[10:13], v[246:249], v[234:237], v[10:13]
	v_mfma_f32_16x16x32_bf16 v[14:17], v[250:253], v[234:237], v[14:17]
	ds_read_b128 v[234:237], v93 offset:8192
	s_waitcnt lgkmcnt(0)
	v_mfma_f32_16x16x32_bf16 v[78:81], v[142:145], v[218:221], v[78:81]
	v_mfma_f32_16x16x32_bf16 v[74:77], v[146:149], v[218:221], v[74:77]
	v_mfma_f32_16x16x32_bf16 v[70:73], v[156:159], v[218:221], v[70:73]
	v_mfma_f32_16x16x32_bf16 v[66:69], v[160:163], v[218:221], v[66:69]
	v_mfma_f32_16x16x32_bf16 v[62:65], v[142:145], v[222:225], v[62:65]
	v_mfma_f32_16x16x32_bf16 v[58:61], v[146:149], v[222:225], v[58:61]
	v_mfma_f32_16x16x32_bf16 v[54:57], v[156:159], v[222:225], v[54:57]
	v_mfma_f32_16x16x32_bf16 v[50:53], v[160:163], v[222:225], v[50:53]
	v_mfma_f32_16x16x32_bf16 v[46:49], v[142:145], v[226:229], v[46:49]
	v_mfma_f32_16x16x32_bf16 v[42:45], v[146:149], v[226:229], v[42:45]
	v_mfma_f32_16x16x32_bf16 v[38:41], v[156:159], v[226:229], v[38:41]
	v_mfma_f32_16x16x32_bf16 v[34:37], v[160:163], v[226:229], v[34:37]
	v_mfma_f32_16x16x32_bf16 v[18:21], v[142:145], v[230:233], v[18:21]
	v_mfma_f32_16x16x32_bf16 v[22:25], v[146:149], v[230:233], v[22:25]
	v_mfma_f32_16x16x32_bf16 v[26:29], v[156:159], v[230:233], v[26:29]
	v_mfma_f32_16x16x32_bf16 v[30:33], v[160:163], v[230:233], v[30:33]
	v_mfma_f32_16x16x32_bf16 v[2:5], v[142:145], v[234:237], v[2:5]
	v_mfma_f32_16x16x32_bf16 v[6:9], v[146:149], v[234:237], v[6:9]
	v_mfma_f32_16x16x32_bf16 v[10:13], v[156:159], v[234:237], v[10:13]
	v_mfma_f32_16x16x32_bf16 v[14:17], v[160:163], v[234:237], v[14:17]
	s_waitcnt vmcnt(0)
	s_waitcnt lgkmcnt(0)
	s_barrier
	s_mov_b32 s49, s46
	s_mov_b32 s46, s47
	s_mov_b32 s47, s48
	s_mov_b32 s48, s49
	s_add_i32 s50, s50, 1
	v_add_u32_e32 v91, s46, v135
	v_add_u32_e32 v93, s46, v137
	ds_read_b128 v[238:241], v139 offset:19456
	ds_read_b128 v[242:245], v139 offset:21504
	ds_read_b128 v[246:249], v139 offset:23552
	ds_read_b128 v[250:253], v139 offset:25600
	ds_read_b128 v[218:221], v91 offset:0
	ds_read_b128 v[222:225], v91 offset:2048
	ds_read_b128 v[226:229], v91 offset:4096
	ds_read_b128 v[230:233], v91 offset:6144
	ds_read_b128 v[234:237], v91 offset:8192
	s_waitcnt lgkmcnt(0)
	v_mfma_f32_16x16x32_bf16 v[78:81], v[238:241], v[218:221], v[78:81]
	v_mfma_f32_16x16x32_bf16 v[74:77], v[242:245], v[218:221], v[74:77]
	v_mfma_f32_16x16x32_bf16 v[70:73], v[246:249], v[218:221], v[70:73]
	v_mfma_f32_16x16x32_bf16 v[66:69], v[250:253], v[218:221], v[66:69]
	ds_read_b128 v[218:221], v93 offset:0
	ds_read_b128 v[142:145], v141 offset:19456
	v_mfma_f32_16x16x32_bf16 v[62:65], v[238:241], v[222:225], v[62:65]
	v_mfma_f32_16x16x32_bf16 v[58:61], v[242:245], v[222:225], v[58:61]
	v_mfma_f32_16x16x32_bf16 v[54:57], v[246:249], v[222:225], v[54:57]
	v_mfma_f32_16x16x32_bf16 v[50:53], v[250:253], v[222:225], v[50:53]
	ds_read_b128 v[222:225], v93 offset:2048
	ds_read_b128 v[146:149], v141 offset:21504
	v_mfma_f32_16x16x32_bf16 v[46:49], v[238:241], v[226:229], v[46:49]
	v_mfma_f32_16x16x32_bf16 v[42:45], v[242:245], v[226:229], v[42:45]
	v_mfma_f32_16x16x32_bf16 v[38:41], v[246:249], v[226:229], v[38:41]
	v_mfma_f32_16x16x32_bf16 v[34:37], v[250:253], v[226:229], v[34:37]
	ds_read_b128 v[226:229], v93 offset:4096
	ds_read_b128 v[156:159], v141 offset:23552
	v_mfma_f32_16x16x32_bf16 v[18:21], v[238:241], v[230:233], v[18:21]
	v_mfma_f32_16x16x32_bf16 v[22:25], v[242:245], v[230:233], v[22:25]
	v_mfma_f32_16x16x32_bf16 v[26:29], v[246:249], v[230:233], v[26:29]
	v_mfma_f32_16x16x32_bf16 v[30:33], v[250:253], v[230:233], v[30:33]
	ds_read_b128 v[230:233], v93 offset:6144
	ds_read_b128 v[160:163], v141 offset:25600
	v_mfma_f32_16x16x32_bf16 v[2:5], v[238:241], v[234:237], v[2:5]
	v_mfma_f32_16x16x32_bf16 v[6:9], v[242:245], v[234:237], v[6:9]
	v_mfma_f32_16x16x32_bf16 v[10:13], v[246:249], v[234:237], v[10:13]
	v_mfma_f32_16x16x32_bf16 v[14:17], v[250:253], v[234:237], v[14:17]
	ds_read_b128 v[234:237], v93 offset:8192
	s_waitcnt lgkmcnt(0)
; #define PG8_LAS __attribute__((address_space(3)))
; __device__ __forceinline__ unsigned cvtpk(float lo, float hi) { f32x2 v = {lo, hi}; bf16x2_t b = __builtin_convertvector(v, bf16x2_t); return __builtin_bit_cast(unsigned, b); }
; #define MD_END(last) do { if (last) asm volatile("s_waitcnt vmcnt(0)" ::: "memory"); else asm volatile("s_waitcnt vmcnt(8)" ::: "memory"); \
;         asm volatile("s_waitcnt lgkmcnt(0)" ::: "memory"); __builtin_amdgcn_s_barrier(); asm volatile("" ::: "memory"); } while (0)
; __device__ __forceinline__ void moe_down_stream(PG8_LAS unsigned char* lds, int e, int cb0, int slot0, int nv, const bf16_t* HIDp, const float* Wd, bf16_t* Y, const float* slot_w, const int* slot_dst) {
;     ...
;         MD_COMPUTE(1);
;         MD_END(t + 4 >= NT);
;         if (((t + 1) & 7) == 7) {
;             const int cb = cb0 + ((t + 1) >> 3);
; #pragma unroll
;             for (int m = 0; m < DNM; ++m) {
;                 const float w_ = lw[4 * (16 * m + fr) + wr];
; #pragma unroll
;                 for (int p = 0; p < 2; ++p) { const f32x4 v0 = acc[m][2 * p] * w_, v1 = acc[m][2 * p + 1] * w_; u32x4 w; w.x = cvtpk(v0[0], v0[1]); w.y = cvtpk(v0[2], v0[3]); w.z = cvtpk(v1[0], v1[1]); w.w = cvtpk(v1[2], v1[3]);
;                     *(PG8_LAS u32x4*)(stg + fr * 128 + (((4 * p + fq) ^ (fr & 7)) * 16)) = w; }
; #pragma unroll
;                 for (int hh = 0; hh < 2; ++hh) { const int r = (lane >> 3) + 8 * hh, cc = lane & 7; const u32x4 d = *(const PG8_LAS u32x4*)(stg + r * 128 + ((cc ^ (r & 7)) * 16)); const int dst_ = ldst[4 * (16 * m + r) + wr];
;                     if (dst_ >= 0) *(u32x4*)(Y + (size_t)dst_ * D + 128 * cb + 64 * wc + 8 * cc) = d; }
; #pragma unroll
;                 for (int n = 0; n < 4; ++n) acc[m][n] = (f32x4){0.f, 0.f, 0.f, 0.f}; } }
	v_mfma_f32_16x16x32_bf16 v[78:81], v[142:145], v[218:221], v[78:81]
	v_mfma_f32_16x16x32_bf16 v[74:77], v[146:149], v[218:221], v[74:77]
	v_mfma_f32_16x16x32_bf16 v[70:73], v[156:159], v[218:221], v[70:73]
	v_mfma_f32_16x16x32_bf16 v[66:69], v[160:163], v[218:221], v[66:69]
	v_mfma_f32_16x16x32_bf16 v[62:65], v[142:145], v[222:225], v[62:65]
	v_mfma_f32_16x16x32_bf16 v[58:61], v[146:149], v[222:225], v[58:61]
	v_mfma_f32_16x16x32_bf16 v[54:57], v[156:159], v[222:225], v[54:57]
	v_mfma_f32_16x16x32_bf16 v[50:53], v[160:163], v[222:225], v[50:53]
	v_mfma_f32_16x16x32_bf16 v[46:49], v[142:145], v[226:229], v[46:49]
	v_mfma_f32_16x16x32_bf16 v[42:45], v[146:149], v[226:229], v[42:45]
	v_mfma_f32_16x16x32_bf16 v[38:41], v[156:159], v[226:229], v[38:41]
	v_mfma_f32_16x16x32_bf16 v[34:37], v[160:163], v[226:229], v[34:37]
	v_mfma_f32_16x16x32_bf16 v[18:21], v[142:145], v[230:233], v[18:21]
	v_mfma_f32_16x16x32_bf16 v[22:25], v[146:149], v[230:233], v[22:25]
	v_mfma_f32_16x16x32_bf16 v[26:29], v[156:159], v[230:233], v[26:29]
	v_mfma_f32_16x16x32_bf16 v[30:33], v[160:163], v[230:233], v[30:33]
	v_mfma_f32_16x16x32_bf16 v[2:5], v[142:145], v[234:237], v[2:5]
	v_mfma_f32_16x16x32_bf16 v[6:9], v[146:149], v[234:237], v[6:9]
	v_mfma_f32_16x16x32_bf16 v[10:13], v[156:159], v[234:237], v[10:13]
	v_mfma_f32_16x16x32_bf16 v[14:17], v[160:163], v[234:237], v[14:17]
	s_waitcnt lgkmcnt(0)
	s_barrier
	s_mov_b32 s49, s46
	s_mov_b32 s46, s47
	s_mov_b32 s47, s48
	s_mov_b32 s48, s49
	s_add_i32 s50, s50, 1
	s_add_i32 s54, s48, s74
	v_add_u32_e32 v164, s54, v84
	v_add_u32_e32 v165, s54, v85
	ds_read_b32 v150, v82 offset:0
	ds_read_b32 v151, v83 offset:0
	ds_read_b32 v166, v83 offset:128
	s_waitcnt lgkmcnt(2)
	v_mul_f32_e32 v78, v150, v78
	v_mul_f32_e32 v79, v150, v79
	v_mul_f32_e32 v80, v150, v80
	v_mul_f32_e32 v81, v150, v81
	v_mul_f32_e32 v74, v150, v74
	v_mul_f32_e32 v75, v150, v75
	v_mul_f32_e32 v76, v150, v76
	v_mul_f32_e32 v77, v150, v77
	v_cvt_pk_bf16_f32 v182, v78, v79
	v_cvt_pk_bf16_f32 v183, v80, v81
	v_cvt_pk_bf16_f32 v184, v74, v75
	v_cvt_pk_bf16_f32 v185, v76, v77
	ds_write_b128 v164, v[182:185]
	v_mul_f32_e32 v70, v150, v70
	v_mul_f32_e32 v71, v150, v71
	v_mul_f32_e32 v72, v150, v72
	v_mul_f32_e32 v73, v150, v73
	v_mul_f32_e32 v66, v150, v66
	v_mul_f32_e32 v67, v150, v67
	v_mul_f32_e32 v68, v150, v68
	v_mul_f32_e32 v69, v150, v69
	v_cvt_pk_bf16_f32 v182, v70, v71
	v_cvt_pk_bf16_f32 v183, v72, v73
	v_cvt_pk_bf16_f32 v184, v66, v67
	v_cvt_pk_bf16_f32 v185, v68, v69
	v_xor_b32_e32 v167, 64, v164
	ds_write_b128 v167, v[182:185]
	v_mov_b32_e32 v78, 0
	v_mov_b32_e32 v74, 0
	v_mov_b32_e32 v70, 0
	v_mov_b32_e32 v66, 0
	v_mov_b32_e32 v79, 0
	v_mov_b32_e32 v75, 0
	v_mov_b32_e32 v71, 0
	v_mov_b32_e32 v67, 0
	v_mov_b32_e32 v80, 0
	v_mov_b32_e32 v76, 0
	v_mov_b32_e32 v72, 0
	v_mov_b32_e32 v68, 0
	v_mov_b32_e32 v81, 0
	v_mov_b32_e32 v77, 0
	v_mov_b32_e32 v73, 0
	v_mov_b32_e32 v69, 0
	ds_read_b128 v[182:185], v165 offset:0
	v_cmp_lt_i32_e32 vcc, -1, v151
	v_lshlrev_b32_e32 v148, 13, v151
	v_mov_b32_e32 v149, 0
	v_lshl_add_u64 v[148:149], v[148:149], 0, v[86:87]
	v_cndmask_b32_e32 v148, v168, v148, vcc
	v_cndmask_b32_e32 v149, v169, v149, vcc
	s_waitcnt lgkmcnt(0)
	global_store_dwordx4 v[148:149], v[182:185], off
	ds_read_b128 v[182:185], v165 offset:8192
	v_cmp_lt_i32_e32 vcc, -1, v166
	v_lshlrev_b32_e32 v148, 13, v166
	v_mov_b32_e32 v149, 0
	v_lshl_add_u64 v[148:149], v[148:149], 0, v[86:87]
	v_cndmask_b32_e32 v148, v168, v148, vcc
	v_cndmask_b32_e32 v149, v169, v149, vcc
	s_waitcnt lgkmcnt(0)
	global_store_dwordx4 v[148:149], v[182:185], off
	ds_read_b32 v150, v82 offset:256
	ds_read_b32 v151, v83 offset:256
	ds_read_b32 v166, v83 offset:384
	s_waitcnt lgkmcnt(2)
	v_mul_f32_e32 v62, v150, v62
	v_mul_f32_e32 v63, v150, v63
	v_mul_f32_e32 v64, v150, v64
	v_mul_f32_e32 v65, v150, v65
	v_mul_f32_e32 v58, v150, v58
	v_mul_f32_e32 v59, v150, v59
	v_mul_f32_e32 v60, v150, v60
	v_mul_f32_e32 v61, v150, v61
	v_cvt_pk_bf16_f32 v182, v62, v63
	v_cvt_pk_bf16_f32 v183, v64, v65
	v_cvt_pk_bf16_f32 v184, v58, v59
	v_cvt_pk_bf16_f32 v185, v60, v61
	ds_write_b128 v164, v[182:185]
	v_mul_f32_e32 v54, v150, v54
	v_mul_f32_e32 v55, v150, v55
	v_mul_f32_e32 v56, v150, v56
	v_mul_f32_e32 v57, v150, v57
	v_mul_f32_e32 v50, v150, v50
	v_mul_f32_e32 v51, v150, v51
	v_mul_f32_e32 v52, v150, v52
	v_mul_f32_e32 v53, v150, v53
	v_cvt_pk_bf16_f32 v182, v54, v55
	v_cvt_pk_bf16_f32 v183, v56, v57
	v_cvt_pk_bf16_f32 v184, v50, v51
	v_cvt_pk_bf16_f32 v185, v52, v53
	v_xor_b32_e32 v167, 64, v164
	ds_write_b128 v167, v[182:185]
	v_mov_b32_e32 v62, 0
	v_mov_b32_e32 v58, 0
	v_mov_b32_e32 v54, 0
	v_mov_b32_e32 v50, 0
	v_mov_b32_e32 v63, 0
	v_mov_b32_e32 v59, 0
	v_mov_b32_e32 v55, 0
	v_mov_b32_e32 v51, 0
	v_mov_b32_e32 v64, 0
	v_mov_b32_e32 v60, 0
	v_mov_b32_e32 v56, 0
	v_mov_b32_e32 v52, 0
	v_mov_b32_e32 v65, 0
	v_mov_b32_e32 v61, 0
	v_mov_b32_e32 v57, 0
	v_mov_b32_e32 v53, 0
	ds_read_b128 v[182:185], v165 offset:0
	v_cmp_lt_i32_e32 vcc, -1, v151
	v_lshlrev_b32_e32 v148, 13, v151
	v_mov_b32_e32 v149, 0
	v_lshl_add_u64 v[148:149], v[148:149], 0, v[86:87]
	v_cndmask_b32_e32 v148, v168, v148, vcc
	v_cndmask_b32_e32 v149, v169, v149, vcc
	s_waitcnt lgkmcnt(0)
	global_store_dwordx4 v[148:149], v[182:185], off
	ds_read_b128 v[182:185], v165 offset:8192
	v_cmp_lt_i32_e32 vcc, -1, v166
	v_lshlrev_b32_e32 v148, 13, v166
	v_mov_b32_e32 v149, 0
	v_lshl_add_u64 v[148:149], v[148:149], 0, v[86:87]
	v_cndmask_b32_e32 v148, v168, v148, vcc
	v_cndmask_b32_e32 v149, v169, v149, vcc
	s_waitcnt lgkmcnt(0)
	global_store_dwordx4 v[148:149], v[182:185], off
	ds_read_b32 v150, v82 offset:512
	ds_read_b32 v151, v83 offset:512
	ds_read_b32 v166, v83 offset:640
	s_waitcnt lgkmcnt(2)
; #define PG8_LAS __attribute__((address_space(3)))
; __device__ __forceinline__ unsigned cvtpk(float lo, float hi) { f32x2 v = {lo, hi}; bf16x2_t b = __builtin_convertvector(v, bf16x2_t); return __builtin_bit_cast(unsigned, b); }
; __device__ __forceinline__ void moe_down_stream(PG8_LAS unsigned char* lds, int e, int cb0, int slot0, int nv, const bf16_t* HIDp, const float* Wd, bf16_t* Y, const float* slot_w, const int* slot_dst) {
;     ...
;         if (((t + 1) & 7) == 7) {
;             const int cb = cb0 + ((t + 1) >> 3);
; #pragma unroll
;             for (int m = 0; m < DNM; ++m) {
;                 const float w_ = lw[4 * (16 * m + fr) + wr];
; #pragma unroll
;                 for (int p = 0; p < 2; ++p) { const f32x4 v0 = acc[m][2 * p] * w_, v1 = acc[m][2 * p + 1] * w_; u32x4 w; w.x = cvtpk(v0[0], v0[1]); w.y = cvtpk(v0[2], v0[3]); w.z = cvtpk(v1[0], v1[1]); w.w = cvtpk(v1[2], v1[3]);
;                     *(PG8_LAS u32x4*)(stg + fr * 128 + (((4 * p + fq) ^ (fr & 7)) * 16)) = w; }
; #pragma unroll
;                 for (int hh = 0; hh < 2; ++hh) { const int r = (lane >> 3) + 8 * hh, cc = lane & 7; const u32x4 d = *(const PG8_LAS u32x4*)(stg + r * 128 + ((cc ^ (r & 7)) * 16)); const int dst_ = ldst[4 * (16 * m + r) + wr];
;                     if (dst_ >= 0) *(u32x4*)(Y + (size_t)dst_ * D + 128 * cb + 64 * wc + 8 * cc) = d; }
; #pragma unroll
;                 for (int n = 0; n < 4; ++n) acc[m][n] = (f32x4){0.f, 0.f, 0.f, 0.f}; } }
	v_mul_f32_e32 v46, v150, v46
	v_mul_f32_e32 v47, v150, v47
	v_mul_f32_e32 v48, v150, v48
	v_mul_f32_e32 v49, v150, v49
	v_mul_f32_e32 v42, v150, v42
	v_mul_f32_e32 v43, v150, v43
	v_mul_f32_e32 v44, v150, v44
	v_mul_f32_e32 v45, v150, v45
	v_cvt_pk_bf16_f32 v182, v46, v47
	v_cvt_pk_bf16_f32 v183, v48, v49
	v_cvt_pk_bf16_f32 v184, v42, v43
	v_cvt_pk_bf16_f32 v185, v44, v45
	ds_write_b128 v164, v[182:185]
	v_mul_f32_e32 v38, v150, v38
	v_mul_f32_e32 v39, v150, v39
	v_mul_f32_e32 v40, v150, v40
	v_mul_f32_e32 v41, v150, v41
	v_mul_f32_e32 v34, v150, v34
	v_mul_f32_e32 v35, v150, v35
	v_mul_f32_e32 v36, v150, v36
	v_mul_f32_e32 v37, v150, v37
	v_cvt_pk_bf16_f32 v182, v38, v39
	v_cvt_pk_bf16_f32 v183, v40, v41
	v_cvt_pk_bf16_f32 v184, v34, v35
	v_cvt_pk_bf16_f32 v185, v36, v37
	v_xor_b32_e32 v167, 64, v164
	ds_write_b128 v167, v[182:185]
	v_mov_b32_e32 v46, 0
	v_mov_b32_e32 v42, 0
	v_mov_b32_e32 v38, 0
	v_mov_b32_e32 v34, 0
	v_mov_b32_e32 v47, 0
	v_mov_b32_e32 v43, 0
	v_mov_b32_e32 v39, 0
	v_mov_b32_e32 v35, 0
	v_mov_b32_e32 v48, 0
	v_mov_b32_e32 v44, 0
	v_mov_b32_e32 v40, 0
	v_mov_b32_e32 v36, 0
	v_mov_b32_e32 v49, 0
	v_mov_b32_e32 v45, 0
	v_mov_b32_e32 v41, 0
	v_mov_b32_e32 v37, 0
	ds_read_b128 v[182:185], v165 offset:0
	v_cmp_lt_i32_e32 vcc, -1, v151
	v_lshlrev_b32_e32 v148, 13, v151
	v_mov_b32_e32 v149, 0
	v_lshl_add_u64 v[148:149], v[148:149], 0, v[86:87]
	v_cndmask_b32_e32 v148, v168, v148, vcc
	v_cndmask_b32_e32 v149, v169, v149, vcc
	s_waitcnt lgkmcnt(0)
	global_store_dwordx4 v[148:149], v[182:185], off
	ds_read_b128 v[182:185], v165 offset:8192
	v_cmp_lt_i32_e32 vcc, -1, v166
	v_lshlrev_b32_e32 v148, 13, v166
	v_mov_b32_e32 v149, 0
	v_lshl_add_u64 v[148:149], v[148:149], 0, v[86:87]
	v_cndmask_b32_e32 v148, v168, v148, vcc
	v_cndmask_b32_e32 v149, v169, v149, vcc
	s_waitcnt lgkmcnt(0)
	global_store_dwordx4 v[148:149], v[182:185], off
	ds_read_b32 v150, v82 offset:768
	ds_read_b32 v151, v83 offset:768
	ds_read_b32 v166, v83 offset:896
	s_waitcnt lgkmcnt(2)
	v_mul_f32_e32 v18, v150, v18
	v_mul_f32_e32 v19, v150, v19
	v_mul_f32_e32 v20, v150, v20
	v_mul_f32_e32 v21, v150, v21
	v_mul_f32_e32 v22, v150, v22
	v_mul_f32_e32 v23, v150, v23
	v_mul_f32_e32 v24, v150, v24
	v_mul_f32_e32 v25, v150, v25
	v_cvt_pk_bf16_f32 v182, v18, v19
	v_cvt_pk_bf16_f32 v183, v20, v21
	v_cvt_pk_bf16_f32 v184, v22, v23
	v_cvt_pk_bf16_f32 v185, v24, v25
	ds_write_b128 v164, v[182:185]
	v_mul_f32_e32 v26, v150, v26
	v_mul_f32_e32 v27, v150, v27
	v_mul_f32_e32 v28, v150, v28
	v_mul_f32_e32 v29, v150, v29
	v_mul_f32_e32 v30, v150, v30
	v_mul_f32_e32 v31, v150, v31
	v_mul_f32_e32 v32, v150, v32
	v_mul_f32_e32 v33, v150, v33
	v_cvt_pk_bf16_f32 v182, v26, v27
	v_cvt_pk_bf16_f32 v183, v28, v29
	v_cvt_pk_bf16_f32 v184, v30, v31
	v_cvt_pk_bf16_f32 v185, v32, v33
	v_xor_b32_e32 v167, 64, v164
	ds_write_b128 v167, v[182:185]
	v_mov_b32_e32 v18, 0
	v_mov_b32_e32 v22, 0
	v_mov_b32_e32 v26, 0
	v_mov_b32_e32 v30, 0
	v_mov_b32_e32 v19, 0
	v_mov_b32_e32 v23, 0
	v_mov_b32_e32 v27, 0
	v_mov_b32_e32 v31, 0
	v_mov_b32_e32 v20, 0
	v_mov_b32_e32 v24, 0
	v_mov_b32_e32 v28, 0
	v_mov_b32_e32 v32, 0
	v_mov_b32_e32 v21, 0
	v_mov_b32_e32 v25, 0
	v_mov_b32_e32 v29, 0
	v_mov_b32_e32 v33, 0
	ds_read_b128 v[182:185], v165 offset:0
	v_cmp_lt_i32_e32 vcc, -1, v151
	v_lshlrev_b32_e32 v148, 13, v151
	v_mov_b32_e32 v149, 0
	v_lshl_add_u64 v[148:149], v[148:149], 0, v[86:87]
	v_cndmask_b32_e32 v148, v168, v148, vcc
	v_cndmask_b32_e32 v149, v169, v149, vcc
	s_waitcnt lgkmcnt(0)
	global_store_dwordx4 v[148:149], v[182:185], off
	ds_read_b128 v[182:185], v165 offset:8192
	v_cmp_lt_i32_e32 vcc, -1, v166
	v_lshlrev_b32_e32 v148, 13, v166
	v_mov_b32_e32 v149, 0
	v_lshl_add_u64 v[148:149], v[148:149], 0, v[86:87]
	v_cndmask_b32_e32 v148, v168, v148, vcc
	v_cndmask_b32_e32 v149, v169, v149, vcc
	s_waitcnt lgkmcnt(0)
	global_store_dwordx4 v[148:149], v[182:185], off
	ds_read_b32 v150, v82 offset:1024
	ds_read_b32 v151, v83 offset:1024
	ds_read_b32 v166, v83 offset:1152
	s_waitcnt lgkmcnt(2)
	v_mul_f32_e32 v2, v150, v2
	v_mul_f32_e32 v3, v150, v3
	v_mul_f32_e32 v4, v150, v4
	v_mul_f32_e32 v5, v150, v5
	v_mul_f32_e32 v6, v150, v6
	v_mul_f32_e32 v7, v150, v7
	v_mul_f32_e32 v8, v150, v8
	v_mul_f32_e32 v9, v150, v9
	v_cvt_pk_bf16_f32 v182, v2, v3
	v_cvt_pk_bf16_f32 v183, v4, v5
	v_cvt_pk_bf16_f32 v184, v6, v7
	v_cvt_pk_bf16_f32 v185, v8, v9
	ds_write_b128 v164, v[182:185]
	v_mul_f32_e32 v10, v150, v10
	v_mul_f32_e32 v11, v150, v11
	v_mul_f32_e32 v12, v150, v12
	v_mul_f32_e32 v13, v150, v13
	v_mul_f32_e32 v14, v150, v14
	v_mul_f32_e32 v15, v150, v15
	v_mul_f32_e32 v16, v150, v16
	v_mul_f32_e32 v17, v150, v17
	v_cvt_pk_bf16_f32 v182, v10, v11
	v_cvt_pk_bf16_f32 v183, v12, v13
	v_cvt_pk_bf16_f32 v184, v14, v15
	v_cvt_pk_bf16_f32 v185, v16, v17
	v_xor_b32_e32 v167, 64, v164
	ds_write_b128 v167, v[182:185]
	v_mov_b32_e32 v2, 0
	v_mov_b32_e32 v6, 0
	v_mov_b32_e32 v10, 0
	v_mov_b32_e32 v14, 0
	v_mov_b32_e32 v3, 0
	v_mov_b32_e32 v7, 0
	v_mov_b32_e32 v11, 0
	v_mov_b32_e32 v15, 0
	v_mov_b32_e32 v4, 0
	v_mov_b32_e32 v8, 0
	v_mov_b32_e32 v12, 0
	v_mov_b32_e32 v16, 0
	v_mov_b32_e32 v5, 0
	v_mov_b32_e32 v9, 0
	v_mov_b32_e32 v13, 0
	v_mov_b32_e32 v17, 0
	ds_read_b128 v[182:185], v165 offset:0
	v_cmp_lt_i32_e32 vcc, -1, v151
	v_lshlrev_b32_e32 v148, 13, v151
	v_mov_b32_e32 v149, 0
	v_lshl_add_u64 v[148:149], v[148:149], 0, v[86:87]
	v_cndmask_b32_e32 v148, v168, v148, vcc
	v_cndmask_b32_e32 v149, v169, v149, vcc
	s_waitcnt lgkmcnt(0)
	global_store_dwordx4 v[148:149], v[182:185], off
	ds_read_b128 v[182:185], v165 offset:8192
	v_cmp_lt_i32_e32 vcc, -1, v166
	v_lshlrev_b32_e32 v148, 13, v166
	v_mov_b32_e32 v149, 0
	v_lshl_add_u64 v[148:149], v[148:149], 0, v[86:87]
	v_cndmask_b32_e32 v148, v168, v148, vcc
	v_cndmask_b32_e32 v149, v169, v149, vcc
	s_waitcnt lgkmcnt(0)
	global_store_dwordx4 v[148:149], v[182:185], off
	v_add_co_u32_e32 v86, vcc, 0x400, v86
	s_nop 1
	v_addc_co_u32_e32 v87, vcc, 0, v87, vcc
	s_waitcnt lgkmcnt(0)
	s_branch .Lmd_done
; #define MD_GLDS_A(buf, tau) do { _Pragma("unroll") for (int i = 0; i < 5; ++i) if (amask & (1u << i)) \
;         __builtin_amdgcn_global_load_lds((const unsigned*)((const char*)HIDp + aoff[i] + (size_t)((tau) & 7) * 128), (PG8_LAS unsigned*)(MD_SA(buf) + wid * 1024 + i * 8192), 16, 0, 0); } while (0)
; #define MD_B_ISSUE(sb, tau) do { const char* kb_ = Bb + (size_t)((tau) >> 3) * 512 + (size_t)((tau) & 7) * (64 * (size_t)RB); _Pragma("unroll") for (int j = 0; j < 8; ++j) { const char* p_ = kb_ + (size_t)j * RB; \
;         asm volatile("global_load_dwordx2 %0, %1, off" : "=&v"(sb[j]) : "v"(p_) : "memory"); } } while (0)
; #define MD_B_WAIT(sb, N) asm volatile("s_waitcnt vmcnt(%8)" : "+v"(sb[0]), "+v"(sb[1]), "+v"(sb[2]), "+v"(sb[3]), "+v"(sb[4]), "+v"(sb[5]), "+v"(sb[6]), "+v"(sb[7]) : "n"(N) : "memory")
; #define MD_END(last) do { if (last) asm volatile("s_waitcnt vmcnt(0)" ::: "memory"); else asm volatile("s_waitcnt vmcnt(8)" ::: "memory"); \
;         asm volatile("s_waitcnt lgkmcnt(0)" ::: "memory"); __builtin_amdgcn_s_barrier(); asm volatile("" ::: "memory"); } while (0)
; __device__ __forceinline__ void moe_down_stream(PG8_LAS unsigned char* lds, int e, int cb0, int slot0, int nv, const bf16_t* HIDp, const float* Wd, bf16_t* Y, const float* slot_w, const int* slot_dst) {
;     ...
;     MD_GLDS_A(0, 0); MD_B_ISSUE(s0, 0); MD_B_ISSUE(s1, 1);
;     MD_B_WAIT(s0, 8); MD_B_WRITE(s0, 0); __builtin_amdgcn_sched_barrier(0); MD_B_ISSUE(s0, 2);
;     asm volatile("s_waitcnt vmcnt(16)" ::: "memory");
;     asm volatile("s_waitcnt lgkmcnt(0)" ::: "memory"); __builtin_amdgcn_s_barrier(); asm volatile("" ::: "memory");
; #pragma unroll 1
;     for (int t = 0; t < NT; t += 2) {
;         if (t + 2 < NT) MD_B_WAIT(s1, 8); else MD_B_WAIT(s1, 0);
;         MD_B_WRITE(s1, 1); __builtin_amdgcn_sched_barrier(0); MD_GLDS_A(1, t + 1); __builtin_amdgcn_sched_barrier(0);
;         if (t + 3 < NT) MD_B_ISSUE(s1, t + 3);
;         MD_COMPUTE(0);
;         MD_END(t + 3 >= NT);
;         if (t + 2 < NT) { MD_B_WAIT(s0, 8); MD_B_WRITE(s0, 0); __builtin_amdgcn_sched_barrier(0); MD_GLDS_A(0, t + 2); __builtin_amdgcn_sched_barrier(0); }
;         if (t + 4 < NT) MD_B_ISSUE(s0, t + 4);
;         MD_COMPUTE(1);
;         MD_END(t + 4 >= NT);
.Lmd_grpY:
	s_add_i32 s49, s48, s74
	s_add_i32 s52, s52, 1
	s_and_b32 s54, s52, 7
	s_cmp_eq_u32 s54, 0
	s_cselect_b32 s54, s53, s32
	s_cselect_b32 s55, -1, 0
	s_add_u32 s30, s30, s54
	s_addc_u32 s31, s31, s55
	s_mov_b32 m0, s49
	s_nop 0
	global_load_lds_dwordx4 v88, s[30:31]
	s_add_i32 m0, s49, 0x2000
	s_nop 0
	global_load_lds_dwordx4 v90, s[30:31]
	s_add_i32 m0, s49, 0x4000
	s_nop 0
	global_load_lds_dwordx4 v92, s[30:31]
	s_add_i32 m0, s49, 0x6000
	s_nop 0
	global_load_lds_dwordx4 v94, s[30:31]
	s_add_i32 m0, s49, 0x8000
	s_nop 0
	global_load_lds_dwordx4 v96, s[30:31]
	s_waitcnt vmcnt(29)
	v_cvt_pk_bf16_f32 v172, v114, v116
	v_cvt_pk_bf16_f32 v173, v118, v120
	v_cvt_pk_bf16_f32 v174, v122, v124
	v_cvt_pk_bf16_f32 v175, v126, v128
	v_cvt_pk_bf16_f32 v176, v115, v117
	v_cvt_pk_bf16_f32 v177, v119, v121
	v_cvt_pk_bf16_f32 v178, v123, v125
	v_cvt_pk_bf16_f32 v179, v127, v129
	ds_write_b128 v95, v[172:175] offset:19456
	ds_write_b128 v95, v[176:179] offset:19584
	v_add_u32_e32 v91, s46, v135
	v_add_u32_e32 v93, s46, v137
	ds_read_b128 v[238:241], v139 offset:0
	ds_read_b128 v[242:245], v139 offset:2048
	ds_read_b128 v[246:249], v139 offset:4096
	ds_read_b128 v[250:253], v139 offset:6144
	ds_read_b128 v[218:221], v91 offset:0
	ds_read_b128 v[222:225], v91 offset:2048
	ds_read_b128 v[226:229], v91 offset:4096
	ds_read_b128 v[230:233], v91 offset:6144
	ds_read_b128 v[234:237], v91 offset:8192
	s_waitcnt lgkmcnt(0)
	v_mfma_f32_16x16x32_bf16 v[78:81], v[238:241], v[218:221], v[78:81]
	v_mfma_f32_16x16x32_bf16 v[74:77], v[242:245], v[218:221], v[74:77]
	v_mfma_f32_16x16x32_bf16 v[70:73], v[246:249], v[218:221], v[70:73]
	v_mfma_f32_16x16x32_bf16 v[66:69], v[250:253], v[218:221], v[66:69]
	ds_read_b128 v[218:221], v93 offset:0
	ds_read_b128 v[142:145], v141 offset:0
	s_add_i32 s51, s51, 1
	s_and_b32 s54, s51, 7
	s_cmp_eq_u32 s54, 0
	s_cselect_b32 s44, s34, s35
	s_cselect_b32 s45, -1, 0
	v_lshl_add_u64 v[132:133], v[132:133], 0, s[44:45]
	global_load_dwordx2 v[114:115], v[132:133], off
	v_lshl_add_u64 v[180:181], v[132:133], 0, s[24:25]
	global_load_dwordx2 v[116:117], v[180:181], off
	v_mfma_f32_16x16x32_bf16 v[62:65], v[238:241], v[222:225], v[62:65]
	v_mfma_f32_16x16x32_bf16 v[58:61], v[242:245], v[222:225], v[58:61]
	v_mfma_f32_16x16x32_bf16 v[54:57], v[246:249], v[222:225], v[54:57]
	v_mfma_f32_16x16x32_bf16 v[50:53], v[250:253], v[222:225], v[50:53]
	ds_read_b128 v[222:225], v93 offset:2048
	ds_read_b128 v[146:149], v141 offset:2048
	v_lshl_add_u64 v[180:181], v[132:133], 0, s[26:27]
	global_load_dwordx2 v[118:119], v[180:181], off
	v_lshl_add_u64 v[180:181], v[132:133], 0, s[28:29]
	global_load_dwordx2 v[120:121], v[180:181], off
	v_mfma_f32_16x16x32_bf16 v[46:49], v[238:241], v[226:229], v[46:49]
	v_mfma_f32_16x16x32_bf16 v[42:45], v[242:245], v[226:229], v[42:45]
	v_mfma_f32_16x16x32_bf16 v[38:41], v[246:249], v[226:229], v[38:41]
	v_mfma_f32_16x16x32_bf16 v[34:37], v[250:253], v[226:229], v[34:37]
	ds_read_b128 v[226:229], v93 offset:4096
	ds_read_b128 v[156:159], v141 offset:4096
	v_lshl_add_u64 v[180:181], v[132:133], 0, s[36:37]
	global_load_dwordx2 v[122:123], v[180:181], off
	v_lshl_add_u64 v[180:181], v[132:133], 0, s[38:39]
	global_load_dwordx2 v[124:125], v[180:181], off
	v_mfma_f32_16x16x32_bf16 v[18:21], v[238:241], v[230:233], v[18:21]
	v_mfma_f32_16x16x32_bf16 v[22:25], v[242:245], v[230:233], v[22:25]
	v_mfma_f32_16x16x32_bf16 v[26:29], v[246:249], v[230:233], v[26:29]
	v_mfma_f32_16x16x32_bf16 v[30:33], v[250:253], v[230:233], v[30:33]
	ds_read_b128 v[230:233], v93 offset:6144
	ds_read_b128 v[160:163], v141 offset:6144
	v_lshl_add_u64 v[180:181], v[132:133], 0, s[40:41]
	global_load_dwordx2 v[126:127], v[180:181], off
	v_lshl_add_u64 v[180:181], v[132:133], 0, s[42:43]
	global_load_dwordx2 v[128:129], v[180:181], off
	v_mfma_f32_16x16x32_bf16 v[2:5], v[238:241], v[234:237], v[2:5]
	v_mfma_f32_16x16x32_bf16 v[6:9], v[242:245], v[234:237], v[6:9]
	v_mfma_f32_16x16x32_bf16 v[10:13], v[246:249], v[234:237], v[10:13]
	v_mfma_f32_16x16x32_bf16 v[14:17], v[250:253], v[234:237], v[14:17]
	ds_read_b128 v[234:237], v93 offset:8192
	s_waitcnt lgkmcnt(0)
	s_barrier
	s_mov_b32 s49, s46
	s_mov_b32 s46, s47
	s_mov_b32 s47, s48
	s_mov_b32 s48, s49
	s_add_i32 s50, s50, 1
	s_add_i32 s49, s48, s74
	s_add_i32 s52, s52, 1
	s_and_b32 s54, s52, 7
	s_cmp_eq_u32 s54, 0
	s_cselect_b32 s54, s53, s32
	s_cselect_b32 s55, -1, 0
	s_add_u32 s30, s30, s54
	s_addc_u32 s31, s31, s55
	v_mfma_f32_16x16x32_bf16 v[78:81], v[142:145], v[218:221], v[78:81]
	v_mfma_f32_16x16x32_bf16 v[74:77], v[146:149], v[218:221], v[74:77]
	v_mfma_f32_16x16x32_bf16 v[70:73], v[156:159], v[218:221], v[70:73]
	v_mfma_f32_16x16x32_bf16 v[66:69], v[160:163], v[218:221], v[66:69]
	s_mov_b32 m0, s49
	s_nop 0
	global_load_lds_dwordx4 v88, s[30:31]
	v_mfma_f32_16x16x32_bf16 v[62:65], v[142:145], v[222:225], v[62:65]
	v_mfma_f32_16x16x32_bf16 v[58:61], v[146:149], v[222:225], v[58:61]
	v_mfma_f32_16x16x32_bf16 v[54:57], v[156:159], v[222:225], v[54:57]
	v_mfma_f32_16x16x32_bf16 v[50:53], v[160:163], v[222:225], v[50:53]
	s_add_i32 m0, s49, 0x2000
	s_nop 0
	global_load_lds_dwordx4 v90, s[30:31]
	v_mfma_f32_16x16x32_bf16 v[46:49], v[142:145], v[226:229], v[46:49]
	v_mfma_f32_16x16x32_bf16 v[42:45], v[146:149], v[226:229], v[42:45]
	v_mfma_f32_16x16x32_bf16 v[38:41], v[156:159], v[226:229], v[38:41]
	v_mfma_f32_16x16x32_bf16 v[34:37], v[160:163], v[226:229], v[34:37]
	s_add_i32 m0, s49, 0x4000
	s_nop 0
	global_load_lds_dwordx4 v92, s[30:31]
	v_mfma_f32_16x16x32_bf16 v[18:21], v[142:145], v[230:233], v[18:21]
	v_mfma_f32_16x16x32_bf16 v[22:25], v[146:149], v[230:233], v[22:25]
	v_mfma_f32_16x16x32_bf16 v[26:29], v[156:159], v[230:233], v[26:29]
	v_mfma_f32_16x16x32_bf16 v[30:33], v[160:163], v[230:233], v[30:33]
	s_add_i32 m0, s49, 0x6000
	s_nop 0
	global_load_lds_dwordx4 v94, s[30:31]
	v_mfma_f32_16x16x32_bf16 v[2:5], v[142:145], v[234:237], v[2:5]
	v_mfma_f32_16x16x32_bf16 v[6:9], v[146:149], v[234:237], v[6:9]
	v_mfma_f32_16x16x32_bf16 v[10:13], v[156:159], v[234:237], v[10:13]
	v_mfma_f32_16x16x32_bf16 v[14:17], v[160:163], v[234:237], v[14:17]
	s_add_i32 m0, s49, 0x8000
	s_nop 0
	global_load_lds_dwordx4 v96, s[30:31]
	s_waitcnt vmcnt(34)
; #define MD_GLDS_A(buf, tau) do { _Pragma("unroll") for (int i = 0; i < 5; ++i) if (amask & (1u << i)) \
;         __builtin_amdgcn_global_load_lds((const unsigned*)((const char*)HIDp + aoff[i] + (size_t)((tau) & 7) * 128), (PG8_LAS unsigned*)(MD_SA(buf) + wid * 1024 + i * 8192), 16, 0, 0); } while (0)
; #define MD_B_ISSUE(sb, tau) do { const char* kb_ = Bb + (size_t)((tau) >> 3) * 512 + (size_t)((tau) & 7) * (64 * (size_t)RB); _Pragma("unroll") for (int j = 0; j < 8; ++j) { const char* p_ = kb_ + (size_t)j * RB; \
;         asm volatile("global_load_dwordx2 %0, %1, off" : "=&v"(sb[j]) : "v"(p_) : "memory"); } } while (0)
; #define MD_B_WAIT(sb, N) asm volatile("s_waitcnt vmcnt(%8)" : "+v"(sb[0]), "+v"(sb[1]), "+v"(sb[2]), "+v"(sb[3]), "+v"(sb[4]), "+v"(sb[5]), "+v"(sb[6]), "+v"(sb[7]) : "n"(N) : "memory")
; #define MD_END(last) do { if (last) asm volatile("s_waitcnt vmcnt(0)" ::: "memory"); else asm volatile("s_waitcnt vmcnt(8)" ::: "memory"); \
;         asm volatile("s_waitcnt lgkmcnt(0)" ::: "memory"); __builtin_amdgcn_s_barrier(); asm volatile("" ::: "memory"); } while (0)
; __device__ __forceinline__ void moe_down_stream(PG8_LAS unsigned char* lds, int e, int cb0, int slot0, int nv, const bf16_t* HIDp, const float* Wd, bf16_t* Y, const float* slot_w, const int* slot_dst) {
;     ...
;     for (int t = 0; t < NT; t += 2) {
;         if (t + 2 < NT) MD_B_WAIT(s1, 8); else MD_B_WAIT(s1, 0);
;         MD_B_WRITE(s1, 1); __builtin_amdgcn_sched_barrier(0); MD_GLDS_A(1, t + 1); __builtin_amdgcn_sched_barrier(0);
;         if (t + 3 < NT) MD_B_ISSUE(s1, t + 3);
;         MD_COMPUTE(0);
;         MD_END(t + 3 >= NT);
;         if (t + 2 < NT) { MD_B_WAIT(s0, 8); MD_B_WRITE(s0, 0); __builtin_amdgcn_sched_barrier(0); MD_GLDS_A(0, t + 2); __builtin_amdgcn_sched_barrier(0); }
;         if (t + 4 < NT) MD_B_ISSUE(s0, t + 4);
;         MD_COMPUTE(1);
;         MD_END(t + 4 >= NT);
	v_cvt_pk_bf16_f32 v172, v186, v188
	v_cvt_pk_bf16_f32 v173, v190, v192
	v_cvt_pk_bf16_f32 v174, v194, v196
	v_cvt_pk_bf16_f32 v175, v198, v200
	v_cvt_pk_bf16_f32 v176, v187, v189
	v_cvt_pk_bf16_f32 v177, v191, v193
	v_cvt_pk_bf16_f32 v178, v195, v197
	v_cvt_pk_bf16_f32 v179, v199, v201
	ds_write_b128 v95, v[172:175] offset:0
	ds_write_b128 v95, v[176:179] offset:128
	v_add_u32_e32 v91, s46, v135
	v_add_u32_e32 v93, s46, v137
	ds_read_b128 v[238:241], v139 offset:19456
	ds_read_b128 v[242:245], v139 offset:21504
	ds_read_b128 v[246:249], v139 offset:23552
	ds_read_b128 v[250:253], v139 offset:25600
	ds_read_b128 v[218:221], v91 offset:0
	ds_read_b128 v[222:225], v91 offset:2048
	ds_read_b128 v[226:229], v91 offset:4096
	ds_read_b128 v[230:233], v91 offset:6144
	ds_read_b128 v[234:237], v91 offset:8192
	s_waitcnt lgkmcnt(0)
	v_mfma_f32_16x16x32_bf16 v[78:81], v[238:241], v[218:221], v[78:81]
	v_mfma_f32_16x16x32_bf16 v[74:77], v[242:245], v[218:221], v[74:77]
	v_mfma_f32_16x16x32_bf16 v[70:73], v[246:249], v[218:221], v[70:73]
	v_mfma_f32_16x16x32_bf16 v[66:69], v[250:253], v[218:221], v[66:69]
	ds_read_b128 v[218:221], v93 offset:0
	ds_read_b128 v[142:145], v141 offset:19456
	s_add_i32 s51, s51, 1
	s_and_b32 s54, s51, 7
	s_cmp_eq_u32 s54, 0
	s_cselect_b32 s44, s34, s35
	s_cselect_b32 s45, -1, 0
	v_lshl_add_u64 v[132:133], v[132:133], 0, s[44:45]
	global_load_dwordx2 v[186:187], v[132:133], off
	v_lshl_add_u64 v[180:181], v[132:133], 0, s[24:25]
	global_load_dwordx2 v[188:189], v[180:181], off
	v_mfma_f32_16x16x32_bf16 v[62:65], v[238:241], v[222:225], v[62:65]
	v_mfma_f32_16x16x32_bf16 v[58:61], v[242:245], v[222:225], v[58:61]
	v_mfma_f32_16x16x32_bf16 v[54:57], v[246:249], v[222:225], v[54:57]
	v_mfma_f32_16x16x32_bf16 v[50:53], v[250:253], v[222:225], v[50:53]
	ds_read_b128 v[222:225], v93 offset:2048
	ds_read_b128 v[146:149], v141 offset:21504
	v_lshl_add_u64 v[180:181], v[132:133], 0, s[26:27]
	global_load_dwordx2 v[190:191], v[180:181], off
	v_lshl_add_u64 v[180:181], v[132:133], 0, s[28:29]
	global_load_dwordx2 v[192:193], v[180:181], off
	v_mfma_f32_16x16x32_bf16 v[46:49], v[238:241], v[226:229], v[46:49]
	v_mfma_f32_16x16x32_bf16 v[42:45], v[242:245], v[226:229], v[42:45]
	v_mfma_f32_16x16x32_bf16 v[38:41], v[246:249], v[226:229], v[38:41]
	v_mfma_f32_16x16x32_bf16 v[34:37], v[250:253], v[226:229], v[34:37]
	ds_read_b128 v[226:229], v93 offset:4096
	ds_read_b128 v[156:159], v141 offset:23552
	v_lshl_add_u64 v[180:181], v[132:133], 0, s[36:37]
	global_load_dwordx2 v[194:195], v[180:181], off
	v_lshl_add_u64 v[180:181], v[132:133], 0, s[38:39]
	global_load_dwordx2 v[196:197], v[180:181], off
	v_mfma_f32_16x16x32_bf16 v[18:21], v[238:241], v[230:233], v[18:21]
	v_mfma_f32_16x16x32_bf16 v[22:25], v[242:245], v[230:233], v[22:25]
	v_mfma_f32_16x16x32_bf16 v[26:29], v[246:249], v[230:233], v[26:29]
	v_mfma_f32_16x16x32_bf16 v[30:33], v[250:253], v[230:233], v[30:33]
	ds_read_b128 v[230:233], v93 offset:6144
	ds_read_b128 v[160:163], v141 offset:25600
	v_lshl_add_u64 v[180:181], v[132:133], 0, s[40:41]
	global_load_dwordx2 v[198:199], v[180:181], off
	v_lshl_add_u64 v[180:181], v[132:133], 0, s[42:43]
	global_load_dwordx2 v[200:201], v[180:181], off
	v_mfma_f32_16x16x32_bf16 v[2:5], v[238:241], v[234:237], v[2:5]
	v_mfma_f32_16x16x32_bf16 v[6:9], v[242:245], v[234:237], v[6:9]
	v_mfma_f32_16x16x32_bf16 v[10:13], v[246:249], v[234:237], v[10:13]
	v_mfma_f32_16x16x32_bf16 v[14:17], v[250:253], v[234:237], v[14:17]
	ds_read_b128 v[234:237], v93 offset:8192
	s_waitcnt vmcnt(21)
	s_waitcnt lgkmcnt(0)
	s_barrier
	s_mov_b32 s49, s46
	s_mov_b32 s46, s47
	s_mov_b32 s47, s48
	s_mov_b32 s48, s49
	s_add_i32 s50, s50, 1
	s_add_i32 s49, s48, s74
	s_add_i32 s52, s52, 1
	s_and_b32 s54, s52, 7
	s_cmp_eq_u32 s54, 0
	s_cselect_b32 s54, s53, s32
	s_cselect_b32 s55, -1, 0
	s_add_u32 s30, s30, s54
	s_addc_u32 s31, s31, s55
	v_mfma_f32_16x16x32_bf16 v[78:81], v[142:145], v[218:221], v[78:81]
	v_mfma_f32_16x16x32_bf16 v[74:77], v[146:149], v[218:221], v[74:77]
	v_mfma_f32_16x16x32_bf16 v[70:73], v[156:159], v[218:221], v[70:73]
	v_mfma_f32_16x16x32_bf16 v[66:69], v[160:163], v[218:221], v[66:69]
	s_mov_b32 m0, s49
	s_nop 0
	global_load_lds_dwordx4 v88, s[30:31]
	v_mfma_f32_16x16x32_bf16 v[62:65], v[142:145], v[222:225], v[62:65]
	v_mfma_f32_16x16x32_bf16 v[58:61], v[146:149], v[222:225], v[58:61]
	v_mfma_f32_16x16x32_bf16 v[54:57], v[156:159], v[222:225], v[54:57]
	v_mfma_f32_16x16x32_bf16 v[50:53], v[160:163], v[222:225], v[50:53]
	s_add_i32 m0, s49, 0x2000
	s_nop 0
	global_load_lds_dwordx4 v90, s[30:31]
	v_mfma_f32_16x16x32_bf16 v[46:49], v[142:145], v[226:229], v[46:49]
	v_mfma_f32_16x16x32_bf16 v[42:45], v[146:149], v[226:229], v[42:45]
	v_mfma_f32_16x16x32_bf16 v[38:41], v[156:159], v[226:229], v[38:41]
	v_mfma_f32_16x16x32_bf16 v[34:37], v[160:163], v[226:229], v[34:37]
	s_add_i32 m0, s49, 0x4000
	s_nop 0
	global_load_lds_dwordx4 v92, s[30:31]
	v_mfma_f32_16x16x32_bf16 v[18:21], v[142:145], v[230:233], v[18:21]
	v_mfma_f32_16x16x32_bf16 v[22:25], v[146:149], v[230:233], v[22:25]
	v_mfma_f32_16x16x32_bf16 v[26:29], v[156:159], v[230:233], v[26:29]
	v_mfma_f32_16x16x32_bf16 v[30:33], v[160:163], v[230:233], v[30:33]
	s_add_i32 m0, s49, 0x6000
	s_nop 0
	global_load_lds_dwordx4 v94, s[30:31]
	v_mfma_f32_16x16x32_bf16 v[2:5], v[142:145], v[234:237], v[2:5]
	v_mfma_f32_16x16x32_bf16 v[6:9], v[146:149], v[234:237], v[6:9]
	v_mfma_f32_16x16x32_bf16 v[10:13], v[156:159], v[234:237], v[10:13]
	v_mfma_f32_16x16x32_bf16 v[14:17], v[160:163], v[234:237], v[14:17]
	s_add_i32 m0, s49, 0x8000
	s_nop 0
	global_load_lds_dwordx4 v96, s[30:31]
	v_cvt_pk_bf16_f32 v172, v202, v204
	v_cvt_pk_bf16_f32 v173, v206, v208
	v_cvt_pk_bf16_f32 v174, v210, v212
	v_cvt_pk_bf16_f32 v175, v214, v216
	v_cvt_pk_bf16_f32 v176, v203, v205
	v_cvt_pk_bf16_f32 v177, v207, v209
	v_cvt_pk_bf16_f32 v178, v211, v213
	v_cvt_pk_bf16_f32 v179, v215, v217
	ds_write_b128 v95, v[172:175] offset:19456
	ds_write_b128 v95, v[176:179] offset:19584
	v_add_u32_e32 v91, s46, v135
	v_add_u32_e32 v93, s46, v137
	ds_read_b128 v[238:241], v139 offset:0
	ds_read_b128 v[242:245], v139 offset:2048
	ds_read_b128 v[246:249], v139 offset:4096
	ds_read_b128 v[250:253], v139 offset:6144
	ds_read_b128 v[218:221], v91 offset:0
	ds_read_b128 v[222:225], v91 offset:2048
	ds_read_b128 v[226:229], v91 offset:4096
	ds_read_b128 v[230:233], v91 offset:6144
	ds_read_b128 v[234:237], v91 offset:8192
	s_waitcnt lgkmcnt(0)
; #define MD_GLDS_A(buf, tau) do { _Pragma("unroll") for (int i = 0; i < 5; ++i) if (amask & (1u << i)) \
;         __builtin_amdgcn_global_load_lds((const unsigned*)((const char*)HIDp + aoff[i] + (size_t)((tau) & 7) * 128), (PG8_LAS unsigned*)(MD_SA(buf) + wid * 1024 + i * 8192), 16, 0, 0); } while (0)
; #define MD_B_ISSUE(sb, tau) do { const char* kb_ = Bb + (size_t)((tau) >> 3) * 512 + (size_t)((tau) & 7) * (64 * (size_t)RB); _Pragma("unroll") for (int j = 0; j < 8; ++j) { const char* p_ = kb_ + (size_t)j * RB; \
;         asm volatile("global_load_dwordx2 %0, %1, off" : "=&v"(sb[j]) : "v"(p_) : "memory"); } } while (0)
; #define MD_B_WAIT(sb, N) asm volatile("s_waitcnt vmcnt(%8)" : "+v"(sb[0]), "+v"(sb[1]), "+v"(sb[2]), "+v"(sb[3]), "+v"(sb[4]), "+v"(sb[5]), "+v"(sb[6]), "+v"(sb[7]) : "n"(N) : "memory")
; #define MD_END(last) do { if (last) asm volatile("s_waitcnt vmcnt(0)" ::: "memory"); else asm volatile("s_waitcnt vmcnt(8)" ::: "memory"); \
;         asm volatile("s_waitcnt lgkmcnt(0)" ::: "memory"); __builtin_amdgcn_s_barrier(); asm volatile("" ::: "memory"); } while (0)
; __device__ __forceinline__ void moe_down_stream(PG8_LAS unsigned char* lds, int e, int cb0, int slot0, int nv, const bf16_t* HIDp, const float* Wd, bf16_t* Y, const float* slot_w, const int* slot_dst) {
;     ...
;     for (int t = 0; t < NT; t += 2) {
;         if (t + 2 < NT) MD_B_WAIT(s1, 8); else MD_B_WAIT(s1, 0);
;         MD_B_WRITE(s1, 1); __builtin_amdgcn_sched_barrier(0); MD_GLDS_A(1, t + 1); __builtin_amdgcn_sched_barrier(0);
;         if (t + 3 < NT) MD_B_ISSUE(s1, t + 3);
;         MD_COMPUTE(0);
;         MD_END(t + 3 >= NT);
;         if (t + 2 < NT) { MD_B_WAIT(s0, 8); MD_B_WRITE(s0, 0); __builtin_amdgcn_sched_barrier(0); MD_GLDS_A(0, t + 2); __builtin_amdgcn_sched_barrier(0); }
;         if (t + 4 < NT) MD_B_ISSUE(s0, t + 4);
;         MD_COMPUTE(1);
;         MD_END(t + 4 >= NT);
	v_mfma_f32_16x16x32_bf16 v[78:81], v[238:241], v[218:221], v[78:81]
	v_mfma_f32_16x16x32_bf16 v[74:77], v[242:245], v[218:221], v[74:77]
	v_mfma_f32_16x16x32_bf16 v[70:73], v[246:249], v[218:221], v[70:73]
	v_mfma_f32_16x16x32_bf16 v[66:69], v[250:253], v[218:221], v[66:69]
	ds_read_b128 v[218:221], v93 offset:0
	ds_read_b128 v[142:145], v141 offset:0
	s_add_i32 s51, s51, 1
	s_and_b32 s54, s51, 7
	s_cmp_eq_u32 s54, 0
	s_cselect_b32 s44, s34, s35
	s_cselect_b32 s45, -1, 0
	v_lshl_add_u64 v[132:133], v[132:133], 0, s[44:45]
	global_load_dwordx2 v[202:203], v[132:133], off
	v_lshl_add_u64 v[180:181], v[132:133], 0, s[24:25]
	global_load_dwordx2 v[204:205], v[180:181], off
	v_mfma_f32_16x16x32_bf16 v[62:65], v[238:241], v[222:225], v[62:65]
	v_mfma_f32_16x16x32_bf16 v[58:61], v[242:245], v[222:225], v[58:61]
	v_mfma_f32_16x16x32_bf16 v[54:57], v[246:249], v[222:225], v[54:57]
	v_mfma_f32_16x16x32_bf16 v[50:53], v[250:253], v[222:225], v[50:53]
	ds_read_b128 v[222:225], v93 offset:2048
	ds_read_b128 v[146:149], v141 offset:2048
	v_lshl_add_u64 v[180:181], v[132:133], 0, s[26:27]
	global_load_dwordx2 v[206:207], v[180:181], off
	v_lshl_add_u64 v[180:181], v[132:133], 0, s[28:29]
	global_load_dwordx2 v[208:209], v[180:181], off
	v_mfma_f32_16x16x32_bf16 v[46:49], v[238:241], v[226:229], v[46:49]
	v_mfma_f32_16x16x32_bf16 v[42:45], v[242:245], v[226:229], v[42:45]
	v_mfma_f32_16x16x32_bf16 v[38:41], v[246:249], v[226:229], v[38:41]
	v_mfma_f32_16x16x32_bf16 v[34:37], v[250:253], v[226:229], v[34:37]
	ds_read_b128 v[226:229], v93 offset:4096
	ds_read_b128 v[156:159], v141 offset:4096
	v_lshl_add_u64 v[180:181], v[132:133], 0, s[36:37]
	global_load_dwordx2 v[210:211], v[180:181], off
	v_lshl_add_u64 v[180:181], v[132:133], 0, s[38:39]
	global_load_dwordx2 v[212:213], v[180:181], off
	v_mfma_f32_16x16x32_bf16 v[18:21], v[238:241], v[230:233], v[18:21]
	v_mfma_f32_16x16x32_bf16 v[22:25], v[242:245], v[230:233], v[22:25]
	v_mfma_f32_16x16x32_bf16 v[26:29], v[246:249], v[230:233], v[26:29]
	v_mfma_f32_16x16x32_bf16 v[30:33], v[250:253], v[230:233], v[30:33]
	ds_read_b128 v[230:233], v93 offset:6144
	ds_read_b128 v[160:163], v141 offset:6144
	v_lshl_add_u64 v[180:181], v[132:133], 0, s[40:41]
	global_load_dwordx2 v[214:215], v[180:181], off
	v_lshl_add_u64 v[180:181], v[132:133], 0, s[42:43]
	global_load_dwordx2 v[216:217], v[180:181], off
	v_mfma_f32_16x16x32_bf16 v[2:5], v[238:241], v[234:237], v[2:5]
	v_mfma_f32_16x16x32_bf16 v[6:9], v[242:245], v[234:237], v[6:9]
	v_mfma_f32_16x16x32_bf16 v[10:13], v[246:249], v[234:237], v[10:13]
	v_mfma_f32_16x16x32_bf16 v[14:17], v[250:253], v[234:237], v[14:17]
	ds_read_b128 v[234:237], v93 offset:8192
	s_waitcnt vmcnt(21)
	s_waitcnt lgkmcnt(0)
	s_barrier
	s_mov_b32 s49, s46
	s_mov_b32 s46, s47
	s_mov_b32 s47, s48
	s_mov_b32 s48, s49
	s_add_i32 s50, s50, 1
	s_add_i32 s49, s48, s74
	s_add_i32 s52, s52, 1
	s_and_b32 s54, s52, 7
	s_cmp_eq_u32 s54, 0
	s_cselect_b32 s54, s53, s32
	s_cselect_b32 s55, -1, 0
	s_add_u32 s30, s30, s54
	s_addc_u32 s31, s31, s55
	v_mfma_f32_16x16x32_bf16 v[78:81], v[142:145], v[218:221], v[78:81]
	v_mfma_f32_16x16x32_bf16 v[74:77], v[146:149], v[218:221], v[74:77]
	v_mfma_f32_16x16x32_bf16 v[70:73], v[156:159], v[218:221], v[70:73]
	v_mfma_f32_16x16x32_bf16 v[66:69], v[160:163], v[218:221], v[66:69]
	s_mov_b32 m0, s49
	s_nop 0
	global_load_lds_dwordx4 v88, s[30:31]
	v_mfma_f32_16x16x32_bf16 v[62:65], v[142:145], v[222:225], v[62:65]
	v_mfma_f32_16x16x32_bf16 v[58:61], v[146:149], v[222:225], v[58:61]
	v_mfma_f32_16x16x32_bf16 v[54:57], v[156:159], v[222:225], v[54:57]
	v_mfma_f32_16x16x32_bf16 v[50:53], v[160:163], v[222:225], v[50:53]
	s_add_i32 m0, s49, 0x2000
	s_nop 0
	global_load_lds_dwordx4 v90, s[30:31]
	v_mfma_f32_16x16x32_bf16 v[46:49], v[142:145], v[226:229], v[46:49]
	v_mfma_f32_16x16x32_bf16 v[42:45], v[146:149], v[226:229], v[42:45]
	v_mfma_f32_16x16x32_bf16 v[38:41], v[156:159], v[226:229], v[38:41]
	v_mfma_f32_16x16x32_bf16 v[34:37], v[160:163], v[226:229], v[34:37]
	s_add_i32 m0, s49, 0x4000
	s_nop 0
	global_load_lds_dwordx4 v92, s[30:31]
	v_mfma_f32_16x16x32_bf16 v[18:21], v[142:145], v[230:233], v[18:21]
	v_mfma_f32_16x16x32_bf16 v[22:25], v[146:149], v[230:233], v[22:25]
	v_mfma_f32_16x16x32_bf16 v[26:29], v[156:159], v[230:233], v[26:29]
	v_mfma_f32_16x16x32_bf16 v[30:33], v[160:163], v[230:233], v[30:33]
	s_add_i32 m0, s49, 0x6000
	s_nop 0
	global_load_lds_dwordx4 v94, s[30:31]
	v_mfma_f32_16x16x32_bf16 v[2:5], v[142:145], v[234:237], v[2:5]
	v_mfma_f32_16x16x32_bf16 v[6:9], v[146:149], v[234:237], v[6:9]
	v_mfma_f32_16x16x32_bf16 v[10:13], v[156:159], v[234:237], v[10:13]
	v_mfma_f32_16x16x32_bf16 v[14:17], v[160:163], v[234:237], v[14:17]
	s_add_i32 m0, s49, 0x8000
	s_nop 0
	global_load_lds_dwordx4 v96, s[30:31]
	v_cvt_pk_bf16_f32 v172, v98, v100
	v_cvt_pk_bf16_f32 v173, v102, v104
	v_cvt_pk_bf16_f32 v174, v106, v108
	v_cvt_pk_bf16_f32 v175, v110, v112
	v_cvt_pk_bf16_f32 v176, v99, v101
	v_cvt_pk_bf16_f32 v177, v103, v105
	v_cvt_pk_bf16_f32 v178, v107, v109
	v_cvt_pk_bf16_f32 v179, v111, v113
	ds_write_b128 v95, v[172:175] offset:0
	ds_write_b128 v95, v[176:179] offset:128
	v_add_u32_e32 v91, s46, v135
	v_add_u32_e32 v93, s46, v137
	ds_read_b128 v[238:241], v139 offset:19456
	ds_read_b128 v[242:245], v139 offset:21504
	ds_read_b128 v[246:249], v139 offset:23552
	ds_read_b128 v[250:253], v139 offset:25600
	ds_read_b128 v[218:221], v91 offset:0
	ds_read_b128 v[222:225], v91 offset:2048
	ds_read_b128 v[226:229], v91 offset:4096
	ds_read_b128 v[230:233], v91 offset:6144
	ds_read_b128 v[234:237], v91 offset:8192
	s_waitcnt lgkmcnt(0)
; #define MD_GLDS_A(buf, tau) do { _Pragma("unroll") for (int i = 0; i < 5; ++i) if (amask & (1u << i)) \
;         __builtin_amdgcn_global_load_lds((const unsigned*)((const char*)HIDp + aoff[i] + (size_t)((tau) & 7) * 128), (PG8_LAS unsigned*)(MD_SA(buf) + wid * 1024 + i * 8192), 16, 0, 0); } while (0)
; #define MD_B_ISSUE(sb, tau) do { const char* kb_ = Bb + (size_t)((tau) >> 3) * 512 + (size_t)((tau) & 7) * (64 * (size_t)RB); _Pragma("unroll") for (int j = 0; j < 8; ++j) { const char* p_ = kb_ + (size_t)j * RB; \
;         asm volatile("global_load_dwordx2 %0, %1, off" : "=&v"(sb[j]) : "v"(p_) : "memory"); } } while (0)
; #define MD_B_WAIT(sb, N) asm volatile("s_waitcnt vmcnt(%8)" : "+v"(sb[0]), "+v"(sb[1]), "+v"(sb[2]), "+v"(sb[3]), "+v"(sb[4]), "+v"(sb[5]), "+v"(sb[6]), "+v"(sb[7]) : "n"(N) : "memory")
; #define MD_END(last) do { if (last) asm volatile("s_waitcnt vmcnt(0)" ::: "memory"); else asm volatile("s_waitcnt vmcnt(8)" ::: "memory"); \
;         asm volatile("s_waitcnt lgkmcnt(0)" ::: "memory"); __builtin_amdgcn_s_barrier(); asm volatile("" ::: "memory"); } while (0)
; __device__ __forceinline__ void moe_down_stream(PG8_LAS unsigned char* lds, int e, int cb0, int slot0, int nv, const bf16_t* HIDp, const float* Wd, bf16_t* Y, const float* slot_w, const int* slot_dst) {
;     ...
;     for (int t = 0; t < NT; t += 2) {
;         if (t + 2 < NT) MD_B_WAIT(s1, 8); else MD_B_WAIT(s1, 0);
;         MD_B_WRITE(s1, 1); __builtin_amdgcn_sched_barrier(0); MD_GLDS_A(1, t + 1); __builtin_amdgcn_sched_barrier(0);
;         if (t + 3 < NT) MD_B_ISSUE(s1, t + 3);
;         MD_COMPUTE(0);
;         MD_END(t + 3 >= NT);
;         if (t + 2 < NT) { MD_B_WAIT(s0, 8); MD_B_WRITE(s0, 0); __builtin_amdgcn_sched_barrier(0); MD_GLDS_A(0, t + 2); __builtin_amdgcn_sched_barrier(0); }
;         if (t + 4 < NT) MD_B_ISSUE(s0, t + 4);
;         MD_COMPUTE(1);
;         MD_END(t + 4 >= NT);
;         if (((t + 1) & 7) == 7) {
;             const int cb = cb0 + ((t + 1) >> 3);
	v_mfma_f32_16x16x32_bf16 v[78:81], v[238:241], v[218:221], v[78:81]
	v_mfma_f32_16x16x32_bf16 v[74:77], v[242:245], v[218:221], v[74:77]
	v_mfma_f32_16x16x32_bf16 v[70:73], v[246:249], v[218:221], v[70:73]
	v_mfma_f32_16x16x32_bf16 v[66:69], v[250:253], v[218:221], v[66:69]
	ds_read_b128 v[218:221], v93 offset:0
	ds_read_b128 v[142:145], v141 offset:19456
	s_add_i32 s51, s51, 1
	s_and_b32 s54, s51, 7
	s_cmp_eq_u32 s54, 0
	s_cselect_b32 s44, s34, s35
	s_cselect_b32 s45, -1, 0
	v_lshl_add_u64 v[132:133], v[132:133], 0, s[44:45]
	global_load_dwordx2 v[98:99], v[132:133], off
	v_lshl_add_u64 v[180:181], v[132:133], 0, s[24:25]
	global_load_dwordx2 v[100:101], v[180:181], off
	v_mfma_f32_16x16x32_bf16 v[62:65], v[238:241], v[222:225], v[62:65]
	v_mfma_f32_16x16x32_bf16 v[58:61], v[242:245], v[222:225], v[58:61]
	v_mfma_f32_16x16x32_bf16 v[54:57], v[246:249], v[222:225], v[54:57]
	v_mfma_f32_16x16x32_bf16 v[50:53], v[250:253], v[222:225], v[50:53]
	ds_read_b128 v[222:225], v93 offset:2048
	ds_read_b128 v[146:149], v141 offset:21504
	v_lshl_add_u64 v[180:181], v[132:133], 0, s[26:27]
	global_load_dwordx2 v[102:103], v[180:181], off
	v_lshl_add_u64 v[180:181], v[132:133], 0, s[28:29]
	global_load_dwordx2 v[104:105], v[180:181], off
	v_mfma_f32_16x16x32_bf16 v[46:49], v[238:241], v[226:229], v[46:49]
	v_mfma_f32_16x16x32_bf16 v[42:45], v[242:245], v[226:229], v[42:45]
	v_mfma_f32_16x16x32_bf16 v[38:41], v[246:249], v[226:229], v[38:41]
	v_mfma_f32_16x16x32_bf16 v[34:37], v[250:253], v[226:229], v[34:37]
	ds_read_b128 v[226:229], v93 offset:4096
	ds_read_b128 v[156:159], v141 offset:23552
	v_lshl_add_u64 v[180:181], v[132:133], 0, s[36:37]
	global_load_dwordx2 v[106:107], v[180:181], off
	v_lshl_add_u64 v[180:181], v[132:133], 0, s[38:39]
	global_load_dwordx2 v[108:109], v[180:181], off
	v_mfma_f32_16x16x32_bf16 v[18:21], v[238:241], v[230:233], v[18:21]
	v_mfma_f32_16x16x32_bf16 v[22:25], v[242:245], v[230:233], v[22:25]
	v_mfma_f32_16x16x32_bf16 v[26:29], v[246:249], v[230:233], v[26:29]
	v_mfma_f32_16x16x32_bf16 v[30:33], v[250:253], v[230:233], v[30:33]
	ds_read_b128 v[230:233], v93 offset:6144
	ds_read_b128 v[160:163], v141 offset:25600
	v_lshl_add_u64 v[180:181], v[132:133], 0, s[40:41]
	global_load_dwordx2 v[110:111], v[180:181], off
	v_lshl_add_u64 v[180:181], v[132:133], 0, s[42:43]
	global_load_dwordx2 v[112:113], v[180:181], off
	v_mfma_f32_16x16x32_bf16 v[2:5], v[238:241], v[234:237], v[2:5]
	v_mfma_f32_16x16x32_bf16 v[6:9], v[242:245], v[234:237], v[6:9]
	v_mfma_f32_16x16x32_bf16 v[10:13], v[246:249], v[234:237], v[10:13]
	v_mfma_f32_16x16x32_bf16 v[14:17], v[250:253], v[234:237], v[14:17]
	ds_read_b128 v[234:237], v93 offset:8192
	s_waitcnt vmcnt(21)
	s_waitcnt lgkmcnt(0)
	s_barrier
	s_mov_b32 s49, s46
	s_mov_b32 s46, s47
	s_mov_b32 s47, s48
	s_mov_b32 s48, s49
	s_add_i32 s50, s50, 1
	s_mov_b32 s56, 13
.Lmd_loop_Y:
	v_mfma_f32_16x16x32_bf16 v[78:81], v[142:145], v[218:221], v[78:81]
	v_mfma_f32_16x16x32_bf16 v[74:77], v[146:149], v[218:221], v[74:77]
	v_mfma_f32_16x16x32_bf16 v[70:73], v[156:159], v[218:221], v[70:73]
	v_mfma_f32_16x16x32_bf16 v[66:69], v[160:163], v[218:221], v[66:69]
	v_mfma_f32_16x16x32_bf16 v[62:65], v[142:145], v[222:225], v[62:65]
	v_mfma_f32_16x16x32_bf16 v[58:61], v[146:149], v[222:225], v[58:61]
	v_mfma_f32_16x16x32_bf16 v[54:57], v[156:159], v[222:225], v[54:57]
	v_mfma_f32_16x16x32_bf16 v[50:53], v[160:163], v[222:225], v[50:53]
	v_mfma_f32_16x16x32_bf16 v[46:49], v[142:145], v[226:229], v[46:49]
	v_mfma_f32_16x16x32_bf16 v[42:45], v[146:149], v[226:229], v[42:45]
	v_mfma_f32_16x16x32_bf16 v[38:41], v[156:159], v[226:229], v[38:41]
	v_mfma_f32_16x16x32_bf16 v[34:37], v[160:163], v[226:229], v[34:37]
	v_mfma_f32_16x16x32_bf16 v[18:21], v[142:145], v[230:233], v[18:21]
	v_mfma_f32_16x16x32_bf16 v[22:25], v[146:149], v[230:233], v[22:25]
	v_mfma_f32_16x16x32_bf16 v[26:29], v[156:159], v[230:233], v[26:29]
	v_mfma_f32_16x16x32_bf16 v[30:33], v[160:163], v[230:233], v[30:33]
	v_mfma_f32_16x16x32_bf16 v[2:5], v[142:145], v[234:237], v[2:5]
	v_mfma_f32_16x16x32_bf16 v[6:9], v[146:149], v[234:237], v[6:9]
	v_mfma_f32_16x16x32_bf16 v[10:13], v[156:159], v[234:237], v[10:13]
	v_mfma_f32_16x16x32_bf16 v[14:17], v[160:163], v[234:237], v[14:17]
	s_and_b32 s54, s50, 7
	s_cmp_lg_u32 s54, 0
	s_cbranch_scc1 .Lmd_noepi_Y
; #define PG8_LAS __attribute__((address_space(3)))
; __device__ __forceinline__ unsigned cvtpk(float lo, float hi) { f32x2 v = {lo, hi}; bf16x2_t b = __builtin_convertvector(v, bf16x2_t); return __builtin_bit_cast(unsigned, b); }
; __device__ __forceinline__ void moe_down_stream(PG8_LAS unsigned char* lds, int e, int cb0, int slot0, int nv, const bf16_t* HIDp, const float* Wd, bf16_t* Y, const float* slot_w, const int* slot_dst) {
;     ...
;         if (((t + 1) & 7) == 7) {
;             const int cb = cb0 + ((t + 1) >> 3);
; #pragma unroll
;             for (int m = 0; m < DNM; ++m) {
;                 const float w_ = lw[4 * (16 * m + fr) + wr];
; #pragma unroll
;                 for (int p = 0; p < 2; ++p) { const f32x4 v0 = acc[m][2 * p] * w_, v1 = acc[m][2 * p + 1] * w_; u32x4 w; w.x = cvtpk(v0[0], v0[1]); w.y = cvtpk(v0[2], v0[3]); w.z = cvtpk(v1[0], v1[1]); w.w = cvtpk(v1[2], v1[3]);
;                     *(PG8_LAS u32x4*)(stg + fr * 128 + (((4 * p + fq) ^ (fr & 7)) * 16)) = w; }
; #pragma unroll
;                 for (int hh = 0; hh < 2; ++hh) { const int r = (lane >> 3) + 8 * hh, cc = lane & 7; const u32x4 d = *(const PG8_LAS u32x4*)(stg + r * 128 + ((cc ^ (r & 7)) * 16)); const int dst_ = ldst[4 * (16 * m + r) + wr];
;                     if (dst_ >= 0) *(u32x4*)(Y + (size_t)dst_ * D + 128 * cb + 64 * wc + 8 * cc) = d; }
; #pragma unroll
;                 for (int n = 0; n < 4; ++n) acc[m][n] = (f32x4){0.f, 0.f, 0.f, 0.f}; } }
	s_add_i32 s54, s48, s74
	v_add_u32_e32 v164, s54, v84
	v_add_u32_e32 v165, s54, v85
	ds_read_b32 v150, v82 offset:0
	ds_read_b32 v151, v83 offset:0
	ds_read_b32 v166, v83 offset:128
	s_waitcnt lgkmcnt(2)
	v_mul_f32_e32 v78, v150, v78
	v_mul_f32_e32 v79, v150, v79
	v_mul_f32_e32 v80, v150, v80
	v_mul_f32_e32 v81, v150, v81
	v_mul_f32_e32 v74, v150, v74
	v_mul_f32_e32 v75, v150, v75
	v_mul_f32_e32 v76, v150, v76
	v_mul_f32_e32 v77, v150, v77
	v_cvt_pk_bf16_f32 v182, v78, v79
	v_cvt_pk_bf16_f32 v183, v80, v81
	v_cvt_pk_bf16_f32 v184, v74, v75
	v_cvt_pk_bf16_f32 v185, v76, v77
	ds_write_b128 v164, v[182:185]
	v_mul_f32_e32 v70, v150, v70
	v_mul_f32_e32 v71, v150, v71
	v_mul_f32_e32 v72, v150, v72
	v_mul_f32_e32 v73, v150, v73
	v_mul_f32_e32 v66, v150, v66
	v_mul_f32_e32 v67, v150, v67
	v_mul_f32_e32 v68, v150, v68
	v_mul_f32_e32 v69, v150, v69
	v_cvt_pk_bf16_f32 v182, v70, v71
	v_cvt_pk_bf16_f32 v183, v72, v73
	v_cvt_pk_bf16_f32 v184, v66, v67
	v_cvt_pk_bf16_f32 v185, v68, v69
	v_xor_b32_e32 v167, 64, v164
	ds_write_b128 v167, v[182:185]
	v_mov_b32_e32 v78, 0
	v_mov_b32_e32 v74, 0
	v_mov_b32_e32 v70, 0
	v_mov_b32_e32 v66, 0
	v_mov_b32_e32 v79, 0
	v_mov_b32_e32 v75, 0
	v_mov_b32_e32 v71, 0
	v_mov_b32_e32 v67, 0
	v_mov_b32_e32 v80, 0
	v_mov_b32_e32 v76, 0
	v_mov_b32_e32 v72, 0
	v_mov_b32_e32 v68, 0
	v_mov_b32_e32 v81, 0
	v_mov_b32_e32 v77, 0
	v_mov_b32_e32 v73, 0
	v_mov_b32_e32 v69, 0
	ds_read_b128 v[182:185], v165 offset:0
	v_cmp_lt_i32_e32 vcc, -1, v151
	v_lshlrev_b32_e32 v148, 13, v151
	v_mov_b32_e32 v149, 0
	v_lshl_add_u64 v[148:149], v[148:149], 0, v[86:87]
	v_cndmask_b32_e32 v148, v168, v148, vcc
	v_cndmask_b32_e32 v149, v169, v149, vcc
	s_waitcnt lgkmcnt(0)
	global_store_dwordx4 v[148:149], v[182:185], off
	ds_read_b128 v[182:185], v165 offset:8192
	v_cmp_lt_i32_e32 vcc, -1, v166
	v_lshlrev_b32_e32 v148, 13, v166
	v_mov_b32_e32 v149, 0
	v_lshl_add_u64 v[148:149], v[148:149], 0, v[86:87]
	v_cndmask_b32_e32 v148, v168, v148, vcc
	v_cndmask_b32_e32 v149, v169, v149, vcc
	s_waitcnt lgkmcnt(0)
	global_store_dwordx4 v[148:149], v[182:185], off
	ds_read_b32 v150, v82 offset:256
	ds_read_b32 v151, v83 offset:256
	ds_read_b32 v166, v83 offset:384
	s_waitcnt lgkmcnt(2)
	v_mul_f32_e32 v62, v150, v62
	v_mul_f32_e32 v63, v150, v63
	v_mul_f32_e32 v64, v150, v64
	v_mul_f32_e32 v65, v150, v65
	v_mul_f32_e32 v58, v150, v58
	v_mul_f32_e32 v59, v150, v59
	v_mul_f32_e32 v60, v150, v60
	v_mul_f32_e32 v61, v150, v61
	v_cvt_pk_bf16_f32 v182, v62, v63
	v_cvt_pk_bf16_f32 v183, v64, v65
	v_cvt_pk_bf16_f32 v184, v58, v59
	v_cvt_pk_bf16_f32 v185, v60, v61
	ds_write_b128 v164, v[182:185]
	v_mul_f32_e32 v54, v150, v54
	v_mul_f32_e32 v55, v150, v55
	v_mul_f32_e32 v56, v150, v56
	v_mul_f32_e32 v57, v150, v57
	v_mul_f32_e32 v50, v150, v50
	v_mul_f32_e32 v51, v150, v51
	v_mul_f32_e32 v52, v150, v52
	v_mul_f32_e32 v53, v150, v53
	v_cvt_pk_bf16_f32 v182, v54, v55
	v_cvt_pk_bf16_f32 v183, v56, v57
	v_cvt_pk_bf16_f32 v184, v50, v51
	v_cvt_pk_bf16_f32 v185, v52, v53
	v_xor_b32_e32 v167, 64, v164
	ds_write_b128 v167, v[182:185]
	v_mov_b32_e32 v62, 0
	v_mov_b32_e32 v58, 0
	v_mov_b32_e32 v54, 0
	v_mov_b32_e32 v50, 0
	v_mov_b32_e32 v63, 0
	v_mov_b32_e32 v59, 0
	v_mov_b32_e32 v55, 0
	v_mov_b32_e32 v51, 0
	v_mov_b32_e32 v64, 0
	v_mov_b32_e32 v60, 0
	v_mov_b32_e32 v56, 0
	v_mov_b32_e32 v52, 0
	v_mov_b32_e32 v65, 0
	v_mov_b32_e32 v61, 0
	v_mov_b32_e32 v57, 0
	v_mov_b32_e32 v53, 0
	ds_read_b128 v[182:185], v165 offset:0
	v_cmp_lt_i32_e32 vcc, -1, v151
	v_lshlrev_b32_e32 v148, 13, v151
	v_mov_b32_e32 v149, 0
	v_lshl_add_u64 v[148:149], v[148:149], 0, v[86:87]
	v_cndmask_b32_e32 v148, v168, v148, vcc
	v_cndmask_b32_e32 v149, v169, v149, vcc
	s_waitcnt lgkmcnt(0)
	global_store_dwordx4 v[148:149], v[182:185], off
	ds_read_b128 v[182:185], v165 offset:8192
	v_cmp_lt_i32_e32 vcc, -1, v166
	v_lshlrev_b32_e32 v148, 13, v166
	v_mov_b32_e32 v149, 0
	v_lshl_add_u64 v[148:149], v[148:149], 0, v[86:87]
	v_cndmask_b32_e32 v148, v168, v148, vcc
	v_cndmask_b32_e32 v149, v169, v149, vcc
	s_waitcnt lgkmcnt(0)
	global_store_dwordx4 v[148:149], v[182:185], off
	ds_read_b32 v150, v82 offset:512
	ds_read_b32 v151, v83 offset:512
	ds_read_b32 v166, v83 offset:640
	s_waitcnt lgkmcnt(2)
	v_mul_f32_e32 v46, v150, v46
	v_mul_f32_e32 v47, v150, v47
	v_mul_f32_e32 v48, v150, v48
	v_mul_f32_e32 v49, v150, v49
	v_mul_f32_e32 v42, v150, v42
	v_mul_f32_e32 v43, v150, v43
	v_mul_f32_e32 v44, v150, v44
	v_mul_f32_e32 v45, v150, v45
	v_cvt_pk_bf16_f32 v182, v46, v47
	v_cvt_pk_bf16_f32 v183, v48, v49
	v_cvt_pk_bf16_f32 v184, v42, v43
	v_cvt_pk_bf16_f32 v185, v44, v45
	ds_write_b128 v164, v[182:185]
	v_mul_f32_e32 v38, v150, v38
	v_mul_f32_e32 v39, v150, v39
	v_mul_f32_e32 v40, v150, v40
	v_mul_f32_e32 v41, v150, v41
	v_mul_f32_e32 v34, v150, v34
	v_mul_f32_e32 v35, v150, v35
	v_mul_f32_e32 v36, v150, v36
	v_mul_f32_e32 v37, v150, v37
	v_cvt_pk_bf16_f32 v182, v38, v39
	v_cvt_pk_bf16_f32 v183, v40, v41
	v_cvt_pk_bf16_f32 v184, v34, v35
	v_cvt_pk_bf16_f32 v185, v36, v37
	v_xor_b32_e32 v167, 64, v164
	ds_write_b128 v167, v[182:185]
	v_mov_b32_e32 v46, 0
	v_mov_b32_e32 v42, 0
	v_mov_b32_e32 v38, 0
	v_mov_b32_e32 v34, 0
	v_mov_b32_e32 v47, 0
	v_mov_b32_e32 v43, 0
	v_mov_b32_e32 v39, 0
	v_mov_b32_e32 v35, 0
	v_mov_b32_e32 v48, 0
	v_mov_b32_e32 v44, 0
	v_mov_b32_e32 v40, 0
	v_mov_b32_e32 v36, 0
	v_mov_b32_e32 v49, 0
	v_mov_b32_e32 v45, 0
	v_mov_b32_e32 v41, 0
	v_mov_b32_e32 v37, 0
	ds_read_b128 v[182:185], v165 offset:0
	v_cmp_lt_i32_e32 vcc, -1, v151
	v_lshlrev_b32_e32 v148, 13, v151
	v_mov_b32_e32 v149, 0
	v_lshl_add_u64 v[148:149], v[148:149], 0, v[86:87]
	v_cndmask_b32_e32 v148, v168, v148, vcc
	v_cndmask_b32_e32 v149, v169, v149, vcc
	s_waitcnt lgkmcnt(0)
; #define PG8_LAS __attribute__((address_space(3)))
; __device__ __forceinline__ unsigned cvtpk(float lo, float hi) { f32x2 v = {lo, hi}; bf16x2_t b = __builtin_convertvector(v, bf16x2_t); return __builtin_bit_cast(unsigned, b); }
; __device__ __forceinline__ void moe_down_stream(PG8_LAS unsigned char* lds, int e, int cb0, int slot0, int nv, const bf16_t* HIDp, const float* Wd, bf16_t* Y, const float* slot_w, const int* slot_dst) {
;     ...
;         if (((t + 1) & 7) == 7) {
;             const int cb = cb0 + ((t + 1) >> 3);
; #pragma unroll
;             for (int m = 0; m < DNM; ++m) {
;                 const float w_ = lw[4 * (16 * m + fr) + wr];
; #pragma unroll
;                 for (int p = 0; p < 2; ++p) { const f32x4 v0 = acc[m][2 * p] * w_, v1 = acc[m][2 * p + 1] * w_; u32x4 w; w.x = cvtpk(v0[0], v0[1]); w.y = cvtpk(v0[2], v0[3]); w.z = cvtpk(v1[0], v1[1]); w.w = cvtpk(v1[2], v1[3]);
;                     *(PG8_LAS u32x4*)(stg + fr * 128 + (((4 * p + fq) ^ (fr & 7)) * 16)) = w; }
; #pragma unroll
;                 for (int hh = 0; hh < 2; ++hh) { const int r = (lane >> 3) + 8 * hh, cc = lane & 7; const u32x4 d = *(const PG8_LAS u32x4*)(stg + r * 128 + ((cc ^ (r & 7)) * 16)); const int dst_ = ldst[4 * (16 * m + r) + wr];
;                     if (dst_ >= 0) *(u32x4*)(Y + (size_t)dst_ * D + 128 * cb + 64 * wc + 8 * cc) = d; }
; #pragma unroll
;                 for (int n = 0; n < 4; ++n) acc[m][n] = (f32x4){0.f, 0.f, 0.f, 0.f}; } }
	global_store_dwordx4 v[148:149], v[182:185], off
	ds_read_b128 v[182:185], v165 offset:8192
	v_cmp_lt_i32_e32 vcc, -1, v166
	v_lshlrev_b32_e32 v148, 13, v166
	v_mov_b32_e32 v149, 0
	v_lshl_add_u64 v[148:149], v[148:149], 0, v[86:87]
	v_cndmask_b32_e32 v148, v168, v148, vcc
	v_cndmask_b32_e32 v149, v169, v149, vcc
	s_waitcnt lgkmcnt(0)
	global_store_dwordx4 v[148:149], v[182:185], off
	ds_read_b32 v150, v82 offset:768
	ds_read_b32 v151, v83 offset:768
	ds_read_b32 v166, v83 offset:896
	s_waitcnt lgkmcnt(2)
	v_mul_f32_e32 v18, v150, v18
	v_mul_f32_e32 v19, v150, v19
	v_mul_f32_e32 v20, v150, v20
	v_mul_f32_e32 v21, v150, v21
	v_mul_f32_e32 v22, v150, v22
	v_mul_f32_e32 v23, v150, v23
	v_mul_f32_e32 v24, v150, v24
	v_mul_f32_e32 v25, v150, v25
	v_cvt_pk_bf16_f32 v182, v18, v19
	v_cvt_pk_bf16_f32 v183, v20, v21
	v_cvt_pk_bf16_f32 v184, v22, v23
	v_cvt_pk_bf16_f32 v185, v24, v25
	ds_write_b128 v164, v[182:185]
	v_mul_f32_e32 v26, v150, v26
	v_mul_f32_e32 v27, v150, v27
	v_mul_f32_e32 v28, v150, v28
	v_mul_f32_e32 v29, v150, v29
	v_mul_f32_e32 v30, v150, v30
	v_mul_f32_e32 v31, v150, v31
	v_mul_f32_e32 v32, v150, v32
	v_mul_f32_e32 v33, v150, v33
	v_cvt_pk_bf16_f32 v182, v26, v27
	v_cvt_pk_bf16_f32 v183, v28, v29
	v_cvt_pk_bf16_f32 v184, v30, v31
	v_cvt_pk_bf16_f32 v185, v32, v33
	v_xor_b32_e32 v167, 64, v164
	ds_write_b128 v167, v[182:185]
	v_mov_b32_e32 v18, 0
	v_mov_b32_e32 v22, 0
	v_mov_b32_e32 v26, 0
	v_mov_b32_e32 v30, 0
	v_mov_b32_e32 v19, 0
	v_mov_b32_e32 v23, 0
	v_mov_b32_e32 v27, 0
	v_mov_b32_e32 v31, 0
	v_mov_b32_e32 v20, 0
	v_mov_b32_e32 v24, 0
	v_mov_b32_e32 v28, 0
	v_mov_b32_e32 v32, 0
	v_mov_b32_e32 v21, 0
	v_mov_b32_e32 v25, 0
	v_mov_b32_e32 v29, 0
	v_mov_b32_e32 v33, 0
	ds_read_b128 v[182:185], v165 offset:0
	v_cmp_lt_i32_e32 vcc, -1, v151
	v_lshlrev_b32_e32 v148, 13, v151
	v_mov_b32_e32 v149, 0
	v_lshl_add_u64 v[148:149], v[148:149], 0, v[86:87]
	v_cndmask_b32_e32 v148, v168, v148, vcc
	v_cndmask_b32_e32 v149, v169, v149, vcc
	s_waitcnt lgkmcnt(0)
	global_store_dwordx4 v[148:149], v[182:185], off
	ds_read_b128 v[182:185], v165 offset:8192
	v_cmp_lt_i32_e32 vcc, -1, v166
	v_lshlrev_b32_e32 v148, 13, v166
	v_mov_b32_e32 v149, 0
	v_lshl_add_u64 v[148:149], v[148:149], 0, v[86:87]
	v_cndmask_b32_e32 v148, v168, v148, vcc
	v_cndmask_b32_e32 v149, v169, v149, vcc
	s_waitcnt lgkmcnt(0)
	global_store_dwordx4 v[148:149], v[182:185], off
	ds_read_b32 v150, v82 offset:1024
	ds_read_b32 v151, v83 offset:1024
	ds_read_b32 v166, v83 offset:1152
	s_waitcnt lgkmcnt(2)
	v_mul_f32_e32 v2, v150, v2
	v_mul_f32_e32 v3, v150, v3
	v_mul_f32_e32 v4, v150, v4
	v_mul_f32_e32 v5, v150, v5
	v_mul_f32_e32 v6, v150, v6
	v_mul_f32_e32 v7, v150, v7
	v_mul_f32_e32 v8, v150, v8
	v_mul_f32_e32 v9, v150, v9
	v_cvt_pk_bf16_f32 v182, v2, v3
	v_cvt_pk_bf16_f32 v183, v4, v5
	v_cvt_pk_bf16_f32 v184, v6, v7
	v_cvt_pk_bf16_f32 v185, v8, v9
	ds_write_b128 v164, v[182:185]
	v_mul_f32_e32 v10, v150, v10
	v_mul_f32_e32 v11, v150, v11
	v_mul_f32_e32 v12, v150, v12
	v_mul_f32_e32 v13, v150, v13
	v_mul_f32_e32 v14, v150, v14
	v_mul_f32_e32 v15, v150, v15
	v_mul_f32_e32 v16, v150, v16
	v_mul_f32_e32 v17, v150, v17
	v_cvt_pk_bf16_f32 v182, v10, v11
	v_cvt_pk_bf16_f32 v183, v12, v13
	v_cvt_pk_bf16_f32 v184, v14, v15
	v_cvt_pk_bf16_f32 v185, v16, v17
	v_xor_b32_e32 v167, 64, v164
	ds_write_b128 v167, v[182:185]
	v_mov_b32_e32 v2, 0
	v_mov_b32_e32 v6, 0
	v_mov_b32_e32 v10, 0
	v_mov_b32_e32 v14, 0
	v_mov_b32_e32 v3, 0
	v_mov_b32_e32 v7, 0
	v_mov_b32_e32 v11, 0
	v_mov_b32_e32 v15, 0
	v_mov_b32_e32 v4, 0
	v_mov_b32_e32 v8, 0
	v_mov_b32_e32 v12, 0
	v_mov_b32_e32 v16, 0
	v_mov_b32_e32 v5, 0
	v_mov_b32_e32 v9, 0
	v_mov_b32_e32 v13, 0
	v_mov_b32_e32 v17, 0
	ds_read_b128 v[182:185], v165 offset:0
	v_cmp_lt_i32_e32 vcc, -1, v151
	v_lshlrev_b32_e32 v148, 13, v151
	v_mov_b32_e32 v149, 0
	v_lshl_add_u64 v[148:149], v[148:149], 0, v[86:87]
	v_cndmask_b32_e32 v148, v168, v148, vcc
	v_cndmask_b32_e32 v149, v169, v149, vcc
	s_waitcnt lgkmcnt(0)
	global_store_dwordx4 v[148:149], v[182:185], off
	ds_read_b128 v[182:185], v165 offset:8192
	v_cmp_lt_i32_e32 vcc, -1, v166
	v_lshlrev_b32_e32 v148, 13, v166
	v_mov_b32_e32 v149, 0
	v_lshl_add_u64 v[148:149], v[148:149], 0, v[86:87]
	v_cndmask_b32_e32 v148, v168, v148, vcc
	v_cndmask_b32_e32 v149, v169, v149, vcc
	s_waitcnt lgkmcnt(0)
	global_store_dwordx4 v[148:149], v[182:185], off
	v_add_co_u32_e32 v86, vcc, 0x400, v86
	s_nop 1
	v_addc_co_u32_e32 v87, vcc, 0, v87, vcc
	s_waitcnt lgkmcnt(0)
; #define MD_GLDS_A(buf, tau) do { _Pragma("unroll") for (int i = 0; i < 5; ++i) if (amask & (1u << i)) \
;         __builtin_amdgcn_global_load_lds((const unsigned*)((const char*)HIDp + aoff[i] + (size_t)((tau) & 7) * 128), (PG8_LAS unsigned*)(MD_SA(buf) + wid * 1024 + i * 8192), 16, 0, 0); } while (0)
; #define MD_B_ISSUE(sb, tau) do { const char* kb_ = Bb + (size_t)((tau) >> 3) * 512 + (size_t)((tau) & 7) * (64 * (size_t)RB); _Pragma("unroll") for (int j = 0; j < 8; ++j) { const char* p_ = kb_ + (size_t)j * RB; \
;         asm volatile("global_load_dwordx2 %0, %1, off" : "=&v"(sb[j]) : "v"(p_) : "memory"); } } while (0)
; #define MD_B_WAIT(sb, N) asm volatile("s_waitcnt vmcnt(%8)" : "+v"(sb[0]), "+v"(sb[1]), "+v"(sb[2]), "+v"(sb[3]), "+v"(sb[4]), "+v"(sb[5]), "+v"(sb[6]), "+v"(sb[7]) : "n"(N) : "memory")
; #define MD_END(last) do { if (last) asm volatile("s_waitcnt vmcnt(0)" ::: "memory"); else asm volatile("s_waitcnt vmcnt(8)" ::: "memory"); \
;         asm volatile("s_waitcnt lgkmcnt(0)" ::: "memory"); __builtin_amdgcn_s_barrier(); asm volatile("" ::: "memory"); } while (0)
; __device__ __forceinline__ void moe_down_stream(PG8_LAS unsigned char* lds, int e, int cb0, int slot0, int nv, const bf16_t* HIDp, const float* Wd, bf16_t* Y, const float* slot_w, const int* slot_dst) {
;     ...
;     for (int t = 0; t < NT; t += 2) {
;         if (t + 2 < NT) MD_B_WAIT(s1, 8); else MD_B_WAIT(s1, 0);
;         MD_B_WRITE(s1, 1); __builtin_amdgcn_sched_barrier(0); MD_GLDS_A(1, t + 1); __builtin_amdgcn_sched_barrier(0);
;         if (t + 3 < NT) MD_B_ISSUE(s1, t + 3);
;         MD_COMPUTE(0);
;         MD_END(t + 3 >= NT);
;         if (t + 2 < NT) { MD_B_WAIT(s0, 8); MD_B_WRITE(s0, 0); __builtin_amdgcn_sched_barrier(0); MD_GLDS_A(0, t + 2); __builtin_amdgcn_sched_barrier(0); }
;         if (t + 4 < NT) MD_B_ISSUE(s0, t + 4);
;         MD_COMPUTE(1);
;         MD_END(t + 4 >= NT);
.Lmd_noepi_Y:
	s_add_i32 s49, s48, s74
	s_add_i32 s52, s52, 1
	s_and_b32 s54, s52, 7
	s_cmp_eq_u32 s54, 0
	s_cselect_b32 s54, s53, s32
	s_cselect_b32 s55, -1, 0
	s_add_u32 s30, s30, s54
	s_addc_u32 s31, s31, s55
	s_mov_b32 m0, s49
	s_nop 0
	global_load_lds_dwordx4 v88, s[30:31]
	s_add_i32 m0, s49, 0x2000
	s_nop 0
	global_load_lds_dwordx4 v90, s[30:31]
	s_add_i32 m0, s49, 0x4000
	s_nop 0
	global_load_lds_dwordx4 v92, s[30:31]
	s_add_i32 m0, s49, 0x6000
	s_nop 0
	global_load_lds_dwordx4 v94, s[30:31]
	s_add_i32 m0, s49, 0x8000
	s_nop 0
	global_load_lds_dwordx4 v96, s[30:31]
	v_cvt_pk_bf16_f32 v172, v114, v116
	v_cvt_pk_bf16_f32 v173, v118, v120
	v_cvt_pk_bf16_f32 v174, v122, v124
	v_cvt_pk_bf16_f32 v175, v126, v128
	v_cvt_pk_bf16_f32 v176, v115, v117
	v_cvt_pk_bf16_f32 v177, v119, v121
	v_cvt_pk_bf16_f32 v178, v123, v125
	v_cvt_pk_bf16_f32 v179, v127, v129
	ds_write_b128 v95, v[172:175] offset:19456
	ds_write_b128 v95, v[176:179] offset:19584
	v_add_u32_e32 v91, s46, v135
	v_add_u32_e32 v93, s46, v137
	ds_read_b128 v[238:241], v139 offset:0
	ds_read_b128 v[242:245], v139 offset:2048
	ds_read_b128 v[246:249], v139 offset:4096
	ds_read_b128 v[250:253], v139 offset:6144
	ds_read_b128 v[218:221], v91 offset:0
	ds_read_b128 v[222:225], v91 offset:2048
	ds_read_b128 v[226:229], v91 offset:4096
	ds_read_b128 v[230:233], v91 offset:6144
	ds_read_b128 v[234:237], v91 offset:8192
	s_waitcnt lgkmcnt(0)
	v_mfma_f32_16x16x32_bf16 v[78:81], v[238:241], v[218:221], v[78:81]
	v_mfma_f32_16x16x32_bf16 v[74:77], v[242:245], v[218:221], v[74:77]
	v_mfma_f32_16x16x32_bf16 v[70:73], v[246:249], v[218:221], v[70:73]
	v_mfma_f32_16x16x32_bf16 v[66:69], v[250:253], v[218:221], v[66:69]
	ds_read_b128 v[218:221], v93 offset:0
	ds_read_b128 v[142:145], v141 offset:0
	s_add_i32 s51, s51, 1
	s_and_b32 s54, s51, 7
	s_cmp_eq_u32 s54, 0
	s_cselect_b32 s44, s34, s35
	s_cselect_b32 s45, -1, 0
	v_lshl_add_u64 v[132:133], v[132:133], 0, s[44:45]
	global_load_dwordx2 v[114:115], v[132:133], off
	v_lshl_add_u64 v[180:181], v[132:133], 0, s[24:25]
	global_load_dwordx2 v[116:117], v[180:181], off
	v_mfma_f32_16x16x32_bf16 v[62:65], v[238:241], v[222:225], v[62:65]
	v_mfma_f32_16x16x32_bf16 v[58:61], v[242:245], v[222:225], v[58:61]
	v_mfma_f32_16x16x32_bf16 v[54:57], v[246:249], v[222:225], v[54:57]
	v_mfma_f32_16x16x32_bf16 v[50:53], v[250:253], v[222:225], v[50:53]
	ds_read_b128 v[222:225], v93 offset:2048
	ds_read_b128 v[146:149], v141 offset:2048
	v_lshl_add_u64 v[180:181], v[132:133], 0, s[26:27]
	global_load_dwordx2 v[118:119], v[180:181], off
	v_lshl_add_u64 v[180:181], v[132:133], 0, s[28:29]
	global_load_dwordx2 v[120:121], v[180:181], off
	v_mfma_f32_16x16x32_bf16 v[46:49], v[238:241], v[226:229], v[46:49]
	v_mfma_f32_16x16x32_bf16 v[42:45], v[242:245], v[226:229], v[42:45]
	v_mfma_f32_16x16x32_bf16 v[38:41], v[246:249], v[226:229], v[38:41]
	v_mfma_f32_16x16x32_bf16 v[34:37], v[250:253], v[226:229], v[34:37]
	ds_read_b128 v[226:229], v93 offset:4096
	ds_read_b128 v[156:159], v141 offset:4096
	v_lshl_add_u64 v[180:181], v[132:133], 0, s[36:37]
	global_load_dwordx2 v[122:123], v[180:181], off
	v_lshl_add_u64 v[180:181], v[132:133], 0, s[38:39]
	global_load_dwordx2 v[124:125], v[180:181], off
	v_mfma_f32_16x16x32_bf16 v[18:21], v[238:241], v[230:233], v[18:21]
	v_mfma_f32_16x16x32_bf16 v[22:25], v[242:245], v[230:233], v[22:25]
	v_mfma_f32_16x16x32_bf16 v[26:29], v[246:249], v[230:233], v[26:29]
	v_mfma_f32_16x16x32_bf16 v[30:33], v[250:253], v[230:233], v[30:33]
	ds_read_b128 v[230:233], v93 offset:6144
	ds_read_b128 v[160:163], v141 offset:6144
	v_lshl_add_u64 v[180:181], v[132:133], 0, s[40:41]
	global_load_dwordx2 v[126:127], v[180:181], off
	v_lshl_add_u64 v[180:181], v[132:133], 0, s[42:43]
	global_load_dwordx2 v[128:129], v[180:181], off
	v_mfma_f32_16x16x32_bf16 v[2:5], v[238:241], v[234:237], v[2:5]
	v_mfma_f32_16x16x32_bf16 v[6:9], v[242:245], v[234:237], v[6:9]
	v_mfma_f32_16x16x32_bf16 v[10:13], v[246:249], v[234:237], v[10:13]
	v_mfma_f32_16x16x32_bf16 v[14:17], v[250:253], v[234:237], v[14:17]
	ds_read_b128 v[234:237], v93 offset:8192
	s_waitcnt vmcnt(21)
	s_waitcnt lgkmcnt(0)
	s_barrier
	s_mov_b32 s49, s46
	s_mov_b32 s46, s47
	s_mov_b32 s47, s48
	s_mov_b32 s48, s49
	s_add_i32 s50, s50, 1
	s_add_i32 s49, s48, s74
	s_add_i32 s52, s52, 1
	s_and_b32 s54, s52, 7
	s_cmp_eq_u32 s54, 0
	s_cselect_b32 s54, s53, s32
	s_cselect_b32 s55, -1, 0
	s_add_u32 s30, s30, s54
	s_addc_u32 s31, s31, s55
	v_mfma_f32_16x16x32_bf16 v[78:81], v[142:145], v[218:221], v[78:81]
	v_mfma_f32_16x16x32_bf16 v[74:77], v[146:149], v[218:221], v[74:77]
	v_mfma_f32_16x16x32_bf16 v[70:73], v[156:159], v[218:221], v[70:73]
	v_mfma_f32_16x16x32_bf16 v[66:69], v[160:163], v[218:221], v[66:69]
	s_mov_b32 m0, s49
	s_nop 0
	global_load_lds_dwordx4 v88, s[30:31]
	v_mfma_f32_16x16x32_bf16 v[62:65], v[142:145], v[222:225], v[62:65]
	v_mfma_f32_16x16x32_bf16 v[58:61], v[146:149], v[222:225], v[58:61]
	v_mfma_f32_16x16x32_bf16 v[54:57], v[156:159], v[222:225], v[54:57]
	v_mfma_f32_16x16x32_bf16 v[50:53], v[160:163], v[222:225], v[50:53]
	s_add_i32 m0, s49, 0x2000
	s_nop 0
	global_load_lds_dwordx4 v90, s[30:31]
	v_mfma_f32_16x16x32_bf16 v[46:49], v[142:145], v[226:229], v[46:49]
	v_mfma_f32_16x16x32_bf16 v[42:45], v[146:149], v[226:229], v[42:45]
	v_mfma_f32_16x16x32_bf16 v[38:41], v[156:159], v[226:229], v[38:41]
	v_mfma_f32_16x16x32_bf16 v[34:37], v[160:163], v[226:229], v[34:37]
	s_add_i32 m0, s49, 0x4000
	s_nop 0
	global_load_lds_dwordx4 v92, s[30:31]
	v_mfma_f32_16x16x32_bf16 v[18:21], v[142:145], v[230:233], v[18:21]
	v_mfma_f32_16x16x32_bf16 v[22:25], v[146:149], v[230:233], v[22:25]
	v_mfma_f32_16x16x32_bf16 v[26:29], v[156:159], v[230:233], v[26:29]
	v_mfma_f32_16x16x32_bf16 v[30:33], v[160:163], v[230:233], v[30:33]
	s_add_i32 m0, s49, 0x6000
	s_nop 0
	global_load_lds_dwordx4 v94, s[30:31]
	v_mfma_f32_16x16x32_bf16 v[2:5], v[142:145], v[234:237], v[2:5]
	v_mfma_f32_16x16x32_bf16 v[6:9], v[146:149], v[234:237], v[6:9]
	v_mfma_f32_16x16x32_bf16 v[10:13], v[156:159], v[234:237], v[10:13]
	v_mfma_f32_16x16x32_bf16 v[14:17], v[160:163], v[234:237], v[14:17]
	s_add_i32 m0, s49, 0x8000
	s_nop 0
	global_load_lds_dwordx4 v96, s[30:31]
	v_cvt_pk_bf16_f32 v172, v186, v188
	v_cvt_pk_bf16_f32 v173, v190, v192
	v_cvt_pk_bf16_f32 v174, v194, v196
	v_cvt_pk_bf16_f32 v175, v198, v200
	v_cvt_pk_bf16_f32 v176, v187, v189
	v_cvt_pk_bf16_f32 v177, v191, v193
	v_cvt_pk_bf16_f32 v178, v195, v197
	v_cvt_pk_bf16_f32 v179, v199, v201
	ds_write_b128 v95, v[172:175] offset:0
	ds_write_b128 v95, v[176:179] offset:128
	v_add_u32_e32 v91, s46, v135
	v_add_u32_e32 v93, s46, v137
	ds_read_b128 v[238:241], v139 offset:19456
	ds_read_b128 v[242:245], v139 offset:21504
	ds_read_b128 v[246:249], v139 offset:23552
	ds_read_b128 v[250:253], v139 offset:25600
	ds_read_b128 v[218:221], v91 offset:0
	ds_read_b128 v[222:225], v91 offset:2048
	ds_read_b128 v[226:229], v91 offset:4096
	ds_read_b128 v[230:233], v91 offset:6144
	ds_read_b128 v[234:237], v91 offset:8192
	s_waitcnt lgkmcnt(0)
; #define MD_GLDS_A(buf, tau) do { _Pragma("unroll") for (int i = 0; i < 5; ++i) if (amask & (1u << i)) \
;         __builtin_amdgcn_global_load_lds((const unsigned*)((const char*)HIDp + aoff[i] + (size_t)((tau) & 7) * 128), (PG8_LAS unsigned*)(MD_SA(buf) + wid * 1024 + i * 8192), 16, 0, 0); } while (0)
; #define MD_B_ISSUE(sb, tau) do { const char* kb_ = Bb + (size_t)((tau) >> 3) * 512 + (size_t)((tau) & 7) * (64 * (size_t)RB); _Pragma("unroll") for (int j = 0; j < 8; ++j) { const char* p_ = kb_ + (size_t)j * RB; \
;         asm volatile("global_load_dwordx2 %0, %1, off" : "=&v"(sb[j]) : "v"(p_) : "memory"); } } while (0)
; #define MD_B_WAIT(sb, N) asm volatile("s_waitcnt vmcnt(%8)" : "+v"(sb[0]), "+v"(sb[1]), "+v"(sb[2]), "+v"(sb[3]), "+v"(sb[4]), "+v"(sb[5]), "+v"(sb[6]), "+v"(sb[7]) : "n"(N) : "memory")
; #define MD_END(last) do { if (last) asm volatile("s_waitcnt vmcnt(0)" ::: "memory"); else asm volatile("s_waitcnt vmcnt(8)" ::: "memory"); \
;         asm volatile("s_waitcnt lgkmcnt(0)" ::: "memory"); __builtin_amdgcn_s_barrier(); asm volatile("" ::: "memory"); } while (0)
; __device__ __forceinline__ void moe_down_stream(PG8_LAS unsigned char* lds, int e, int cb0, int slot0, int nv, const bf16_t* HIDp, const float* Wd, bf16_t* Y, const float* slot_w, const int* slot_dst) {
;     ...
;     for (int t = 0; t < NT; t += 2) {
;         if (t + 2 < NT) MD_B_WAIT(s1, 8); else MD_B_WAIT(s1, 0);
;         MD_B_WRITE(s1, 1); __builtin_amdgcn_sched_barrier(0); MD_GLDS_A(1, t + 1); __builtin_amdgcn_sched_barrier(0);
;         if (t + 3 < NT) MD_B_ISSUE(s1, t + 3);
;         MD_COMPUTE(0);
;         MD_END(t + 3 >= NT);
;         if (t + 2 < NT) { MD_B_WAIT(s0, 8); MD_B_WRITE(s0, 0); __builtin_amdgcn_sched_barrier(0); MD_GLDS_A(0, t + 2); __builtin_amdgcn_sched_barrier(0); }
;         if (t + 4 < NT) MD_B_ISSUE(s0, t + 4);
;         MD_COMPUTE(1);
;         MD_END(t + 4 >= NT);
	v_mfma_f32_16x16x32_bf16 v[78:81], v[238:241], v[218:221], v[78:81]
	v_mfma_f32_16x16x32_bf16 v[74:77], v[242:245], v[218:221], v[74:77]
	v_mfma_f32_16x16x32_bf16 v[70:73], v[246:249], v[218:221], v[70:73]
	v_mfma_f32_16x16x32_bf16 v[66:69], v[250:253], v[218:221], v[66:69]
	ds_read_b128 v[218:221], v93 offset:0
	ds_read_b128 v[142:145], v141 offset:19456
	s_add_i32 s51, s51, 1
	s_and_b32 s54, s51, 7
	s_cmp_eq_u32 s54, 0
	s_cselect_b32 s44, s34, s35
	s_cselect_b32 s45, -1, 0
	v_lshl_add_u64 v[132:133], v[132:133], 0, s[44:45]
	global_load_dwordx2 v[186:187], v[132:133], off
	v_lshl_add_u64 v[180:181], v[132:133], 0, s[24:25]
	global_load_dwordx2 v[188:189], v[180:181], off
	v_mfma_f32_16x16x32_bf16 v[62:65], v[238:241], v[222:225], v[62:65]
	v_mfma_f32_16x16x32_bf16 v[58:61], v[242:245], v[222:225], v[58:61]
	v_mfma_f32_16x16x32_bf16 v[54:57], v[246:249], v[222:225], v[54:57]
	v_mfma_f32_16x16x32_bf16 v[50:53], v[250:253], v[222:225], v[50:53]
	ds_read_b128 v[222:225], v93 offset:2048
	ds_read_b128 v[146:149], v141 offset:21504
	v_lshl_add_u64 v[180:181], v[132:133], 0, s[26:27]
	global_load_dwordx2 v[190:191], v[180:181], off
	v_lshl_add_u64 v[180:181], v[132:133], 0, s[28:29]
	global_load_dwordx2 v[192:193], v[180:181], off
	v_mfma_f32_16x16x32_bf16 v[46:49], v[238:241], v[226:229], v[46:49]
	v_mfma_f32_16x16x32_bf16 v[42:45], v[242:245], v[226:229], v[42:45]
	v_mfma_f32_16x16x32_bf16 v[38:41], v[246:249], v[226:229], v[38:41]
	v_mfma_f32_16x16x32_bf16 v[34:37], v[250:253], v[226:229], v[34:37]
	ds_read_b128 v[226:229], v93 offset:4096
	ds_read_b128 v[156:159], v141 offset:23552
	v_lshl_add_u64 v[180:181], v[132:133], 0, s[36:37]
	global_load_dwordx2 v[194:195], v[180:181], off
	v_lshl_add_u64 v[180:181], v[132:133], 0, s[38:39]
	global_load_dwordx2 v[196:197], v[180:181], off
	v_mfma_f32_16x16x32_bf16 v[18:21], v[238:241], v[230:233], v[18:21]
	v_mfma_f32_16x16x32_bf16 v[22:25], v[242:245], v[230:233], v[22:25]
	v_mfma_f32_16x16x32_bf16 v[26:29], v[246:249], v[230:233], v[26:29]
	v_mfma_f32_16x16x32_bf16 v[30:33], v[250:253], v[230:233], v[30:33]
	ds_read_b128 v[230:233], v93 offset:6144
	ds_read_b128 v[160:163], v141 offset:25600
	v_lshl_add_u64 v[180:181], v[132:133], 0, s[40:41]
	global_load_dwordx2 v[198:199], v[180:181], off
	v_lshl_add_u64 v[180:181], v[132:133], 0, s[42:43]
	global_load_dwordx2 v[200:201], v[180:181], off
	v_mfma_f32_16x16x32_bf16 v[2:5], v[238:241], v[234:237], v[2:5]
	v_mfma_f32_16x16x32_bf16 v[6:9], v[242:245], v[234:237], v[6:9]
	v_mfma_f32_16x16x32_bf16 v[10:13], v[246:249], v[234:237], v[10:13]
	v_mfma_f32_16x16x32_bf16 v[14:17], v[250:253], v[234:237], v[14:17]
	ds_read_b128 v[234:237], v93 offset:8192
	s_waitcnt vmcnt(21)
	s_waitcnt lgkmcnt(0)
	s_barrier
	s_mov_b32 s49, s46
	s_mov_b32 s46, s47
	s_mov_b32 s47, s48
	s_mov_b32 s48, s49
	s_add_i32 s50, s50, 1
	s_add_i32 s49, s48, s74
	s_add_i32 s52, s52, 1
	s_and_b32 s54, s52, 7
	s_cmp_eq_u32 s54, 0
	s_cselect_b32 s54, s53, s32
	s_cselect_b32 s55, -1, 0
	s_add_u32 s30, s30, s54
	s_addc_u32 s31, s31, s55
	v_mfma_f32_16x16x32_bf16 v[78:81], v[142:145], v[218:221], v[78:81]
	v_mfma_f32_16x16x32_bf16 v[74:77], v[146:149], v[218:221], v[74:77]
	v_mfma_f32_16x16x32_bf16 v[70:73], v[156:159], v[218:221], v[70:73]
	v_mfma_f32_16x16x32_bf16 v[66:69], v[160:163], v[218:221], v[66:69]
	s_mov_b32 m0, s49
	s_nop 0
	global_load_lds_dwordx4 v88, s[30:31]
	v_mfma_f32_16x16x32_bf16 v[62:65], v[142:145], v[222:225], v[62:65]
	v_mfma_f32_16x16x32_bf16 v[58:61], v[146:149], v[222:225], v[58:61]
	v_mfma_f32_16x16x32_bf16 v[54:57], v[156:159], v[222:225], v[54:57]
	v_mfma_f32_16x16x32_bf16 v[50:53], v[160:163], v[222:225], v[50:53]
	s_add_i32 m0, s49, 0x2000
	s_nop 0
	global_load_lds_dwordx4 v90, s[30:31]
	v_mfma_f32_16x16x32_bf16 v[46:49], v[142:145], v[226:229], v[46:49]
	v_mfma_f32_16x16x32_bf16 v[42:45], v[146:149], v[226:229], v[42:45]
	v_mfma_f32_16x16x32_bf16 v[38:41], v[156:159], v[226:229], v[38:41]
	v_mfma_f32_16x16x32_bf16 v[34:37], v[160:163], v[226:229], v[34:37]
	s_add_i32 m0, s49, 0x4000
	s_nop 0
	global_load_lds_dwordx4 v92, s[30:31]
	v_mfma_f32_16x16x32_bf16 v[18:21], v[142:145], v[230:233], v[18:21]
	v_mfma_f32_16x16x32_bf16 v[22:25], v[146:149], v[230:233], v[22:25]
	v_mfma_f32_16x16x32_bf16 v[26:29], v[156:159], v[230:233], v[26:29]
	v_mfma_f32_16x16x32_bf16 v[30:33], v[160:163], v[230:233], v[30:33]
	s_add_i32 m0, s49, 0x6000
	s_nop 0
	global_load_lds_dwordx4 v94, s[30:31]
	v_mfma_f32_16x16x32_bf16 v[2:5], v[142:145], v[234:237], v[2:5]
	v_mfma_f32_16x16x32_bf16 v[6:9], v[146:149], v[234:237], v[6:9]
	v_mfma_f32_16x16x32_bf16 v[10:13], v[156:159], v[234:237], v[10:13]
	v_mfma_f32_16x16x32_bf16 v[14:17], v[160:163], v[234:237], v[14:17]
	s_add_i32 m0, s49, 0x8000
	s_nop 0
	global_load_lds_dwordx4 v96, s[30:31]
	v_cvt_pk_bf16_f32 v172, v202, v204
	v_cvt_pk_bf16_f32 v173, v206, v208
	v_cvt_pk_bf16_f32 v174, v210, v212
	v_cvt_pk_bf16_f32 v175, v214, v216
	v_cvt_pk_bf16_f32 v176, v203, v205
	v_cvt_pk_bf16_f32 v177, v207, v209
	v_cvt_pk_bf16_f32 v178, v211, v213
	v_cvt_pk_bf16_f32 v179, v215, v217
	ds_write_b128 v95, v[172:175] offset:19456
	ds_write_b128 v95, v[176:179] offset:19584
	v_add_u32_e32 v91, s46, v135
	v_add_u32_e32 v93, s46, v137
	ds_read_b128 v[238:241], v139 offset:0
	ds_read_b128 v[242:245], v139 offset:2048
	ds_read_b128 v[246:249], v139 offset:4096
	ds_read_b128 v[250:253], v139 offset:6144
	ds_read_b128 v[218:221], v91 offset:0
	ds_read_b128 v[222:225], v91 offset:2048
	ds_read_b128 v[226:229], v91 offset:4096
	ds_read_b128 v[230:233], v91 offset:6144
	ds_read_b128 v[234:237], v91 offset:8192
	s_waitcnt lgkmcnt(0)
; #define MD_GLDS_A(buf, tau) do { _Pragma("unroll") for (int i = 0; i < 5; ++i) if (amask & (1u << i)) \
;         __builtin_amdgcn_global_load_lds((const unsigned*)((const char*)HIDp + aoff[i] + (size_t)((tau) & 7) * 128), (PG8_LAS unsigned*)(MD_SA(buf) + wid * 1024 + i * 8192), 16, 0, 0); } while (0)
; #define MD_B_ISSUE(sb, tau) do { const char* kb_ = Bb + (size_t)((tau) >> 3) * 512 + (size_t)((tau) & 7) * (64 * (size_t)RB); _Pragma("unroll") for (int j = 0; j < 8; ++j) { const char* p_ = kb_ + (size_t)j * RB; \
;         asm volatile("global_load_dwordx2 %0, %1, off" : "=&v"(sb[j]) : "v"(p_) : "memory"); } } while (0)
; #define MD_B_WAIT(sb, N) asm volatile("s_waitcnt vmcnt(%8)" : "+v"(sb[0]), "+v"(sb[1]), "+v"(sb[2]), "+v"(sb[3]), "+v"(sb[4]), "+v"(sb[5]), "+v"(sb[6]), "+v"(sb[7]) : "n"(N) : "memory")
; #define MD_END(last) do { if (last) asm volatile("s_waitcnt vmcnt(0)" ::: "memory"); else asm volatile("s_waitcnt vmcnt(8)" ::: "memory"); \
;         asm volatile("s_waitcnt lgkmcnt(0)" ::: "memory"); __builtin_amdgcn_s_barrier(); asm volatile("" ::: "memory"); } while (0)
; __device__ __forceinline__ void moe_down_stream(PG8_LAS unsigned char* lds, int e, int cb0, int slot0, int nv, const bf16_t* HIDp, const float* Wd, bf16_t* Y, const float* slot_w, const int* slot_dst) {
;     ...
;     for (int t = 0; t < NT; t += 2) {
;         if (t + 2 < NT) MD_B_WAIT(s1, 8); else MD_B_WAIT(s1, 0);
;         MD_B_WRITE(s1, 1); __builtin_amdgcn_sched_barrier(0); MD_GLDS_A(1, t + 1); __builtin_amdgcn_sched_barrier(0);
;         if (t + 3 < NT) MD_B_ISSUE(s1, t + 3);
;         MD_COMPUTE(0);
;         MD_END(t + 3 >= NT);
;         if (t + 2 < NT) { MD_B_WAIT(s0, 8); MD_B_WRITE(s0, 0); __builtin_amdgcn_sched_barrier(0); MD_GLDS_A(0, t + 2); __builtin_amdgcn_sched_barrier(0); }
;         if (t + 4 < NT) MD_B_ISSUE(s0, t + 4);
;         MD_COMPUTE(1);
;         MD_END(t + 4 >= NT);
	v_mfma_f32_16x16x32_bf16 v[78:81], v[238:241], v[218:221], v[78:81]
	v_mfma_f32_16x16x32_bf16 v[74:77], v[242:245], v[218:221], v[74:77]
	v_mfma_f32_16x16x32_bf16 v[70:73], v[246:249], v[218:221], v[70:73]
	v_mfma_f32_16x16x32_bf16 v[66:69], v[250:253], v[218:221], v[66:69]
	ds_read_b128 v[218:221], v93 offset:0
	ds_read_b128 v[142:145], v141 offset:0
	s_add_i32 s51, s51, 1
	s_and_b32 s54, s51, 7
	s_cmp_eq_u32 s54, 0
	s_cselect_b32 s44, s34, s35
	s_cselect_b32 s45, -1, 0
	v_lshl_add_u64 v[132:133], v[132:133], 0, s[44:45]
	global_load_dwordx2 v[202:203], v[132:133], off
	v_lshl_add_u64 v[180:181], v[132:133], 0, s[24:25]
	global_load_dwordx2 v[204:205], v[180:181], off
	v_mfma_f32_16x16x32_bf16 v[62:65], v[238:241], v[222:225], v[62:65]
	v_mfma_f32_16x16x32_bf16 v[58:61], v[242:245], v[222:225], v[58:61]
	v_mfma_f32_16x16x32_bf16 v[54:57], v[246:249], v[222:225], v[54:57]
	v_mfma_f32_16x16x32_bf16 v[50:53], v[250:253], v[222:225], v[50:53]
	ds_read_b128 v[222:225], v93 offset:2048
	ds_read_b128 v[146:149], v141 offset:2048
	v_lshl_add_u64 v[180:181], v[132:133], 0, s[26:27]
	global_load_dwordx2 v[206:207], v[180:181], off
	v_lshl_add_u64 v[180:181], v[132:133], 0, s[28:29]
	global_load_dwordx2 v[208:209], v[180:181], off
	v_mfma_f32_16x16x32_bf16 v[46:49], v[238:241], v[226:229], v[46:49]
	v_mfma_f32_16x16x32_bf16 v[42:45], v[242:245], v[226:229], v[42:45]
	v_mfma_f32_16x16x32_bf16 v[38:41], v[246:249], v[226:229], v[38:41]
	v_mfma_f32_16x16x32_bf16 v[34:37], v[250:253], v[226:229], v[34:37]
	ds_read_b128 v[226:229], v93 offset:4096
	ds_read_b128 v[156:159], v141 offset:4096
	v_lshl_add_u64 v[180:181], v[132:133], 0, s[36:37]
	global_load_dwordx2 v[210:211], v[180:181], off
	v_lshl_add_u64 v[180:181], v[132:133], 0, s[38:39]
	global_load_dwordx2 v[212:213], v[180:181], off
	v_mfma_f32_16x16x32_bf16 v[18:21], v[238:241], v[230:233], v[18:21]
	v_mfma_f32_16x16x32_bf16 v[22:25], v[242:245], v[230:233], v[22:25]
	v_mfma_f32_16x16x32_bf16 v[26:29], v[246:249], v[230:233], v[26:29]
	v_mfma_f32_16x16x32_bf16 v[30:33], v[250:253], v[230:233], v[30:33]
	ds_read_b128 v[230:233], v93 offset:6144
	ds_read_b128 v[160:163], v141 offset:6144
	v_lshl_add_u64 v[180:181], v[132:133], 0, s[40:41]
	global_load_dwordx2 v[214:215], v[180:181], off
	v_lshl_add_u64 v[180:181], v[132:133], 0, s[42:43]
	global_load_dwordx2 v[216:217], v[180:181], off
	v_mfma_f32_16x16x32_bf16 v[2:5], v[238:241], v[234:237], v[2:5]
	v_mfma_f32_16x16x32_bf16 v[6:9], v[242:245], v[234:237], v[6:9]
	v_mfma_f32_16x16x32_bf16 v[10:13], v[246:249], v[234:237], v[10:13]
	v_mfma_f32_16x16x32_bf16 v[14:17], v[250:253], v[234:237], v[14:17]
	ds_read_b128 v[234:237], v93 offset:8192
	s_waitcnt vmcnt(21)
	s_waitcnt lgkmcnt(0)
	s_barrier
	s_mov_b32 s49, s46
	s_mov_b32 s46, s47
	s_mov_b32 s47, s48
	s_mov_b32 s48, s49
	s_add_i32 s50, s50, 1
	s_add_i32 s49, s48, s74
	s_add_i32 s52, s52, 1
	s_and_b32 s54, s52, 7
	s_cmp_eq_u32 s54, 0
	s_cselect_b32 s54, s53, s32
	s_cselect_b32 s55, -1, 0
	s_add_u32 s30, s30, s54
	s_addc_u32 s31, s31, s55
	v_mfma_f32_16x16x32_bf16 v[78:81], v[142:145], v[218:221], v[78:81]
	v_mfma_f32_16x16x32_bf16 v[74:77], v[146:149], v[218:221], v[74:77]
	v_mfma_f32_16x16x32_bf16 v[70:73], v[156:159], v[218:221], v[70:73]
	v_mfma_f32_16x16x32_bf16 v[66:69], v[160:163], v[218:221], v[66:69]
	s_mov_b32 m0, s49
	s_nop 0
	global_load_lds_dwordx4 v88, s[30:31]
	v_mfma_f32_16x16x32_bf16 v[62:65], v[142:145], v[222:225], v[62:65]
	v_mfma_f32_16x16x32_bf16 v[58:61], v[146:149], v[222:225], v[58:61]
	v_mfma_f32_16x16x32_bf16 v[54:57], v[156:159], v[222:225], v[54:57]
	v_mfma_f32_16x16x32_bf16 v[50:53], v[160:163], v[222:225], v[50:53]
	s_add_i32 m0, s49, 0x2000
	s_nop 0
	global_load_lds_dwordx4 v90, s[30:31]
	v_mfma_f32_16x16x32_bf16 v[46:49], v[142:145], v[226:229], v[46:49]
	v_mfma_f32_16x16x32_bf16 v[42:45], v[146:149], v[226:229], v[42:45]
	v_mfma_f32_16x16x32_bf16 v[38:41], v[156:159], v[226:229], v[38:41]
	v_mfma_f32_16x16x32_bf16 v[34:37], v[160:163], v[226:229], v[34:37]
	s_add_i32 m0, s49, 0x4000
	s_nop 0
	global_load_lds_dwordx4 v92, s[30:31]
	v_mfma_f32_16x16x32_bf16 v[18:21], v[142:145], v[230:233], v[18:21]
	v_mfma_f32_16x16x32_bf16 v[22:25], v[146:149], v[230:233], v[22:25]
	v_mfma_f32_16x16x32_bf16 v[26:29], v[156:159], v[230:233], v[26:29]
	v_mfma_f32_16x16x32_bf16 v[30:33], v[160:163], v[230:233], v[30:33]
	s_add_i32 m0, s49, 0x6000
	s_nop 0
	global_load_lds_dwordx4 v94, s[30:31]
	v_mfma_f32_16x16x32_bf16 v[2:5], v[142:145], v[234:237], v[2:5]
	v_mfma_f32_16x16x32_bf16 v[6:9], v[146:149], v[234:237], v[6:9]
	v_mfma_f32_16x16x32_bf16 v[10:13], v[156:159], v[234:237], v[10:13]
	v_mfma_f32_16x16x32_bf16 v[14:17], v[160:163], v[234:237], v[14:17]
	s_add_i32 m0, s49, 0x8000
	s_nop 0
	global_load_lds_dwordx4 v96, s[30:31]
	v_cvt_pk_bf16_f32 v172, v98, v100
	v_cvt_pk_bf16_f32 v173, v102, v104
	v_cvt_pk_bf16_f32 v174, v106, v108
	v_cvt_pk_bf16_f32 v175, v110, v112
	v_cvt_pk_bf16_f32 v176, v99, v101
	v_cvt_pk_bf16_f32 v177, v103, v105
	v_cvt_pk_bf16_f32 v178, v107, v109
	v_cvt_pk_bf16_f32 v179, v111, v113
	ds_write_b128 v95, v[172:175] offset:0
	ds_write_b128 v95, v[176:179] offset:128
	v_add_u32_e32 v91, s46, v135
	v_add_u32_e32 v93, s46, v137
	ds_read_b128 v[238:241], v139 offset:19456
	ds_read_b128 v[242:245], v139 offset:21504
	ds_read_b128 v[246:249], v139 offset:23552
	ds_read_b128 v[250:253], v139 offset:25600
	ds_read_b128 v[218:221], v91 offset:0
	ds_read_b128 v[222:225], v91 offset:2048
	ds_read_b128 v[226:229], v91 offset:4096
	ds_read_b128 v[230:233], v91 offset:6144
	ds_read_b128 v[234:237], v91 offset:8192
	s_waitcnt lgkmcnt(0)
; #define PG8_LAS __attribute__((address_space(3)))
; __device__ __forceinline__ unsigned cvtpk(float lo, float hi) { f32x2 v = {lo, hi}; bf16x2_t b = __builtin_convertvector(v, bf16x2_t); return __builtin_bit_cast(unsigned, b); }
; #define MD_GLDS_A(buf, tau) do { _Pragma("unroll") for (int i = 0; i < 5; ++i) if (amask & (1u << i)) \
;         __builtin_amdgcn_global_load_lds((const unsigned*)((const char*)HIDp + aoff[i] + (size_t)((tau) & 7) * 128), (PG8_LAS unsigned*)(MD_SA(buf) + wid * 1024 + i * 8192), 16, 0, 0); } while (0)
; __device__ __forceinline__ void moe_down_stream(PG8_LAS unsigned char* lds, int e, int cb0, int slot0, int nv, const bf16_t* HIDp, const float* Wd, bf16_t* Y, const float* slot_w, const int* slot_dst) {
;     ...
;     for (int t = 0; t < NT; t += 2) {
;         if (t + 2 < NT) MD_B_WAIT(s1, 8); else MD_B_WAIT(s1, 0);
;         MD_B_WRITE(s1, 1); __builtin_amdgcn_sched_barrier(0); MD_GLDS_A(1, t + 1); __builtin_amdgcn_sched_barrier(0);
;         if (t + 3 < NT) MD_B_ISSUE(s1, t + 3);
;         MD_COMPUTE(0);
;         MD_END(t + 3 >= NT);
;         if (t + 2 < NT) { MD_B_WAIT(s0, 8); MD_B_WRITE(s0, 0); __builtin_amdgcn_sched_barrier(0); MD_GLDS_A(0, t + 2); __builtin_amdgcn_sched_barrier(0); }
;         if (t + 4 < NT) MD_B_ISSUE(s0, t + 4);
;         MD_COMPUTE(1);
;         MD_END(t + 4 >= NT);
;         if (((t + 1) & 7) == 7) {
;             const int cb = cb0 + ((t + 1) >> 3);
; #pragma unroll
;             for (int m = 0; m < DNM; ++m) {
;                 const float w_ = lw[4 * (16 * m + fr) + wr];
; #pragma unroll
;                 for (int p = 0; p < 2; ++p) { const f32x4 v0 = acc[m][2 * p] * w_, v1 = acc[m][2 * p + 1] * w_; u32x4 w; w.x = cvtpk(v0[0], v0[1]); w.y = cvtpk(v0[2], v0[3]); w.z = cvtpk(v1[0], v1[1]); w.w = cvtpk(v1[2], v1[3]);
;                     *(PG8_LAS u32x4*)(stg + fr * 128 + (((4 * p + fq) ^ (fr & 7)) * 16)) = w; }
; #pragma unroll
;                 for (int hh = 0; hh < 2; ++hh) { const int r = (lane >> 3) + 8 * hh, cc = lane & 7; const u32x4 d = *(const PG8_LAS u32x4*)(stg + r * 128 + ((cc ^ (r & 7)) * 16)); const int dst_ = ldst[4 * (16 * m + r) + wr];
;                     if (dst_ >= 0) *(u32x4*)(Y + (size_t)dst_ * D + 128 * cb + 64 * wc + 8 * cc) = d; }
; #pragma unroll
;                 for (int n = 0; n < 4; ++n) acc[m][n] = (f32x4){0.f, 0.f, 0.f, 0.f}; } }
	v_mfma_f32_16x16x32_bf16 v[78:81], v[238:241], v[218:221], v[78:81]
	v_mfma_f32_16x16x32_bf16 v[74:77], v[242:245], v[218:221], v[74:77]
	v_mfma_f32_16x16x32_bf16 v[70:73], v[246:249], v[218:221], v[70:73]
	v_mfma_f32_16x16x32_bf16 v[66:69], v[250:253], v[218:221], v[66:69]
	ds_read_b128 v[218:221], v93 offset:0
	ds_read_b128 v[142:145], v141 offset:19456
	s_add_i32 s51, s51, 1
	s_and_b32 s54, s51, 7
	s_cmp_eq_u32 s54, 0
	s_cselect_b32 s44, s34, s35
	s_cselect_b32 s45, -1, 0
	v_lshl_add_u64 v[132:133], v[132:133], 0, s[44:45]
	global_load_dwordx2 v[98:99], v[132:133], off
	v_lshl_add_u64 v[180:181], v[132:133], 0, s[24:25]
	global_load_dwordx2 v[100:101], v[180:181], off
	v_mfma_f32_16x16x32_bf16 v[62:65], v[238:241], v[222:225], v[62:65]
	v_mfma_f32_16x16x32_bf16 v[58:61], v[242:245], v[222:225], v[58:61]
	v_mfma_f32_16x16x32_bf16 v[54:57], v[246:249], v[222:225], v[54:57]
	v_mfma_f32_16x16x32_bf16 v[50:53], v[250:253], v[222:225], v[50:53]
	ds_read_b128 v[222:225], v93 offset:2048
	ds_read_b128 v[146:149], v141 offset:21504
	v_lshl_add_u64 v[180:181], v[132:133], 0, s[26:27]
	global_load_dwordx2 v[102:103], v[180:181], off
	v_lshl_add_u64 v[180:181], v[132:133], 0, s[28:29]
	global_load_dwordx2 v[104:105], v[180:181], off
	v_mfma_f32_16x16x32_bf16 v[46:49], v[238:241], v[226:229], v[46:49]
	v_mfma_f32_16x16x32_bf16 v[42:45], v[242:245], v[226:229], v[42:45]
	v_mfma_f32_16x16x32_bf16 v[38:41], v[246:249], v[226:229], v[38:41]
	v_mfma_f32_16x16x32_bf16 v[34:37], v[250:253], v[226:229], v[34:37]
	ds_read_b128 v[226:229], v93 offset:4096
	ds_read_b128 v[156:159], v141 offset:23552
	v_lshl_add_u64 v[180:181], v[132:133], 0, s[36:37]
	global_load_dwordx2 v[106:107], v[180:181], off
	v_lshl_add_u64 v[180:181], v[132:133], 0, s[38:39]
	global_load_dwordx2 v[108:109], v[180:181], off
	v_mfma_f32_16x16x32_bf16 v[18:21], v[238:241], v[230:233], v[18:21]
	v_mfma_f32_16x16x32_bf16 v[22:25], v[242:245], v[230:233], v[22:25]
	v_mfma_f32_16x16x32_bf16 v[26:29], v[246:249], v[230:233], v[26:29]
	v_mfma_f32_16x16x32_bf16 v[30:33], v[250:253], v[230:233], v[30:33]
	ds_read_b128 v[230:233], v93 offset:6144
	ds_read_b128 v[160:163], v141 offset:25600
	v_lshl_add_u64 v[180:181], v[132:133], 0, s[40:41]
	global_load_dwordx2 v[110:111], v[180:181], off
	v_lshl_add_u64 v[180:181], v[132:133], 0, s[42:43]
	global_load_dwordx2 v[112:113], v[180:181], off
	v_mfma_f32_16x16x32_bf16 v[2:5], v[238:241], v[234:237], v[2:5]
	v_mfma_f32_16x16x32_bf16 v[6:9], v[242:245], v[234:237], v[6:9]
	v_mfma_f32_16x16x32_bf16 v[10:13], v[246:249], v[234:237], v[10:13]
	v_mfma_f32_16x16x32_bf16 v[14:17], v[250:253], v[234:237], v[14:17]
	ds_read_b128 v[234:237], v93 offset:8192
	s_waitcnt vmcnt(21)
	s_waitcnt lgkmcnt(0)
	s_barrier
	s_mov_b32 s49, s46
	s_mov_b32 s46, s47
	s_mov_b32 s47, s48
	s_mov_b32 s48, s49
	s_add_i32 s50, s50, 1
	s_sub_u32 s56, s56, 1
	s_cmp_lg_u32 s56, 0
	s_cbranch_scc1 .Lmd_loop_Y
	v_mfma_f32_16x16x32_bf16 v[78:81], v[142:145], v[218:221], v[78:81]
	v_mfma_f32_16x16x32_bf16 v[74:77], v[146:149], v[218:221], v[74:77]
	v_mfma_f32_16x16x32_bf16 v[70:73], v[156:159], v[218:221], v[70:73]
	v_mfma_f32_16x16x32_bf16 v[66:69], v[160:163], v[218:221], v[66:69]
	v_mfma_f32_16x16x32_bf16 v[62:65], v[142:145], v[222:225], v[62:65]
	v_mfma_f32_16x16x32_bf16 v[58:61], v[146:149], v[222:225], v[58:61]
	v_mfma_f32_16x16x32_bf16 v[54:57], v[156:159], v[222:225], v[54:57]
	v_mfma_f32_16x16x32_bf16 v[50:53], v[160:163], v[222:225], v[50:53]
	v_mfma_f32_16x16x32_bf16 v[46:49], v[142:145], v[226:229], v[46:49]
	v_mfma_f32_16x16x32_bf16 v[42:45], v[146:149], v[226:229], v[42:45]
	v_mfma_f32_16x16x32_bf16 v[38:41], v[156:159], v[226:229], v[38:41]
	v_mfma_f32_16x16x32_bf16 v[34:37], v[160:163], v[226:229], v[34:37]
	v_mfma_f32_16x16x32_bf16 v[18:21], v[142:145], v[230:233], v[18:21]
	v_mfma_f32_16x16x32_bf16 v[22:25], v[146:149], v[230:233], v[22:25]
	v_mfma_f32_16x16x32_bf16 v[26:29], v[156:159], v[230:233], v[26:29]
	v_mfma_f32_16x16x32_bf16 v[30:33], v[160:163], v[230:233], v[30:33]
	v_mfma_f32_16x16x32_bf16 v[2:5], v[142:145], v[234:237], v[2:5]
	v_mfma_f32_16x16x32_bf16 v[6:9], v[146:149], v[234:237], v[6:9]
	v_mfma_f32_16x16x32_bf16 v[10:13], v[156:159], v[234:237], v[10:13]
	v_mfma_f32_16x16x32_bf16 v[14:17], v[160:163], v[234:237], v[14:17]
	s_add_i32 s54, s48, s74
	v_add_u32_e32 v164, s54, v84
	v_add_u32_e32 v165, s54, v85
	ds_read_b32 v150, v82 offset:0
	ds_read_b32 v151, v83 offset:0
	ds_read_b32 v166, v83 offset:128
	s_waitcnt lgkmcnt(2)
	v_mul_f32_e32 v78, v150, v78
	v_mul_f32_e32 v79, v150, v79
	v_mul_f32_e32 v80, v150, v80
	v_mul_f32_e32 v81, v150, v81
	v_mul_f32_e32 v74, v150, v74
	v_mul_f32_e32 v75, v150, v75
	v_mul_f32_e32 v76, v150, v76
	v_mul_f32_e32 v77, v150, v77
	v_cvt_pk_bf16_f32 v182, v78, v79
	v_cvt_pk_bf16_f32 v183, v80, v81
	v_cvt_pk_bf16_f32 v184, v74, v75
	v_cvt_pk_bf16_f32 v185, v76, v77
	ds_write_b128 v164, v[182:185]
	v_mul_f32_e32 v70, v150, v70
	v_mul_f32_e32 v71, v150, v71
	v_mul_f32_e32 v72, v150, v72
	v_mul_f32_e32 v73, v150, v73
	v_mul_f32_e32 v66, v150, v66
	v_mul_f32_e32 v67, v150, v67
	v_mul_f32_e32 v68, v150, v68
	v_mul_f32_e32 v69, v150, v69
	v_cvt_pk_bf16_f32 v182, v70, v71
	v_cvt_pk_bf16_f32 v183, v72, v73
	v_cvt_pk_bf16_f32 v184, v66, v67
	v_cvt_pk_bf16_f32 v185, v68, v69
	v_xor_b32_e32 v167, 64, v164
	ds_write_b128 v167, v[182:185]
	v_mov_b32_e32 v78, 0
	v_mov_b32_e32 v74, 0
	v_mov_b32_e32 v70, 0
	v_mov_b32_e32 v66, 0
	v_mov_b32_e32 v79, 0
	v_mov_b32_e32 v75, 0
	v_mov_b32_e32 v71, 0
	v_mov_b32_e32 v67, 0
	v_mov_b32_e32 v80, 0
	v_mov_b32_e32 v76, 0
	v_mov_b32_e32 v72, 0
	v_mov_b32_e32 v68, 0
	v_mov_b32_e32 v81, 0
	v_mov_b32_e32 v77, 0
	v_mov_b32_e32 v73, 0
	v_mov_b32_e32 v69, 0
	ds_read_b128 v[182:185], v165 offset:0
	v_cmp_lt_i32_e32 vcc, -1, v151
	v_lshlrev_b32_e32 v148, 13, v151
	v_mov_b32_e32 v149, 0
	v_lshl_add_u64 v[148:149], v[148:149], 0, v[86:87]
	v_cndmask_b32_e32 v148, v168, v148, vcc
	v_cndmask_b32_e32 v149, v169, v149, vcc
	s_waitcnt lgkmcnt(0)
; #define PG8_LAS __attribute__((address_space(3)))
; __device__ __forceinline__ unsigned cvtpk(float lo, float hi) { f32x2 v = {lo, hi}; bf16x2_t b = __builtin_convertvector(v, bf16x2_t); return __builtin_bit_cast(unsigned, b); }
; __device__ __forceinline__ void moe_down_stream(PG8_LAS unsigned char* lds, int e, int cb0, int slot0, int nv, const bf16_t* HIDp, const float* Wd, bf16_t* Y, const float* slot_w, const int* slot_dst) {
;     ...
;         if (((t + 1) & 7) == 7) {
;             const int cb = cb0 + ((t + 1) >> 3);
; #pragma unroll
;             for (int m = 0; m < DNM; ++m) {
;                 const float w_ = lw[4 * (16 * m + fr) + wr];
; #pragma unroll
;                 for (int p = 0; p < 2; ++p) { const f32x4 v0 = acc[m][2 * p] * w_, v1 = acc[m][2 * p + 1] * w_; u32x4 w; w.x = cvtpk(v0[0], v0[1]); w.y = cvtpk(v0[2], v0[3]); w.z = cvtpk(v1[0], v1[1]); w.w = cvtpk(v1[2], v1[3]);
;                     *(PG8_LAS u32x4*)(stg + fr * 128 + (((4 * p + fq) ^ (fr & 7)) * 16)) = w; }
; #pragma unroll
;                 for (int hh = 0; hh < 2; ++hh) { const int r = (lane >> 3) + 8 * hh, cc = lane & 7; const u32x4 d = *(const PG8_LAS u32x4*)(stg + r * 128 + ((cc ^ (r & 7)) * 16)); const int dst_ = ldst[4 * (16 * m + r) + wr];
;                     if (dst_ >= 0) *(u32x4*)(Y + (size_t)dst_ * D + 128 * cb + 64 * wc + 8 * cc) = d; }
; #pragma unroll
;                 for (int n = 0; n < 4; ++n) acc[m][n] = (f32x4){0.f, 0.f, 0.f, 0.f}; } }
	global_store_dwordx4 v[148:149], v[182:185], off
	ds_read_b128 v[182:185], v165 offset:8192
	v_cmp_lt_i32_e32 vcc, -1, v166
	v_lshlrev_b32_e32 v148, 13, v166
	v_mov_b32_e32 v149, 0
	v_lshl_add_u64 v[148:149], v[148:149], 0, v[86:87]
	v_cndmask_b32_e32 v148, v168, v148, vcc
	v_cndmask_b32_e32 v149, v169, v149, vcc
	s_waitcnt lgkmcnt(0)
	global_store_dwordx4 v[148:149], v[182:185], off
	ds_read_b32 v150, v82 offset:256
	ds_read_b32 v151, v83 offset:256
	ds_read_b32 v166, v83 offset:384
	s_waitcnt lgkmcnt(2)
	v_mul_f32_e32 v62, v150, v62
	v_mul_f32_e32 v63, v150, v63
	v_mul_f32_e32 v64, v150, v64
	v_mul_f32_e32 v65, v150, v65
	v_mul_f32_e32 v58, v150, v58
	v_mul_f32_e32 v59, v150, v59
	v_mul_f32_e32 v60, v150, v60
	v_mul_f32_e32 v61, v150, v61
	v_cvt_pk_bf16_f32 v182, v62, v63
	v_cvt_pk_bf16_f32 v183, v64, v65
	v_cvt_pk_bf16_f32 v184, v58, v59
	v_cvt_pk_bf16_f32 v185, v60, v61
	ds_write_b128 v164, v[182:185]
	v_mul_f32_e32 v54, v150, v54
	v_mul_f32_e32 v55, v150, v55
	v_mul_f32_e32 v56, v150, v56
	v_mul_f32_e32 v57, v150, v57
	v_mul_f32_e32 v50, v150, v50
	v_mul_f32_e32 v51, v150, v51
	v_mul_f32_e32 v52, v150, v52
	v_mul_f32_e32 v53, v150, v53
	v_cvt_pk_bf16_f32 v182, v54, v55
	v_cvt_pk_bf16_f32 v183, v56, v57
	v_cvt_pk_bf16_f32 v184, v50, v51
	v_cvt_pk_bf16_f32 v185, v52, v53
	v_xor_b32_e32 v167, 64, v164
	ds_write_b128 v167, v[182:185]
	v_mov_b32_e32 v62, 0
	v_mov_b32_e32 v58, 0
	v_mov_b32_e32 v54, 0
	v_mov_b32_e32 v50, 0
	v_mov_b32_e32 v63, 0
	v_mov_b32_e32 v59, 0
	v_mov_b32_e32 v55, 0
	v_mov_b32_e32 v51, 0
	v_mov_b32_e32 v64, 0
	v_mov_b32_e32 v60, 0
	v_mov_b32_e32 v56, 0
	v_mov_b32_e32 v52, 0
	v_mov_b32_e32 v65, 0
	v_mov_b32_e32 v61, 0
	v_mov_b32_e32 v57, 0
	v_mov_b32_e32 v53, 0
	ds_read_b128 v[182:185], v165 offset:0
	v_cmp_lt_i32_e32 vcc, -1, v151
	v_lshlrev_b32_e32 v148, 13, v151
	v_mov_b32_e32 v149, 0
	v_lshl_add_u64 v[148:149], v[148:149], 0, v[86:87]
	v_cndmask_b32_e32 v148, v168, v148, vcc
	v_cndmask_b32_e32 v149, v169, v149, vcc
	s_waitcnt lgkmcnt(0)
	global_store_dwordx4 v[148:149], v[182:185], off
	ds_read_b128 v[182:185], v165 offset:8192
	v_cmp_lt_i32_e32 vcc, -1, v166
	v_lshlrev_b32_e32 v148, 13, v166
	v_mov_b32_e32 v149, 0
	v_lshl_add_u64 v[148:149], v[148:149], 0, v[86:87]
	v_cndmask_b32_e32 v148, v168, v148, vcc
	v_cndmask_b32_e32 v149, v169, v149, vcc
	s_waitcnt lgkmcnt(0)
	global_store_dwordx4 v[148:149], v[182:185], off
	ds_read_b32 v150, v82 offset:512
	ds_read_b32 v151, v83 offset:512
	ds_read_b32 v166, v83 offset:640
	s_waitcnt lgkmcnt(2)
	v_mul_f32_e32 v46, v150, v46
	v_mul_f32_e32 v47, v150, v47
	v_mul_f32_e32 v48, v150, v48
	v_mul_f32_e32 v49, v150, v49
	v_mul_f32_e32 v42, v150, v42
	v_mul_f32_e32 v43, v150, v43
	v_mul_f32_e32 v44, v150, v44
	v_mul_f32_e32 v45, v150, v45
	v_cvt_pk_bf16_f32 v182, v46, v47
	v_cvt_pk_bf16_f32 v183, v48, v49
	v_cvt_pk_bf16_f32 v184, v42, v43
	v_cvt_pk_bf16_f32 v185, v44, v45
	ds_write_b128 v164, v[182:185]
	v_mul_f32_e32 v38, v150, v38
	v_mul_f32_e32 v39, v150, v39
	v_mul_f32_e32 v40, v150, v40
	v_mul_f32_e32 v41, v150, v41
	v_mul_f32_e32 v34, v150, v34
	v_mul_f32_e32 v35, v150, v35
	v_mul_f32_e32 v36, v150, v36
	v_mul_f32_e32 v37, v150, v37
	v_cvt_pk_bf16_f32 v182, v38, v39
	v_cvt_pk_bf16_f32 v183, v40, v41
	v_cvt_pk_bf16_f32 v184, v34, v35
	v_cvt_pk_bf16_f32 v185, v36, v37
	v_xor_b32_e32 v167, 64, v164
	ds_write_b128 v167, v[182:185]
	v_mov_b32_e32 v46, 0
	v_mov_b32_e32 v42, 0
	v_mov_b32_e32 v38, 0
	v_mov_b32_e32 v34, 0
	v_mov_b32_e32 v47, 0
	v_mov_b32_e32 v43, 0
	v_mov_b32_e32 v39, 0
	v_mov_b32_e32 v35, 0
	v_mov_b32_e32 v48, 0
	v_mov_b32_e32 v44, 0
	v_mov_b32_e32 v40, 0
	v_mov_b32_e32 v36, 0
	v_mov_b32_e32 v49, 0
	v_mov_b32_e32 v45, 0
	v_mov_b32_e32 v41, 0
	v_mov_b32_e32 v37, 0
	ds_read_b128 v[182:185], v165 offset:0
	v_cmp_lt_i32_e32 vcc, -1, v151
	v_lshlrev_b32_e32 v148, 13, v151
	v_mov_b32_e32 v149, 0
	v_lshl_add_u64 v[148:149], v[148:149], 0, v[86:87]
	v_cndmask_b32_e32 v148, v168, v148, vcc
	v_cndmask_b32_e32 v149, v169, v149, vcc
	s_waitcnt lgkmcnt(0)
	global_store_dwordx4 v[148:149], v[182:185], off
	ds_read_b128 v[182:185], v165 offset:8192
	v_cmp_lt_i32_e32 vcc, -1, v166
	v_lshlrev_b32_e32 v148, 13, v166
	v_mov_b32_e32 v149, 0
	v_lshl_add_u64 v[148:149], v[148:149], 0, v[86:87]
	v_cndmask_b32_e32 v148, v168, v148, vcc
	v_cndmask_b32_e32 v149, v169, v149, vcc
	s_waitcnt lgkmcnt(0)
	global_store_dwordx4 v[148:149], v[182:185], off
	ds_read_b32 v150, v82 offset:768
	ds_read_b32 v151, v83 offset:768
	ds_read_b32 v166, v83 offset:896
	s_waitcnt lgkmcnt(2)
	v_mul_f32_e32 v18, v150, v18
	v_mul_f32_e32 v19, v150, v19
	v_mul_f32_e32 v20, v150, v20
	v_mul_f32_e32 v21, v150, v21
	v_mul_f32_e32 v22, v150, v22
	v_mul_f32_e32 v23, v150, v23
	v_mul_f32_e32 v24, v150, v24
	v_mul_f32_e32 v25, v150, v25
	v_cvt_pk_bf16_f32 v182, v18, v19
	v_cvt_pk_bf16_f32 v183, v20, v21
	v_cvt_pk_bf16_f32 v184, v22, v23
	v_cvt_pk_bf16_f32 v185, v24, v25
	ds_write_b128 v164, v[182:185]
	v_mul_f32_e32 v26, v150, v26
	v_mul_f32_e32 v27, v150, v27
	v_mul_f32_e32 v28, v150, v28
	v_mul_f32_e32 v29, v150, v29
	v_mul_f32_e32 v30, v150, v30
	v_mul_f32_e32 v31, v150, v31
	v_mul_f32_e32 v32, v150, v32
	v_mul_f32_e32 v33, v150, v33
	v_cvt_pk_bf16_f32 v182, v26, v27
	v_cvt_pk_bf16_f32 v183, v28, v29
	v_cvt_pk_bf16_f32 v184, v30, v31
	v_cvt_pk_bf16_f32 v185, v32, v33
	v_xor_b32_e32 v167, 64, v164
	ds_write_b128 v167, v[182:185]
	v_mov_b32_e32 v18, 0
	v_mov_b32_e32 v22, 0
	v_mov_b32_e32 v26, 0
	v_mov_b32_e32 v30, 0
	v_mov_b32_e32 v19, 0
	v_mov_b32_e32 v23, 0
	v_mov_b32_e32 v27, 0
	v_mov_b32_e32 v31, 0
	v_mov_b32_e32 v20, 0
	v_mov_b32_e32 v24, 0
	v_mov_b32_e32 v28, 0
	v_mov_b32_e32 v32, 0
	v_mov_b32_e32 v21, 0
	v_mov_b32_e32 v25, 0
	v_mov_b32_e32 v29, 0
	v_mov_b32_e32 v33, 0
	ds_read_b128 v[182:185], v165 offset:0
	v_cmp_lt_i32_e32 vcc, -1, v151
	v_lshlrev_b32_e32 v148, 13, v151
	v_mov_b32_e32 v149, 0
	v_lshl_add_u64 v[148:149], v[148:149], 0, v[86:87]
	v_cndmask_b32_e32 v148, v168, v148, vcc
	v_cndmask_b32_e32 v149, v169, v149, vcc
	s_waitcnt lgkmcnt(0)
; #define PG8_LAS __attribute__((address_space(3)))
; __device__ __forceinline__ unsigned cvtpk(float lo, float hi) { f32x2 v = {lo, hi}; bf16x2_t b = __builtin_convertvector(v, bf16x2_t); return __builtin_bit_cast(unsigned, b); }
; #define MD_GLDS_A(buf, tau) do { _Pragma("unroll") for (int i = 0; i < 5; ++i) if (amask & (1u << i)) \
;         __builtin_amdgcn_global_load_lds((const unsigned*)((const char*)HIDp + aoff[i] + (size_t)((tau) & 7) * 128), (PG8_LAS unsigned*)(MD_SA(buf) + wid * 1024 + i * 8192), 16, 0, 0); } while (0)
; __device__ __forceinline__ void moe_down_stream(PG8_LAS unsigned char* lds, int e, int cb0, int slot0, int nv, const bf16_t* HIDp, const float* Wd, bf16_t* Y, const float* slot_w, const int* slot_dst) {
;     ...
;     for (int t = 0; t < NT; t += 2) {
;         if (t + 2 < NT) MD_B_WAIT(s1, 8); else MD_B_WAIT(s1, 0);
;         MD_B_WRITE(s1, 1); __builtin_amdgcn_sched_barrier(0); MD_GLDS_A(1, t + 1); __builtin_amdgcn_sched_barrier(0);
;         if (t + 3 < NT) MD_B_ISSUE(s1, t + 3);
;         MD_COMPUTE(0);
;         MD_END(t + 3 >= NT);
;         if (t + 2 < NT) { MD_B_WAIT(s0, 8); MD_B_WRITE(s0, 0); __builtin_amdgcn_sched_barrier(0); MD_GLDS_A(0, t + 2); __builtin_amdgcn_sched_barrier(0); }
;         if (t + 4 < NT) MD_B_ISSUE(s0, t + 4);
;         MD_COMPUTE(1);
;         MD_END(t + 4 >= NT);
;         if (((t + 1) & 7) == 7) {
;             const int cb = cb0 + ((t + 1) >> 3);
; #pragma unroll
;             for (int m = 0; m < DNM; ++m) {
;                 const float w_ = lw[4 * (16 * m + fr) + wr];
; #pragma unroll
;                 for (int p = 0; p < 2; ++p) { const f32x4 v0 = acc[m][2 * p] * w_, v1 = acc[m][2 * p + 1] * w_; u32x4 w; w.x = cvtpk(v0[0], v0[1]); w.y = cvtpk(v0[2], v0[3]); w.z = cvtpk(v1[0], v1[1]); w.w = cvtpk(v1[2], v1[3]);
;                     *(PG8_LAS u32x4*)(stg + fr * 128 + (((4 * p + fq) ^ (fr & 7)) * 16)) = w; }
; #pragma unroll
;                 for (int hh = 0; hh < 2; ++hh) { const int r = (lane >> 3) + 8 * hh, cc = lane & 7; const u32x4 d = *(const PG8_LAS u32x4*)(stg + r * 128 + ((cc ^ (r & 7)) * 16)); const int dst_ = ldst[4 * (16 * m + r) + wr];
;                     if (dst_ >= 0) *(u32x4*)(Y + (size_t)dst_ * D + 128 * cb + 64 * wc + 8 * cc) = d; }
; #pragma unroll
;                 for (int n = 0; n < 4; ++n) acc[m][n] = (f32x4){0.f, 0.f, 0.f, 0.f}; } }
	global_store_dwordx4 v[148:149], v[182:185], off
	ds_read_b128 v[182:185], v165 offset:8192
	v_cmp_lt_i32_e32 vcc, -1, v166
	v_lshlrev_b32_e32 v148, 13, v166
	v_mov_b32_e32 v149, 0
	v_lshl_add_u64 v[148:149], v[148:149], 0, v[86:87]
	v_cndmask_b32_e32 v148, v168, v148, vcc
	v_cndmask_b32_e32 v149, v169, v149, vcc
	s_waitcnt lgkmcnt(0)
	global_store_dwordx4 v[148:149], v[182:185], off
	ds_read_b32 v150, v82 offset:1024
	ds_read_b32 v151, v83 offset:1024
	ds_read_b32 v166, v83 offset:1152
	s_waitcnt lgkmcnt(2)
	v_mul_f32_e32 v2, v150, v2
	v_mul_f32_e32 v3, v150, v3
	v_mul_f32_e32 v4, v150, v4
	v_mul_f32_e32 v5, v150, v5
	v_mul_f32_e32 v6, v150, v6
	v_mul_f32_e32 v7, v150, v7
	v_mul_f32_e32 v8, v150, v8
	v_mul_f32_e32 v9, v150, v9
	v_cvt_pk_bf16_f32 v182, v2, v3
	v_cvt_pk_bf16_f32 v183, v4, v5
	v_cvt_pk_bf16_f32 v184, v6, v7
	v_cvt_pk_bf16_f32 v185, v8, v9
	ds_write_b128 v164, v[182:185]
	v_mul_f32_e32 v10, v150, v10
	v_mul_f32_e32 v11, v150, v11
	v_mul_f32_e32 v12, v150, v12
	v_mul_f32_e32 v13, v150, v13
	v_mul_f32_e32 v14, v150, v14
	v_mul_f32_e32 v15, v150, v15
	v_mul_f32_e32 v16, v150, v16
	v_mul_f32_e32 v17, v150, v17
	v_cvt_pk_bf16_f32 v182, v10, v11
	v_cvt_pk_bf16_f32 v183, v12, v13
	v_cvt_pk_bf16_f32 v184, v14, v15
	v_cvt_pk_bf16_f32 v185, v16, v17
	v_xor_b32_e32 v167, 64, v164
	ds_write_b128 v167, v[182:185]
	v_mov_b32_e32 v2, 0
	v_mov_b32_e32 v6, 0
	v_mov_b32_e32 v10, 0
	v_mov_b32_e32 v14, 0
	v_mov_b32_e32 v3, 0
	v_mov_b32_e32 v7, 0
	v_mov_b32_e32 v11, 0
	v_mov_b32_e32 v15, 0
	v_mov_b32_e32 v4, 0
	v_mov_b32_e32 v8, 0
	v_mov_b32_e32 v12, 0
	v_mov_b32_e32 v16, 0
	v_mov_b32_e32 v5, 0
	v_mov_b32_e32 v9, 0
	v_mov_b32_e32 v13, 0
	v_mov_b32_e32 v17, 0
	ds_read_b128 v[182:185], v165 offset:0
	v_cmp_lt_i32_e32 vcc, -1, v151
	v_lshlrev_b32_e32 v148, 13, v151
	v_mov_b32_e32 v149, 0
	v_lshl_add_u64 v[148:149], v[148:149], 0, v[86:87]
	v_cndmask_b32_e32 v148, v168, v148, vcc
	v_cndmask_b32_e32 v149, v169, v149, vcc
	s_waitcnt lgkmcnt(0)
	global_store_dwordx4 v[148:149], v[182:185], off
	ds_read_b128 v[182:185], v165 offset:8192
	v_cmp_lt_i32_e32 vcc, -1, v166
	v_lshlrev_b32_e32 v148, 13, v166
	v_mov_b32_e32 v149, 0
	v_lshl_add_u64 v[148:149], v[148:149], 0, v[86:87]
	v_cndmask_b32_e32 v148, v168, v148, vcc
	v_cndmask_b32_e32 v149, v169, v149, vcc
	s_waitcnt lgkmcnt(0)
	global_store_dwordx4 v[148:149], v[182:185], off
	v_add_co_u32_e32 v86, vcc, 0x400, v86
	s_nop 1
	v_addc_co_u32_e32 v87, vcc, 0, v87, vcc
	s_waitcnt lgkmcnt(0)
	s_add_i32 s49, s48, s74
	s_add_i32 s52, s52, 1
	s_and_b32 s54, s52, 7
	s_cmp_eq_u32 s54, 0
	s_cselect_b32 s54, s53, s32
	s_cselect_b32 s55, -1, 0
	s_add_u32 s30, s30, s54
	s_addc_u32 s31, s31, s55
	s_mov_b32 m0, s49
	s_nop 0
	global_load_lds_dwordx4 v88, s[30:31]
	s_add_i32 m0, s49, 0x2000
	s_nop 0
	global_load_lds_dwordx4 v90, s[30:31]
	s_add_i32 m0, s49, 0x4000
	s_nop 0
	global_load_lds_dwordx4 v92, s[30:31]
	s_add_i32 m0, s49, 0x6000
	s_nop 0
	global_load_lds_dwordx4 v94, s[30:31]
	s_add_i32 m0, s49, 0x8000
	s_nop 0
	global_load_lds_dwordx4 v96, s[30:31]
	v_cvt_pk_bf16_f32 v172, v114, v116
	v_cvt_pk_bf16_f32 v173, v118, v120
	v_cvt_pk_bf16_f32 v174, v122, v124
	v_cvt_pk_bf16_f32 v175, v126, v128
	v_cvt_pk_bf16_f32 v176, v115, v117
	v_cvt_pk_bf16_f32 v177, v119, v121
	v_cvt_pk_bf16_f32 v178, v123, v125
	v_cvt_pk_bf16_f32 v179, v127, v129
	ds_write_b128 v95, v[172:175] offset:19456
	ds_write_b128 v95, v[176:179] offset:19584
	v_add_u32_e32 v91, s46, v135
	v_add_u32_e32 v93, s46, v137
	ds_read_b128 v[238:241], v139 offset:0
	ds_read_b128 v[242:245], v139 offset:2048
	ds_read_b128 v[246:249], v139 offset:4096
	ds_read_b128 v[250:253], v139 offset:6144
	ds_read_b128 v[218:221], v91 offset:0
	ds_read_b128 v[222:225], v91 offset:2048
	ds_read_b128 v[226:229], v91 offset:4096
	ds_read_b128 v[230:233], v91 offset:6144
	ds_read_b128 v[234:237], v91 offset:8192
	s_waitcnt lgkmcnt(0)
	v_mfma_f32_16x16x32_bf16 v[78:81], v[238:241], v[218:221], v[78:81]
	v_mfma_f32_16x16x32_bf16 v[74:77], v[242:245], v[218:221], v[74:77]
	v_mfma_f32_16x16x32_bf16 v[70:73], v[246:249], v[218:221], v[70:73]
	v_mfma_f32_16x16x32_bf16 v[66:69], v[250:253], v[218:221], v[66:69]
	ds_read_b128 v[218:221], v93 offset:0
	ds_read_b128 v[142:145], v141 offset:0
	s_add_i32 s51, s51, 1
	s_and_b32 s54, s51, 7
	s_cmp_eq_u32 s54, 0
	s_cselect_b32 s44, s34, s35
	s_cselect_b32 s45, -1, 0
	v_lshl_add_u64 v[132:133], v[132:133], 0, s[44:45]
	global_load_dwordx2 v[114:115], v[132:133], off
	v_lshl_add_u64 v[180:181], v[132:133], 0, s[24:25]
	global_load_dwordx2 v[116:117], v[180:181], off
	v_mfma_f32_16x16x32_bf16 v[62:65], v[238:241], v[222:225], v[62:65]
	v_mfma_f32_16x16x32_bf16 v[58:61], v[242:245], v[222:225], v[58:61]
	v_mfma_f32_16x16x32_bf16 v[54:57], v[246:249], v[222:225], v[54:57]
	v_mfma_f32_16x16x32_bf16 v[50:53], v[250:253], v[222:225], v[50:53]
	ds_read_b128 v[222:225], v93 offset:2048
	ds_read_b128 v[146:149], v141 offset:2048
	v_lshl_add_u64 v[180:181], v[132:133], 0, s[26:27]
	global_load_dwordx2 v[118:119], v[180:181], off
	v_lshl_add_u64 v[180:181], v[132:133], 0, s[28:29]
	global_load_dwordx2 v[120:121], v[180:181], off
	v_mfma_f32_16x16x32_bf16 v[46:49], v[238:241], v[226:229], v[46:49]
	v_mfma_f32_16x16x32_bf16 v[42:45], v[242:245], v[226:229], v[42:45]
	v_mfma_f32_16x16x32_bf16 v[38:41], v[246:249], v[226:229], v[38:41]
	v_mfma_f32_16x16x32_bf16 v[34:37], v[250:253], v[226:229], v[34:37]
	ds_read_b128 v[226:229], v93 offset:4096
	ds_read_b128 v[156:159], v141 offset:4096
	v_lshl_add_u64 v[180:181], v[132:133], 0, s[36:37]
	global_load_dwordx2 v[122:123], v[180:181], off
	v_lshl_add_u64 v[180:181], v[132:133], 0, s[38:39]
	global_load_dwordx2 v[124:125], v[180:181], off
	v_mfma_f32_16x16x32_bf16 v[18:21], v[238:241], v[230:233], v[18:21]
	v_mfma_f32_16x16x32_bf16 v[22:25], v[242:245], v[230:233], v[22:25]
	v_mfma_f32_16x16x32_bf16 v[26:29], v[246:249], v[230:233], v[26:29]
	v_mfma_f32_16x16x32_bf16 v[30:33], v[250:253], v[230:233], v[30:33]
	ds_read_b128 v[230:233], v93 offset:6144
	ds_read_b128 v[160:163], v141 offset:6144
	v_lshl_add_u64 v[180:181], v[132:133], 0, s[40:41]
	global_load_dwordx2 v[126:127], v[180:181], off
	v_lshl_add_u64 v[180:181], v[132:133], 0, s[42:43]
	global_load_dwordx2 v[128:129], v[180:181], off
	v_mfma_f32_16x16x32_bf16 v[2:5], v[238:241], v[234:237], v[2:5]
	v_mfma_f32_16x16x32_bf16 v[6:9], v[242:245], v[234:237], v[6:9]
	v_mfma_f32_16x16x32_bf16 v[10:13], v[246:249], v[234:237], v[10:13]
	v_mfma_f32_16x16x32_bf16 v[14:17], v[250:253], v[234:237], v[14:17]
	ds_read_b128 v[234:237], v93 offset:8192
	s_waitcnt vmcnt(31)
	s_waitcnt lgkmcnt(0)
	s_barrier
; #define MD_GLDS_A(buf, tau) do { _Pragma("unroll") for (int i = 0; i < 5; ++i) if (amask & (1u << i)) \
;         __builtin_amdgcn_global_load_lds((const unsigned*)((const char*)HIDp + aoff[i] + (size_t)((tau) & 7) * 128), (PG8_LAS unsigned*)(MD_SA(buf) + wid * 1024 + i * 8192), 16, 0, 0); } while (0)
; #define MD_B_ISSUE(sb, tau) do { const char* kb_ = Bb + (size_t)((tau) >> 3) * 512 + (size_t)((tau) & 7) * (64 * (size_t)RB); _Pragma("unroll") for (int j = 0; j < 8; ++j) { const char* p_ = kb_ + (size_t)j * RB; \
;         asm volatile("global_load_dwordx2 %0, %1, off" : "=&v"(sb[j]) : "v"(p_) : "memory"); } } while (0)
; #define MD_B_WAIT(sb, N) asm volatile("s_waitcnt vmcnt(%8)" : "+v"(sb[0]), "+v"(sb[1]), "+v"(sb[2]), "+v"(sb[3]), "+v"(sb[4]), "+v"(sb[5]), "+v"(sb[6]), "+v"(sb[7]) : "n"(N) : "memory")
; #define MD_END(last) do { if (last) asm volatile("s_waitcnt vmcnt(0)" ::: "memory"); else asm volatile("s_waitcnt vmcnt(8)" ::: "memory"); \
;         asm volatile("s_waitcnt lgkmcnt(0)" ::: "memory"); __builtin_amdgcn_s_barrier(); asm volatile("" ::: "memory"); } while (0)
; __device__ __forceinline__ void moe_down_stream(PG8_LAS unsigned char* lds, int e, int cb0, int slot0, int nv, const bf16_t* HIDp, const float* Wd, bf16_t* Y, const float* slot_w, const int* slot_dst) {
;     ...
;     for (int t = 0; t < NT; t += 2) {
;         if (t + 2 < NT) MD_B_WAIT(s1, 8); else MD_B_WAIT(s1, 0);
;         MD_B_WRITE(s1, 1); __builtin_amdgcn_sched_barrier(0); MD_GLDS_A(1, t + 1); __builtin_amdgcn_sched_barrier(0);
;         if (t + 3 < NT) MD_B_ISSUE(s1, t + 3);
;         MD_COMPUTE(0);
;         MD_END(t + 3 >= NT);
;         if (t + 2 < NT) { MD_B_WAIT(s0, 8); MD_B_WRITE(s0, 0); __builtin_amdgcn_sched_barrier(0); MD_GLDS_A(0, t + 2); __builtin_amdgcn_sched_barrier(0); }
;         if (t + 4 < NT) MD_B_ISSUE(s0, t + 4);
;         MD_COMPUTE(1);
;         MD_END(t + 4 >= NT);
	s_mov_b32 s49, s46
	s_mov_b32 s46, s47
	s_mov_b32 s47, s48
	s_mov_b32 s48, s49
	s_add_i32 s50, s50, 1
	s_add_i32 s49, s48, s74
	s_add_i32 s52, s52, 1
	s_and_b32 s54, s52, 7
	s_cmp_eq_u32 s54, 0
	s_cselect_b32 s54, s53, s32
	s_cselect_b32 s55, -1, 0
	s_add_u32 s30, s30, s54
	s_addc_u32 s31, s31, s55
	v_mfma_f32_16x16x32_bf16 v[78:81], v[142:145], v[218:221], v[78:81]
	v_mfma_f32_16x16x32_bf16 v[74:77], v[146:149], v[218:221], v[74:77]
	v_mfma_f32_16x16x32_bf16 v[70:73], v[156:159], v[218:221], v[70:73]
	v_mfma_f32_16x16x32_bf16 v[66:69], v[160:163], v[218:221], v[66:69]
	s_mov_b32 m0, s49
	s_nop 0
	global_load_lds_dwordx4 v88, s[30:31]
	v_mfma_f32_16x16x32_bf16 v[62:65], v[142:145], v[222:225], v[62:65]
	v_mfma_f32_16x16x32_bf16 v[58:61], v[146:149], v[222:225], v[58:61]
	v_mfma_f32_16x16x32_bf16 v[54:57], v[156:159], v[222:225], v[54:57]
	v_mfma_f32_16x16x32_bf16 v[50:53], v[160:163], v[222:225], v[50:53]
	s_add_i32 m0, s49, 0x2000
	s_nop 0
	global_load_lds_dwordx4 v90, s[30:31]
	v_mfma_f32_16x16x32_bf16 v[46:49], v[142:145], v[226:229], v[46:49]
	v_mfma_f32_16x16x32_bf16 v[42:45], v[146:149], v[226:229], v[42:45]
	v_mfma_f32_16x16x32_bf16 v[38:41], v[156:159], v[226:229], v[38:41]
	v_mfma_f32_16x16x32_bf16 v[34:37], v[160:163], v[226:229], v[34:37]
	s_add_i32 m0, s49, 0x4000
	s_nop 0
	global_load_lds_dwordx4 v92, s[30:31]
	v_mfma_f32_16x16x32_bf16 v[18:21], v[142:145], v[230:233], v[18:21]
	v_mfma_f32_16x16x32_bf16 v[22:25], v[146:149], v[230:233], v[22:25]
	v_mfma_f32_16x16x32_bf16 v[26:29], v[156:159], v[230:233], v[26:29]
	v_mfma_f32_16x16x32_bf16 v[30:33], v[160:163], v[230:233], v[30:33]
	s_add_i32 m0, s49, 0x6000
	s_nop 0
	global_load_lds_dwordx4 v94, s[30:31]
	v_mfma_f32_16x16x32_bf16 v[2:5], v[142:145], v[234:237], v[2:5]
	v_mfma_f32_16x16x32_bf16 v[6:9], v[146:149], v[234:237], v[6:9]
	v_mfma_f32_16x16x32_bf16 v[10:13], v[156:159], v[234:237], v[10:13]
	v_mfma_f32_16x16x32_bf16 v[14:17], v[160:163], v[234:237], v[14:17]
	s_add_i32 m0, s49, 0x8000
	s_nop 0
	global_load_lds_dwordx4 v96, s[30:31]
	v_cvt_pk_bf16_f32 v172, v186, v188
	v_cvt_pk_bf16_f32 v173, v190, v192
	v_cvt_pk_bf16_f32 v174, v194, v196
	v_cvt_pk_bf16_f32 v175, v198, v200
	v_cvt_pk_bf16_f32 v176, v187, v189
	v_cvt_pk_bf16_f32 v177, v191, v193
	v_cvt_pk_bf16_f32 v178, v195, v197
	v_cvt_pk_bf16_f32 v179, v199, v201
	ds_write_b128 v95, v[172:175] offset:0
	ds_write_b128 v95, v[176:179] offset:128
	v_add_u32_e32 v91, s46, v135
	v_add_u32_e32 v93, s46, v137
	ds_read_b128 v[238:241], v139 offset:19456
	ds_read_b128 v[242:245], v139 offset:21504
	ds_read_b128 v[246:249], v139 offset:23552
	ds_read_b128 v[250:253], v139 offset:25600
	ds_read_b128 v[218:221], v91 offset:0
	ds_read_b128 v[222:225], v91 offset:2048
	ds_read_b128 v[226:229], v91 offset:4096
	ds_read_b128 v[230:233], v91 offset:6144
	ds_read_b128 v[234:237], v91 offset:8192
	s_waitcnt lgkmcnt(0)
	v_mfma_f32_16x16x32_bf16 v[78:81], v[238:241], v[218:221], v[78:81]
	v_mfma_f32_16x16x32_bf16 v[74:77], v[242:245], v[218:221], v[74:77]
	v_mfma_f32_16x16x32_bf16 v[70:73], v[246:249], v[218:221], v[70:73]
	v_mfma_f32_16x16x32_bf16 v[66:69], v[250:253], v[218:221], v[66:69]
	ds_read_b128 v[218:221], v93 offset:0
	ds_read_b128 v[142:145], v141 offset:19456
	s_add_i32 s51, s51, 1
	s_and_b32 s54, s51, 7
	s_cmp_eq_u32 s54, 0
	s_cselect_b32 s44, s34, s35
	s_cselect_b32 s45, -1, 0
	v_lshl_add_u64 v[132:133], v[132:133], 0, s[44:45]
	global_load_dwordx2 v[186:187], v[132:133], off
	v_lshl_add_u64 v[180:181], v[132:133], 0, s[24:25]
	global_load_dwordx2 v[188:189], v[180:181], off
	v_mfma_f32_16x16x32_bf16 v[62:65], v[238:241], v[222:225], v[62:65]
	v_mfma_f32_16x16x32_bf16 v[58:61], v[242:245], v[222:225], v[58:61]
	v_mfma_f32_16x16x32_bf16 v[54:57], v[246:249], v[222:225], v[54:57]
	v_mfma_f32_16x16x32_bf16 v[50:53], v[250:253], v[222:225], v[50:53]
	ds_read_b128 v[222:225], v93 offset:2048
	ds_read_b128 v[146:149], v141 offset:21504
	v_lshl_add_u64 v[180:181], v[132:133], 0, s[26:27]
	global_load_dwordx2 v[190:191], v[180:181], off
	v_lshl_add_u64 v[180:181], v[132:133], 0, s[28:29]
	global_load_dwordx2 v[192:193], v[180:181], off
	v_mfma_f32_16x16x32_bf16 v[46:49], v[238:241], v[226:229], v[46:49]
	v_mfma_f32_16x16x32_bf16 v[42:45], v[242:245], v[226:229], v[42:45]
	v_mfma_f32_16x16x32_bf16 v[38:41], v[246:249], v[226:229], v[38:41]
	v_mfma_f32_16x16x32_bf16 v[34:37], v[250:253], v[226:229], v[34:37]
	ds_read_b128 v[226:229], v93 offset:4096
	ds_read_b128 v[156:159], v141 offset:23552
	v_lshl_add_u64 v[180:181], v[132:133], 0, s[36:37]
	global_load_dwordx2 v[194:195], v[180:181], off
	v_lshl_add_u64 v[180:181], v[132:133], 0, s[38:39]
	global_load_dwordx2 v[196:197], v[180:181], off
	v_mfma_f32_16x16x32_bf16 v[18:21], v[238:241], v[230:233], v[18:21]
	v_mfma_f32_16x16x32_bf16 v[22:25], v[242:245], v[230:233], v[22:25]
	v_mfma_f32_16x16x32_bf16 v[26:29], v[246:249], v[230:233], v[26:29]
	v_mfma_f32_16x16x32_bf16 v[30:33], v[250:253], v[230:233], v[30:33]
	ds_read_b128 v[230:233], v93 offset:6144
	ds_read_b128 v[160:163], v141 offset:25600
	v_lshl_add_u64 v[180:181], v[132:133], 0, s[40:41]
	global_load_dwordx2 v[198:199], v[180:181], off
	v_lshl_add_u64 v[180:181], v[132:133], 0, s[42:43]
	global_load_dwordx2 v[200:201], v[180:181], off
	v_mfma_f32_16x16x32_bf16 v[2:5], v[238:241], v[234:237], v[2:5]
	v_mfma_f32_16x16x32_bf16 v[6:9], v[242:245], v[234:237], v[6:9]
	v_mfma_f32_16x16x32_bf16 v[10:13], v[246:249], v[234:237], v[10:13]
	v_mfma_f32_16x16x32_bf16 v[14:17], v[250:253], v[234:237], v[14:17]
	ds_read_b128 v[234:237], v93 offset:8192
	s_waitcnt vmcnt(21)
	s_waitcnt lgkmcnt(0)
	s_barrier
; #define MD_GLDS_A(buf, tau) do { _Pragma("unroll") for (int i = 0; i < 5; ++i) if (amask & (1u << i)) \
;         __builtin_amdgcn_global_load_lds((const unsigned*)((const char*)HIDp + aoff[i] + (size_t)((tau) & 7) * 128), (PG8_LAS unsigned*)(MD_SA(buf) + wid * 1024 + i * 8192), 16, 0, 0); } while (0)
; #define MD_B_ISSUE(sb, tau) do { const char* kb_ = Bb + (size_t)((tau) >> 3) * 512 + (size_t)((tau) & 7) * (64 * (size_t)RB); _Pragma("unroll") for (int j = 0; j < 8; ++j) { const char* p_ = kb_ + (size_t)j * RB; \
;         asm volatile("global_load_dwordx2 %0, %1, off" : "=&v"(sb[j]) : "v"(p_) : "memory"); } } while (0)
; #define MD_B_WAIT(sb, N) asm volatile("s_waitcnt vmcnt(%8)" : "+v"(sb[0]), "+v"(sb[1]), "+v"(sb[2]), "+v"(sb[3]), "+v"(sb[4]), "+v"(sb[5]), "+v"(sb[6]), "+v"(sb[7]) : "n"(N) : "memory")
; #define MD_END(last) do { if (last) asm volatile("s_waitcnt vmcnt(0)" ::: "memory"); else asm volatile("s_waitcnt vmcnt(8)" ::: "memory"); \
;         asm volatile("s_waitcnt lgkmcnt(0)" ::: "memory"); __builtin_amdgcn_s_barrier(); asm volatile("" ::: "memory"); } while (0)
; __device__ __forceinline__ void moe_down_stream(PG8_LAS unsigned char* lds, int e, int cb0, int slot0, int nv, const bf16_t* HIDp, const float* Wd, bf16_t* Y, const float* slot_w, const int* slot_dst) {
;     ...
;     for (int t = 0; t < NT; t += 2) {
;         if (t + 2 < NT) MD_B_WAIT(s1, 8); else MD_B_WAIT(s1, 0);
;         MD_B_WRITE(s1, 1); __builtin_amdgcn_sched_barrier(0); MD_GLDS_A(1, t + 1); __builtin_amdgcn_sched_barrier(0);
;         if (t + 3 < NT) MD_B_ISSUE(s1, t + 3);
;         MD_COMPUTE(0);
;         MD_END(t + 3 >= NT);
;         if (t + 2 < NT) { MD_B_WAIT(s0, 8); MD_B_WRITE(s0, 0); __builtin_amdgcn_sched_barrier(0); MD_GLDS_A(0, t + 2); __builtin_amdgcn_sched_barrier(0); }
;         if (t + 4 < NT) MD_B_ISSUE(s0, t + 4);
;         MD_COMPUTE(1);
;         MD_END(t + 4 >= NT);
	s_mov_b32 s49, s46
	s_mov_b32 s46, s47
	s_mov_b32 s47, s48
	s_mov_b32 s48, s49
	s_add_i32 s50, s50, 1
	s_add_i32 s49, s48, s74
	s_add_i32 s52, s52, 1
	s_and_b32 s54, s52, 7
	s_cmp_eq_u32 s54, 0
	s_cselect_b32 s54, s53, s32
	s_cselect_b32 s55, -1, 0
	s_add_u32 s30, s30, s54
	s_addc_u32 s31, s31, s55
	v_mfma_f32_16x16x32_bf16 v[78:81], v[142:145], v[218:221], v[78:81]
	v_mfma_f32_16x16x32_bf16 v[74:77], v[146:149], v[218:221], v[74:77]
	v_mfma_f32_16x16x32_bf16 v[70:73], v[156:159], v[218:221], v[70:73]
	v_mfma_f32_16x16x32_bf16 v[66:69], v[160:163], v[218:221], v[66:69]
	s_mov_b32 m0, s49
	s_nop 0
	global_load_lds_dwordx4 v88, s[30:31]
	v_mfma_f32_16x16x32_bf16 v[62:65], v[142:145], v[222:225], v[62:65]
	v_mfma_f32_16x16x32_bf16 v[58:61], v[146:149], v[222:225], v[58:61]
	v_mfma_f32_16x16x32_bf16 v[54:57], v[156:159], v[222:225], v[54:57]
	v_mfma_f32_16x16x32_bf16 v[50:53], v[160:163], v[222:225], v[50:53]
	s_add_i32 m0, s49, 0x2000
	s_nop 0
	global_load_lds_dwordx4 v90, s[30:31]
	v_mfma_f32_16x16x32_bf16 v[46:49], v[142:145], v[226:229], v[46:49]
	v_mfma_f32_16x16x32_bf16 v[42:45], v[146:149], v[226:229], v[42:45]
	v_mfma_f32_16x16x32_bf16 v[38:41], v[156:159], v[226:229], v[38:41]
	v_mfma_f32_16x16x32_bf16 v[34:37], v[160:163], v[226:229], v[34:37]
	s_add_i32 m0, s49, 0x4000
	s_nop 0
	global_load_lds_dwordx4 v92, s[30:31]
	v_mfma_f32_16x16x32_bf16 v[18:21], v[142:145], v[230:233], v[18:21]
	v_mfma_f32_16x16x32_bf16 v[22:25], v[146:149], v[230:233], v[22:25]
	v_mfma_f32_16x16x32_bf16 v[26:29], v[156:159], v[230:233], v[26:29]
	v_mfma_f32_16x16x32_bf16 v[30:33], v[160:163], v[230:233], v[30:33]
	s_add_i32 m0, s49, 0x6000
	s_nop 0
	global_load_lds_dwordx4 v94, s[30:31]
	v_mfma_f32_16x16x32_bf16 v[2:5], v[142:145], v[234:237], v[2:5]
	v_mfma_f32_16x16x32_bf16 v[6:9], v[146:149], v[234:237], v[6:9]
	v_mfma_f32_16x16x32_bf16 v[10:13], v[156:159], v[234:237], v[10:13]
	v_mfma_f32_16x16x32_bf16 v[14:17], v[160:163], v[234:237], v[14:17]
	s_add_i32 m0, s49, 0x8000
	s_nop 0
	global_load_lds_dwordx4 v96, s[30:31]
	v_cvt_pk_bf16_f32 v172, v202, v204
	v_cvt_pk_bf16_f32 v173, v206, v208
	v_cvt_pk_bf16_f32 v174, v210, v212
	v_cvt_pk_bf16_f32 v175, v214, v216
	v_cvt_pk_bf16_f32 v176, v203, v205
	v_cvt_pk_bf16_f32 v177, v207, v209
	v_cvt_pk_bf16_f32 v178, v211, v213
	v_cvt_pk_bf16_f32 v179, v215, v217
	ds_write_b128 v95, v[172:175] offset:19456
	ds_write_b128 v95, v[176:179] offset:19584
	v_add_u32_e32 v91, s46, v135
	v_add_u32_e32 v93, s46, v137
	ds_read_b128 v[238:241], v139 offset:0
	ds_read_b128 v[242:245], v139 offset:2048
	ds_read_b128 v[246:249], v139 offset:4096
	ds_read_b128 v[250:253], v139 offset:6144
	ds_read_b128 v[218:221], v91 offset:0
	ds_read_b128 v[222:225], v91 offset:2048
	ds_read_b128 v[226:229], v91 offset:4096
	ds_read_b128 v[230:233], v91 offset:6144
	ds_read_b128 v[234:237], v91 offset:8192
	s_waitcnt lgkmcnt(0)
	v_mfma_f32_16x16x32_bf16 v[78:81], v[238:241], v[218:221], v[78:81]
	v_mfma_f32_16x16x32_bf16 v[74:77], v[242:245], v[218:221], v[74:77]
	v_mfma_f32_16x16x32_bf16 v[70:73], v[246:249], v[218:221], v[70:73]
	v_mfma_f32_16x16x32_bf16 v[66:69], v[250:253], v[218:221], v[66:69]
	ds_read_b128 v[218:221], v93 offset:0
	ds_read_b128 v[142:145], v141 offset:0
	s_add_i32 s51, s51, 1
	s_and_b32 s54, s51, 7
	s_cmp_eq_u32 s54, 0
	s_cselect_b32 s44, s34, s35
	s_cselect_b32 s45, -1, 0
	v_lshl_add_u64 v[132:133], v[132:133], 0, s[44:45]
	global_load_dwordx2 v[202:203], v[132:133], off
	v_lshl_add_u64 v[180:181], v[132:133], 0, s[24:25]
	global_load_dwordx2 v[204:205], v[180:181], off
	v_mfma_f32_16x16x32_bf16 v[62:65], v[238:241], v[222:225], v[62:65]
	v_mfma_f32_16x16x32_bf16 v[58:61], v[242:245], v[222:225], v[58:61]
	v_mfma_f32_16x16x32_bf16 v[54:57], v[246:249], v[222:225], v[54:57]
	v_mfma_f32_16x16x32_bf16 v[50:53], v[250:253], v[222:225], v[50:53]
	ds_read_b128 v[222:225], v93 offset:2048
	ds_read_b128 v[146:149], v141 offset:2048
	v_lshl_add_u64 v[180:181], v[132:133], 0, s[26:27]
	global_load_dwordx2 v[206:207], v[180:181], off
	v_lshl_add_u64 v[180:181], v[132:133], 0, s[28:29]
	global_load_dwordx2 v[208:209], v[180:181], off
	v_mfma_f32_16x16x32_bf16 v[46:49], v[238:241], v[226:229], v[46:49]
	v_mfma_f32_16x16x32_bf16 v[42:45], v[242:245], v[226:229], v[42:45]
	v_mfma_f32_16x16x32_bf16 v[38:41], v[246:249], v[226:229], v[38:41]
	v_mfma_f32_16x16x32_bf16 v[34:37], v[250:253], v[226:229], v[34:37]
	ds_read_b128 v[226:229], v93 offset:4096
	ds_read_b128 v[156:159], v141 offset:4096
	v_lshl_add_u64 v[180:181], v[132:133], 0, s[36:37]
	global_load_dwordx2 v[210:211], v[180:181], off
	v_lshl_add_u64 v[180:181], v[132:133], 0, s[38:39]
	global_load_dwordx2 v[212:213], v[180:181], off
	v_mfma_f32_16x16x32_bf16 v[18:21], v[238:241], v[230:233], v[18:21]
	v_mfma_f32_16x16x32_bf16 v[22:25], v[242:245], v[230:233], v[22:25]
	v_mfma_f32_16x16x32_bf16 v[26:29], v[246:249], v[230:233], v[26:29]
	v_mfma_f32_16x16x32_bf16 v[30:33], v[250:253], v[230:233], v[30:33]
	ds_read_b128 v[230:233], v93 offset:6144
	ds_read_b128 v[160:163], v141 offset:6144
	v_lshl_add_u64 v[180:181], v[132:133], 0, s[40:41]
	global_load_dwordx2 v[214:215], v[180:181], off
	v_lshl_add_u64 v[180:181], v[132:133], 0, s[42:43]
	global_load_dwordx2 v[216:217], v[180:181], off
	v_mfma_f32_16x16x32_bf16 v[2:5], v[238:241], v[234:237], v[2:5]
	v_mfma_f32_16x16x32_bf16 v[6:9], v[242:245], v[234:237], v[6:9]
	v_mfma_f32_16x16x32_bf16 v[10:13], v[246:249], v[234:237], v[10:13]
	v_mfma_f32_16x16x32_bf16 v[14:17], v[250:253], v[234:237], v[14:17]
	ds_read_b128 v[234:237], v93 offset:8192
	s_waitcnt vmcnt(21)
	s_waitcnt lgkmcnt(0)
	s_barrier
; #define MD_GLDS_A(buf, tau) do { _Pragma("unroll") for (int i = 0; i < 5; ++i) if (amask & (1u << i)) \
;         __builtin_amdgcn_global_load_lds((const unsigned*)((const char*)HIDp + aoff[i] + (size_t)((tau) & 7) * 128), (PG8_LAS unsigned*)(MD_SA(buf) + wid * 1024 + i * 8192), 16, 0, 0); } while (0)
; #define MD_B_ISSUE(sb, tau) do { const char* kb_ = Bb + (size_t)((tau) >> 3) * 512 + (size_t)((tau) & 7) * (64 * (size_t)RB); _Pragma("unroll") for (int j = 0; j < 8; ++j) { const char* p_ = kb_ + (size_t)j * RB; \
;         asm volatile("global_load_dwordx2 %0, %1, off" : "=&v"(sb[j]) : "v"(p_) : "memory"); } } while (0)
; #define MD_B_WAIT(sb, N) asm volatile("s_waitcnt vmcnt(%8)" : "+v"(sb[0]), "+v"(sb[1]), "+v"(sb[2]), "+v"(sb[3]), "+v"(sb[4]), "+v"(sb[5]), "+v"(sb[6]), "+v"(sb[7]) : "n"(N) : "memory")
; #define MD_END(last) do { if (last) asm volatile("s_waitcnt vmcnt(0)" ::: "memory"); else asm volatile("s_waitcnt vmcnt(8)" ::: "memory"); \
;         asm volatile("s_waitcnt lgkmcnt(0)" ::: "memory"); __builtin_amdgcn_s_barrier(); asm volatile("" ::: "memory"); } while (0)
; __device__ __forceinline__ void moe_down_stream(PG8_LAS unsigned char* lds, int e, int cb0, int slot0, int nv, const bf16_t* HIDp, const float* Wd, bf16_t* Y, const float* slot_w, const int* slot_dst) {
;     ...
;     for (int t = 0; t < NT; t += 2) {
;         if (t + 2 < NT) MD_B_WAIT(s1, 8); else MD_B_WAIT(s1, 0);
;         MD_B_WRITE(s1, 1); __builtin_amdgcn_sched_barrier(0); MD_GLDS_A(1, t + 1); __builtin_amdgcn_sched_barrier(0);
;         if (t + 3 < NT) MD_B_ISSUE(s1, t + 3);
;         MD_COMPUTE(0);
;         MD_END(t + 3 >= NT);
;         if (t + 2 < NT) { MD_B_WAIT(s0, 8); MD_B_WRITE(s0, 0); __builtin_amdgcn_sched_barrier(0); MD_GLDS_A(0, t + 2); __builtin_amdgcn_sched_barrier(0); }
;         if (t + 4 < NT) MD_B_ISSUE(s0, t + 4);
;         MD_COMPUTE(1);
;         MD_END(t + 4 >= NT);
	s_mov_b32 s49, s46
	s_mov_b32 s46, s47
	s_mov_b32 s47, s48
	s_mov_b32 s48, s49
	s_add_i32 s50, s50, 1
	s_add_i32 s49, s48, s74
	s_add_i32 s52, s52, 1
	s_and_b32 s54, s52, 7
	s_cmp_eq_u32 s54, 0
	s_cselect_b32 s54, s53, s32
	s_cselect_b32 s55, -1, 0
	s_add_u32 s30, s30, s54
	s_addc_u32 s31, s31, s55
	v_mfma_f32_16x16x32_bf16 v[78:81], v[142:145], v[218:221], v[78:81]
	v_mfma_f32_16x16x32_bf16 v[74:77], v[146:149], v[218:221], v[74:77]
	v_mfma_f32_16x16x32_bf16 v[70:73], v[156:159], v[218:221], v[70:73]
	v_mfma_f32_16x16x32_bf16 v[66:69], v[160:163], v[218:221], v[66:69]
	s_mov_b32 m0, s49
	s_nop 0
	global_load_lds_dwordx4 v88, s[30:31]
	v_mfma_f32_16x16x32_bf16 v[62:65], v[142:145], v[222:225], v[62:65]
	v_mfma_f32_16x16x32_bf16 v[58:61], v[146:149], v[222:225], v[58:61]
	v_mfma_f32_16x16x32_bf16 v[54:57], v[156:159], v[222:225], v[54:57]
	v_mfma_f32_16x16x32_bf16 v[50:53], v[160:163], v[222:225], v[50:53]
	s_add_i32 m0, s49, 0x2000
	s_nop 0
	global_load_lds_dwordx4 v90, s[30:31]
	v_mfma_f32_16x16x32_bf16 v[46:49], v[142:145], v[226:229], v[46:49]
	v_mfma_f32_16x16x32_bf16 v[42:45], v[146:149], v[226:229], v[42:45]
	v_mfma_f32_16x16x32_bf16 v[38:41], v[156:159], v[226:229], v[38:41]
	v_mfma_f32_16x16x32_bf16 v[34:37], v[160:163], v[226:229], v[34:37]
	s_add_i32 m0, s49, 0x4000
	s_nop 0
	global_load_lds_dwordx4 v92, s[30:31]
	v_mfma_f32_16x16x32_bf16 v[18:21], v[142:145], v[230:233], v[18:21]
	v_mfma_f32_16x16x32_bf16 v[22:25], v[146:149], v[230:233], v[22:25]
	v_mfma_f32_16x16x32_bf16 v[26:29], v[156:159], v[230:233], v[26:29]
	v_mfma_f32_16x16x32_bf16 v[30:33], v[160:163], v[230:233], v[30:33]
	s_add_i32 m0, s49, 0x6000
	s_nop 0
	global_load_lds_dwordx4 v94, s[30:31]
	v_mfma_f32_16x16x32_bf16 v[2:5], v[142:145], v[234:237], v[2:5]
	v_mfma_f32_16x16x32_bf16 v[6:9], v[146:149], v[234:237], v[6:9]
	v_mfma_f32_16x16x32_bf16 v[10:13], v[156:159], v[234:237], v[10:13]
	v_mfma_f32_16x16x32_bf16 v[14:17], v[160:163], v[234:237], v[14:17]
	s_add_i32 m0, s49, 0x8000
	s_nop 0
	global_load_lds_dwordx4 v96, s[30:31]
	v_cvt_pk_bf16_f32 v172, v98, v100
	v_cvt_pk_bf16_f32 v173, v102, v104
	v_cvt_pk_bf16_f32 v174, v106, v108
	v_cvt_pk_bf16_f32 v175, v110, v112
	v_cvt_pk_bf16_f32 v176, v99, v101
	v_cvt_pk_bf16_f32 v177, v103, v105
	v_cvt_pk_bf16_f32 v178, v107, v109
	v_cvt_pk_bf16_f32 v179, v111, v113
	ds_write_b128 v95, v[172:175] offset:0
	ds_write_b128 v95, v[176:179] offset:128
	v_add_u32_e32 v91, s46, v135
	v_add_u32_e32 v93, s46, v137
	ds_read_b128 v[238:241], v139 offset:19456
	ds_read_b128 v[242:245], v139 offset:21504
	ds_read_b128 v[246:249], v139 offset:23552
	ds_read_b128 v[250:253], v139 offset:25600
	ds_read_b128 v[218:221], v91 offset:0
	ds_read_b128 v[222:225], v91 offset:2048
	ds_read_b128 v[226:229], v91 offset:4096
	ds_read_b128 v[230:233], v91 offset:6144
	ds_read_b128 v[234:237], v91 offset:8192
	s_waitcnt lgkmcnt(0)
	v_mfma_f32_16x16x32_bf16 v[78:81], v[238:241], v[218:221], v[78:81]
	v_mfma_f32_16x16x32_bf16 v[74:77], v[242:245], v[218:221], v[74:77]
	v_mfma_f32_16x16x32_bf16 v[70:73], v[246:249], v[218:221], v[70:73]
	v_mfma_f32_16x16x32_bf16 v[66:69], v[250:253], v[218:221], v[66:69]
	ds_read_b128 v[218:221], v93 offset:0
	ds_read_b128 v[142:145], v141 offset:19456
	v_mfma_f32_16x16x32_bf16 v[62:65], v[238:241], v[222:225], v[62:65]
	v_mfma_f32_16x16x32_bf16 v[58:61], v[242:245], v[222:225], v[58:61]
	v_mfma_f32_16x16x32_bf16 v[54:57], v[246:249], v[222:225], v[54:57]
	v_mfma_f32_16x16x32_bf16 v[50:53], v[250:253], v[222:225], v[50:53]
	ds_read_b128 v[222:225], v93 offset:2048
	ds_read_b128 v[146:149], v141 offset:21504
	v_mfma_f32_16x16x32_bf16 v[46:49], v[238:241], v[226:229], v[46:49]
	v_mfma_f32_16x16x32_bf16 v[42:45], v[242:245], v[226:229], v[42:45]
	v_mfma_f32_16x16x32_bf16 v[38:41], v[246:249], v[226:229], v[38:41]
	v_mfma_f32_16x16x32_bf16 v[34:37], v[250:253], v[226:229], v[34:37]
	ds_read_b128 v[226:229], v93 offset:4096
	ds_read_b128 v[156:159], v141 offset:23552
	v_mfma_f32_16x16x32_bf16 v[18:21], v[238:241], v[230:233], v[18:21]
	v_mfma_f32_16x16x32_bf16 v[22:25], v[242:245], v[230:233], v[22:25]
	v_mfma_f32_16x16x32_bf16 v[26:29], v[246:249], v[230:233], v[26:29]
	v_mfma_f32_16x16x32_bf16 v[30:33], v[250:253], v[230:233], v[30:33]
	ds_read_b128 v[230:233], v93 offset:6144
	ds_read_b128 v[160:163], v141 offset:25600
	v_mfma_f32_16x16x32_bf16 v[2:5], v[238:241], v[234:237], v[2:5]
	v_mfma_f32_16x16x32_bf16 v[6:9], v[242:245], v[234:237], v[6:9]
	v_mfma_f32_16x16x32_bf16 v[10:13], v[246:249], v[234:237], v[10:13]
	v_mfma_f32_16x16x32_bf16 v[14:17], v[250:253], v[234:237], v[14:17]
	ds_read_b128 v[234:237], v93 offset:8192
	s_waitcnt vmcnt(13)
	s_waitcnt lgkmcnt(0)
	s_barrier
; #define MD_GLDS_A(buf, tau) do { _Pragma("unroll") for (int i = 0; i < 5; ++i) if (amask & (1u << i)) \
;         __builtin_amdgcn_global_load_lds((const unsigned*)((const char*)HIDp + aoff[i] + (size_t)((tau) & 7) * 128), (PG8_LAS unsigned*)(MD_SA(buf) + wid * 1024 + i * 8192), 16, 0, 0); } while (0)
; #define MD_B_ISSUE(sb, tau) do { const char* kb_ = Bb + (size_t)((tau) >> 3) * 512 + (size_t)((tau) & 7) * (64 * (size_t)RB); _Pragma("unroll") for (int j = 0; j < 8; ++j) { const char* p_ = kb_ + (size_t)j * RB; \
;         asm volatile("global_load_dwordx2 %0, %1, off" : "=&v"(sb[j]) : "v"(p_) : "memory"); } } while (0)
; #define MD_B_WAIT(sb, N) asm volatile("s_waitcnt vmcnt(%8)" : "+v"(sb[0]), "+v"(sb[1]), "+v"(sb[2]), "+v"(sb[3]), "+v"(sb[4]), "+v"(sb[5]), "+v"(sb[6]), "+v"(sb[7]) : "n"(N) : "memory")
; #define MD_END(last) do { if (last) asm volatile("s_waitcnt vmcnt(0)" ::: "memory"); else asm volatile("s_waitcnt vmcnt(8)" ::: "memory"); \
;         asm volatile("s_waitcnt lgkmcnt(0)" ::: "memory"); __builtin_amdgcn_s_barrier(); asm volatile("" ::: "memory"); } while (0)
; __device__ __forceinline__ void moe_down_stream(PG8_LAS unsigned char* lds, int e, int cb0, int slot0, int nv, const bf16_t* HIDp, const float* Wd, bf16_t* Y, const float* slot_w, const int* slot_dst) {
;     ...
;     for (int t = 0; t < NT; t += 2) {
;         if (t + 2 < NT) MD_B_WAIT(s1, 8); else MD_B_WAIT(s1, 0);
;         MD_B_WRITE(s1, 1); __builtin_amdgcn_sched_barrier(0); MD_GLDS_A(1, t + 1); __builtin_amdgcn_sched_barrier(0);
;         if (t + 3 < NT) MD_B_ISSUE(s1, t + 3);
;         MD_COMPUTE(0);
;         MD_END(t + 3 >= NT);
;         if (t + 2 < NT) { MD_B_WAIT(s0, 8); MD_B_WRITE(s0, 0); __builtin_amdgcn_sched_barrier(0); MD_GLDS_A(0, t + 2); __builtin_amdgcn_sched_barrier(0); }
;         if (t + 4 < NT) MD_B_ISSUE(s0, t + 4);
;         MD_COMPUTE(1);
;         MD_END(t + 4 >= NT);
	s_mov_b32 s49, s46
	s_mov_b32 s46, s47
	s_mov_b32 s47, s48
	s_mov_b32 s48, s49
	s_add_i32 s50, s50, 1
	s_add_i32 s49, s48, s74
	s_add_i32 s52, s52, 1
	s_and_b32 s54, s52, 7
	s_cmp_eq_u32 s54, 0
	s_cselect_b32 s54, s53, s32
	s_cselect_b32 s55, -1, 0
	s_add_u32 s30, s30, s54
	s_addc_u32 s31, s31, s55
	v_mfma_f32_16x16x32_bf16 v[78:81], v[142:145], v[218:221], v[78:81]
	v_mfma_f32_16x16x32_bf16 v[74:77], v[146:149], v[218:221], v[74:77]
	v_mfma_f32_16x16x32_bf16 v[70:73], v[156:159], v[218:221], v[70:73]
	v_mfma_f32_16x16x32_bf16 v[66:69], v[160:163], v[218:221], v[66:69]
	s_mov_b32 m0, s49
	s_nop 0
	global_load_lds_dwordx4 v88, s[30:31]
	v_mfma_f32_16x16x32_bf16 v[62:65], v[142:145], v[222:225], v[62:65]
	v_mfma_f32_16x16x32_bf16 v[58:61], v[146:149], v[222:225], v[58:61]
	v_mfma_f32_16x16x32_bf16 v[54:57], v[156:159], v[222:225], v[54:57]
	v_mfma_f32_16x16x32_bf16 v[50:53], v[160:163], v[222:225], v[50:53]
	s_add_i32 m0, s49, 0x2000
	s_nop 0
	global_load_lds_dwordx4 v90, s[30:31]
	v_mfma_f32_16x16x32_bf16 v[46:49], v[142:145], v[226:229], v[46:49]
	v_mfma_f32_16x16x32_bf16 v[42:45], v[146:149], v[226:229], v[42:45]
	v_mfma_f32_16x16x32_bf16 v[38:41], v[156:159], v[226:229], v[38:41]
	v_mfma_f32_16x16x32_bf16 v[34:37], v[160:163], v[226:229], v[34:37]
	s_add_i32 m0, s49, 0x4000
	s_nop 0
	global_load_lds_dwordx4 v92, s[30:31]
	v_mfma_f32_16x16x32_bf16 v[18:21], v[142:145], v[230:233], v[18:21]
	v_mfma_f32_16x16x32_bf16 v[22:25], v[146:149], v[230:233], v[22:25]
	v_mfma_f32_16x16x32_bf16 v[26:29], v[156:159], v[230:233], v[26:29]
	v_mfma_f32_16x16x32_bf16 v[30:33], v[160:163], v[230:233], v[30:33]
	s_add_i32 m0, s49, 0x6000
	s_nop 0
	global_load_lds_dwordx4 v94, s[30:31]
	v_mfma_f32_16x16x32_bf16 v[2:5], v[142:145], v[234:237], v[2:5]
	v_mfma_f32_16x16x32_bf16 v[6:9], v[146:149], v[234:237], v[6:9]
	v_mfma_f32_16x16x32_bf16 v[10:13], v[156:159], v[234:237], v[10:13]
	v_mfma_f32_16x16x32_bf16 v[14:17], v[160:163], v[234:237], v[14:17]
	s_add_i32 m0, s49, 0x8000
	s_nop 0
	global_load_lds_dwordx4 v96, s[30:31]
	v_cvt_pk_bf16_f32 v172, v114, v116
	v_cvt_pk_bf16_f32 v173, v118, v120
	v_cvt_pk_bf16_f32 v174, v122, v124
	v_cvt_pk_bf16_f32 v175, v126, v128
	v_cvt_pk_bf16_f32 v176, v115, v117
	v_cvt_pk_bf16_f32 v177, v119, v121
	v_cvt_pk_bf16_f32 v178, v123, v125
	v_cvt_pk_bf16_f32 v179, v127, v129
	ds_write_b128 v95, v[172:175] offset:19456
	ds_write_b128 v95, v[176:179] offset:19584
	v_add_u32_e32 v91, s46, v135
	v_add_u32_e32 v93, s46, v137
	ds_read_b128 v[238:241], v139 offset:0
	ds_read_b128 v[242:245], v139 offset:2048
	ds_read_b128 v[246:249], v139 offset:4096
	ds_read_b128 v[250:253], v139 offset:6144
	ds_read_b128 v[218:221], v91 offset:0
	ds_read_b128 v[222:225], v91 offset:2048
	ds_read_b128 v[226:229], v91 offset:4096
	ds_read_b128 v[230:233], v91 offset:6144
	ds_read_b128 v[234:237], v91 offset:8192
	s_waitcnt lgkmcnt(0)
	v_mfma_f32_16x16x32_bf16 v[78:81], v[238:241], v[218:221], v[78:81]
	v_mfma_f32_16x16x32_bf16 v[74:77], v[242:245], v[218:221], v[74:77]
	v_mfma_f32_16x16x32_bf16 v[70:73], v[246:249], v[218:221], v[70:73]
	v_mfma_f32_16x16x32_bf16 v[66:69], v[250:253], v[218:221], v[66:69]
	ds_read_b128 v[218:221], v93 offset:0
	ds_read_b128 v[142:145], v141 offset:0
	v_mfma_f32_16x16x32_bf16 v[62:65], v[238:241], v[222:225], v[62:65]
	v_mfma_f32_16x16x32_bf16 v[58:61], v[242:245], v[222:225], v[58:61]
	v_mfma_f32_16x16x32_bf16 v[54:57], v[246:249], v[222:225], v[54:57]
	v_mfma_f32_16x16x32_bf16 v[50:53], v[250:253], v[222:225], v[50:53]
	ds_read_b128 v[222:225], v93 offset:2048
	ds_read_b128 v[146:149], v141 offset:2048
	v_mfma_f32_16x16x32_bf16 v[46:49], v[238:241], v[226:229], v[46:49]
	v_mfma_f32_16x16x32_bf16 v[42:45], v[242:245], v[226:229], v[42:45]
	v_mfma_f32_16x16x32_bf16 v[38:41], v[246:249], v[226:229], v[38:41]
	v_mfma_f32_16x16x32_bf16 v[34:37], v[250:253], v[226:229], v[34:37]
	ds_read_b128 v[226:229], v93 offset:4096
	ds_read_b128 v[156:159], v141 offset:4096
	v_mfma_f32_16x16x32_bf16 v[18:21], v[238:241], v[230:233], v[18:21]
	v_mfma_f32_16x16x32_bf16 v[22:25], v[242:245], v[230:233], v[22:25]
	v_mfma_f32_16x16x32_bf16 v[26:29], v[246:249], v[230:233], v[26:29]
	v_mfma_f32_16x16x32_bf16 v[30:33], v[250:253], v[230:233], v[30:33]
	ds_read_b128 v[230:233], v93 offset:6144
	ds_read_b128 v[160:163], v141 offset:6144
	v_mfma_f32_16x16x32_bf16 v[2:5], v[238:241], v[234:237], v[2:5]
	v_mfma_f32_16x16x32_bf16 v[6:9], v[242:245], v[234:237], v[6:9]
	v_mfma_f32_16x16x32_bf16 v[10:13], v[246:249], v[234:237], v[10:13]
	v_mfma_f32_16x16x32_bf16 v[14:17], v[250:253], v[234:237], v[14:17]
	ds_read_b128 v[234:237], v93 offset:8192
	s_waitcnt vmcnt(5)
	s_waitcnt lgkmcnt(0)
	s_barrier
; #define MD_GLDS_A(buf, tau) do { _Pragma("unroll") for (int i = 0; i < 5; ++i) if (amask & (1u << i)) \
;         __builtin_amdgcn_global_load_lds((const unsigned*)((const char*)HIDp + aoff[i] + (size_t)((tau) & 7) * 128), (PG8_LAS unsigned*)(MD_SA(buf) + wid * 1024 + i * 8192), 16, 0, 0); } while (0)
; #define MD_B_ISSUE(sb, tau) do { const char* kb_ = Bb + (size_t)((tau) >> 3) * 512 + (size_t)((tau) & 7) * (64 * (size_t)RB); _Pragma("unroll") for (int j = 0; j < 8; ++j) { const char* p_ = kb_ + (size_t)j * RB; \
;         asm volatile("global_load_dwordx2 %0, %1, off" : "=&v"(sb[j]) : "v"(p_) : "memory"); } } while (0)
; #define MD_B_WAIT(sb, N) asm volatile("s_waitcnt vmcnt(%8)" : "+v"(sb[0]), "+v"(sb[1]), "+v"(sb[2]), "+v"(sb[3]), "+v"(sb[4]), "+v"(sb[5]), "+v"(sb[6]), "+v"(sb[7]) : "n"(N) : "memory")
; #define MD_END(last) do { if (last) asm volatile("s_waitcnt vmcnt(0)" ::: "memory"); else asm volatile("s_waitcnt vmcnt(8)" ::: "memory"); \
;         asm volatile("s_waitcnt lgkmcnt(0)" ::: "memory"); __builtin_amdgcn_s_barrier(); asm volatile("" ::: "memory"); } while (0)
; __device__ __forceinline__ void moe_down_stream(PG8_LAS unsigned char* lds, int e, int cb0, int slot0, int nv, const bf16_t* HIDp, const float* Wd, bf16_t* Y, const float* slot_w, const int* slot_dst) {
;     ...
;     for (int t = 0; t < NT; t += 2) {
;         if (t + 2 < NT) MD_B_WAIT(s1, 8); else MD_B_WAIT(s1, 0);
;         MD_B_WRITE(s1, 1); __builtin_amdgcn_sched_barrier(0); MD_GLDS_A(1, t + 1); __builtin_amdgcn_sched_barrier(0);
;         if (t + 3 < NT) MD_B_ISSUE(s1, t + 3);
;         MD_COMPUTE(0);
;         MD_END(t + 3 >= NT);
;         if (t + 2 < NT) { MD_B_WAIT(s0, 8); MD_B_WRITE(s0, 0); __builtin_amdgcn_sched_barrier(0); MD_GLDS_A(0, t + 2); __builtin_amdgcn_sched_barrier(0); }
;         if (t + 4 < NT) MD_B_ISSUE(s0, t + 4);
;         MD_COMPUTE(1);
;         MD_END(t + 4 >= NT);
	s_mov_b32 s49, s46
	s_mov_b32 s46, s47
	s_mov_b32 s47, s48
	s_mov_b32 s48, s49
	s_add_i32 s50, s50, 1
	s_add_i32 s49, s48, s74
	s_add_i32 s52, s52, 1
	s_and_b32 s54, s52, 7
	s_cmp_eq_u32 s54, 0
	s_cselect_b32 s54, s53, s32
	s_cselect_b32 s55, -1, 0
	s_add_u32 s30, s30, s54
	s_addc_u32 s31, s31, s55
	v_mfma_f32_16x16x32_bf16 v[78:81], v[142:145], v[218:221], v[78:81]
	v_mfma_f32_16x16x32_bf16 v[74:77], v[146:149], v[218:221], v[74:77]
	v_mfma_f32_16x16x32_bf16 v[70:73], v[156:159], v[218:221], v[70:73]
	v_mfma_f32_16x16x32_bf16 v[66:69], v[160:163], v[218:221], v[66:69]
	s_mov_b32 m0, s49
	s_nop 0
	global_load_lds_dwordx4 v88, s[30:31]
	v_mfma_f32_16x16x32_bf16 v[62:65], v[142:145], v[222:225], v[62:65]
	v_mfma_f32_16x16x32_bf16 v[58:61], v[146:149], v[222:225], v[58:61]
	v_mfma_f32_16x16x32_bf16 v[54:57], v[156:159], v[222:225], v[54:57]
	v_mfma_f32_16x16x32_bf16 v[50:53], v[160:163], v[222:225], v[50:53]
	s_add_i32 m0, s49, 0x2000
	s_nop 0
	global_load_lds_dwordx4 v90, s[30:31]
	v_mfma_f32_16x16x32_bf16 v[46:49], v[142:145], v[226:229], v[46:49]
	v_mfma_f32_16x16x32_bf16 v[42:45], v[146:149], v[226:229], v[42:45]
	v_mfma_f32_16x16x32_bf16 v[38:41], v[156:159], v[226:229], v[38:41]
	v_mfma_f32_16x16x32_bf16 v[34:37], v[160:163], v[226:229], v[34:37]
	s_add_i32 m0, s49, 0x4000
	s_nop 0
	global_load_lds_dwordx4 v92, s[30:31]
	v_mfma_f32_16x16x32_bf16 v[18:21], v[142:145], v[230:233], v[18:21]
	v_mfma_f32_16x16x32_bf16 v[22:25], v[146:149], v[230:233], v[22:25]
	v_mfma_f32_16x16x32_bf16 v[26:29], v[156:159], v[230:233], v[26:29]
	v_mfma_f32_16x16x32_bf16 v[30:33], v[160:163], v[230:233], v[30:33]
	s_add_i32 m0, s49, 0x6000
	s_nop 0
	global_load_lds_dwordx4 v94, s[30:31]
	v_mfma_f32_16x16x32_bf16 v[2:5], v[142:145], v[234:237], v[2:5]
	v_mfma_f32_16x16x32_bf16 v[6:9], v[146:149], v[234:237], v[6:9]
	v_mfma_f32_16x16x32_bf16 v[10:13], v[156:159], v[234:237], v[10:13]
	v_mfma_f32_16x16x32_bf16 v[14:17], v[160:163], v[234:237], v[14:17]
	s_add_i32 m0, s49, 0x8000
	s_nop 0
	global_load_lds_dwordx4 v96, s[30:31]
	v_cvt_pk_bf16_f32 v172, v186, v188
	v_cvt_pk_bf16_f32 v173, v190, v192
	v_cvt_pk_bf16_f32 v174, v194, v196
	v_cvt_pk_bf16_f32 v175, v198, v200
	v_cvt_pk_bf16_f32 v176, v187, v189
	v_cvt_pk_bf16_f32 v177, v191, v193
	v_cvt_pk_bf16_f32 v178, v195, v197
	v_cvt_pk_bf16_f32 v179, v199, v201
	ds_write_b128 v95, v[172:175] offset:0
	ds_write_b128 v95, v[176:179] offset:128
	v_add_u32_e32 v91, s46, v135
	v_add_u32_e32 v93, s46, v137
	ds_read_b128 v[238:241], v139 offset:19456
	ds_read_b128 v[242:245], v139 offset:21504
	ds_read_b128 v[246:249], v139 offset:23552
	ds_read_b128 v[250:253], v139 offset:25600
	ds_read_b128 v[218:221], v91 offset:0
	ds_read_b128 v[222:225], v91 offset:2048
	ds_read_b128 v[226:229], v91 offset:4096
	ds_read_b128 v[230:233], v91 offset:6144
	ds_read_b128 v[234:237], v91 offset:8192
	s_waitcnt lgkmcnt(0)
	v_mfma_f32_16x16x32_bf16 v[78:81], v[238:241], v[218:221], v[78:81]
	v_mfma_f32_16x16x32_bf16 v[74:77], v[242:245], v[218:221], v[74:77]
	v_mfma_f32_16x16x32_bf16 v[70:73], v[246:249], v[218:221], v[70:73]
	v_mfma_f32_16x16x32_bf16 v[66:69], v[250:253], v[218:221], v[66:69]
	ds_read_b128 v[218:221], v93 offset:0
	ds_read_b128 v[142:145], v141 offset:19456
	v_mfma_f32_16x16x32_bf16 v[62:65], v[238:241], v[222:225], v[62:65]
	v_mfma_f32_16x16x32_bf16 v[58:61], v[242:245], v[222:225], v[58:61]
	v_mfma_f32_16x16x32_bf16 v[54:57], v[246:249], v[222:225], v[54:57]
	v_mfma_f32_16x16x32_bf16 v[50:53], v[250:253], v[222:225], v[50:53]
	ds_read_b128 v[222:225], v93 offset:2048
	ds_read_b128 v[146:149], v141 offset:21504
	v_mfma_f32_16x16x32_bf16 v[46:49], v[238:241], v[226:229], v[46:49]
	v_mfma_f32_16x16x32_bf16 v[42:45], v[242:245], v[226:229], v[42:45]
	v_mfma_f32_16x16x32_bf16 v[38:41], v[246:249], v[226:229], v[38:41]
	v_mfma_f32_16x16x32_bf16 v[34:37], v[250:253], v[226:229], v[34:37]
	ds_read_b128 v[226:229], v93 offset:4096
	ds_read_b128 v[156:159], v141 offset:23552
	v_mfma_f32_16x16x32_bf16 v[18:21], v[238:241], v[230:233], v[18:21]
	v_mfma_f32_16x16x32_bf16 v[22:25], v[242:245], v[230:233], v[22:25]
	v_mfma_f32_16x16x32_bf16 v[26:29], v[246:249], v[230:233], v[26:29]
	v_mfma_f32_16x16x32_bf16 v[30:33], v[250:253], v[230:233], v[30:33]
	ds_read_b128 v[230:233], v93 offset:6144
	ds_read_b128 v[160:163], v141 offset:25600
	v_mfma_f32_16x16x32_bf16 v[2:5], v[238:241], v[234:237], v[2:5]
	v_mfma_f32_16x16x32_bf16 v[6:9], v[242:245], v[234:237], v[6:9]
	v_mfma_f32_16x16x32_bf16 v[10:13], v[246:249], v[234:237], v[10:13]
	v_mfma_f32_16x16x32_bf16 v[14:17], v[250:253], v[234:237], v[14:17]
	ds_read_b128 v[234:237], v93 offset:8192
	s_waitcnt vmcnt(5)
	s_waitcnt lgkmcnt(0)
	s_barrier
; #define MD_GLDS_A(buf, tau) do { _Pragma("unroll") for (int i = 0; i < 5; ++i) if (amask & (1u << i)) \
;         __builtin_amdgcn_global_load_lds((const unsigned*)((const char*)HIDp + aoff[i] + (size_t)((tau) & 7) * 128), (PG8_LAS unsigned*)(MD_SA(buf) + wid * 1024 + i * 8192), 16, 0, 0); } while (0)
; #define MD_B_ISSUE(sb, tau) do { const char* kb_ = Bb + (size_t)((tau) >> 3) * 512 + (size_t)((tau) & 7) * (64 * (size_t)RB); _Pragma("unroll") for (int j = 0; j < 8; ++j) { const char* p_ = kb_ + (size_t)j * RB; \
;         asm volatile("global_load_dwordx2 %0, %1, off" : "=&v"(sb[j]) : "v"(p_) : "memory"); } } while (0)
; #define MD_B_WAIT(sb, N) asm volatile("s_waitcnt vmcnt(%8)" : "+v"(sb[0]), "+v"(sb[1]), "+v"(sb[2]), "+v"(sb[3]), "+v"(sb[4]), "+v"(sb[5]), "+v"(sb[6]), "+v"(sb[7]) : "n"(N) : "memory")
; #define MD_END(last) do { if (last) asm volatile("s_waitcnt vmcnt(0)" ::: "memory"); else asm volatile("s_waitcnt vmcnt(8)" ::: "memory"); \
;         asm volatile("s_waitcnt lgkmcnt(0)" ::: "memory"); __builtin_amdgcn_s_barrier(); asm volatile("" ::: "memory"); } while (0)
; __device__ __forceinline__ void moe_down_stream(PG8_LAS unsigned char* lds, int e, int cb0, int slot0, int nv, const bf16_t* HIDp, const float* Wd, bf16_t* Y, const float* slot_w, const int* slot_dst) {
;     ...
;     for (int t = 0; t < NT; t += 2) {
;         if (t + 2 < NT) MD_B_WAIT(s1, 8); else MD_B_WAIT(s1, 0);
;         MD_B_WRITE(s1, 1); __builtin_amdgcn_sched_barrier(0); MD_GLDS_A(1, t + 1); __builtin_amdgcn_sched_barrier(0);
;         if (t + 3 < NT) MD_B_ISSUE(s1, t + 3);
;         MD_COMPUTE(0);
;         MD_END(t + 3 >= NT);
;         if (t + 2 < NT) { MD_B_WAIT(s0, 8); MD_B_WRITE(s0, 0); __builtin_amdgcn_sched_barrier(0); MD_GLDS_A(0, t + 2); __builtin_amdgcn_sched_barrier(0); }
;         if (t + 4 < NT) MD_B_ISSUE(s0, t + 4);
;         MD_COMPUTE(1);
;         MD_END(t + 4 >= NT);
	s_mov_b32 s49, s46
	s_mov_b32 s46, s47
	s_mov_b32 s47, s48
	s_mov_b32 s48, s49
	s_add_i32 s50, s50, 1
	v_mfma_f32_16x16x32_bf16 v[78:81], v[142:145], v[218:221], v[78:81]
	v_mfma_f32_16x16x32_bf16 v[74:77], v[146:149], v[218:221], v[74:77]
	v_mfma_f32_16x16x32_bf16 v[70:73], v[156:159], v[218:221], v[70:73]
	v_mfma_f32_16x16x32_bf16 v[66:69], v[160:163], v[218:221], v[66:69]
	v_mfma_f32_16x16x32_bf16 v[62:65], v[142:145], v[222:225], v[62:65]
	v_mfma_f32_16x16x32_bf16 v[58:61], v[146:149], v[222:225], v[58:61]
	v_mfma_f32_16x16x32_bf16 v[54:57], v[156:159], v[222:225], v[54:57]
	v_mfma_f32_16x16x32_bf16 v[50:53], v[160:163], v[222:225], v[50:53]
	v_mfma_f32_16x16x32_bf16 v[46:49], v[142:145], v[226:229], v[46:49]
	v_mfma_f32_16x16x32_bf16 v[42:45], v[146:149], v[226:229], v[42:45]
	v_mfma_f32_16x16x32_bf16 v[38:41], v[156:159], v[226:229], v[38:41]
	v_mfma_f32_16x16x32_bf16 v[34:37], v[160:163], v[226:229], v[34:37]
	v_mfma_f32_16x16x32_bf16 v[18:21], v[142:145], v[230:233], v[18:21]
	v_mfma_f32_16x16x32_bf16 v[22:25], v[146:149], v[230:233], v[22:25]
	v_mfma_f32_16x16x32_bf16 v[26:29], v[156:159], v[230:233], v[26:29]
	v_mfma_f32_16x16x32_bf16 v[30:33], v[160:163], v[230:233], v[30:33]
	v_mfma_f32_16x16x32_bf16 v[2:5], v[142:145], v[234:237], v[2:5]
	v_mfma_f32_16x16x32_bf16 v[6:9], v[146:149], v[234:237], v[6:9]
	v_mfma_f32_16x16x32_bf16 v[10:13], v[156:159], v[234:237], v[10:13]
	v_mfma_f32_16x16x32_bf16 v[14:17], v[160:163], v[234:237], v[14:17]
	v_cvt_pk_bf16_f32 v172, v202, v204
	v_cvt_pk_bf16_f32 v173, v206, v208
	v_cvt_pk_bf16_f32 v174, v210, v212
	v_cvt_pk_bf16_f32 v175, v214, v216
	v_cvt_pk_bf16_f32 v176, v203, v205
	v_cvt_pk_bf16_f32 v177, v207, v209
	v_cvt_pk_bf16_f32 v178, v211, v213
	v_cvt_pk_bf16_f32 v179, v215, v217
	ds_write_b128 v95, v[172:175] offset:19456
	ds_write_b128 v95, v[176:179] offset:19584
	v_add_u32_e32 v91, s46, v135
	v_add_u32_e32 v93, s46, v137
	ds_read_b128 v[238:241], v139 offset:0
	ds_read_b128 v[242:245], v139 offset:2048
	ds_read_b128 v[246:249], v139 offset:4096
	ds_read_b128 v[250:253], v139 offset:6144
	ds_read_b128 v[218:221], v91 offset:0
	ds_read_b128 v[222:225], v91 offset:2048
	ds_read_b128 v[226:229], v91 offset:4096
	ds_read_b128 v[230:233], v91 offset:6144
	ds_read_b128 v[234:237], v91 offset:8192
	s_waitcnt lgkmcnt(0)
	v_mfma_f32_16x16x32_bf16 v[78:81], v[238:241], v[218:221], v[78:81]
	v_mfma_f32_16x16x32_bf16 v[74:77], v[242:245], v[218:221], v[74:77]
	v_mfma_f32_16x16x32_bf16 v[70:73], v[246:249], v[218:221], v[70:73]
	v_mfma_f32_16x16x32_bf16 v[66:69], v[250:253], v[218:221], v[66:69]
	ds_read_b128 v[218:221], v93 offset:0
	ds_read_b128 v[142:145], v141 offset:0
	v_mfma_f32_16x16x32_bf16 v[62:65], v[238:241], v[222:225], v[62:65]
	v_mfma_f32_16x16x32_bf16 v[58:61], v[242:245], v[222:225], v[58:61]
	v_mfma_f32_16x16x32_bf16 v[54:57], v[246:249], v[222:225], v[54:57]
	v_mfma_f32_16x16x32_bf16 v[50:53], v[250:253], v[222:225], v[50:53]
	ds_read_b128 v[222:225], v93 offset:2048
	ds_read_b128 v[146:149], v141 offset:2048
	v_mfma_f32_16x16x32_bf16 v[46:49], v[238:241], v[226:229], v[46:49]
	v_mfma_f32_16x16x32_bf16 v[42:45], v[242:245], v[226:229], v[42:45]
	v_mfma_f32_16x16x32_bf16 v[38:41], v[246:249], v[226:229], v[38:41]
	v_mfma_f32_16x16x32_bf16 v[34:37], v[250:253], v[226:229], v[34:37]
	ds_read_b128 v[226:229], v93 offset:4096
	ds_read_b128 v[156:159], v141 offset:4096
	v_mfma_f32_16x16x32_bf16 v[18:21], v[238:241], v[230:233], v[18:21]
	v_mfma_f32_16x16x32_bf16 v[22:25], v[242:245], v[230:233], v[22:25]
	v_mfma_f32_16x16x32_bf16 v[26:29], v[246:249], v[230:233], v[26:29]
	v_mfma_f32_16x16x32_bf16 v[30:33], v[250:253], v[230:233], v[30:33]
	ds_read_b128 v[230:233], v93 offset:6144
	ds_read_b128 v[160:163], v141 offset:6144
	v_mfma_f32_16x16x32_bf16 v[2:5], v[238:241], v[234:237], v[2:5]
	v_mfma_f32_16x16x32_bf16 v[6:9], v[242:245], v[234:237], v[6:9]
	v_mfma_f32_16x16x32_bf16 v[10:13], v[246:249], v[234:237], v[10:13]
	v_mfma_f32_16x16x32_bf16 v[14:17], v[250:253], v[234:237], v[14:17]
	ds_read_b128 v[234:237], v93 offset:8192
	s_waitcnt vmcnt(0)
	s_waitcnt lgkmcnt(0)
	s_barrier
	s_mov_b32 s49, s46
	s_mov_b32 s46, s47
	s_mov_b32 s47, s48
	s_mov_b32 s48, s49
	s_add_i32 s50, s50, 1
	v_mfma_f32_16x16x32_bf16 v[78:81], v[142:145], v[218:221], v[78:81]
	v_mfma_f32_16x16x32_bf16 v[74:77], v[146:149], v[218:221], v[74:77]
	v_mfma_f32_16x16x32_bf16 v[70:73], v[156:159], v[218:221], v[70:73]
	v_mfma_f32_16x16x32_bf16 v[66:69], v[160:163], v[218:221], v[66:69]
	v_mfma_f32_16x16x32_bf16 v[62:65], v[142:145], v[222:225], v[62:65]
	v_mfma_f32_16x16x32_bf16 v[58:61], v[146:149], v[222:225], v[58:61]
	v_mfma_f32_16x16x32_bf16 v[54:57], v[156:159], v[222:225], v[54:57]
	v_mfma_f32_16x16x32_bf16 v[50:53], v[160:163], v[222:225], v[50:53]
	v_mfma_f32_16x16x32_bf16 v[46:49], v[142:145], v[226:229], v[46:49]
	v_mfma_f32_16x16x32_bf16 v[42:45], v[146:149], v[226:229], v[42:45]
	v_mfma_f32_16x16x32_bf16 v[38:41], v[156:159], v[226:229], v[38:41]
	v_mfma_f32_16x16x32_bf16 v[34:37], v[160:163], v[226:229], v[34:37]
	v_mfma_f32_16x16x32_bf16 v[18:21], v[142:145], v[230:233], v[18:21]
	v_mfma_f32_16x16x32_bf16 v[22:25], v[146:149], v[230:233], v[22:25]
	v_mfma_f32_16x16x32_bf16 v[26:29], v[156:159], v[230:233], v[26:29]
	v_mfma_f32_16x16x32_bf16 v[30:33], v[160:163], v[230:233], v[30:33]
	v_mfma_f32_16x16x32_bf16 v[2:5], v[142:145], v[234:237], v[2:5]
	v_mfma_f32_16x16x32_bf16 v[6:9], v[146:149], v[234:237], v[6:9]
	v_mfma_f32_16x16x32_bf16 v[10:13], v[156:159], v[234:237], v[10:13]
	v_mfma_f32_16x16x32_bf16 v[14:17], v[160:163], v[234:237], v[14:17]
	v_add_u32_e32 v91, s46, v135
	v_add_u32_e32 v93, s46, v137
	ds_read_b128 v[238:241], v139 offset:19456
	ds_read_b128 v[242:245], v139 offset:21504
	ds_read_b128 v[246:249], v139 offset:23552
	ds_read_b128 v[250:253], v139 offset:25600
	ds_read_b128 v[218:221], v91 offset:0
	ds_read_b128 v[222:225], v91 offset:2048
	ds_read_b128 v[226:229], v91 offset:4096
	ds_read_b128 v[230:233], v91 offset:6144
	ds_read_b128 v[234:237], v91 offset:8192
	s_waitcnt lgkmcnt(0)
; #define PG8_LAS __attribute__((address_space(3)))
; __device__ __forceinline__ unsigned cvtpk(float lo, float hi) { f32x2 v = {lo, hi}; bf16x2_t b = __builtin_convertvector(v, bf16x2_t); return __builtin_bit_cast(unsigned, b); }
; __device__ __forceinline__ void moe_down_stream(PG8_LAS unsigned char* lds, int e, int cb0, int slot0, int nv, const bf16_t* HIDp, const float* Wd, bf16_t* Y, const float* slot_w, const int* slot_dst) {
;     ...
;         if (((t + 1) & 7) == 7) {
;             const int cb = cb0 + ((t + 1) >> 3);
; #pragma unroll
;             for (int m = 0; m < DNM; ++m) {
;                 const float w_ = lw[4 * (16 * m + fr) + wr];
; #pragma unroll
;                 for (int p = 0; p < 2; ++p) { const f32x4 v0 = acc[m][2 * p] * w_, v1 = acc[m][2 * p + 1] * w_; u32x4 w; w.x = cvtpk(v0[0], v0[1]); w.y = cvtpk(v0[2], v0[3]); w.z = cvtpk(v1[0], v1[1]); w.w = cvtpk(v1[2], v1[3]);
;                     *(PG8_LAS u32x4*)(stg + fr * 128 + (((4 * p + fq) ^ (fr & 7)) * 16)) = w; }
; #pragma unroll
;                 for (int hh = 0; hh < 2; ++hh) { const int r = (lane >> 3) + 8 * hh, cc = lane & 7; const u32x4 d = *(const PG8_LAS u32x4*)(stg + r * 128 + ((cc ^ (r & 7)) * 16)); const int dst_ = ldst[4 * (16 * m + r) + wr];
;                     if (dst_ >= 0) *(u32x4*)(Y + (size_t)dst_ * D + 128 * cb + 64 * wc + 8 * cc) = d; }
; #pragma unroll
;                 for (int n = 0; n < 4; ++n) acc[m][n] = (f32x4){0.f, 0.f, 0.f, 0.f}; } }
	v_mfma_f32_16x16x32_bf16 v[78:81], v[238:241], v[218:221], v[78:81]
	v_mfma_f32_16x16x32_bf16 v[74:77], v[242:245], v[218:221], v[74:77]
	v_mfma_f32_16x16x32_bf16 v[70:73], v[246:249], v[218:221], v[70:73]
	v_mfma_f32_16x16x32_bf16 v[66:69], v[250:253], v[218:221], v[66:69]
	ds_read_b128 v[218:221], v93 offset:0
	ds_read_b128 v[142:145], v141 offset:19456
	v_mfma_f32_16x16x32_bf16 v[62:65], v[238:241], v[222:225], v[62:65]
	v_mfma_f32_16x16x32_bf16 v[58:61], v[242:245], v[222:225], v[58:61]
	v_mfma_f32_16x16x32_bf16 v[54:57], v[246:249], v[222:225], v[54:57]
	v_mfma_f32_16x16x32_bf16 v[50:53], v[250:253], v[222:225], v[50:53]
	ds_read_b128 v[222:225], v93 offset:2048
	ds_read_b128 v[146:149], v141 offset:21504
	v_mfma_f32_16x16x32_bf16 v[46:49], v[238:241], v[226:229], v[46:49]
	v_mfma_f32_16x16x32_bf16 v[42:45], v[242:245], v[226:229], v[42:45]
	v_mfma_f32_16x16x32_bf16 v[38:41], v[246:249], v[226:229], v[38:41]
	v_mfma_f32_16x16x32_bf16 v[34:37], v[250:253], v[226:229], v[34:37]
	ds_read_b128 v[226:229], v93 offset:4096
	ds_read_b128 v[156:159], v141 offset:23552
	v_mfma_f32_16x16x32_bf16 v[18:21], v[238:241], v[230:233], v[18:21]
	v_mfma_f32_16x16x32_bf16 v[22:25], v[242:245], v[230:233], v[22:25]
	v_mfma_f32_16x16x32_bf16 v[26:29], v[246:249], v[230:233], v[26:29]
	v_mfma_f32_16x16x32_bf16 v[30:33], v[250:253], v[230:233], v[30:33]
	ds_read_b128 v[230:233], v93 offset:6144
	ds_read_b128 v[160:163], v141 offset:25600
	v_mfma_f32_16x16x32_bf16 v[2:5], v[238:241], v[234:237], v[2:5]
	v_mfma_f32_16x16x32_bf16 v[6:9], v[242:245], v[234:237], v[6:9]
	v_mfma_f32_16x16x32_bf16 v[10:13], v[246:249], v[234:237], v[10:13]
	v_mfma_f32_16x16x32_bf16 v[14:17], v[250:253], v[234:237], v[14:17]
	ds_read_b128 v[234:237], v93 offset:8192
	s_waitcnt lgkmcnt(0)
	s_barrier
	s_mov_b32 s49, s46
	s_mov_b32 s46, s47
	s_mov_b32 s47, s48
	s_mov_b32 s48, s49
	s_add_i32 s50, s50, 1
	v_mfma_f32_16x16x32_bf16 v[78:81], v[142:145], v[218:221], v[78:81]
	v_mfma_f32_16x16x32_bf16 v[74:77], v[146:149], v[218:221], v[74:77]
	v_mfma_f32_16x16x32_bf16 v[70:73], v[156:159], v[218:221], v[70:73]
	v_mfma_f32_16x16x32_bf16 v[66:69], v[160:163], v[218:221], v[66:69]
	v_mfma_f32_16x16x32_bf16 v[62:65], v[142:145], v[222:225], v[62:65]
	v_mfma_f32_16x16x32_bf16 v[58:61], v[146:149], v[222:225], v[58:61]
	v_mfma_f32_16x16x32_bf16 v[54:57], v[156:159], v[222:225], v[54:57]
	v_mfma_f32_16x16x32_bf16 v[50:53], v[160:163], v[222:225], v[50:53]
	v_mfma_f32_16x16x32_bf16 v[46:49], v[142:145], v[226:229], v[46:49]
	v_mfma_f32_16x16x32_bf16 v[42:45], v[146:149], v[226:229], v[42:45]
	v_mfma_f32_16x16x32_bf16 v[38:41], v[156:159], v[226:229], v[38:41]
	v_mfma_f32_16x16x32_bf16 v[34:37], v[160:163], v[226:229], v[34:37]
	v_mfma_f32_16x16x32_bf16 v[18:21], v[142:145], v[230:233], v[18:21]
	v_mfma_f32_16x16x32_bf16 v[22:25], v[146:149], v[230:233], v[22:25]
	v_mfma_f32_16x16x32_bf16 v[26:29], v[156:159], v[230:233], v[26:29]
	v_mfma_f32_16x16x32_bf16 v[30:33], v[160:163], v[230:233], v[30:33]
	v_mfma_f32_16x16x32_bf16 v[2:5], v[142:145], v[234:237], v[2:5]
	v_mfma_f32_16x16x32_bf16 v[6:9], v[146:149], v[234:237], v[6:9]
	v_mfma_f32_16x16x32_bf16 v[10:13], v[156:159], v[234:237], v[10:13]
	v_mfma_f32_16x16x32_bf16 v[14:17], v[160:163], v[234:237], v[14:17]
	s_add_i32 s54, s48, s74
	v_add_u32_e32 v164, s54, v84
	v_add_u32_e32 v165, s54, v85
	ds_read_b32 v150, v82 offset:0
	ds_read_b32 v151, v83 offset:0
	ds_read_b32 v166, v83 offset:128
	s_waitcnt lgkmcnt(2)
	v_mul_f32_e32 v78, v150, v78
	v_mul_f32_e32 v79, v150, v79
	v_mul_f32_e32 v80, v150, v80
	v_mul_f32_e32 v81, v150, v81
	v_mul_f32_e32 v74, v150, v74
	v_mul_f32_e32 v75, v150, v75
	v_mul_f32_e32 v76, v150, v76
	v_mul_f32_e32 v77, v150, v77
	v_cvt_pk_bf16_f32 v182, v78, v79
	v_cvt_pk_bf16_f32 v183, v80, v81
	v_cvt_pk_bf16_f32 v184, v74, v75
	v_cvt_pk_bf16_f32 v185, v76, v77
	ds_write_b128 v164, v[182:185]
	v_mul_f32_e32 v70, v150, v70
	v_mul_f32_e32 v71, v150, v71
	v_mul_f32_e32 v72, v150, v72
	v_mul_f32_e32 v73, v150, v73
	v_mul_f32_e32 v66, v150, v66
	v_mul_f32_e32 v67, v150, v67
	v_mul_f32_e32 v68, v150, v68
	v_mul_f32_e32 v69, v150, v69
	v_cvt_pk_bf16_f32 v182, v70, v71
	v_cvt_pk_bf16_f32 v183, v72, v73
	v_cvt_pk_bf16_f32 v184, v66, v67
	v_cvt_pk_bf16_f32 v185, v68, v69
	v_xor_b32_e32 v167, 64, v164
	ds_write_b128 v167, v[182:185]
	v_mov_b32_e32 v78, 0
	v_mov_b32_e32 v74, 0
	v_mov_b32_e32 v70, 0
	v_mov_b32_e32 v66, 0
	v_mov_b32_e32 v79, 0
	v_mov_b32_e32 v75, 0
	v_mov_b32_e32 v71, 0
	v_mov_b32_e32 v67, 0
	v_mov_b32_e32 v80, 0
	v_mov_b32_e32 v76, 0
	v_mov_b32_e32 v72, 0
	v_mov_b32_e32 v68, 0
	v_mov_b32_e32 v81, 0
	v_mov_b32_e32 v77, 0
	v_mov_b32_e32 v73, 0
	v_mov_b32_e32 v69, 0
	ds_read_b128 v[182:185], v165 offset:0
	v_cmp_lt_i32_e32 vcc, -1, v151
	v_lshlrev_b32_e32 v148, 13, v151
	v_mov_b32_e32 v149, 0
	v_lshl_add_u64 v[148:149], v[148:149], 0, v[86:87]
	v_cndmask_b32_e32 v148, v168, v148, vcc
	v_cndmask_b32_e32 v149, v169, v149, vcc
	s_waitcnt lgkmcnt(0)
	global_store_dwordx4 v[148:149], v[182:185], off
	ds_read_b128 v[182:185], v165 offset:8192
	v_cmp_lt_i32_e32 vcc, -1, v166
	v_lshlrev_b32_e32 v148, 13, v166
	v_mov_b32_e32 v149, 0
	v_lshl_add_u64 v[148:149], v[148:149], 0, v[86:87]
	v_cndmask_b32_e32 v148, v168, v148, vcc
	v_cndmask_b32_e32 v149, v169, v149, vcc
	s_waitcnt lgkmcnt(0)
	global_store_dwordx4 v[148:149], v[182:185], off
	ds_read_b32 v150, v82 offset:256
	ds_read_b32 v151, v83 offset:256
	ds_read_b32 v166, v83 offset:384
	s_waitcnt lgkmcnt(2)
; #define PG8_LAS __attribute__((address_space(3)))
; __device__ __forceinline__ unsigned cvtpk(float lo, float hi) { f32x2 v = {lo, hi}; bf16x2_t b = __builtin_convertvector(v, bf16x2_t); return __builtin_bit_cast(unsigned, b); }
; __device__ __forceinline__ void moe_down_stream(PG8_LAS unsigned char* lds, int e, int cb0, int slot0, int nv, const bf16_t* HIDp, const float* Wd, bf16_t* Y, const float* slot_w, const int* slot_dst) {
;     ...
;             for (int m = 0; m < DNM; ++m) {
;                 const float w_ = lw[4 * (16 * m + fr) + wr];
; #pragma unroll
;                 for (int p = 0; p < 2; ++p) { const f32x4 v0 = acc[m][2 * p] * w_, v1 = acc[m][2 * p + 1] * w_; u32x4 w; w.x = cvtpk(v0[0], v0[1]); w.y = cvtpk(v0[2], v0[3]); w.z = cvtpk(v1[0], v1[1]); w.w = cvtpk(v1[2], v1[3]);
;                     *(PG8_LAS u32x4*)(stg + fr * 128 + (((4 * p + fq) ^ (fr & 7)) * 16)) = w; }
; #pragma unroll
;                 for (int hh = 0; hh < 2; ++hh) { const int r = (lane >> 3) + 8 * hh, cc = lane & 7; const u32x4 d = *(const PG8_LAS u32x4*)(stg + r * 128 + ((cc ^ (r & 7)) * 16)); const int dst_ = ldst[4 * (16 * m + r) + wr];
;                     if (dst_ >= 0) *(u32x4*)(Y + (size_t)dst_ * D + 128 * cb + 64 * wc + 8 * cc) = d; }
; #pragma unroll
;                 for (int n = 0; n < 4; ++n) acc[m][n] = (f32x4){0.f, 0.f, 0.f, 0.f}; } }
	v_mul_f32_e32 v62, v150, v62
	v_mul_f32_e32 v63, v150, v63
	v_mul_f32_e32 v64, v150, v64
	v_mul_f32_e32 v65, v150, v65
	v_mul_f32_e32 v58, v150, v58
	v_mul_f32_e32 v59, v150, v59
	v_mul_f32_e32 v60, v150, v60
	v_mul_f32_e32 v61, v150, v61
	v_cvt_pk_bf16_f32 v182, v62, v63
	v_cvt_pk_bf16_f32 v183, v64, v65
	v_cvt_pk_bf16_f32 v184, v58, v59
	v_cvt_pk_bf16_f32 v185, v60, v61
	ds_write_b128 v164, v[182:185]
	v_mul_f32_e32 v54, v150, v54
	v_mul_f32_e32 v55, v150, v55
	v_mul_f32_e32 v56, v150, v56
	v_mul_f32_e32 v57, v150, v57
	v_mul_f32_e32 v50, v150, v50
	v_mul_f32_e32 v51, v150, v51
	v_mul_f32_e32 v52, v150, v52
	v_mul_f32_e32 v53, v150, v53
	v_cvt_pk_bf16_f32 v182, v54, v55
	v_cvt_pk_bf16_f32 v183, v56, v57
	v_cvt_pk_bf16_f32 v184, v50, v51
	v_cvt_pk_bf16_f32 v185, v52, v53
	v_xor_b32_e32 v167, 64, v164
	ds_write_b128 v167, v[182:185]
	v_mov_b32_e32 v62, 0
	v_mov_b32_e32 v58, 0
	v_mov_b32_e32 v54, 0
	v_mov_b32_e32 v50, 0
	v_mov_b32_e32 v63, 0
	v_mov_b32_e32 v59, 0
	v_mov_b32_e32 v55, 0
	v_mov_b32_e32 v51, 0
	v_mov_b32_e32 v64, 0
	v_mov_b32_e32 v60, 0
	v_mov_b32_e32 v56, 0
	v_mov_b32_e32 v52, 0
	v_mov_b32_e32 v65, 0
	v_mov_b32_e32 v61, 0
	v_mov_b32_e32 v57, 0
	v_mov_b32_e32 v53, 0
	ds_read_b128 v[182:185], v165 offset:0
	v_cmp_lt_i32_e32 vcc, -1, v151
	v_lshlrev_b32_e32 v148, 13, v151
	v_mov_b32_e32 v149, 0
	v_lshl_add_u64 v[148:149], v[148:149], 0, v[86:87]
	v_cndmask_b32_e32 v148, v168, v148, vcc
	v_cndmask_b32_e32 v149, v169, v149, vcc
	s_waitcnt lgkmcnt(0)
	global_store_dwordx4 v[148:149], v[182:185], off
	ds_read_b128 v[182:185], v165 offset:8192
	v_cmp_lt_i32_e32 vcc, -1, v166
	v_lshlrev_b32_e32 v148, 13, v166
	v_mov_b32_e32 v149, 0
	v_lshl_add_u64 v[148:149], v[148:149], 0, v[86:87]
	v_cndmask_b32_e32 v148, v168, v148, vcc
	v_cndmask_b32_e32 v149, v169, v149, vcc
	s_waitcnt lgkmcnt(0)
	global_store_dwordx4 v[148:149], v[182:185], off
	ds_read_b32 v150, v82 offset:512
	ds_read_b32 v151, v83 offset:512
	ds_read_b32 v166, v83 offset:640
	s_waitcnt lgkmcnt(2)
	v_mul_f32_e32 v46, v150, v46
	v_mul_f32_e32 v47, v150, v47
	v_mul_f32_e32 v48, v150, v48
	v_mul_f32_e32 v49, v150, v49
	v_mul_f32_e32 v42, v150, v42
	v_mul_f32_e32 v43, v150, v43
	v_mul_f32_e32 v44, v150, v44
	v_mul_f32_e32 v45, v150, v45
	v_cvt_pk_bf16_f32 v182, v46, v47
	v_cvt_pk_bf16_f32 v183, v48, v49
	v_cvt_pk_bf16_f32 v184, v42, v43
	v_cvt_pk_bf16_f32 v185, v44, v45
	ds_write_b128 v164, v[182:185]
	v_mul_f32_e32 v38, v150, v38
	v_mul_f32_e32 v39, v150, v39
	v_mul_f32_e32 v40, v150, v40
	v_mul_f32_e32 v41, v150, v41
	v_mul_f32_e32 v34, v150, v34
	v_mul_f32_e32 v35, v150, v35
	v_mul_f32_e32 v36, v150, v36
	v_mul_f32_e32 v37, v150, v37
	v_cvt_pk_bf16_f32 v182, v38, v39
	v_cvt_pk_bf16_f32 v183, v40, v41
	v_cvt_pk_bf16_f32 v184, v34, v35
	v_cvt_pk_bf16_f32 v185, v36, v37
	v_xor_b32_e32 v167, 64, v164
	ds_write_b128 v167, v[182:185]
	v_mov_b32_e32 v46, 0
	v_mov_b32_e32 v42, 0
	v_mov_b32_e32 v38, 0
	v_mov_b32_e32 v34, 0
	v_mov_b32_e32 v47, 0
	v_mov_b32_e32 v43, 0
	v_mov_b32_e32 v39, 0
	v_mov_b32_e32 v35, 0
	v_mov_b32_e32 v48, 0
	v_mov_b32_e32 v44, 0
	v_mov_b32_e32 v40, 0
	v_mov_b32_e32 v36, 0
	v_mov_b32_e32 v49, 0
	v_mov_b32_e32 v45, 0
	v_mov_b32_e32 v41, 0
	v_mov_b32_e32 v37, 0
	ds_read_b128 v[182:185], v165 offset:0
	v_cmp_lt_i32_e32 vcc, -1, v151
	v_lshlrev_b32_e32 v148, 13, v151
	v_mov_b32_e32 v149, 0
	v_lshl_add_u64 v[148:149], v[148:149], 0, v[86:87]
	v_cndmask_b32_e32 v148, v168, v148, vcc
	v_cndmask_b32_e32 v149, v169, v149, vcc
	s_waitcnt lgkmcnt(0)
	global_store_dwordx4 v[148:149], v[182:185], off
	ds_read_b128 v[182:185], v165 offset:8192
	v_cmp_lt_i32_e32 vcc, -1, v166
	v_lshlrev_b32_e32 v148, 13, v166
	v_mov_b32_e32 v149, 0
	v_lshl_add_u64 v[148:149], v[148:149], 0, v[86:87]
	v_cndmask_b32_e32 v148, v168, v148, vcc
	v_cndmask_b32_e32 v149, v169, v149, vcc
	s_waitcnt lgkmcnt(0)
	global_store_dwordx4 v[148:149], v[182:185], off
	ds_read_b32 v150, v82 offset:768
	ds_read_b32 v151, v83 offset:768
	ds_read_b32 v166, v83 offset:896
	s_waitcnt lgkmcnt(2)
; #define PG8_LAS __attribute__((address_space(3)))
; __device__ __forceinline__ unsigned cvtpk(float lo, float hi) { f32x2 v = {lo, hi}; bf16x2_t b = __builtin_convertvector(v, bf16x2_t); return __builtin_bit_cast(unsigned, b); }
; __device__ __forceinline__ void moe_down_stream(PG8_LAS unsigned char* lds, int e, int cb0, int slot0, int nv, const bf16_t* HIDp, const float* Wd, bf16_t* Y, const float* slot_w, const int* slot_dst) {
;     ...
;         if (((t + 1) & 7) == 7) {
;             const int cb = cb0 + ((t + 1) >> 3);
; #pragma unroll
;             for (int m = 0; m < DNM; ++m) {
;                 const float w_ = lw[4 * (16 * m + fr) + wr];
; #pragma unroll
;                 for (int p = 0; p < 2; ++p) { const f32x4 v0 = acc[m][2 * p] * w_, v1 = acc[m][2 * p + 1] * w_; u32x4 w; w.x = cvtpk(v0[0], v0[1]); w.y = cvtpk(v0[2], v0[3]); w.z = cvtpk(v1[0], v1[1]); w.w = cvtpk(v1[2], v1[3]);
;                     *(PG8_LAS u32x4*)(stg + fr * 128 + (((4 * p + fq) ^ (fr & 7)) * 16)) = w; }
; #pragma unroll
;                 for (int hh = 0; hh < 2; ++hh) { const int r = (lane >> 3) + 8 * hh, cc = lane & 7; const u32x4 d = *(const PG8_LAS u32x4*)(stg + r * 128 + ((cc ^ (r & 7)) * 16)); const int dst_ = ldst[4 * (16 * m + r) + wr];
;                     if (dst_ >= 0) *(u32x4*)(Y + (size_t)dst_ * D + 128 * cb + 64 * wc + 8 * cc) = d; }
; #pragma unroll
;                 for (int n = 0; n < 4; ++n) acc[m][n] = (f32x4){0.f, 0.f, 0.f, 0.f}; } }
	v_mul_f32_e32 v18, v150, v18
	v_mul_f32_e32 v19, v150, v19
	v_mul_f32_e32 v20, v150, v20
	v_mul_f32_e32 v21, v150, v21
	v_mul_f32_e32 v22, v150, v22
	v_mul_f32_e32 v23, v150, v23
	v_mul_f32_e32 v24, v150, v24
	v_mul_f32_e32 v25, v150, v25
	v_cvt_pk_bf16_f32 v182, v18, v19
	v_cvt_pk_bf16_f32 v183, v20, v21
	v_cvt_pk_bf16_f32 v184, v22, v23
	v_cvt_pk_bf16_f32 v185, v24, v25
	ds_write_b128 v164, v[182:185]
	v_mul_f32_e32 v26, v150, v26
	v_mul_f32_e32 v27, v150, v27
	v_mul_f32_e32 v28, v150, v28
	v_mul_f32_e32 v29, v150, v29
	v_mul_f32_e32 v30, v150, v30
	v_mul_f32_e32 v31, v150, v31
	v_mul_f32_e32 v32, v150, v32
	v_mul_f32_e32 v33, v150, v33
	v_cvt_pk_bf16_f32 v182, v26, v27
	v_cvt_pk_bf16_f32 v183, v28, v29
	v_cvt_pk_bf16_f32 v184, v30, v31
	v_cvt_pk_bf16_f32 v185, v32, v33
	v_xor_b32_e32 v167, 64, v164
	ds_write_b128 v167, v[182:185]
	v_mov_b32_e32 v18, 0
	v_mov_b32_e32 v22, 0
	v_mov_b32_e32 v26, 0
	v_mov_b32_e32 v30, 0
	v_mov_b32_e32 v19, 0
	v_mov_b32_e32 v23, 0
	v_mov_b32_e32 v27, 0
	v_mov_b32_e32 v31, 0
	v_mov_b32_e32 v20, 0
	v_mov_b32_e32 v24, 0
	v_mov_b32_e32 v28, 0
	v_mov_b32_e32 v32, 0
	v_mov_b32_e32 v21, 0
	v_mov_b32_e32 v25, 0
	v_mov_b32_e32 v29, 0
	v_mov_b32_e32 v33, 0
	ds_read_b128 v[182:185], v165 offset:0
	v_cmp_lt_i32_e32 vcc, -1, v151
	v_lshlrev_b32_e32 v148, 13, v151
	v_mov_b32_e32 v149, 0
	v_lshl_add_u64 v[148:149], v[148:149], 0, v[86:87]
	v_cndmask_b32_e32 v148, v168, v148, vcc
	v_cndmask_b32_e32 v149, v169, v149, vcc
	s_waitcnt lgkmcnt(0)
	global_store_dwordx4 v[148:149], v[182:185], off
	ds_read_b128 v[182:185], v165 offset:8192
	v_cmp_lt_i32_e32 vcc, -1, v166
	v_lshlrev_b32_e32 v148, 13, v166
	v_mov_b32_e32 v149, 0
	v_lshl_add_u64 v[148:149], v[148:149], 0, v[86:87]
	v_cndmask_b32_e32 v148, v168, v148, vcc
	v_cndmask_b32_e32 v149, v169, v149, vcc
	s_waitcnt lgkmcnt(0)
	global_store_dwordx4 v[148:149], v[182:185], off
	ds_read_b32 v150, v82 offset:1024
	ds_read_b32 v151, v83 offset:1024
	ds_read_b32 v166, v83 offset:1152
	s_waitcnt lgkmcnt(2)
	v_mul_f32_e32 v2, v150, v2
	v_mul_f32_e32 v3, v150, v3
	v_mul_f32_e32 v4, v150, v4
	v_mul_f32_e32 v5, v150, v5
	v_mul_f32_e32 v6, v150, v6
	v_mul_f32_e32 v7, v150, v7
	v_mul_f32_e32 v8, v150, v8
	v_mul_f32_e32 v9, v150, v9
	v_cvt_pk_bf16_f32 v182, v2, v3
	v_cvt_pk_bf16_f32 v183, v4, v5
	v_cvt_pk_bf16_f32 v184, v6, v7
	v_cvt_pk_bf16_f32 v185, v8, v9
	ds_write_b128 v164, v[182:185]
	v_mul_f32_e32 v10, v150, v10
	v_mul_f32_e32 v11, v150, v11
	v_mul_f32_e32 v12, v150, v12
	v_mul_f32_e32 v13, v150, v13
	v_mul_f32_e32 v14, v150, v14
	v_mul_f32_e32 v15, v150, v15
	v_mul_f32_e32 v16, v150, v16
	v_mul_f32_e32 v17, v150, v17
	v_cvt_pk_bf16_f32 v182, v10, v11
	v_cvt_pk_bf16_f32 v183, v12, v13
	v_cvt_pk_bf16_f32 v184, v14, v15
	v_cvt_pk_bf16_f32 v185, v16, v17
	v_xor_b32_e32 v167, 64, v164
	ds_write_b128 v167, v[182:185]
	v_mov_b32_e32 v2, 0
	v_mov_b32_e32 v6, 0
	v_mov_b32_e32 v10, 0
	v_mov_b32_e32 v14, 0
	v_mov_b32_e32 v3, 0
	v_mov_b32_e32 v7, 0
	v_mov_b32_e32 v11, 0
	v_mov_b32_e32 v15, 0
	v_mov_b32_e32 v4, 0
	v_mov_b32_e32 v8, 0
	v_mov_b32_e32 v12, 0
	v_mov_b32_e32 v16, 0
	v_mov_b32_e32 v5, 0
	v_mov_b32_e32 v9, 0
	v_mov_b32_e32 v13, 0
	v_mov_b32_e32 v17, 0
	ds_read_b128 v[182:185], v165 offset:0
	v_cmp_lt_i32_e32 vcc, -1, v151
	v_lshlrev_b32_e32 v148, 13, v151
	v_mov_b32_e32 v149, 0
	v_lshl_add_u64 v[148:149], v[148:149], 0, v[86:87]
	v_cndmask_b32_e32 v148, v168, v148, vcc
	v_cndmask_b32_e32 v149, v169, v149, vcc
	s_waitcnt lgkmcnt(0)
	global_store_dwordx4 v[148:149], v[182:185], off
	ds_read_b128 v[182:185], v165 offset:8192
	v_cmp_lt_i32_e32 vcc, -1, v166
	v_lshlrev_b32_e32 v148, 13, v166
	v_mov_b32_e32 v149, 0
	v_lshl_add_u64 v[148:149], v[148:149], 0, v[86:87]
	v_cndmask_b32_e32 v148, v168, v148, vcc
	v_cndmask_b32_e32 v149, v169, v149, vcc
	s_waitcnt lgkmcnt(0)
	global_store_dwordx4 v[148:149], v[182:185], off
	v_add_co_u32_e32 v86, vcc, 0x400, v86
	s_nop 1
	v_addc_co_u32_e32 v87, vcc, 0, v87, vcc
	s_waitcnt lgkmcnt(0)
